# v78 with sc1 nt (write-through streaming) instead of nt on the 116 expert-weight conversion stores
# speedup vs baseline: 1.0020x; 1.0020x over previous
; #define LAS __attribute__((address_space(3)))
; __device__ __forceinline__ void tr_item8(const float* W, int ld, int K, int nblk, int item, unsigned char* WT, bool gu, float scale, LAS float* scr, int lane) {
;     const int kb = item / nblk, nb = item % nblk, k0 = 64 * kb, n0 = 32 * nb;
;     int drow0 = n0;
;     if (gu) { const int bj = n0 / FF, j = n0 - bj * FF; drow0 = 256 * (j / 128) + 128 * bj + (j % 128); }
;     { float t_[32];
; #pragma unroll
;       for (int i = 0; i < 32; ++i) t_[i] = W[(size_t)(k0 + 2 * i + (lane >> 5)) * ld + n0 + (lane & 31)];
; #pragma unroll
;       for (int i = 0; i < 32; ++i) scr[(2 * i + (lane >> 5)) * 33 + (lane & 31)] = t_[i] * scale; }
; __device__ __forceinline__ void convert_items(Frame& F, const Args& a, int lo, int hi, int w, int nw) {
;     ...
;         if (r < NE * I_GU) { const int e = r / I_GU, rr = r % I_GU; tr_item8(a.in[18] + (size_t)e * D * 2 * FF, 2 * FF, D, 224, rr, F.ws + WS_WMGU + (size_t)e * 2 * FF * D, true, WSC_GU, scr, lane); continue; } r -= NE * I_GU;
.LBB0_1132:
	s_cmpk_gt_i32 s37, 0x5ff
	s_mov_b64 s[24:25], -1
	s_cbranch_scc0 .LBB0_1154
	s_cmpk_gt_u32 s37, 0x7ff
	s_cbranch_scc0 .LBB0_1151
	s_cmpk_gt_u32 s37, 0xaff
	s_cbranch_scc0 .LBB0_1148
	s_cmpk_gt_u32 s37, 0xcff
	s_cbranch_scc0 .LBB0_1145
	s_cmpk_gt_u32 s37, 0x1aff
	s_cbranch_scc0 .LBB0_1142
	s_cmpk_gt_u32 s37, 0x21ff
	s_cbranch_scc0 .LBB0_1139
	s_add_i32 s16, s37, 0xde00
	s_bfe_u32 s24, s16, 0x70009
	s_mulk_i32 s24, 0x2493
	s_lshr_b32 s24, s24, 16
	s_mul_i32 s25, s24, 0xe00
	s_sub_i32 s16, s16, s25
	s_mul_i32 s25, s24, 0x1c00000
	s_add_u32 s27, s72, s25
	s_addc_u32 s51, s73, 0
	s_mul_i32 s24, s24, 0x700000
	s_add_u32 s24, s3, s24
	s_addc_u32 s25, s30, 0
	s_bfe_u32 s26, s16, 0xb0005
	s_mulk_i32 s26, 0x2493
	s_lshr_b32 s26, s26, 16
	s_mul_i32 s50, s26, 0xe0
	s_sub_i32 s50, s16, s50
	s_lshl_b32 s16, s50, 5
	s_and_b32 s52, s50, 0xffff
	s_cmpk_gt_u32 s52, 0x6f
	s_cselect_b32 s52, 0xfffff200, 0
	s_cselect_b32 s53, 0x80, 0
	s_add_i32 s16, s52, s16
	s_sext_i32_i16 s52, s16
	s_bfe_u32 s52, s52, 0x70018
	s_add_i32 s52, s16, s52
	s_sext_i32_i16 s54, s52
	s_and_b32 s52, s52, 0xff80
	s_sub_i32 s16, s16, s52
	s_lshl_b32 s54, s54, 1
	s_sext_i32_i16 s16, s16
	s_and_b32 s54, s54, 0xffffff00
	s_add_i32 s16, s53, s16
	s_lshl_b32 s50, s50, 7
	s_add_i32 s16, s16, s54
	s_lshl_b32 s26, s26, 6
	s_and_b32 s50, s50, 0x3ff80
	s_add_u32 s50, s27, s50
	s_addc_u32 s51, s51, 0
	v_add_u32_e32 v50, s26, v30
	v_lshl_add_u64 v[28:29], s[50:51], 0, v[0:1]
	v_mad_i64_i32 v[48:49], s[50:51], v50, s45, v[28:29]
	global_load_dword v51, v[48:49], off nt
	v_add_u32_e32 v48, 2, v50
	v_mad_i64_i32 v[48:49], s[50:51], v48, s45, v[28:29]
	global_load_dword v52, v[48:49], off nt
	v_add_u32_e32 v48, 4, v50
	v_mad_i64_i32 v[48:49], s[50:51], v48, s45, v[28:29]
	global_load_dword v53, v[48:49], off nt
	v_add_u32_e32 v48, 6, v50
	v_mad_i64_i32 v[48:49], s[50:51], v48, s45, v[28:29]
	global_load_dword v54, v[48:49], off nt
	v_add_u32_e32 v48, 8, v50
	v_mad_i64_i32 v[48:49], s[50:51], v48, s45, v[28:29]
	global_load_dword v55, v[48:49], off nt
	v_add_u32_e32 v48, 10, v50
	v_mad_i64_i32 v[48:49], s[50:51], v48, s45, v[28:29]
	global_load_dword v56, v[48:49], off nt
	v_add_u32_e32 v48, 12, v50
	v_mad_i64_i32 v[48:49], s[50:51], v48, s45, v[28:29]
	global_load_dword v57, v[48:49], off nt
	v_add_u32_e32 v48, 14, v50
	v_mad_i64_i32 v[48:49], s[50:51], v48, s45, v[28:29]
	global_load_dword v58, v[48:49], off nt
	v_add_u32_e32 v48, 16, v50
	v_mad_i64_i32 v[48:49], s[50:51], v48, s45, v[28:29]
	global_load_dword v59, v[48:49], off nt
	v_add_u32_e32 v48, 18, v50
	v_mad_i64_i32 v[48:49], s[50:51], v48, s45, v[28:29]
	global_load_dword v60, v[48:49], off nt
	v_add_u32_e32 v48, 20, v50
	v_mad_i64_i32 v[48:49], s[50:51], v48, s45, v[28:29]
	global_load_dword v61, v[48:49], off nt
	v_add_u32_e32 v48, 22, v50
	v_mad_i64_i32 v[48:49], s[50:51], v48, s45, v[28:29]
	global_load_dword v62, v[48:49], off nt
	v_add_u32_e32 v48, 24, v50
	v_mad_i64_i32 v[48:49], s[50:51], v48, s45, v[28:29]
	global_load_dword v63, v[48:49], off nt
	v_add_u32_e32 v48, 26, v50
	v_mad_i64_i32 v[48:49], s[50:51], v48, s45, v[28:29]
	global_load_dword v64, v[48:49], off nt
	v_add_u32_e32 v48, 28, v50
	v_mad_i64_i32 v[48:49], s[50:51], v48, s45, v[28:29]
	global_load_dword v65, v[48:49], off nt
	v_add_u32_e32 v48, 30, v50
	v_mad_i64_i32 v[48:49], s[50:51], v48, s45, v[28:29]
	global_load_dword v66, v[48:49], off nt
	v_add_u32_e32 v48, 32, v50
	v_mad_i64_i32 v[48:49], s[50:51], v48, s45, v[28:29]
	global_load_dword v67, v[48:49], off nt
	v_add_u32_e32 v48, 34, v50
	v_mad_i64_i32 v[48:49], s[50:51], v48, s45, v[28:29]
	global_load_dword v68, v[48:49], off nt
	v_add_u32_e32 v48, 36, v50
	v_mad_i64_i32 v[48:49], s[50:51], v48, s45, v[28:29]
	global_load_dword v69, v[48:49], off nt
	v_add_u32_e32 v48, 38, v50
	v_mad_i64_i32 v[48:49], s[50:51], v48, s45, v[28:29]
	global_load_dword v70, v[48:49], off nt
	v_add_u32_e32 v48, 40, v50
	v_mad_i64_i32 v[48:49], s[50:51], v48, s45, v[28:29]
	global_load_dword v71, v[48:49], off nt
	v_add_u32_e32 v48, 42, v50
	v_mad_i64_i32 v[48:49], s[50:51], v48, s45, v[28:29]
	global_load_dword v72, v[48:49], off nt
	v_add_u32_e32 v48, 44, v50
	v_mad_i64_i32 v[48:49], s[50:51], v48, s45, v[28:29]
	global_load_dword v73, v[48:49], off nt
	v_add_u32_e32 v48, 46, v50
	v_mad_i64_i32 v[48:49], s[50:51], v48, s45, v[28:29]
	global_load_dword v74, v[48:49], off nt
	v_add_u32_e32 v48, 48, v50
	v_mad_i64_i32 v[48:49], s[50:51], v48, s45, v[28:29]
	global_load_dword v75, v[48:49], off nt
	v_add_u32_e32 v48, 50, v50
	v_mad_i64_i32 v[48:49], s[50:51], v48, s45, v[28:29]
	global_load_dword v76, v[48:49], off nt
	v_add_u32_e32 v48, 52, v50
	v_mad_i64_i32 v[48:49], s[50:51], v48, s45, v[28:29]
	global_load_dword v77, v[48:49], off nt
	v_add_u32_e32 v48, 54, v50
	v_mad_i64_i32 v[48:49], s[50:51], v48, s45, v[28:29]
	global_load_dword v78, v[48:49], off nt
	v_add_u32_e32 v48, 56, v50
	v_mad_i64_i32 v[48:49], s[50:51], v48, s45, v[28:29]
	global_load_dword v79, v[48:49], off nt
	v_add_u32_e32 v48, 58, v50
	v_mad_i64_i32 v[48:49], s[50:51], v48, s45, v[28:29]
	global_load_dword v80, v[48:49], off nt
	v_add_u32_e32 v48, 60, v50
	v_mad_i64_i32 v[48:49], s[50:51], v48, s45, v[28:29]
	global_load_dword v48, v[48:49], off nt
	v_add_u32_e32 v49, 62, v50
	v_mad_i64_i32 v[28:29], s[50:51], v49, s45, v[28:29]
	global_load_dword v28, v[28:29], off nt
	s_waitcnt vmcnt(0)
; __device__ __forceinline__ unsigned cvt_pk4_fp8(float a, float b, float c, float d) { int w = 0; w = __builtin_amdgcn_cvt_pk_fp8_f32(a, b, w, false); w = __builtin_amdgcn_cvt_pk_fp8_f32(c, d, w, true); return (unsigned)w; }
; #define GAS __attribute__((address_space(1)))
; #define LAS __attribute__((address_space(3)))
; #define LDS_WAIT() asm volatile("s_waitcnt lgkmcnt(0)" ::: "memory")
; __device__ __forceinline__ void tr_item8(const float* W, int ld, int K, int nblk, int item, unsigned char* WT, bool gu, float scale, LAS float* scr, int lane) {
;     ...
;       for (int i = 0; i < 32; ++i) scr[(2 * i + (lane >> 5)) * 33 + (lane & 31)] = t_[i] * scale; }
;     LDS_WAIT(); asm volatile("" ::: "memory");
;     const int c = lane & 3;
; #pragma unroll
;     for (int j = 0; j < 2; ++j) { const int n = (lane >> 2) + 16 * j; const LAS float* sp = scr + (16 * c) * 33 + n;
;         v4u o; o.x = pg8::cvt_pk4_fp8(sp[0 * 33], sp[1 * 33], sp[2 * 33], sp[3 * 33]); o.y = pg8::cvt_pk4_fp8(sp[4 * 33], sp[5 * 33], sp[6 * 33], sp[7 * 33]);
;         o.z = pg8::cvt_pk4_fp8(sp[8 * 33], sp[9 * 33], sp[10 * 33], sp[11 * 33]); o.w = pg8::cvt_pk4_fp8(sp[12 * 33], sp[13 * 33], sp[14 * 33], sp[15 * 33]);
;         *(GAS v4u*)(WT + (size_t)(drow0 + n) * K + k0 + 16 * c) = o; }
;     LDS_WAIT(); asm volatile("" ::: "memory");
	v_mul_f32_e32 v29, 0x42800000, v51
	v_mul_f32_e32 v49, 0x42800000, v52
	ds_write2_b32 v31, v29, v49 offset1:66
	v_mul_f32_e32 v29, 0x42800000, v53
	v_mul_f32_e32 v49, 0x42800000, v54
	ds_write2_b32 v31, v29, v49 offset0:132 offset1:198
	v_mul_f32_e32 v29, 0x42800000, v55
	v_mul_f32_e32 v49, 0x42800000, v56
	ds_write2_b32 v40, v29, v49 offset0:8 offset1:74
	v_mul_f32_e32 v29, 0x42800000, v57
	v_mul_f32_e32 v49, 0x42800000, v58
	ds_write2_b32 v40, v29, v49 offset0:140 offset1:206
	v_mul_f32_e32 v29, 0x42800000, v59
	v_mul_f32_e32 v49, 0x42800000, v60
	ds_write2_b32 v41, v29, v49 offset0:16 offset1:82
	v_mul_f32_e32 v29, 0x42800000, v61
	v_mul_f32_e32 v49, 0x42800000, v62
	ds_write2_b32 v41, v29, v49 offset0:148 offset1:214
	v_mul_f32_e32 v29, 0x42800000, v63
	v_mul_f32_e32 v49, 0x42800000, v64
	ds_write2_b32 v42, v29, v49 offset0:24 offset1:90
	v_mul_f32_e32 v29, 0x42800000, v65
	v_mul_f32_e32 v49, 0x42800000, v66
	ds_write2_b32 v42, v29, v49 offset0:156 offset1:222
	v_mul_f32_e32 v29, 0x42800000, v67
	v_mul_f32_e32 v49, 0x42800000, v68
	ds_write2_b32 v43, v29, v49 offset0:32 offset1:98
	v_mul_f32_e32 v29, 0x42800000, v69
	v_mov_b32_e32 v50, v1
	v_mov_b32_e32 v51, v1
	s_add_u32 s24, s24, s26
	v_mul_f32_e32 v49, 0x42800000, v70
	ds_write2_b32 v43, v29, v49 offset0:164 offset1:230
	v_add_u32_e32 v84, s16, v32
	s_addc_u32 s25, s25, 0
	v_mul_f32_e32 v29, 0x42800000, v71
	v_ashrrev_i32_e32 v85, 31, v84
	v_lshlrev_b64 v[84:85], 10, v[84:85]
	v_readlane_b32 s52, v254, 36
	v_mul_f32_e32 v49, 0x42800000, v72
	ds_write2_b32 v44, v29, v49 offset0:40 offset1:106
	v_readlane_b32 s58, v254, 42
	v_readlane_b32 s59, v254, 43
	v_mul_f32_e32 v29, 0x42800000, v73
	v_readlane_b32 s60, v254, 44
	v_readlane_b32 s61, v254, 45
	v_readlane_b32 s62, v254, 46
	v_mul_f32_e32 v49, 0x42800000, v74
	ds_write2_b32 v44, v29, v49 offset0:172 offset1:238
	v_readlane_b32 s63, v254, 47
	v_readlane_b32 s64, v254, 48
	v_mul_f32_e32 v29, 0x42800000, v75
	v_readlane_b32 s65, v254, 49
	v_readlane_b32 s66, v254, 50
	v_readlane_b32 s67, v254, 51
	v_mul_f32_e32 v49, 0x42800000, v76
	ds_write2_b32 v45, v29, v49 offset0:48 offset1:114
	s_mov_b64 s[58:59], s[62:63]
	s_mov_b64 s[60:61], s[64:65]
	v_mul_f32_e32 v29, 0x42800000, v77
	v_readlane_b32 s53, v254, 37
	v_readlane_b32 s54, v254, 38
	v_readlane_b32 s55, v254, 39
	v_mul_f32_e32 v49, 0x42800000, v78
	ds_write2_b32 v45, v29, v49 offset0:180 offset1:246
	v_readlane_b32 s56, v254, 40
	v_readlane_b32 s57, v254, 41
	v_mul_f32_e32 v29, 0x42800000, v79
	s_mov_b64 s[62:63], s[66:67]
	v_mul_f32_e32 v49, 0x42800000, v80
	ds_write2_b32 v46, v29, v49 offset0:56 offset1:122
	v_mov_b32_e32 v49, v1
	v_mul_f32_e32 v29, 0x42800000, v48
	v_mov_b32_e32 v48, v1
	v_mul_f32_e32 v28, 0x42800000, v28
	ds_write2_b32 v46, v29, v28 offset0:188 offset1:254
	s_waitcnt lgkmcnt(0)
	ds_read2_b32 v[52:53], v33 offset1:16
	ds_read2_b32 v[54:55], v33 offset0:33 offset1:49
	ds_read2_b32 v[56:57], v33 offset0:66 offset1:82
	ds_read2_b32 v[58:59], v33 offset0:99 offset1:115
	ds_read2_b32 v[60:61], v33 offset0:132 offset1:148
	ds_read2_b32 v[62:63], v33 offset0:165 offset1:181
	ds_read2_b32 v[64:65], v33 offset0:198 offset1:214
	ds_read2_b32 v[66:67], v33 offset0:231 offset1:247
	ds_read2_b32 v[68:69], v47 offset0:8 offset1:24
	ds_read2_b32 v[70:71], v47 offset0:41 offset1:57
	ds_read2_b32 v[72:73], v47 offset0:74 offset1:90
	ds_read2_b32 v[74:75], v47 offset0:107 offset1:123
	ds_read2_b32 v[76:77], v47 offset0:140 offset1:156
	ds_read2_b32 v[78:79], v47 offset0:173 offset1:189
	ds_read2_b32 v[80:81], v47 offset0:206 offset1:222
	ds_read2_b32 v[82:83], v47 offset0:239 offset1:255
	s_waitcnt lgkmcnt(14)
	v_cvt_pk_fp8_f32 v48, v52, v54
	s_waitcnt lgkmcnt(10)
	v_cvt_pk_fp8_f32 v49, v60, v62
	s_waitcnt lgkmcnt(6)
	v_cvt_pk_fp8_f32 v50, v68, v70
	s_waitcnt lgkmcnt(2)
	v_cvt_pk_fp8_f32 v51, v76, v78
	v_cvt_pk_fp8_f32 v48, v56, v58 op_sel:[0,0,1]
	v_cvt_pk_fp8_f32 v49, v64, v66 op_sel:[0,0,1]
	v_cvt_pk_fp8_f32 v50, v72, v74 op_sel:[0,0,1]
	s_waitcnt lgkmcnt(0)
	v_cvt_pk_fp8_f32 v51, v80, v82 op_sel:[0,0,1]
	v_lshl_add_u64 v[28:29], s[24:25], 0, v[2:3]
	v_lshl_add_u64 v[84:85], v[28:29], 0, v[84:85]
	v_add_u32_e32 v52, s16, v34
	global_store_dwordx4 v[84:85], v[48:51], off sc1 nt
	s_mov_b64 s[24:25], 0
	s_nop 0
	v_mov_b32_e32 v48, v1
	v_mov_b32_e32 v49, v1
	v_mov_b32_e32 v50, v1
	v_mov_b32_e32 v51, v1
	v_cvt_pk_fp8_f32 v48, v53, v55
	v_cvt_pk_fp8_f32 v49, v61, v63
	v_cvt_pk_fp8_f32 v50, v69, v71
	v_cvt_pk_fp8_f32 v51, v77, v79
	v_cvt_pk_fp8_f32 v48, v57, v59 op_sel:[0,0,1]
	v_cvt_pk_fp8_f32 v49, v65, v67 op_sel:[0,0,1]
	v_cvt_pk_fp8_f32 v50, v73, v75 op_sel:[0,0,1]
	v_cvt_pk_fp8_f32 v51, v81, v83 op_sel:[0,0,1]
	v_ashrrev_i32_e32 v53, 31, v52
	v_lshlrev_b64 v[52:53], 10, v[52:53]
	v_lshl_add_u64 v[28:29], v[28:29], 0, v[52:53]
	global_store_dwordx4 v[28:29], v[48:51], off sc1 nt
	s_waitcnt lgkmcnt(0)
; #define LAS __attribute__((address_space(3)))
; __device__ __forceinline__ void tr_item8(const float* W, int ld, int K, int nblk, int item, unsigned char* WT, bool gu, float scale, LAS float* scr, int lane) {
;     const int kb = item / nblk, nb = item % nblk, k0 = 64 * kb, n0 = 32 * nb;
;     int drow0 = n0;
;     if (gu) { const int bj = n0 / FF, j = n0 - bj * FF; drow0 = 256 * (j / 128) + 128 * bj + (j % 128); }
;     { float t_[32];
; #pragma unroll
;       for (int i = 0; i < 32; ++i) t_[i] = W[(size_t)(k0 + 2 * i + (lane >> 5)) * ld + n0 + (lane & 31)];
; #pragma unroll
;       for (int i = 0; i < 32; ++i) scr[(2 * i + (lane >> 5)) * 33 + (lane & 31)] = t_[i] * scale; }
; __device__ __forceinline__ void convert_items(Frame& F, const Args& a, int lo, int hi, int w, int nw) {
;     ...
;         if (r < I_DN) { tr_item8(a.in[15], D, FF, 32, r, F.ws + WS_WDN, false, WSC_DN, scr, lane); continue; } r -= I_DN;
.LBB0_1139:
	s_andn2_b64 vcc, exec, s[24:25]
	s_cbranch_vccnz .LBB0_1141
	s_lshl_b32 s16, s37, 5
	s_and_b32 s24, s42, 0x1ffc0
	s_and_b32 s26, s16, 0x3e0
	v_add_u32_e32 v28, s24, v30
	s_lshl_b32 s16, s26, 2
	v_ashrrev_i32_e32 v29, 31, v28
	v_lshl_add_u64 v[48:49], v[4:5], 0, s[16:17]
	v_lshlrev_b64 v[28:29], 12, v[28:29]
	v_lshl_add_u64 v[28:29], v[48:49], 0, v[28:29]
	v_add_co_u32_e32 v48, vcc, 0x2000, v28
	global_load_dword v50, v[28:29], off nt
	s_nop 0
	v_addc_co_u32_e32 v49, vcc, 0, v29, vcc
	global_load_dword v51, v[48:49], off nt
	v_add_co_u32_e32 v48, vcc, 0x4000, v28
	s_mov_b32 s25, s17
	s_nop 0
	v_addc_co_u32_e32 v49, vcc, 0, v29, vcc
	global_load_dword v52, v[48:49], off nt
	v_add_co_u32_e32 v48, vcc, 0x6000, v28
	s_nop 1
	v_addc_co_u32_e32 v49, vcc, 0, v29, vcc
	global_load_dword v53, v[48:49], off nt
	v_add_co_u32_e32 v48, vcc, 0x8000, v28
	s_nop 1
	v_addc_co_u32_e32 v49, vcc, 0, v29, vcc
	global_load_dword v54, v[48:49], off nt
	v_add_co_u32_e32 v48, vcc, 0xa000, v28
	s_nop 1
	v_addc_co_u32_e32 v49, vcc, 0, v29, vcc
	global_load_dword v55, v[48:49], off nt
	v_add_co_u32_e32 v48, vcc, 0xc000, v28
	s_nop 1
	v_addc_co_u32_e32 v49, vcc, 0, v29, vcc
	global_load_dword v56, v[48:49], off nt
	v_add_co_u32_e32 v48, vcc, 0xe000, v28
	s_nop 1
	v_addc_co_u32_e32 v49, vcc, 0, v29, vcc
	global_load_dword v57, v[48:49], off nt
	v_add_co_u32_e32 v48, vcc, 0x10000, v28
	s_nop 1
	v_addc_co_u32_e32 v49, vcc, 0, v29, vcc
	global_load_dword v58, v[48:49], off nt
	v_add_co_u32_e32 v48, vcc, 0x12000, v28
	s_nop 1
	v_addc_co_u32_e32 v49, vcc, 0, v29, vcc
	global_load_dword v59, v[48:49], off nt
	v_add_co_u32_e32 v48, vcc, 0x14000, v28
	s_nop 1
	v_addc_co_u32_e32 v49, vcc, 0, v29, vcc
	global_load_dword v60, v[48:49], off nt
	v_add_co_u32_e32 v48, vcc, 0x16000, v28
	s_nop 1
	v_addc_co_u32_e32 v49, vcc, 0, v29, vcc
	global_load_dword v61, v[48:49], off nt
	v_add_co_u32_e32 v48, vcc, 0x18000, v28
	s_nop 1
	v_addc_co_u32_e32 v49, vcc, 0, v29, vcc
	global_load_dword v62, v[48:49], off nt
	v_add_co_u32_e32 v48, vcc, 0x1a000, v28
	s_nop 1
	v_addc_co_u32_e32 v49, vcc, 0, v29, vcc
	global_load_dword v63, v[48:49], off nt
	v_add_co_u32_e32 v48, vcc, 0x1c000, v28
	s_nop 1
	v_addc_co_u32_e32 v49, vcc, 0, v29, vcc
	global_load_dword v64, v[48:49], off nt
	v_add_co_u32_e32 v48, vcc, 0x1e000, v28
	s_nop 1
	v_addc_co_u32_e32 v49, vcc, 0, v29, vcc
	global_load_dword v65, v[48:49], off nt
	v_add_co_u32_e32 v48, vcc, 0x20000, v28
	s_nop 1
	v_addc_co_u32_e32 v49, vcc, 0, v29, vcc
	global_load_dword v66, v[48:49], off nt
	v_add_co_u32_e32 v48, vcc, 0x22000, v28
	s_nop 1
	v_addc_co_u32_e32 v49, vcc, 0, v29, vcc
	global_load_dword v67, v[48:49], off nt
	v_add_co_u32_e32 v48, vcc, 0x24000, v28
	s_nop 1
	v_addc_co_u32_e32 v49, vcc, 0, v29, vcc
	global_load_dword v68, v[48:49], off nt
	v_add_co_u32_e32 v48, vcc, 0x26000, v28
	s_nop 1
	v_addc_co_u32_e32 v49, vcc, 0, v29, vcc
	global_load_dword v69, v[48:49], off nt
	v_add_co_u32_e32 v48, vcc, 0x28000, v28
	s_nop 1
	v_addc_co_u32_e32 v49, vcc, 0, v29, vcc
	global_load_dword v70, v[48:49], off nt
	v_add_co_u32_e32 v48, vcc, 0x2a000, v28
	s_nop 1
	v_addc_co_u32_e32 v49, vcc, 0, v29, vcc
	global_load_dword v71, v[48:49], off nt
	v_add_co_u32_e32 v48, vcc, 0x2c000, v28
	s_nop 1
	v_addc_co_u32_e32 v49, vcc, 0, v29, vcc
	global_load_dword v72, v[48:49], off nt
	v_add_co_u32_e32 v48, vcc, 0x2e000, v28
	s_nop 1
	v_addc_co_u32_e32 v49, vcc, 0, v29, vcc
	global_load_dword v73, v[48:49], off nt
	v_add_co_u32_e32 v48, vcc, 0x30000, v28
	s_nop 1
	v_addc_co_u32_e32 v49, vcc, 0, v29, vcc
	global_load_dword v74, v[48:49], off nt
	v_add_co_u32_e32 v48, vcc, 0x32000, v28
	s_nop 1
	v_addc_co_u32_e32 v49, vcc, 0, v29, vcc
	global_load_dword v75, v[48:49], off nt
	v_add_co_u32_e32 v48, vcc, 0x34000, v28
	s_nop 1
	v_addc_co_u32_e32 v49, vcc, 0, v29, vcc
	global_load_dword v76, v[48:49], off nt
	v_add_co_u32_e32 v48, vcc, 0x36000, v28
	s_nop 1
	v_addc_co_u32_e32 v49, vcc, 0, v29, vcc
	global_load_dword v77, v[48:49], off nt
	v_add_co_u32_e32 v48, vcc, 0x38000, v28
	s_nop 1
	v_addc_co_u32_e32 v49, vcc, 0, v29, vcc
	global_load_dword v78, v[48:49], off nt
	v_add_co_u32_e32 v48, vcc, 0x3a000, v28
	s_nop 1
	v_addc_co_u32_e32 v49, vcc, 0, v29, vcc
	global_load_dword v79, v[48:49], off nt
	v_add_co_u32_e32 v48, vcc, 0x3c000, v28
	s_nop 1
	v_addc_co_u32_e32 v49, vcc, 0, v29, vcc
	v_add_co_u32_e32 v28, vcc, 0x3e000, v28
	global_load_dword v48, v[48:49], off nt
	s_nop 0
	v_addc_co_u32_e32 v29, vcc, 0, v29, vcc
	global_load_dword v28, v[28:29], off nt
	s_waitcnt vmcnt(0)
; __device__ __forceinline__ unsigned cvt_pk4_fp8(float a, float b, float c, float d) { int w = 0; w = __builtin_amdgcn_cvt_pk_fp8_f32(a, b, w, false); w = __builtin_amdgcn_cvt_pk_fp8_f32(c, d, w, true); return (unsigned)w; }
; #define GAS __attribute__((address_space(1)))
; #define LAS __attribute__((address_space(3)))
; #define LDS_WAIT() asm volatile("s_waitcnt lgkmcnt(0)" ::: "memory")
; __device__ __forceinline__ void tr_item8(const float* W, int ld, int K, int nblk, int item, unsigned char* WT, bool gu, float scale, LAS float* scr, int lane) {
;     ...
;       for (int i = 0; i < 32; ++i) scr[(2 * i + (lane >> 5)) * 33 + (lane & 31)] = t_[i] * scale; }
;     LDS_WAIT(); asm volatile("" ::: "memory");
;     const int c = lane & 3;
; #pragma unroll
;     for (int j = 0; j < 2; ++j) { const int n = (lane >> 2) + 16 * j; const LAS float* sp = scr + (16 * c) * 33 + n;
;         v4u o; o.x = pg8::cvt_pk4_fp8(sp[0 * 33], sp[1 * 33], sp[2 * 33], sp[3 * 33]); o.y = pg8::cvt_pk4_fp8(sp[4 * 33], sp[5 * 33], sp[6 * 33], sp[7 * 33]);
;         o.z = pg8::cvt_pk4_fp8(sp[8 * 33], sp[9 * 33], sp[10 * 33], sp[11 * 33]); o.w = pg8::cvt_pk4_fp8(sp[12 * 33], sp[13 * 33], sp[14 * 33], sp[15 * 33]);
;         *(GAS v4u*)(WT + (size_t)(drow0 + n) * K + k0 + 16 * c) = o; }
;     LDS_WAIT(); asm volatile("" ::: "memory");
	v_mul_f32_e32 v29, 0x43000000, v50
	v_mul_f32_e32 v49, 0x43000000, v51
	ds_write2_b32 v31, v29, v49 offset1:66
	v_mul_f32_e32 v29, 0x43000000, v52
	v_mul_f32_e32 v49, 0x43000000, v53
	ds_write2_b32 v31, v29, v49 offset0:132 offset1:198
	v_mul_f32_e32 v29, 0x43000000, v54
	v_mul_f32_e32 v49, 0x43000000, v55
	ds_write2_b32 v40, v29, v49 offset0:8 offset1:74
	v_mul_f32_e32 v29, 0x43000000, v56
	v_mul_f32_e32 v49, 0x43000000, v57
	ds_write2_b32 v40, v29, v49 offset0:140 offset1:206
	v_mul_f32_e32 v29, 0x43000000, v58
	v_mul_f32_e32 v49, 0x43000000, v59
	ds_write2_b32 v41, v29, v49 offset0:16 offset1:82
	v_mul_f32_e32 v29, 0x43000000, v60
	v_mul_f32_e32 v49, 0x43000000, v61
	ds_write2_b32 v41, v29, v49 offset0:148 offset1:214
	v_mul_f32_e32 v29, 0x43000000, v62
	v_mul_f32_e32 v49, 0x43000000, v63
	ds_write2_b32 v42, v29, v49 offset0:24 offset1:90
	v_mul_f32_e32 v29, 0x43000000, v64
	v_mul_f32_e32 v49, 0x43000000, v65
	ds_write2_b32 v42, v29, v49 offset0:156 offset1:222
	v_mul_f32_e32 v29, 0x43000000, v66
	v_mul_f32_e32 v49, 0x43000000, v67
	ds_write2_b32 v43, v29, v49 offset0:32 offset1:98
	v_mul_f32_e32 v29, 0x43000000, v68
	v_mul_f32_e32 v49, 0x43000000, v69
	ds_write2_b32 v43, v29, v49 offset0:164 offset1:230
	v_mul_f32_e32 v29, 0x43000000, v70
	v_mul_f32_e32 v49, 0x43000000, v71
	ds_write2_b32 v44, v29, v49 offset0:40 offset1:106
	v_mul_f32_e32 v29, 0x43000000, v72
	v_mul_f32_e32 v49, 0x43000000, v73
	ds_write2_b32 v44, v29, v49 offset0:172 offset1:238
	v_mov_b32_e32 v50, 0
	v_mov_b32_e32 v51, 0
	v_mul_f32_e32 v29, 0x43000000, v74
	v_mul_f32_e32 v49, 0x43000000, v75
	ds_write2_b32 v45, v29, v49 offset0:48 offset1:114
	v_mul_f32_e32 v29, 0x43000000, v76
	v_mul_f32_e32 v49, 0x43000000, v77
	ds_write2_b32 v45, v29, v49 offset0:180 offset1:246
	v_mul_f32_e32 v29, 0x43000000, v78
	v_mul_f32_e32 v49, 0x43000000, v79
	ds_write2_b32 v46, v29, v49 offset0:56 offset1:122
	v_mov_b32_e32 v49, 0
	v_mul_f32_e32 v29, 0x43000000, v48
	v_mov_b32_e32 v48, 0
	v_mul_f32_e32 v28, 0x43000000, v28
	ds_write2_b32 v46, v29, v28 offset0:188 offset1:254
	s_waitcnt lgkmcnt(0)
	ds_read2_b32 v[52:53], v33 offset1:16
	ds_read2_b32 v[54:55], v33 offset0:33 offset1:49
	ds_read2_b32 v[56:57], v33 offset0:66 offset1:82
	ds_read2_b32 v[58:59], v33 offset0:99 offset1:115
	ds_read2_b32 v[60:61], v33 offset0:132 offset1:148
	ds_read2_b32 v[62:63], v33 offset0:165 offset1:181
	ds_read2_b32 v[64:65], v33 offset0:198 offset1:214
	ds_read2_b32 v[66:67], v33 offset0:231 offset1:247
	ds_read2_b32 v[68:69], v47 offset0:8 offset1:24
	ds_read2_b32 v[70:71], v47 offset0:41 offset1:57
	ds_read2_b32 v[72:73], v47 offset0:74 offset1:90
	ds_read2_b32 v[74:75], v47 offset0:107 offset1:123
	ds_read2_b32 v[76:77], v47 offset0:140 offset1:156
	ds_read2_b32 v[78:79], v47 offset0:173 offset1:189
	ds_read2_b32 v[80:81], v47 offset0:206 offset1:222
	ds_read2_b32 v[82:83], v47 offset0:239 offset1:255
	s_waitcnt lgkmcnt(14)
	v_cvt_pk_fp8_f32 v48, v52, v54
	s_waitcnt lgkmcnt(10)
	v_cvt_pk_fp8_f32 v49, v60, v62
	s_waitcnt lgkmcnt(6)
	v_cvt_pk_fp8_f32 v50, v68, v70
	s_waitcnt lgkmcnt(2)
	v_cvt_pk_fp8_f32 v51, v76, v78
	v_cvt_pk_fp8_f32 v48, v56, v58 op_sel:[0,0,1]
	v_cvt_pk_fp8_f32 v49, v64, v66 op_sel:[0,0,1]
	v_cvt_pk_fp8_f32 v50, v72, v74 op_sel:[0,0,1]
	s_waitcnt lgkmcnt(0)
	v_cvt_pk_fp8_f32 v51, v80, v82 op_sel:[0,0,1]
	v_lshl_add_u64 v[28:29], v[18:19], 0, s[24:25]
	v_add_u32_e32 v52, s26, v32
	v_mad_i64_i32 v[84:85], s[24:25], v52, s44, v[28:29]
	global_store_dwordx4 v[84:85], v[48:51], off sc1 nt
	v_add_u32_e32 v52, s26, v34
	v_mad_i64_i32 v[28:29], s[24:25], v52, s44, v[28:29]
	v_mov_b32_e32 v48, 0
	v_mov_b32_e32 v49, 0
	v_mov_b32_e32 v50, 0
	v_mov_b32_e32 v51, 0
	v_cvt_pk_fp8_f32 v48, v53, v55
	v_cvt_pk_fp8_f32 v49, v61, v63
	v_cvt_pk_fp8_f32 v50, v69, v71
	v_cvt_pk_fp8_f32 v51, v77, v79
	v_cvt_pk_fp8_f32 v48, v57, v59 op_sel:[0,0,1]
	v_cvt_pk_fp8_f32 v49, v65, v67 op_sel:[0,0,1]
	v_cvt_pk_fp8_f32 v50, v73, v75 op_sel:[0,0,1]
	v_cvt_pk_fp8_f32 v51, v81, v83 op_sel:[0,0,1]
	global_store_dwordx4 v[28:29], v[48:51], off sc1 nt
	s_waitcnt lgkmcnt(0)

; #define LAS __attribute__((address_space(3)))
; __device__ __forceinline__ void tr_item8(const float* W, int ld, int K, int nblk, int item, unsigned char* WT, bool gu, float scale, LAS float* scr, int lane) {
;     const int kb = item / nblk, nb = item % nblk, k0 = 64 * kb, n0 = 32 * nb;
;     int drow0 = n0;
;     if (gu) { const int bj = n0 / FF, j = n0 - bj * FF; drow0 = 256 * (j / 128) + 128 * bj + (j % 128); }
;     { float t_[32];
; #pragma unroll
;       for (int i = 0; i < 32; ++i) t_[i] = W[(size_t)(k0 + 2 * i + (lane >> 5)) * ld + n0 + (lane & 31)];
; #pragma unroll
;       for (int i = 0; i < 32; ++i) scr[(2 * i + (lane >> 5)) * 33 + (lane & 31)] = t_[i] * scale; }
; __device__ __forceinline__ void convert_items(Frame& F, const Args& a, int lo, int hi, int w, int nw) {
;     ...
;         if (r < I_GU) { tr_item8(a.in[14], 2 * FF, D, 224, r, F.ws + WS_WGU, true, WSC_GU, scr, lane); continue; } r -= I_GU;
.LBB0_1142:
	s_andn2_b64 vcc, exec, s[24:25]
	s_cbranch_vccnz .LBB0_1144
	s_add_i32 s16, s37, 0xf300
	s_bfe_u32 s24, s16, 0xb0005
	s_mulk_i32 s24, 0x2493
	s_lshr_b32 s24, s24, 16
	s_mul_i32 s25, s24, 0xe0
	s_sub_i32 s16, s16, s25
	s_lshl_b32 s25, s16, 5
	s_and_b32 s26, s16, 0xffff
	s_cmpk_gt_u32 s26, 0x6f
	s_cselect_b32 s50, 0xfffff200, 0
	s_cselect_b32 s51, 0x80, 0
	s_lshl_b32 s16, s16, 7
	s_lshl_b32 s24, s24, 6
	s_and_b32 s16, s16, 0x3ff80
	v_add_u32_e32 v64, s24, v30
	v_lshl_add_u64 v[28:29], v[6:7], 0, s[16:17]
	v_mad_i64_i32 v[48:49], s[26:27], v64, s45, v[28:29]
	v_add_u32_e32 v50, 2, v64
	v_add_u32_e32 v52, 4, v64
	v_add_u32_e32 v54, 6, v64
	v_add_u32_e32 v56, 8, v64
	v_add_u32_e32 v58, 10, v64
	v_add_u32_e32 v60, 12, v64
	v_add_u32_e32 v62, 14, v64
	v_mad_i64_i32 v[50:51], s[26:27], v50, s45, v[28:29]
	v_mad_i64_i32 v[52:53], s[26:27], v52, s45, v[28:29]
	v_mad_i64_i32 v[54:55], s[26:27], v54, s45, v[28:29]
	v_mad_i64_i32 v[56:57], s[26:27], v56, s45, v[28:29]
	v_mad_i64_i32 v[58:59], s[26:27], v58, s45, v[28:29]
	v_mad_i64_i32 v[60:61], s[26:27], v60, s45, v[28:29]
	v_mad_i64_i32 v[62:63], s[26:27], v62, s45, v[28:29]
	global_load_dword v65, v[48:49], off nt
	global_load_dword v66, v[50:51], off nt
	global_load_dword v67, v[52:53], off nt
	global_load_dword v68, v[54:55], off nt
	global_load_dword v69, v[56:57], off nt
	global_load_dword v70, v[58:59], off nt
	global_load_dword v71, v[60:61], off nt
	global_load_dword v72, v[62:63], off nt
	v_add_u32_e32 v48, 16, v64
	v_mad_i64_i32 v[48:49], s[26:27], v48, s45, v[28:29]
	v_add_u32_e32 v50, 18, v64
	v_add_u32_e32 v52, 20, v64
	v_add_u32_e32 v54, 22, v64
	v_add_u32_e32 v56, 24, v64
	v_add_u32_e32 v58, 26, v64
	v_add_u32_e32 v60, 28, v64
	v_add_u32_e32 v62, 30, v64
	v_mad_i64_i32 v[50:51], s[26:27], v50, s45, v[28:29]
	v_mad_i64_i32 v[52:53], s[26:27], v52, s45, v[28:29]
	v_mad_i64_i32 v[54:55], s[26:27], v54, s45, v[28:29]
	v_mad_i64_i32 v[56:57], s[26:27], v56, s45, v[28:29]
	v_mad_i64_i32 v[58:59], s[26:27], v58, s45, v[28:29]
	v_mad_i64_i32 v[60:61], s[26:27], v60, s45, v[28:29]
	v_mad_i64_i32 v[62:63], s[26:27], v62, s45, v[28:29]
	global_load_dword v73, v[48:49], off nt
	global_load_dword v74, v[50:51], off nt
	global_load_dword v75, v[52:53], off nt
	global_load_dword v76, v[54:55], off nt
	global_load_dword v77, v[56:57], off nt
	global_load_dword v78, v[58:59], off nt
	global_load_dword v79, v[60:61], off nt
	global_load_dword v80, v[62:63], off nt
	v_add_u32_e32 v48, 32, v64
	v_add_u32_e32 v50, 34, v64
	v_add_u32_e32 v52, 36, v64
	v_add_u32_e32 v54, 38, v64
	v_add_u32_e32 v60, 44, v64
	v_mad_i64_i32 v[48:49], s[26:27], v48, s45, v[28:29]
	v_mad_i64_i32 v[50:51], s[26:27], v50, s45, v[28:29]
	v_mad_i64_i32 v[52:53], s[26:27], v52, s45, v[28:29]
	v_mad_i64_i32 v[54:55], s[26:27], v54, s45, v[28:29]
	v_add_u32_e32 v56, 40, v64
	v_add_u32_e32 v58, 42, v64
	v_mad_i64_i32 v[60:61], s[26:27], v60, s45, v[28:29]
	v_add_u32_e32 v62, 46, v64
	v_mad_i64_i32 v[56:57], s[26:27], v56, s45, v[28:29]
	v_mad_i64_i32 v[58:59], s[26:27], v58, s45, v[28:29]
	v_mad_i64_i32 v[62:63], s[26:27], v62, s45, v[28:29]
	global_load_dword v81, v[48:49], off nt
	global_load_dword v82, v[50:51], off nt
	global_load_dword v83, v[52:53], off nt
	global_load_dword v84, v[54:55], off nt
	global_load_dword v85, v[56:57], off nt
	global_load_dword v86, v[58:59], off nt
	s_nop 0
	global_load_dword v60, v[60:61], off nt
	s_nop 0
	global_load_dword v61, v[62:63], off nt
	v_add_u32_e32 v48, 48, v64
	v_add_u32_e32 v50, 50, v64
	v_add_u32_e32 v52, 52, v64
	v_add_u32_e32 v54, 54, v64
	v_mad_i64_i32 v[48:49], s[26:27], v48, s45, v[28:29]
	v_mad_i64_i32 v[50:51], s[26:27], v50, s45, v[28:29]
	v_mad_i64_i32 v[52:53], s[26:27], v52, s45, v[28:29]
	v_mad_i64_i32 v[54:55], s[26:27], v54, s45, v[28:29]
	v_add_u32_e32 v56, 56, v64
	v_add_u32_e32 v58, 58, v64
	v_mad_i64_i32 v[56:57], s[26:27], v56, s45, v[28:29]
	v_mad_i64_i32 v[58:59], s[26:27], v58, s45, v[28:29]
	global_load_dword v62, v[48:49], off nt
	s_nop 0
	global_load_dword v50, v[50:51], off nt
	s_nop 0
	global_load_dword v51, v[52:53], off nt
	s_nop 0
	global_load_dword v52, v[54:55], off nt
	global_load_dword v53, v[56:57], off nt
	s_nop 0
	global_load_dword v54, v[58:59], off nt
	v_add_u32_e32 v48, 60, v64
	v_add_u32_e32 v55, 62, v64
	v_mad_i64_i32 v[48:49], s[26:27], v48, s45, v[28:29]
	v_mad_i64_i32 v[28:29], s[26:27], v55, s45, v[28:29]
	global_load_dword v48, v[48:49], off nt
	s_nop 0
	global_load_dword v28, v[28:29], off nt
	s_waitcnt vmcnt(0)
; __device__ __forceinline__ unsigned cvt_pk4_fp8(float a, float b, float c, float d) { int w = 0; w = __builtin_amdgcn_cvt_pk_fp8_f32(a, b, w, false); w = __builtin_amdgcn_cvt_pk_fp8_f32(c, d, w, true); return (unsigned)w; }
; #define GAS __attribute__((address_space(1)))
; #define LAS __attribute__((address_space(3)))
; #define LDS_WAIT() asm volatile("s_waitcnt lgkmcnt(0)" ::: "memory")
; __device__ __forceinline__ void tr_item8(const float* W, int ld, int K, int nblk, int item, unsigned char* WT, bool gu, float scale, LAS float* scr, int lane) {
;     ...
;       for (int i = 0; i < 32; ++i) scr[(2 * i + (lane >> 5)) * 33 + (lane & 31)] = t_[i] * scale; }
;     LDS_WAIT(); asm volatile("" ::: "memory");
;     const int c = lane & 3;
; #pragma unroll
;     for (int j = 0; j < 2; ++j) { const int n = (lane >> 2) + 16 * j; const LAS float* sp = scr + (16 * c) * 33 + n;
;         v4u o; o.x = pg8::cvt_pk4_fp8(sp[0 * 33], sp[1 * 33], sp[2 * 33], sp[3 * 33]); o.y = pg8::cvt_pk4_fp8(sp[4 * 33], sp[5 * 33], sp[6 * 33], sp[7 * 33]);
;         o.z = pg8::cvt_pk4_fp8(sp[8 * 33], sp[9 * 33], sp[10 * 33], sp[11 * 33]); o.w = pg8::cvt_pk4_fp8(sp[12 * 33], sp[13 * 33], sp[14 * 33], sp[15 * 33]);
;         *(GAS v4u*)(WT + (size_t)(drow0 + n) * K + k0 + 16 * c) = o; }
;     LDS_WAIT(); asm volatile("" ::: "memory");
	v_mul_f32_e32 v29, 0x42800000, v65
	v_mul_f32_e32 v49, 0x42800000, v66
	ds_write2_b32 v31, v29, v49 offset1:66
	v_mul_f32_e32 v29, 0x42800000, v67
	v_mul_f32_e32 v49, 0x42800000, v68
	ds_write2_b32 v31, v29, v49 offset0:132 offset1:198
	v_mul_f32_e32 v29, 0x42800000, v69
	v_mul_f32_e32 v49, 0x42800000, v70
	ds_write2_b32 v40, v29, v49 offset0:8 offset1:74
	v_mul_f32_e32 v29, 0x42800000, v71
	v_mul_f32_e32 v49, 0x42800000, v72
	ds_write2_b32 v40, v29, v49 offset0:140 offset1:206
	s_add_i32 s16, s50, s25
	s_sext_i32_i16 s25, s16
	s_bfe_u32 s25, s25, 0x70018
	s_add_i32 s25, s16, s25
	s_sext_i32_i16 s26, s25
	s_and_b32 s25, s25, 0xff80
	s_sub_i32 s16, s16, s25
	s_lshl_b32 s26, s26, 1
	s_sext_i32_i16 s16, s16
	v_mul_f32_e32 v29, 0x42800000, v73
	v_mul_f32_e32 v49, 0x42800000, v74
	ds_write2_b32 v41, v29, v49 offset0:16 offset1:82
	v_mul_f32_e32 v29, 0x42800000, v75
	v_mul_f32_e32 v49, 0x42800000, v76
	ds_write2_b32 v41, v29, v49 offset0:148 offset1:214
	v_mul_f32_e32 v29, 0x42800000, v77
	v_mul_f32_e32 v49, 0x42800000, v78
	ds_write2_b32 v42, v29, v49 offset0:24 offset1:90
	v_mul_f32_e32 v29, 0x42800000, v79
	v_mul_f32_e32 v49, 0x42800000, v80
	ds_write2_b32 v42, v29, v49 offset0:156 offset1:222
	s_and_b32 s26, s26, 0xffffff00
	s_add_i32 s16, s51, s16
	s_add_i32 s16, s16, s26
	s_mov_b32 s25, s17
	v_mul_f32_e32 v29, 0x42800000, v81
	v_mul_f32_e32 v49, 0x42800000, v82
	ds_write2_b32 v43, v29, v49 offset0:32 offset1:98
	v_mul_f32_e32 v29, 0x42800000, v83
	v_mul_f32_e32 v49, 0x42800000, v84
	ds_write2_b32 v43, v29, v49 offset0:164 offset1:230
	v_mul_f32_e32 v29, 0x42800000, v85
	v_mul_f32_e32 v49, 0x42800000, v86
	ds_write2_b32 v44, v29, v49 offset0:40 offset1:106
	v_mul_f32_e32 v29, 0x42800000, v60
	v_mul_f32_e32 v49, 0x42800000, v61
	ds_write2_b32 v44, v29, v49 offset0:172 offset1:238
	v_add_u32_e32 v84, s16, v32
	v_ashrrev_i32_e32 v85, 31, v84
	v_lshlrev_b64 v[84:85], 10, v[84:85]
	v_mul_f32_e32 v29, 0x42800000, v62
	v_mul_f32_e32 v49, 0x42800000, v50
	ds_write2_b32 v45, v29, v49 offset0:48 offset1:114
	v_mul_f32_e32 v29, 0x42800000, v51
	v_mul_f32_e32 v49, 0x42800000, v52
	ds_write2_b32 v45, v29, v49 offset0:180 offset1:246
	v_mul_f32_e32 v29, 0x42800000, v53
	v_mul_f32_e32 v49, 0x42800000, v54
	ds_write2_b32 v46, v29, v49 offset0:56 offset1:122
	v_mov_b32_e32 v49, 0
	v_mov_b32_e32 v50, 0
	v_mul_f32_e32 v29, 0x42800000, v48
	v_mul_f32_e32 v28, 0x42800000, v28
	ds_write2_b32 v46, v29, v28 offset0:188 offset1:254
	s_waitcnt lgkmcnt(0)
	ds_read2_b32 v[52:53], v33 offset1:16
	ds_read2_b32 v[54:55], v33 offset0:33 offset1:49
	ds_read2_b32 v[56:57], v33 offset0:66 offset1:82
	ds_read2_b32 v[58:59], v33 offset0:99 offset1:115
	ds_read2_b32 v[60:61], v33 offset0:132 offset1:148
	ds_read2_b32 v[62:63], v33 offset0:165 offset1:181
	ds_read2_b32 v[64:65], v33 offset0:198 offset1:214
	ds_read2_b32 v[66:67], v33 offset0:231 offset1:247
	ds_read2_b32 v[68:69], v47 offset0:8 offset1:24
	ds_read2_b32 v[70:71], v47 offset0:41 offset1:57
	ds_read2_b32 v[72:73], v47 offset0:74 offset1:90
	ds_read2_b32 v[74:75], v47 offset0:107 offset1:123
	ds_read2_b32 v[76:77], v47 offset0:140 offset1:156
	ds_read2_b32 v[78:79], v47 offset0:173 offset1:189
	v_mov_b32_e32 v48, 0
	ds_read2_b32 v[80:81], v47 offset0:206 offset1:222
	ds_read2_b32 v[82:83], v47 offset0:239 offset1:255
	v_mov_b32_e32 v51, 0
	s_waitcnt lgkmcnt(14)
	v_cvt_pk_fp8_f32 v48, v52, v54
	s_waitcnt lgkmcnt(10)
	v_cvt_pk_fp8_f32 v49, v60, v62
	s_waitcnt lgkmcnt(6)
	v_cvt_pk_fp8_f32 v50, v68, v70
	s_waitcnt lgkmcnt(2)
	v_cvt_pk_fp8_f32 v51, v76, v78
	v_cvt_pk_fp8_f32 v48, v56, v58 op_sel:[0,0,1]
	v_cvt_pk_fp8_f32 v49, v64, v66 op_sel:[0,0,1]
	v_cvt_pk_fp8_f32 v50, v72, v74 op_sel:[0,0,1]
	s_waitcnt lgkmcnt(0)
	v_cvt_pk_fp8_f32 v51, v80, v82 op_sel:[0,0,1]
	v_lshl_add_u64 v[28:29], v[20:21], 0, s[24:25]
	v_lshl_add_u64 v[84:85], v[28:29], 0, v[84:85]
	v_add_u32_e32 v52, s16, v34
	global_store_dwordx4 v[84:85], v[48:51], off sc1 nt
	s_nop 1
	v_mov_b32_e32 v48, 0
	v_mov_b32_e32 v49, 0
	v_mov_b32_e32 v50, 0
	v_mov_b32_e32 v51, 0
	v_cvt_pk_fp8_f32 v48, v53, v55
	v_cvt_pk_fp8_f32 v49, v61, v63
	v_cvt_pk_fp8_f32 v50, v69, v71
	v_cvt_pk_fp8_f32 v51, v77, v79
	v_cvt_pk_fp8_f32 v48, v57, v59 op_sel:[0,0,1]
	v_cvt_pk_fp8_f32 v49, v65, v67 op_sel:[0,0,1]
	v_cvt_pk_fp8_f32 v50, v73, v75 op_sel:[0,0,1]
	v_cvt_pk_fp8_f32 v51, v81, v83 op_sel:[0,0,1]
	v_ashrrev_i32_e32 v53, 31, v52
	v_lshlrev_b64 v[52:53], 10, v[52:53]
	v_lshl_add_u64 v[28:29], v[28:29], 0, v[52:53]
	global_store_dwordx4 v[28:29], v[48:51], off sc1 nt
	s_waitcnt lgkmcnt(0)

; #define LAS __attribute__((address_space(3)))
; #define LDS_WAIT() asm volatile("s_waitcnt lgkmcnt(0)" ::: "memory")
; __device__ __forceinline__ void tr_item(const float* W, int ld, int K, int nblk, int item, bf16* WT, bool gu, LAS float* scr, int lane) {
;     const int kb = item / nblk, nb = item % nblk, k0 = 64 * kb, n0 = 32 * nb;
;     int drow0 = n0;
;     if (gu) { const int bj = n0 / FF, j = n0 - bj * FF; drow0 = 256 * (j / 128) + 128 * bj + (j % 128); }
;     { float t_[32];
; #pragma unroll
;       for (int i = 0; i < 32; ++i) t_[i] = W[(size_t)(k0 + 2 * i + (lane >> 5)) * ld + n0 + (lane & 31)];
; #pragma unroll
;       for (int i = 0; i < 32; ++i) scr[(2 * i + (lane >> 5)) * 33 + (lane & 31)] = t_[i]; }
;     LDS_WAIT(); asm volatile("" ::: "memory");
; __device__ __forceinline__ void convert_items(Frame& F, const Args& a, int lo, int hi, int w, int nw) {
;     ...
;         if (r < I_SO) { tr_item(a.in[12], D, D, 32, r, (bf16*)(F.ws + WS_WSWAOUT), false, scr, lane); continue; } r -= I_SO;
.LBB0_1145:
	s_andn2_b64 vcc, exec, s[24:25]
	s_cbranch_vccnz .LBB0_1147
	s_add_i32 s16, s42, 0x2000
	s_and_b32 s25, s16, 0x1ffc0
	s_and_b32 s24, s40, 0x3e0
	v_add_u32_e32 v28, s25, v30
	s_lshl_b32 s16, s24, 2
	v_ashrrev_i32_e32 v29, 31, v28
	v_lshl_add_u64 v[48:49], v[8:9], 0, s[16:17]
	v_lshlrev_b64 v[28:29], 12, v[28:29]
	v_lshl_add_u64 v[28:29], v[48:49], 0, v[28:29]
	v_add_co_u32_e32 v48, vcc, 0x2000, v28
	global_load_dword v50, v[28:29], off nt
	s_nop 0
	v_addc_co_u32_e32 v49, vcc, 0, v29, vcc
	global_load_dword v51, v[48:49], off nt
	v_add_co_u32_e32 v48, vcc, 0x4000, v28
	s_lshl_b32 s16, s25, 1
	s_nop 0
	v_addc_co_u32_e32 v49, vcc, 0, v29, vcc
	global_load_dword v52, v[48:49], off nt
	v_add_co_u32_e32 v48, vcc, 0x6000, v28
	s_nop 1
	v_addc_co_u32_e32 v49, vcc, 0, v29, vcc
	global_load_dword v53, v[48:49], off nt
	v_add_co_u32_e32 v48, vcc, 0x8000, v28
	s_nop 1
	v_addc_co_u32_e32 v49, vcc, 0, v29, vcc
	global_load_dword v54, v[48:49], off nt
	v_add_co_u32_e32 v48, vcc, 0xa000, v28
	s_nop 1
	v_addc_co_u32_e32 v49, vcc, 0, v29, vcc
	global_load_dword v55, v[48:49], off nt
	v_add_co_u32_e32 v48, vcc, 0xc000, v28
	s_nop 1
	v_addc_co_u32_e32 v49, vcc, 0, v29, vcc
	global_load_dword v56, v[48:49], off nt
	v_add_co_u32_e32 v48, vcc, 0xe000, v28
	s_nop 1
	v_addc_co_u32_e32 v49, vcc, 0, v29, vcc
	global_load_dword v57, v[48:49], off nt
	v_add_co_u32_e32 v48, vcc, 0x10000, v28
	s_nop 1
	v_addc_co_u32_e32 v49, vcc, 0, v29, vcc
	global_load_dword v58, v[48:49], off nt
	v_add_co_u32_e32 v48, vcc, 0x12000, v28
	s_nop 1
	v_addc_co_u32_e32 v49, vcc, 0, v29, vcc
	global_load_dword v59, v[48:49], off nt
	v_add_co_u32_e32 v48, vcc, 0x14000, v28
	s_nop 1
	v_addc_co_u32_e32 v49, vcc, 0, v29, vcc
	global_load_dword v60, v[48:49], off nt
	v_add_co_u32_e32 v48, vcc, 0x16000, v28
	s_nop 1
	v_addc_co_u32_e32 v49, vcc, 0, v29, vcc
	global_load_dword v61, v[48:49], off nt
	v_add_co_u32_e32 v48, vcc, 0x18000, v28
	s_nop 1
	v_addc_co_u32_e32 v49, vcc, 0, v29, vcc
	global_load_dword v62, v[48:49], off nt
	v_add_co_u32_e32 v48, vcc, 0x1a000, v28
	s_nop 1
	v_addc_co_u32_e32 v49, vcc, 0, v29, vcc
	global_load_dword v63, v[48:49], off nt
	v_add_co_u32_e32 v48, vcc, 0x1c000, v28
	s_nop 1
	v_addc_co_u32_e32 v49, vcc, 0, v29, vcc
	global_load_dword v64, v[48:49], off nt
	v_add_co_u32_e32 v48, vcc, 0x1e000, v28
	s_nop 1
	v_addc_co_u32_e32 v49, vcc, 0, v29, vcc
	global_load_dword v65, v[48:49], off nt
	v_add_co_u32_e32 v48, vcc, 0x20000, v28
	s_nop 1
	v_addc_co_u32_e32 v49, vcc, 0, v29, vcc
	global_load_dword v66, v[48:49], off nt
	v_add_co_u32_e32 v48, vcc, 0x22000, v28
	s_nop 1
	v_addc_co_u32_e32 v49, vcc, 0, v29, vcc
	global_load_dword v67, v[48:49], off nt
	v_add_co_u32_e32 v48, vcc, 0x24000, v28
	s_nop 1
	v_addc_co_u32_e32 v49, vcc, 0, v29, vcc
	global_load_dword v68, v[48:49], off nt
	v_add_co_u32_e32 v48, vcc, 0x26000, v28
	s_nop 1
	v_addc_co_u32_e32 v49, vcc, 0, v29, vcc
	global_load_dword v69, v[48:49], off nt
	v_add_co_u32_e32 v48, vcc, 0x28000, v28
	s_nop 1
	v_addc_co_u32_e32 v49, vcc, 0, v29, vcc
	global_load_dword v70, v[48:49], off nt
	v_add_co_u32_e32 v48, vcc, 0x2a000, v28
	s_nop 1
	v_addc_co_u32_e32 v49, vcc, 0, v29, vcc
	global_load_dword v71, v[48:49], off nt
	v_add_co_u32_e32 v48, vcc, 0x2c000, v28
	s_nop 1
	v_addc_co_u32_e32 v49, vcc, 0, v29, vcc
	global_load_dword v72, v[48:49], off nt
	v_add_co_u32_e32 v48, vcc, 0x2e000, v28
	s_nop 1
	v_addc_co_u32_e32 v49, vcc, 0, v29, vcc
	global_load_dword v73, v[48:49], off nt
	v_add_co_u32_e32 v48, vcc, 0x30000, v28
	s_nop 1
	v_addc_co_u32_e32 v49, vcc, 0, v29, vcc
	global_load_dword v74, v[48:49], off nt
	v_add_co_u32_e32 v48, vcc, 0x32000, v28
	s_nop 1
	v_addc_co_u32_e32 v49, vcc, 0, v29, vcc
	global_load_dword v75, v[48:49], off nt
	v_add_co_u32_e32 v48, vcc, 0x34000, v28
	s_nop 1
	v_addc_co_u32_e32 v49, vcc, 0, v29, vcc
	global_load_dword v76, v[48:49], off nt
	v_add_co_u32_e32 v48, vcc, 0x36000, v28
	s_nop 1
	v_addc_co_u32_e32 v49, vcc, 0, v29, vcc
	global_load_dword v77, v[48:49], off nt
	v_add_co_u32_e32 v48, vcc, 0x38000, v28
	s_nop 1
	v_addc_co_u32_e32 v49, vcc, 0, v29, vcc
	global_load_dword v78, v[48:49], off nt
	v_add_co_u32_e32 v48, vcc, 0x3a000, v28
	s_nop 1
	v_addc_co_u32_e32 v49, vcc, 0, v29, vcc
	global_load_dword v79, v[48:49], off nt
	v_add_co_u32_e32 v48, vcc, 0x3c000, v28
	s_nop 1
	v_addc_co_u32_e32 v49, vcc, 0, v29, vcc
	v_add_co_u32_e32 v28, vcc, 0x3e000, v28
	global_load_dword v48, v[48:49], off nt
	s_nop 0
	v_addc_co_u32_e32 v29, vcc, 0, v29, vcc
	global_load_dword v28, v[28:29], off nt
	s_waitcnt vmcnt(0)
	ds_write2_b32 v31, v50, v51 offset1:66
	ds_write2_b32 v31, v52, v53 offset0:132 offset1:198
	ds_write2_b32 v40, v54, v55 offset0:8 offset1:74
	ds_write2_b32 v40, v56, v57 offset0:140 offset1:206
	ds_write2_b32 v41, v58, v59 offset0:16 offset1:82
	ds_write2_b32 v41, v60, v61 offset0:148 offset1:214
	ds_write2_b32 v42, v62, v63 offset0:24 offset1:90
	ds_write2_b32 v42, v64, v65 offset0:156 offset1:222
	ds_write2_b32 v43, v66, v67 offset0:32 offset1:98
	ds_write2_b32 v43, v68, v69 offset0:164 offset1:230
	ds_write2_b32 v44, v70, v71 offset0:40 offset1:106
	ds_write2_b32 v44, v72, v73 offset0:172 offset1:238
	ds_write2_b32 v45, v74, v75 offset0:48 offset1:114
	ds_write2_b32 v45, v76, v77 offset0:180 offset1:246
	ds_write2_b32 v46, v78, v79 offset0:56 offset1:122
	ds_write2_b32 v46, v48, v28 offset0:188 offset1:254
	s_waitcnt lgkmcnt(0)
; #define GAS __attribute__((address_space(1)))
; #define LAS __attribute__((address_space(3)))
; #define LDS_WAIT() asm volatile("s_waitcnt lgkmcnt(0)" ::: "memory")
; __device__ __forceinline__ unsigned pk2(float lo, float hi) { return f2bf(lo) | (f2bf(hi) << 16); }
; __device__ __forceinline__ void tr_item(const float* W, int ld, int K, int nblk, int item, bf16* WT, bool gu, LAS float* scr, int lane) {
;     ...
;     const int c = lane & 7;
; #pragma unroll
;     for (int j = 0; j < 4; ++j) { const int n = (lane >> 3) + 8 * j; const LAS float* s = scr + (8 * c) * 33 + n;
;         v4u o; o.x = pk2(s[0 * 33], s[1 * 33]); o.y = pk2(s[2 * 33], s[3 * 33]); o.z = pk2(s[4 * 33], s[5 * 33]); o.w = pk2(s[6 * 33], s[7 * 33]);
;         *(GAS v4u*)(WT + (size_t)(drow0 + n) * K + k0 + 8 * c) = o; }
;     LDS_WAIT(); asm volatile("" ::: "memory");
	ds_read2_b32 v[52:53], v36 offset0:33 offset1:41
	ds_read2_b32 v[54:55], v36 offset1:8
	ds_read2_b32 v[56:57], v36 offset0:66 offset1:74
	ds_read2_b32 v[58:59], v36 offset0:99 offset1:107
	ds_read2_b32 v[60:61], v36 offset0:132 offset1:140
	ds_read2_b32 v[62:63], v36 offset0:165 offset1:173
	ds_read2_b32 v[64:65], v36 offset0:198 offset1:206
	ds_read2_b32 v[66:67], v36 offset0:231 offset1:239
	s_waitcnt lgkmcnt(7)
	v_bfe_u32 v49, v52, 16, 1
	s_waitcnt lgkmcnt(6)
	v_bfe_u32 v48, v54, 16, 1
	v_add3_u32 v48, v54, v48, s46
	v_lshrrev_b32_e32 v48, 16, v48
	v_add3_u32 v49, v52, v49, s46
	v_and_or_b32 v48, v49, s47, v48
	s_waitcnt lgkmcnt(5)
	v_bfe_u32 v49, v56, 16, 1
	v_add3_u32 v49, v56, v49, s46
	s_waitcnt lgkmcnt(4)
	v_bfe_u32 v50, v58, 16, 1
	v_lshrrev_b32_e32 v49, 16, v49
	v_add3_u32 v50, v58, v50, s46
	v_and_or_b32 v49, v50, s47, v49
	s_waitcnt lgkmcnt(3)
	v_bfe_u32 v50, v60, 16, 1
	v_add3_u32 v50, v60, v50, s46
	s_waitcnt lgkmcnt(2)
	v_bfe_u32 v51, v62, 16, 1
	v_lshrrev_b32_e32 v50, 16, v50
	v_add3_u32 v51, v62, v51, s46
	v_and_or_b32 v50, v51, s47, v50
	s_waitcnt lgkmcnt(1)
	v_bfe_u32 v51, v64, 16, 1
	v_add_u32_e32 v68, s24, v35
	v_add3_u32 v51, v64, v51, s46
	s_waitcnt lgkmcnt(0)
	v_bfe_u32 v52, v66, 16, 1
	v_ashrrev_i32_e32 v69, 31, v68
	v_lshl_add_u64 v[28:29], v[22:23], 0, s[16:17]
	v_lshrrev_b32_e32 v51, 16, v51
	v_add3_u32 v52, v66, v52, s46
	v_lshlrev_b64 v[68:69], 11, v[68:69]
	v_and_or_b32 v51, v52, s47, v51
	v_lshl_add_u64 v[68:69], v[28:29], 0, v[68:69]
	global_store_dwordx4 v[68:69], v[48:51], off sc1 nt
	v_bfe_u32 v52, v67, 16, 1
	v_add3_u32 v52, v67, v52, s46
	v_bfe_u32 v48, v55, 16, 1
	v_add3_u32 v48, v55, v48, s46
	v_bfe_u32 v49, v53, 16, 1
	v_lshrrev_b32_e32 v48, 16, v48
	v_add3_u32 v49, v53, v49, s46
	v_and_or_b32 v48, v49, s47, v48
	v_bfe_u32 v49, v57, 16, 1
	v_add3_u32 v49, v57, v49, s46
	v_bfe_u32 v50, v59, 16, 1
	v_lshrrev_b32_e32 v49, 16, v49
	v_add3_u32 v50, v59, v50, s46
	v_and_or_b32 v49, v50, s47, v49
	v_bfe_u32 v50, v61, 16, 1
	v_add3_u32 v50, v61, v50, s46
	v_bfe_u32 v51, v63, 16, 1
	v_lshrrev_b32_e32 v50, 16, v50
	v_add3_u32 v51, v63, v51, s46
	v_and_or_b32 v50, v51, s47, v50
	v_bfe_u32 v51, v65, 16, 1
	v_add3_u32 v51, v65, v51, s46
	v_lshrrev_b32_e32 v51, 16, v51
	v_and_or_b32 v51, v52, s47, v51
	v_add_u32_e32 v52, s24, v37
	v_ashrrev_i32_e32 v53, 31, v52
	v_lshlrev_b64 v[52:53], 11, v[52:53]
	v_lshl_add_u64 v[52:53], v[28:29], 0, v[52:53]
	global_store_dwordx4 v[52:53], v[48:51], off sc1 nt
	ds_read2_b32 v[52:53], v36 offset0:49 offset1:57
	ds_read2_b32 v[54:55], v36 offset0:16 offset1:24
	ds_read2_b32 v[56:57], v36 offset0:82 offset1:90
	ds_read2_b32 v[58:59], v36 offset0:115 offset1:123
	ds_read2_b32 v[60:61], v36 offset0:148 offset1:156
	ds_read2_b32 v[62:63], v36 offset0:181 offset1:189
	ds_read2_b32 v[64:65], v36 offset0:214 offset1:222
	ds_read2_b32 v[66:67], v36 offset0:247 offset1:255
	s_waitcnt lgkmcnt(7)
	v_bfe_u32 v49, v52, 16, 1
	s_waitcnt lgkmcnt(6)
	v_bfe_u32 v48, v54, 16, 1
	v_add3_u32 v48, v54, v48, s46
	v_lshrrev_b32_e32 v48, 16, v48
	v_add3_u32 v49, v52, v49, s46
	v_and_or_b32 v48, v49, s47, v48
	s_waitcnt lgkmcnt(5)
	v_bfe_u32 v49, v56, 16, 1
	v_add3_u32 v49, v56, v49, s46
	s_waitcnt lgkmcnt(4)
	v_bfe_u32 v50, v58, 16, 1
	v_lshrrev_b32_e32 v49, 16, v49
	v_add3_u32 v50, v58, v50, s46
	v_and_or_b32 v49, v50, s47, v49
	s_waitcnt lgkmcnt(3)
	v_bfe_u32 v50, v60, 16, 1
	v_add3_u32 v50, v60, v50, s46
	s_waitcnt lgkmcnt(2)
	v_bfe_u32 v51, v62, 16, 1
	v_lshrrev_b32_e32 v50, 16, v50
	v_add3_u32 v51, v62, v51, s46
	v_and_or_b32 v50, v51, s47, v50
	s_waitcnt lgkmcnt(1)
	v_bfe_u32 v51, v64, 16, 1
	v_add_u32_e32 v68, s24, v38
	v_add3_u32 v51, v64, v51, s46
	s_waitcnt lgkmcnt(0)
	v_bfe_u32 v52, v66, 16, 1
	v_ashrrev_i32_e32 v69, 31, v68
	v_lshrrev_b32_e32 v51, 16, v51
	v_add3_u32 v52, v66, v52, s46
	v_lshlrev_b64 v[68:69], 11, v[68:69]
	v_and_or_b32 v51, v52, s47, v51
	v_lshl_add_u64 v[68:69], v[28:29], 0, v[68:69]
	global_store_dwordx4 v[68:69], v[48:51], off sc1 nt
	v_bfe_u32 v52, v67, 16, 1
	v_add3_u32 v52, v67, v52, s46
	v_bfe_u32 v48, v55, 16, 1
	v_add3_u32 v48, v55, v48, s46
	v_bfe_u32 v49, v53, 16, 1
	v_lshrrev_b32_e32 v48, 16, v48
	v_add3_u32 v49, v53, v49, s46
	v_and_or_b32 v48, v49, s47, v48
	v_bfe_u32 v49, v57, 16, 1
	v_add3_u32 v49, v57, v49, s46
	v_bfe_u32 v50, v59, 16, 1
	v_lshrrev_b32_e32 v49, 16, v49
	v_add3_u32 v50, v59, v50, s46
	v_and_or_b32 v49, v50, s47, v49
	v_bfe_u32 v50, v61, 16, 1
	v_add3_u32 v50, v61, v50, s46
	v_bfe_u32 v51, v63, 16, 1
	v_lshrrev_b32_e32 v50, 16, v50
	v_add3_u32 v51, v63, v51, s46
	v_and_or_b32 v50, v51, s47, v50
	v_bfe_u32 v51, v65, 16, 1
	v_add3_u32 v51, v65, v51, s46
	v_lshrrev_b32_e32 v51, 16, v51
	v_and_or_b32 v51, v52, s47, v51
	v_add_u32_e32 v52, s24, v39
	v_ashrrev_i32_e32 v53, 31, v52
	v_lshlrev_b64 v[52:53], 11, v[52:53]
	v_lshl_add_u64 v[28:29], v[28:29], 0, v[52:53]
	global_store_dwordx4 v[28:29], v[48:51], off sc1 nt
	s_waitcnt lgkmcnt(0)

; #define LAS __attribute__((address_space(3)))
; #define LDS_WAIT() asm volatile("s_waitcnt lgkmcnt(0)" ::: "memory")
; __device__ __forceinline__ void tr_item(const float* W, int ld, int K, int nblk, int item, bf16* WT, bool gu, LAS float* scr, int lane) {
;     const int kb = item / nblk, nb = item % nblk, k0 = 64 * kb, n0 = 32 * nb;
;     int drow0 = n0;
;     if (gu) { const int bj = n0 / FF, j = n0 - bj * FF; drow0 = 256 * (j / 128) + 128 * bj + (j % 128); }
;     { float t_[32];
; #pragma unroll
;       for (int i = 0; i < 32; ++i) t_[i] = W[(size_t)(k0 + 2 * i + (lane >> 5)) * ld + n0 + (lane & 31)];
; #pragma unroll
;       for (int i = 0; i < 32; ++i) scr[(2 * i + (lane >> 5)) * 33 + (lane & 31)] = t_[i]; }
;     LDS_WAIT(); asm volatile("" ::: "memory");
; __device__ __forceinline__ void convert_items(Frame& F, const Args& a, int lo, int hi, int w, int nw) {
;     ...
;         if (r < I_SI) { tr_item(a.in[10], D + 512, D, 48, r, (bf16*)(F.ws + WS_WSWAIN), false, scr, lane); continue; } r -= I_SI;
.LBB0_1148:
	s_andn2_b64 vcc, exec, s[24:25]
	s_cbranch_vccnz .LBB0_1150
	s_add_i32 s16, s37, 0xf800
	s_and_b32 s24, s16, 0xffff
	s_mul_i32 s24, s24, 0xaaab
	s_lshr_b32 s25, s24, 21
	s_mul_i32 s24, s25, 48
	s_sub_i32 s16, s16, s24
	s_lshl_b32 s16, s16, 5
	s_and_b32 s24, s16, 0xffe0
	v_lshl_add_u32 v64, s25, 6, v30
	s_lshl_b32 s16, s24, 2
	v_lshl_add_u64 v[28:29], v[10:11], 0, s[16:17]
	v_add_u32_e32 v50, 2, v64
	v_add_u32_e32 v52, 4, v64
	v_add_u32_e32 v54, 6, v64
	v_add_u32_e32 v56, 8, v64
	v_add_u32_e32 v58, 10, v64
	v_add_u32_e32 v60, 12, v64
	v_add_u32_e32 v62, 14, v64
	v_mad_i64_i32 v[48:49], s[26:27], v64, s48, v[28:29]
	v_mad_i64_i32 v[50:51], s[26:27], v50, s48, v[28:29]
	v_mad_i64_i32 v[52:53], s[26:27], v52, s48, v[28:29]
	v_mad_i64_i32 v[54:55], s[26:27], v54, s48, v[28:29]
	v_mad_i64_i32 v[56:57], s[26:27], v56, s48, v[28:29]
	v_mad_i64_i32 v[58:59], s[26:27], v58, s48, v[28:29]
	v_mad_i64_i32 v[60:61], s[26:27], v60, s48, v[28:29]
	v_mad_i64_i32 v[62:63], s[26:27], v62, s48, v[28:29]
	global_load_dword v65, v[48:49], off nt
	global_load_dword v66, v[50:51], off nt
	global_load_dword v67, v[52:53], off nt
	global_load_dword v68, v[54:55], off nt
	global_load_dword v69, v[56:57], off nt
	global_load_dword v70, v[58:59], off nt
	global_load_dword v71, v[60:61], off nt
	global_load_dword v72, v[62:63], off nt
	v_add_u32_e32 v48, 16, v64
	v_add_u32_e32 v50, 18, v64
	v_add_u32_e32 v52, 20, v64
	v_add_u32_e32 v54, 22, v64
	v_add_u32_e32 v56, 24, v64
	v_add_u32_e32 v58, 26, v64
	v_add_u32_e32 v60, 28, v64
	v_add_u32_e32 v62, 30, v64
	v_mad_i64_i32 v[48:49], s[26:27], v48, s48, v[28:29]
	v_mad_i64_i32 v[50:51], s[26:27], v50, s48, v[28:29]
	v_mad_i64_i32 v[52:53], s[26:27], v52, s48, v[28:29]
	v_mad_i64_i32 v[54:55], s[26:27], v54, s48, v[28:29]
	v_mad_i64_i32 v[56:57], s[26:27], v56, s48, v[28:29]
	v_mad_i64_i32 v[58:59], s[26:27], v58, s48, v[28:29]
	v_mad_i64_i32 v[60:61], s[26:27], v60, s48, v[28:29]
	v_mad_i64_i32 v[62:63], s[26:27], v62, s48, v[28:29]
	global_load_dword v73, v[48:49], off nt
	global_load_dword v74, v[50:51], off nt
	global_load_dword v75, v[52:53], off nt
	global_load_dword v76, v[54:55], off nt
	global_load_dword v77, v[56:57], off nt
	global_load_dword v78, v[58:59], off nt
	global_load_dword v79, v[60:61], off nt
	global_load_dword v80, v[62:63], off nt
	v_add_u32_e32 v48, 32, v64
	v_add_u32_e32 v50, 34, v64
	v_add_u32_e32 v52, 36, v64
	v_add_u32_e32 v54, 38, v64
	v_add_u32_e32 v56, 40, v64
	v_add_u32_e32 v58, 42, v64
	v_add_u32_e32 v60, 44, v64
	v_add_u32_e32 v62, 46, v64
	v_mad_i64_i32 v[48:49], s[26:27], v48, s48, v[28:29]
	v_mad_i64_i32 v[50:51], s[26:27], v50, s48, v[28:29]
	v_mad_i64_i32 v[52:53], s[26:27], v52, s48, v[28:29]
	v_mad_i64_i32 v[54:55], s[26:27], v54, s48, v[28:29]
	v_mad_i64_i32 v[56:57], s[26:27], v56, s48, v[28:29]
	v_mad_i64_i32 v[58:59], s[26:27], v58, s48, v[28:29]
	v_mad_i64_i32 v[60:61], s[26:27], v60, s48, v[28:29]
	v_mad_i64_i32 v[62:63], s[26:27], v62, s48, v[28:29]
	global_load_dword v81, v[48:49], off nt
	global_load_dword v82, v[50:51], off nt
	global_load_dword v83, v[52:53], off nt
	global_load_dword v84, v[54:55], off nt
	global_load_dword v85, v[56:57], off nt
	global_load_dword v86, v[58:59], off nt
	global_load_dword v87, v[60:61], off nt
	s_nop 0
	global_load_dword v62, v[62:63], off nt
	v_add_u32_e32 v48, 48, v64
	v_add_u32_e32 v50, 50, v64
	v_add_u32_e32 v52, 52, v64
	v_add_u32_e32 v54, 54, v64
	v_add_u32_e32 v56, 56, v64
	v_add_u32_e32 v58, 58, v64
	v_add_u32_e32 v60, 60, v64
	v_add_u32_e32 v63, 62, v64
	v_mad_i64_i32 v[48:49], s[26:27], v48, s48, v[28:29]
	v_mad_i64_i32 v[50:51], s[26:27], v50, s48, v[28:29]
	v_mad_i64_i32 v[52:53], s[26:27], v52, s48, v[28:29]
	v_mad_i64_i32 v[54:55], s[26:27], v54, s48, v[28:29]
	v_mad_i64_i32 v[56:57], s[26:27], v56, s48, v[28:29]
	v_mad_i64_i32 v[58:59], s[26:27], v58, s48, v[28:29]
	v_mad_i64_i32 v[60:61], s[26:27], v60, s48, v[28:29]
	v_mad_i64_i32 v[28:29], s[26:27], v63, s48, v[28:29]
	global_load_dword v48, v[48:49], off nt
	s_nop 0
	global_load_dword v49, v[50:51], off nt
	s_nop 0
	global_load_dword v50, v[52:53], off nt
	global_load_dword v51, v[54:55], off nt
	s_nop 0
	global_load_dword v52, v[56:57], off nt
	global_load_dword v53, v[58:59], off nt
	global_load_dword v54, v[60:61], off nt
	s_nop 0
	global_load_dword v28, v[28:29], off nt
	s_waitcnt vmcnt(0)
	ds_write2_b32 v31, v65, v66 offset1:66
	ds_write2_b32 v31, v67, v68 offset0:132 offset1:198
	ds_write2_b32 v40, v69, v70 offset0:8 offset1:74
	ds_write2_b32 v40, v71, v72 offset0:140 offset1:206
	ds_write2_b32 v41, v73, v74 offset0:16 offset1:82
	ds_write2_b32 v41, v75, v76 offset0:148 offset1:214
	ds_write2_b32 v42, v77, v78 offset0:24 offset1:90
	ds_write2_b32 v42, v79, v80 offset0:156 offset1:222
	ds_write2_b32 v43, v81, v82 offset0:32 offset1:98
	ds_write2_b32 v43, v83, v84 offset0:164 offset1:230
	ds_write2_b32 v44, v85, v86 offset0:40 offset1:106
	ds_write2_b32 v44, v87, v62 offset0:172 offset1:238
	ds_write2_b32 v45, v48, v49 offset0:48 offset1:114
	ds_write2_b32 v45, v50, v51 offset0:180 offset1:246
	ds_write2_b32 v46, v52, v53 offset0:56 offset1:122
	ds_write2_b32 v46, v54, v28 offset0:188 offset1:254
	s_waitcnt lgkmcnt(0)
; #define GAS __attribute__((address_space(1)))
; #define LAS __attribute__((address_space(3)))
; #define LDS_WAIT() asm volatile("s_waitcnt lgkmcnt(0)" ::: "memory")
; __device__ __forceinline__ unsigned pk2(float lo, float hi) { return f2bf(lo) | (f2bf(hi) << 16); }
; __device__ __forceinline__ void tr_item(const float* W, int ld, int K, int nblk, int item, bf16* WT, bool gu, LAS float* scr, int lane) {
;     ...
;     const int c = lane & 7;
; #pragma unroll
;     for (int j = 0; j < 4; ++j) { const int n = (lane >> 3) + 8 * j; const LAS float* s = scr + (8 * c) * 33 + n;
;         v4u o; o.x = pk2(s[0 * 33], s[1 * 33]); o.y = pk2(s[2 * 33], s[3 * 33]); o.z = pk2(s[4 * 33], s[5 * 33]); o.w = pk2(s[6 * 33], s[7 * 33]);
;         *(GAS v4u*)(WT + (size_t)(drow0 + n) * K + k0 + 8 * c) = o; }
;     LDS_WAIT(); asm volatile("" ::: "memory");
	ds_read2_b32 v[28:29], v36 offset1:8
	ds_read2_b32 v[54:55], v36 offset0:33 offset1:41
	ds_read2_b32 v[56:57], v36 offset0:66 offset1:74
	ds_read2_b32 v[58:59], v36 offset0:99 offset1:107
	ds_read2_b32 v[60:61], v36 offset0:132 offset1:140
	s_waitcnt lgkmcnt(4)
	v_bfe_u32 v48, v28, 16, 1
	v_add3_u32 v28, v28, v48, s46
	s_waitcnt lgkmcnt(3)
	v_bfe_u32 v48, v54, 16, 1
	v_lshrrev_b32_e32 v28, 16, v28
	v_add3_u32 v48, v54, v48, s46
	ds_read2_b32 v[62:63], v36 offset0:165 offset1:173
	v_and_or_b32 v48, v48, s47, v28
	s_waitcnt lgkmcnt(3)
	v_bfe_u32 v28, v56, 16, 1
	v_add3_u32 v28, v56, v28, s46
	s_waitcnt lgkmcnt(2)
	v_bfe_u32 v49, v58, 16, 1
	ds_read2_b32 v[64:65], v36 offset0:198 offset1:206
	v_lshrrev_b32_e32 v28, 16, v28
	v_add3_u32 v49, v58, v49, s46
	ds_read2_b32 v[66:67], v36 offset0:231 offset1:239
	v_and_or_b32 v49, v49, s47, v28
	s_waitcnt lgkmcnt(3)
	v_bfe_u32 v28, v60, 16, 1
	v_add3_u32 v28, v60, v28, s46
	s_waitcnt lgkmcnt(2)
	v_bfe_u32 v50, v62, 16, 1
	v_lshrrev_b32_e32 v28, 16, v28
	v_add3_u32 v50, v62, v50, s46
	v_and_or_b32 v50, v50, s47, v28
	s_waitcnt lgkmcnt(1)
	v_bfe_u32 v28, v64, 16, 1
	v_add3_u32 v28, v64, v28, s46
	s_waitcnt lgkmcnt(0)
	v_bfe_u32 v51, v66, 16, 1
	v_lshrrev_b32_e32 v28, 16, v28
	v_add3_u32 v51, v66, v51, s46
	v_add_u32_e32 v68, s24, v35
	s_lshl_b32 s16, s25, 7
	v_and_or_b32 v51, v51, s47, v28
	v_ashrrev_i32_e32 v69, 31, v68
	v_bfe_u32 v28, v29, 16, 1
	v_lshl_add_u64 v[52:53], v[12:13], 0, s[16:17]
	v_lshlrev_b64 v[68:69], 11, v[68:69]
	v_add3_u32 v28, v29, v28, s46
	v_bfe_u32 v29, v55, 16, 1
	v_lshl_add_u64 v[68:69], v[52:53], 0, v[68:69]
	v_lshrrev_b32_e32 v28, 16, v28
	v_add3_u32 v29, v55, v29, s46
	global_store_dwordx4 v[68:69], v[48:51], off sc1 nt
	ds_read2_b32 v[54:55], v36 offset0:16 offset1:24
	v_add_u32_e32 v68, s24, v38
	v_and_or_b32 v48, v29, s47, v28
	v_bfe_u32 v28, v57, 16, 1
	v_add3_u32 v28, v57, v28, s46
	v_bfe_u32 v29, v59, 16, 1
	v_lshrrev_b32_e32 v28, 16, v28
	v_add3_u32 v29, v59, v29, s46
	v_and_or_b32 v49, v29, s47, v28
	v_bfe_u32 v28, v61, 16, 1
	v_add3_u32 v28, v61, v28, s46
	v_bfe_u32 v29, v63, 16, 1
	v_lshrrev_b32_e32 v28, 16, v28
	v_add3_u32 v29, v63, v29, s46
	v_and_or_b32 v50, v29, s47, v28
	v_bfe_u32 v28, v65, 16, 1
	v_add3_u32 v28, v65, v28, s46
	v_bfe_u32 v29, v67, 16, 1
	v_lshrrev_b32_e32 v28, 16, v28
	v_add3_u32 v29, v67, v29, s46
	v_and_or_b32 v51, v29, s47, v28
	v_add_u32_e32 v28, s24, v37
	v_ashrrev_i32_e32 v29, 31, v28
	v_lshlrev_b64 v[28:29], 11, v[28:29]
	v_lshl_add_u64 v[28:29], v[52:53], 0, v[28:29]
	global_store_dwordx4 v[28:29], v[48:51], off sc1 nt
	ds_read2_b32 v[28:29], v36 offset0:49 offset1:57
	ds_read2_b32 v[56:57], v36 offset0:82 offset1:90
	ds_read2_b32 v[58:59], v36 offset0:115 offset1:123
	s_waitcnt lgkmcnt(3)
	v_bfe_u32 v48, v54, 16, 1
	v_add3_u32 v48, v54, v48, s46
	s_waitcnt lgkmcnt(2)
	v_bfe_u32 v49, v28, 16, 1
	ds_read2_b32 v[60:61], v36 offset0:148 offset1:156
	v_lshrrev_b32_e32 v48, 16, v48
	v_add3_u32 v28, v28, v49, s46
	ds_read2_b32 v[62:63], v36 offset0:181 offset1:189
	v_and_or_b32 v48, v28, s47, v48
	s_waitcnt lgkmcnt(3)
	v_bfe_u32 v28, v56, 16, 1
	v_add3_u32 v28, v56, v28, s46
	s_waitcnt lgkmcnt(2)
	v_bfe_u32 v49, v58, 16, 1
	ds_read2_b32 v[64:65], v36 offset0:214 offset1:222
	v_lshrrev_b32_e32 v28, 16, v28
	v_add3_u32 v49, v58, v49, s46
	ds_read2_b32 v[66:67], v36 offset0:247 offset1:255
	v_and_or_b32 v49, v49, s47, v28
	s_waitcnt lgkmcnt(3)
	v_bfe_u32 v28, v60, 16, 1
	v_add3_u32 v28, v60, v28, s46
	s_waitcnt lgkmcnt(2)
	v_bfe_u32 v50, v62, 16, 1
	v_lshrrev_b32_e32 v28, 16, v28
	v_add3_u32 v50, v62, v50, s46
	v_and_or_b32 v50, v50, s47, v28
	s_waitcnt lgkmcnt(1)
	v_bfe_u32 v28, v64, 16, 1
	v_add3_u32 v28, v64, v28, s46
	s_waitcnt lgkmcnt(0)
	v_bfe_u32 v51, v66, 16, 1
	v_ashrrev_i32_e32 v69, 31, v68
	v_lshrrev_b32_e32 v28, 16, v28
	v_add3_u32 v51, v66, v51, s46
	v_lshlrev_b64 v[68:69], 11, v[68:69]
	v_and_or_b32 v51, v51, s47, v28
	v_lshl_add_u64 v[68:69], v[52:53], 0, v[68:69]
	v_bfe_u32 v28, v55, 16, 1
	global_store_dwordx4 v[68:69], v[48:51], off sc1 nt
	v_add3_u32 v28, v55, v28, s46
	v_lshrrev_b32_e32 v28, 16, v28
	v_bfe_u32 v48, v29, 16, 1
	v_add3_u32 v29, v29, v48, s46
	v_and_or_b32 v48, v29, s47, v28
	v_bfe_u32 v28, v57, 16, 1
	v_add3_u32 v28, v57, v28, s46
	v_bfe_u32 v29, v59, 16, 1
	v_lshrrev_b32_e32 v28, 16, v28
	v_add3_u32 v29, v59, v29, s46
	v_and_or_b32 v49, v29, s47, v28
	v_bfe_u32 v28, v61, 16, 1
	v_add3_u32 v28, v61, v28, s46
	v_bfe_u32 v29, v63, 16, 1
	v_lshrrev_b32_e32 v28, 16, v28
	v_add3_u32 v29, v63, v29, s46
	v_and_or_b32 v50, v29, s47, v28
	v_bfe_u32 v28, v65, 16, 1
	v_add3_u32 v28, v65, v28, s46
	v_bfe_u32 v29, v67, 16, 1
	v_lshrrev_b32_e32 v28, 16, v28
	v_add3_u32 v29, v67, v29, s46
	v_and_or_b32 v51, v29, s47, v28
	v_add_u32_e32 v28, s24, v39
	v_ashrrev_i32_e32 v29, 31, v28
	v_lshlrev_b64 v[28:29], 11, v[28:29]
	v_lshl_add_u64 v[28:29], v[52:53], 0, v[28:29]
	global_store_dwordx4 v[28:29], v[48:51], off sc1 nt
	s_waitcnt lgkmcnt(0)

; #define LAS __attribute__((address_space(3)))
; #define LDS_WAIT() asm volatile("s_waitcnt lgkmcnt(0)" ::: "memory")
; __device__ __forceinline__ void tr_item(const float* W, int ld, int K, int nblk, int item, bf16* WT, bool gu, LAS float* scr, int lane) {
;     const int kb = item / nblk, nb = item % nblk, k0 = 64 * kb, n0 = 32 * nb;
;     int drow0 = n0;
;     if (gu) { const int bj = n0 / FF, j = n0 - bj * FF; drow0 = 256 * (j / 128) + 128 * bj + (j % 128); }
;     { float t_[32];
; #pragma unroll
;       for (int i = 0; i < 32; ++i) t_[i] = W[(size_t)(k0 + 2 * i + (lane >> 5)) * ld + n0 + (lane & 31)];
; #pragma unroll
;       for (int i = 0; i < 32; ++i) scr[(2 * i + (lane >> 5)) * 33 + (lane & 31)] = t_[i]; }
;     LDS_WAIT(); asm volatile("" ::: "memory");
; __device__ __forceinline__ void convert_items(Frame& F, const Args& a, int lo, int hi, int w, int nw) {
;     ...
;         if (r < I_FO) { tr_item(a.in[9], D, D, 32, r, (bf16*)(F.ws + WS_WFOXOUT), false, scr, lane); continue; } r -= I_FO;
.LBB0_1151:
	s_andn2_b64 vcc, exec, s[24:25]
	s_cbranch_vccnz .LBB0_1153
	s_add_i32 s16, s42, 0x2a00
	s_and_b32 s25, s16, 0x1ffc0
	s_and_b32 s24, s40, 0x3e0
	v_add_u32_e32 v28, s25, v30
	s_lshl_b32 s16, s24, 2
	v_ashrrev_i32_e32 v29, 31, v28
	v_lshl_add_u64 v[48:49], v[14:15], 0, s[16:17]
	v_lshlrev_b64 v[28:29], 12, v[28:29]
	v_lshl_add_u64 v[28:29], v[48:49], 0, v[28:29]
	v_add_co_u32_e32 v48, vcc, 0x2000, v28
	global_load_dword v50, v[28:29], off nt
	s_nop 0
	v_addc_co_u32_e32 v49, vcc, 0, v29, vcc
	global_load_dword v51, v[48:49], off nt
	v_add_co_u32_e32 v48, vcc, 0x4000, v28
	s_lshl_b32 s16, s25, 1
	s_nop 0
	v_addc_co_u32_e32 v49, vcc, 0, v29, vcc
	global_load_dword v52, v[48:49], off nt
	v_add_co_u32_e32 v48, vcc, 0x6000, v28
	s_nop 1
	v_addc_co_u32_e32 v49, vcc, 0, v29, vcc
	global_load_dword v53, v[48:49], off nt
	v_add_co_u32_e32 v48, vcc, 0x8000, v28
	s_nop 1
	v_addc_co_u32_e32 v49, vcc, 0, v29, vcc
	global_load_dword v54, v[48:49], off nt
	v_add_co_u32_e32 v48, vcc, 0xa000, v28
	s_nop 1
	v_addc_co_u32_e32 v49, vcc, 0, v29, vcc
	global_load_dword v55, v[48:49], off nt
	v_add_co_u32_e32 v48, vcc, 0xc000, v28
	s_nop 1
	v_addc_co_u32_e32 v49, vcc, 0, v29, vcc
	global_load_dword v56, v[48:49], off nt
	v_add_co_u32_e32 v48, vcc, 0xe000, v28
	s_nop 1
	v_addc_co_u32_e32 v49, vcc, 0, v29, vcc
	global_load_dword v57, v[48:49], off nt
	v_add_co_u32_e32 v48, vcc, 0x10000, v28
	s_nop 1
	v_addc_co_u32_e32 v49, vcc, 0, v29, vcc
	global_load_dword v58, v[48:49], off nt
	v_add_co_u32_e32 v48, vcc, 0x12000, v28
	s_nop 1
	v_addc_co_u32_e32 v49, vcc, 0, v29, vcc
	global_load_dword v59, v[48:49], off nt
	v_add_co_u32_e32 v48, vcc, 0x14000, v28
	s_nop 1
	v_addc_co_u32_e32 v49, vcc, 0, v29, vcc
	global_load_dword v60, v[48:49], off nt
	v_add_co_u32_e32 v48, vcc, 0x16000, v28
	s_nop 1
	v_addc_co_u32_e32 v49, vcc, 0, v29, vcc
	global_load_dword v61, v[48:49], off nt
	v_add_co_u32_e32 v48, vcc, 0x18000, v28
	s_nop 1
	v_addc_co_u32_e32 v49, vcc, 0, v29, vcc
	global_load_dword v62, v[48:49], off nt
	v_add_co_u32_e32 v48, vcc, 0x1a000, v28
	s_nop 1
	v_addc_co_u32_e32 v49, vcc, 0, v29, vcc
	global_load_dword v63, v[48:49], off nt
	v_add_co_u32_e32 v48, vcc, 0x1c000, v28
	s_nop 1
	v_addc_co_u32_e32 v49, vcc, 0, v29, vcc
	global_load_dword v64, v[48:49], off nt
	v_add_co_u32_e32 v48, vcc, 0x1e000, v28
	s_nop 1
	v_addc_co_u32_e32 v49, vcc, 0, v29, vcc
	global_load_dword v65, v[48:49], off nt
	v_add_co_u32_e32 v48, vcc, 0x20000, v28
	s_nop 1
	v_addc_co_u32_e32 v49, vcc, 0, v29, vcc
	global_load_dword v66, v[48:49], off nt
	v_add_co_u32_e32 v48, vcc, 0x22000, v28
	s_nop 1
	v_addc_co_u32_e32 v49, vcc, 0, v29, vcc
	global_load_dword v67, v[48:49], off nt
	v_add_co_u32_e32 v48, vcc, 0x24000, v28
	s_nop 1
	v_addc_co_u32_e32 v49, vcc, 0, v29, vcc
	global_load_dword v68, v[48:49], off nt
	v_add_co_u32_e32 v48, vcc, 0x26000, v28
	s_nop 1
	v_addc_co_u32_e32 v49, vcc, 0, v29, vcc
	global_load_dword v69, v[48:49], off nt
	v_add_co_u32_e32 v48, vcc, 0x28000, v28
	s_nop 1
	v_addc_co_u32_e32 v49, vcc, 0, v29, vcc
	global_load_dword v70, v[48:49], off nt
	v_add_co_u32_e32 v48, vcc, 0x2a000, v28
	s_nop 1
	v_addc_co_u32_e32 v49, vcc, 0, v29, vcc
	global_load_dword v71, v[48:49], off nt
	v_add_co_u32_e32 v48, vcc, 0x2c000, v28
	s_nop 1
	v_addc_co_u32_e32 v49, vcc, 0, v29, vcc
	global_load_dword v72, v[48:49], off nt
	v_add_co_u32_e32 v48, vcc, 0x2e000, v28
	s_nop 1
	v_addc_co_u32_e32 v49, vcc, 0, v29, vcc
	global_load_dword v73, v[48:49], off nt
	v_add_co_u32_e32 v48, vcc, 0x30000, v28
	s_nop 1
	v_addc_co_u32_e32 v49, vcc, 0, v29, vcc
	global_load_dword v74, v[48:49], off nt
	v_add_co_u32_e32 v48, vcc, 0x32000, v28
	s_nop 1
	v_addc_co_u32_e32 v49, vcc, 0, v29, vcc
	global_load_dword v75, v[48:49], off nt
	v_add_co_u32_e32 v48, vcc, 0x34000, v28
	s_nop 1
	v_addc_co_u32_e32 v49, vcc, 0, v29, vcc
	global_load_dword v76, v[48:49], off nt
	v_add_co_u32_e32 v48, vcc, 0x36000, v28
	s_nop 1
	v_addc_co_u32_e32 v49, vcc, 0, v29, vcc
	global_load_dword v77, v[48:49], off nt
	v_add_co_u32_e32 v48, vcc, 0x38000, v28
	s_nop 1
	v_addc_co_u32_e32 v49, vcc, 0, v29, vcc
	global_load_dword v78, v[48:49], off nt
	v_add_co_u32_e32 v48, vcc, 0x3a000, v28
	s_nop 1
	v_addc_co_u32_e32 v49, vcc, 0, v29, vcc
	global_load_dword v79, v[48:49], off nt
	v_add_co_u32_e32 v48, vcc, 0x3c000, v28
	s_nop 1
	v_addc_co_u32_e32 v49, vcc, 0, v29, vcc
	v_add_co_u32_e32 v28, vcc, 0x3e000, v28
	global_load_dword v48, v[48:49], off nt
	s_nop 0
	v_addc_co_u32_e32 v29, vcc, 0, v29, vcc
	global_load_dword v28, v[28:29], off nt
	s_waitcnt vmcnt(0)
	ds_write2_b32 v31, v50, v51 offset1:66
	ds_write2_b32 v31, v52, v53 offset0:132 offset1:198
	ds_write2_b32 v40, v54, v55 offset0:8 offset1:74
	ds_write2_b32 v40, v56, v57 offset0:140 offset1:206
	ds_write2_b32 v41, v58, v59 offset0:16 offset1:82
	ds_write2_b32 v41, v60, v61 offset0:148 offset1:214
	ds_write2_b32 v42, v62, v63 offset0:24 offset1:90
	ds_write2_b32 v42, v64, v65 offset0:156 offset1:222
	ds_write2_b32 v43, v66, v67 offset0:32 offset1:98
	ds_write2_b32 v43, v68, v69 offset0:164 offset1:230
	ds_write2_b32 v44, v70, v71 offset0:40 offset1:106
	ds_write2_b32 v44, v72, v73 offset0:172 offset1:238
	ds_write2_b32 v45, v74, v75 offset0:48 offset1:114
	ds_write2_b32 v45, v76, v77 offset0:180 offset1:246
	ds_write2_b32 v46, v78, v79 offset0:56 offset1:122
	ds_write2_b32 v46, v48, v28 offset0:188 offset1:254
	s_waitcnt lgkmcnt(0)
; #define GAS __attribute__((address_space(1)))
; #define LAS __attribute__((address_space(3)))
; #define LDS_WAIT() asm volatile("s_waitcnt lgkmcnt(0)" ::: "memory")
; __device__ __forceinline__ unsigned pk2(float lo, float hi) { return f2bf(lo) | (f2bf(hi) << 16); }
; __device__ __forceinline__ void tr_item(const float* W, int ld, int K, int nblk, int item, bf16* WT, bool gu, LAS float* scr, int lane) {
;     ...
;     const int c = lane & 7;
; #pragma unroll
;     for (int j = 0; j < 4; ++j) { const int n = (lane >> 3) + 8 * j; const LAS float* s = scr + (8 * c) * 33 + n;
;         v4u o; o.x = pk2(s[0 * 33], s[1 * 33]); o.y = pk2(s[2 * 33], s[3 * 33]); o.z = pk2(s[4 * 33], s[5 * 33]); o.w = pk2(s[6 * 33], s[7 * 33]);
;         *(GAS v4u*)(WT + (size_t)(drow0 + n) * K + k0 + 8 * c) = o; }
;     LDS_WAIT(); asm volatile("" ::: "memory");
	ds_read2_b32 v[52:53], v36 offset0:33 offset1:41
	ds_read2_b32 v[54:55], v36 offset1:8
	ds_read2_b32 v[56:57], v36 offset0:66 offset1:74
	ds_read2_b32 v[58:59], v36 offset0:99 offset1:107
	ds_read2_b32 v[60:61], v36 offset0:132 offset1:140
	ds_read2_b32 v[62:63], v36 offset0:165 offset1:173
	ds_read2_b32 v[64:65], v36 offset0:198 offset1:206
	ds_read2_b32 v[66:67], v36 offset0:231 offset1:239
	s_waitcnt lgkmcnt(7)
	v_bfe_u32 v49, v52, 16, 1
	s_waitcnt lgkmcnt(6)
	v_bfe_u32 v48, v54, 16, 1
	v_add3_u32 v48, v54, v48, s46
	v_lshrrev_b32_e32 v48, 16, v48
	v_add3_u32 v49, v52, v49, s46
	v_and_or_b32 v48, v49, s47, v48
	s_waitcnt lgkmcnt(5)
	v_bfe_u32 v49, v56, 16, 1
	v_add3_u32 v49, v56, v49, s46
	s_waitcnt lgkmcnt(4)
	v_bfe_u32 v50, v58, 16, 1
	v_lshrrev_b32_e32 v49, 16, v49
	v_add3_u32 v50, v58, v50, s46
	v_and_or_b32 v49, v50, s47, v49
	s_waitcnt lgkmcnt(3)
	v_bfe_u32 v50, v60, 16, 1
	v_add3_u32 v50, v60, v50, s46
	s_waitcnt lgkmcnt(2)
	v_bfe_u32 v51, v62, 16, 1
	v_lshrrev_b32_e32 v50, 16, v50
	v_add3_u32 v51, v62, v51, s46
	v_and_or_b32 v50, v51, s47, v50
	s_waitcnt lgkmcnt(1)
	v_bfe_u32 v51, v64, 16, 1
	v_add_u32_e32 v68, s24, v35
	v_add3_u32 v51, v64, v51, s46
	s_waitcnt lgkmcnt(0)
	v_bfe_u32 v52, v66, 16, 1
	v_ashrrev_i32_e32 v69, 31, v68
	v_lshl_add_u64 v[28:29], v[24:25], 0, s[16:17]
	v_lshrrev_b32_e32 v51, 16, v51
	v_add3_u32 v52, v66, v52, s46
	v_lshlrev_b64 v[68:69], 11, v[68:69]
	v_and_or_b32 v51, v52, s47, v51
	v_lshl_add_u64 v[68:69], v[28:29], 0, v[68:69]
	global_store_dwordx4 v[68:69], v[48:51], off sc1 nt
	v_bfe_u32 v52, v67, 16, 1
	v_add3_u32 v52, v67, v52, s46
	v_bfe_u32 v48, v55, 16, 1
	v_add3_u32 v48, v55, v48, s46
	v_bfe_u32 v49, v53, 16, 1
	v_lshrrev_b32_e32 v48, 16, v48
	v_add3_u32 v49, v53, v49, s46
	v_and_or_b32 v48, v49, s47, v48
	v_bfe_u32 v49, v57, 16, 1
	v_add3_u32 v49, v57, v49, s46
	v_bfe_u32 v50, v59, 16, 1
	v_lshrrev_b32_e32 v49, 16, v49
	v_add3_u32 v50, v59, v50, s46
	v_and_or_b32 v49, v50, s47, v49
	v_bfe_u32 v50, v61, 16, 1
	v_add3_u32 v50, v61, v50, s46
	v_bfe_u32 v51, v63, 16, 1
	v_lshrrev_b32_e32 v50, 16, v50
	v_add3_u32 v51, v63, v51, s46
	v_and_or_b32 v50, v51, s47, v50
	v_bfe_u32 v51, v65, 16, 1
	v_add3_u32 v51, v65, v51, s46
	v_lshrrev_b32_e32 v51, 16, v51
	v_and_or_b32 v51, v52, s47, v51
	v_add_u32_e32 v52, s24, v37
	v_ashrrev_i32_e32 v53, 31, v52
	v_lshlrev_b64 v[52:53], 11, v[52:53]
	v_lshl_add_u64 v[52:53], v[28:29], 0, v[52:53]
	global_store_dwordx4 v[52:53], v[48:51], off sc1 nt
	ds_read2_b32 v[52:53], v36 offset0:49 offset1:57
	ds_read2_b32 v[54:55], v36 offset0:16 offset1:24
	ds_read2_b32 v[56:57], v36 offset0:82 offset1:90
	ds_read2_b32 v[58:59], v36 offset0:115 offset1:123
	ds_read2_b32 v[60:61], v36 offset0:148 offset1:156
	ds_read2_b32 v[62:63], v36 offset0:181 offset1:189
	ds_read2_b32 v[64:65], v36 offset0:214 offset1:222
	ds_read2_b32 v[66:67], v36 offset0:247 offset1:255
	s_waitcnt lgkmcnt(7)
	v_bfe_u32 v49, v52, 16, 1
	s_waitcnt lgkmcnt(6)
	v_bfe_u32 v48, v54, 16, 1
	v_add3_u32 v48, v54, v48, s46
	v_lshrrev_b32_e32 v48, 16, v48
	v_add3_u32 v49, v52, v49, s46
	v_and_or_b32 v48, v49, s47, v48
	s_waitcnt lgkmcnt(5)
	v_bfe_u32 v49, v56, 16, 1
	v_add3_u32 v49, v56, v49, s46
	s_waitcnt lgkmcnt(4)
	v_bfe_u32 v50, v58, 16, 1
	v_lshrrev_b32_e32 v49, 16, v49
	v_add3_u32 v50, v58, v50, s46
	v_and_or_b32 v49, v50, s47, v49
	s_waitcnt lgkmcnt(3)
	v_bfe_u32 v50, v60, 16, 1
	v_add3_u32 v50, v60, v50, s46
	s_waitcnt lgkmcnt(2)
	v_bfe_u32 v51, v62, 16, 1
	v_lshrrev_b32_e32 v50, 16, v50
	v_add3_u32 v51, v62, v51, s46
	v_and_or_b32 v50, v51, s47, v50
	s_waitcnt lgkmcnt(1)
	v_bfe_u32 v51, v64, 16, 1
	v_add_u32_e32 v68, s24, v38
	v_add3_u32 v51, v64, v51, s46
	s_waitcnt lgkmcnt(0)
	v_bfe_u32 v52, v66, 16, 1
	v_ashrrev_i32_e32 v69, 31, v68
	v_lshrrev_b32_e32 v51, 16, v51
	v_add3_u32 v52, v66, v52, s46
	v_lshlrev_b64 v[68:69], 11, v[68:69]
	v_and_or_b32 v51, v52, s47, v51
	v_lshl_add_u64 v[68:69], v[28:29], 0, v[68:69]
	global_store_dwordx4 v[68:69], v[48:51], off sc1 nt
	v_bfe_u32 v52, v67, 16, 1
	v_add3_u32 v52, v67, v52, s46
	v_bfe_u32 v48, v55, 16, 1
	v_add3_u32 v48, v55, v48, s46
	v_bfe_u32 v49, v53, 16, 1
	v_lshrrev_b32_e32 v48, 16, v48
	v_add3_u32 v49, v53, v49, s46
	v_and_or_b32 v48, v49, s47, v48
	v_bfe_u32 v49, v57, 16, 1
	v_add3_u32 v49, v57, v49, s46
	v_bfe_u32 v50, v59, 16, 1
	v_lshrrev_b32_e32 v49, 16, v49
	v_add3_u32 v50, v59, v50, s46
	v_and_or_b32 v49, v50, s47, v49
	v_bfe_u32 v50, v61, 16, 1
	v_add3_u32 v50, v61, v50, s46
	v_bfe_u32 v51, v63, 16, 1
	v_lshrrev_b32_e32 v50, 16, v50
	v_add3_u32 v51, v63, v51, s46
	v_and_or_b32 v50, v51, s47, v50
	v_bfe_u32 v51, v65, 16, 1
	v_add3_u32 v51, v65, v51, s46
	v_lshrrev_b32_e32 v51, 16, v51
	v_and_or_b32 v51, v52, s47, v51
	v_add_u32_e32 v52, s24, v39
	v_ashrrev_i32_e32 v53, 31, v52
	v_lshlrev_b64 v[52:53], 11, v[52:53]
	v_lshl_add_u64 v[28:29], v[28:29], 0, v[52:53]
	global_store_dwordx4 v[28:29], v[48:51], off sc1 nt
	s_waitcnt lgkmcnt(0)

; #define LAS __attribute__((address_space(3)))
; #define LDS_WAIT() asm volatile("s_waitcnt lgkmcnt(0)" ::: "memory")
; __device__ __forceinline__ void tr_item(const float* W, int ld, int K, int nblk, int item, bf16* WT, bool gu, LAS float* scr, int lane) {
;     const int kb = item / nblk, nb = item % nblk, k0 = 64 * kb, n0 = 32 * nb;
;     int drow0 = n0;
;     if (gu) { const int bj = n0 / FF, j = n0 - bj * FF; drow0 = 256 * (j / 128) + 128 * bj + (j % 128); }
;     { float t_[32];
; #pragma unroll
;       for (int i = 0; i < 32; ++i) t_[i] = W[(size_t)(k0 + 2 * i + (lane >> 5)) * ld + n0 + (lane & 31)];
; #pragma unroll
;       for (int i = 0; i < 32; ++i) scr[(2 * i + (lane >> 5)) * 33 + (lane & 31)] = t_[i]; }
;     LDS_WAIT(); asm volatile("" ::: "memory");
; __device__ __forceinline__ void convert_items(Frame& F, const Args& a, int lo, int hi, int w, int nw) {
;     ...
;         if (r < I_FI) { tr_item(a.in[7], 3 * D + 16, D, 96, r, (bf16*)(F.ws + WS_WFOXIN), false, scr, lane); continue; } r -= I_FI;
.LBB0_1154:
	s_andn2_b64 vcc, exec, s[24:25]
	s_cbranch_vccnz .LBB0_1131
	s_mul_hi_i32 s16, s37, 0x2aaaaaab
	s_lshr_b32 s24, s16, 31
	s_ashr_i32 s16, s16, 4
	s_add_i32 s16, s16, s24
	s_lshl_b32 s26, s16, 6
	s_mulk_i32 s16, 0xf400
	s_add_i32 s24, s40, s16
	v_add_u32_e32 v64, s26, v30
	s_ashr_i32 s25, s24, 31
	v_lshl_add_u64 v[28:29], s[24:25], 2, v[16:17]
	v_add_u32_e32 v50, 2, v64
	v_add_u32_e32 v52, 4, v64
	v_add_u32_e32 v54, 6, v64
	v_add_u32_e32 v56, 8, v64
	v_add_u32_e32 v58, 10, v64
	v_add_u32_e32 v60, 12, v64
	v_add_u32_e32 v62, 14, v64
	v_mad_i64_i32 v[48:49], s[50:51], v64, s49, v[28:29]
	v_mad_i64_i32 v[50:51], s[50:51], v50, s49, v[28:29]
	v_mad_i64_i32 v[52:53], s[50:51], v52, s49, v[28:29]
	v_mad_i64_i32 v[54:55], s[50:51], v54, s49, v[28:29]
	v_mad_i64_i32 v[56:57], s[50:51], v56, s49, v[28:29]
	v_mad_i64_i32 v[58:59], s[50:51], v58, s49, v[28:29]
	v_mad_i64_i32 v[60:61], s[50:51], v60, s49, v[28:29]
	v_mad_i64_i32 v[62:63], s[50:51], v62, s49, v[28:29]
	global_load_dword v65, v[48:49], off nt
	global_load_dword v66, v[50:51], off nt
	global_load_dword v67, v[52:53], off nt
	global_load_dword v68, v[54:55], off nt
	global_load_dword v69, v[56:57], off nt
	global_load_dword v70, v[58:59], off nt
	global_load_dword v71, v[60:61], off nt
	global_load_dword v72, v[62:63], off nt
	v_add_u32_e32 v48, 16, v64
	v_add_u32_e32 v50, 18, v64
	v_add_u32_e32 v52, 20, v64
	v_add_u32_e32 v54, 22, v64
	v_add_u32_e32 v56, 24, v64
	v_add_u32_e32 v58, 26, v64
	v_add_u32_e32 v60, 28, v64
	v_add_u32_e32 v62, 30, v64
	v_mad_i64_i32 v[48:49], s[50:51], v48, s49, v[28:29]
	v_mad_i64_i32 v[50:51], s[50:51], v50, s49, v[28:29]
	v_mad_i64_i32 v[52:53], s[50:51], v52, s49, v[28:29]
	v_mad_i64_i32 v[54:55], s[50:51], v54, s49, v[28:29]
	v_mad_i64_i32 v[56:57], s[50:51], v56, s49, v[28:29]
	v_mad_i64_i32 v[58:59], s[50:51], v58, s49, v[28:29]
	v_mad_i64_i32 v[60:61], s[50:51], v60, s49, v[28:29]
	v_mad_i64_i32 v[62:63], s[50:51], v62, s49, v[28:29]
	global_load_dword v73, v[48:49], off nt
	global_load_dword v74, v[50:51], off nt
	global_load_dword v75, v[52:53], off nt
	global_load_dword v76, v[54:55], off nt
	global_load_dword v77, v[56:57], off nt
	global_load_dword v78, v[58:59], off nt
	global_load_dword v79, v[60:61], off nt
	global_load_dword v80, v[62:63], off nt
	v_add_u32_e32 v48, 32, v64
	v_add_u32_e32 v50, 34, v64
	v_add_u32_e32 v52, 36, v64
	v_add_u32_e32 v54, 38, v64
	v_add_u32_e32 v56, 40, v64
	v_add_u32_e32 v58, 42, v64
	v_add_u32_e32 v60, 44, v64
	v_add_u32_e32 v62, 46, v64
	v_mad_i64_i32 v[48:49], s[50:51], v48, s49, v[28:29]
	v_mad_i64_i32 v[50:51], s[50:51], v50, s49, v[28:29]
	v_mad_i64_i32 v[52:53], s[50:51], v52, s49, v[28:29]
	v_mad_i64_i32 v[54:55], s[50:51], v54, s49, v[28:29]
	v_mad_i64_i32 v[56:57], s[50:51], v56, s49, v[28:29]
	v_mad_i64_i32 v[58:59], s[50:51], v58, s49, v[28:29]
	v_mad_i64_i32 v[60:61], s[50:51], v60, s49, v[28:29]
	v_mad_i64_i32 v[62:63], s[50:51], v62, s49, v[28:29]
	global_load_dword v81, v[48:49], off nt
	global_load_dword v82, v[50:51], off nt
	global_load_dword v83, v[52:53], off nt
	global_load_dword v84, v[54:55], off nt
	global_load_dword v85, v[56:57], off nt
	global_load_dword v86, v[58:59], off nt
	global_load_dword v87, v[60:61], off nt
	s_nop 0
	global_load_dword v62, v[62:63], off nt
	v_add_u32_e32 v48, 48, v64
	v_add_u32_e32 v50, 50, v64
	v_add_u32_e32 v52, 52, v64
	v_add_u32_e32 v54, 54, v64
	v_add_u32_e32 v56, 56, v64
	v_add_u32_e32 v58, 58, v64
	v_add_u32_e32 v60, 60, v64
	v_add_u32_e32 v63, 62, v64
	v_mad_i64_i32 v[48:49], s[50:51], v48, s49, v[28:29]
	v_mad_i64_i32 v[50:51], s[50:51], v50, s49, v[28:29]
	v_mad_i64_i32 v[52:53], s[50:51], v52, s49, v[28:29]
	v_mad_i64_i32 v[54:55], s[50:51], v54, s49, v[28:29]
	v_mad_i64_i32 v[56:57], s[50:51], v56, s49, v[28:29]
	v_mad_i64_i32 v[58:59], s[50:51], v58, s49, v[28:29]
	v_mad_i64_i32 v[60:61], s[50:51], v60, s49, v[28:29]
	v_mad_i64_i32 v[28:29], s[50:51], v63, s49, v[28:29]
	global_load_dword v48, v[48:49], off nt
	s_nop 0
	global_load_dword v49, v[50:51], off nt
	s_nop 0
	global_load_dword v50, v[52:53], off nt
	global_load_dword v51, v[54:55], off nt
	s_nop 0
	global_load_dword v52, v[56:57], off nt
	global_load_dword v53, v[58:59], off nt
	global_load_dword v54, v[60:61], off nt
	s_nop 0
	global_load_dword v28, v[28:29], off nt
	s_waitcnt vmcnt(0)
	ds_write2_b32 v31, v65, v66 offset1:66
	ds_write2_b32 v31, v67, v68 offset0:132 offset1:198
	ds_write2_b32 v40, v69, v70 offset0:8 offset1:74
	ds_write2_b32 v40, v71, v72 offset0:140 offset1:206
	ds_write2_b32 v41, v73, v74 offset0:16 offset1:82
	ds_write2_b32 v41, v75, v76 offset0:148 offset1:214
	ds_write2_b32 v42, v77, v78 offset0:24 offset1:90
	ds_write2_b32 v42, v79, v80 offset0:156 offset1:222
	ds_write2_b32 v43, v81, v82 offset0:32 offset1:98
	ds_write2_b32 v43, v83, v84 offset0:164 offset1:230
	ds_write2_b32 v44, v85, v86 offset0:40 offset1:106
	ds_write2_b32 v44, v87, v62 offset0:172 offset1:238
	ds_write2_b32 v45, v48, v49 offset0:48 offset1:114
	ds_write2_b32 v45, v50, v51 offset0:180 offset1:246
	ds_write2_b32 v46, v52, v53 offset0:56 offset1:122
	ds_write2_b32 v46, v54, v28 offset0:188 offset1:254
	s_waitcnt lgkmcnt(0)
; #define GAS __attribute__((address_space(1)))
; #define LAS __attribute__((address_space(3)))
; #define LDS_WAIT() asm volatile("s_waitcnt lgkmcnt(0)" ::: "memory")
; __device__ __forceinline__ unsigned pk2(float lo, float hi) { return f2bf(lo) | (f2bf(hi) << 16); }
; __device__ __forceinline__ void tr_item(const float* W, int ld, int K, int nblk, int item, bf16* WT, bool gu, LAS float* scr, int lane) {
;     ...
;     const int c = lane & 7;
; #pragma unroll
;     for (int j = 0; j < 4; ++j) { const int n = (lane >> 3) + 8 * j; const LAS float* s = scr + (8 * c) * 33 + n;
;         v4u o; o.x = pk2(s[0 * 33], s[1 * 33]); o.y = pk2(s[2 * 33], s[3 * 33]); o.z = pk2(s[4 * 33], s[5 * 33]); o.w = pk2(s[6 * 33], s[7 * 33]);
;         *(GAS v4u*)(WT + (size_t)(drow0 + n) * K + k0 + 8 * c) = o; }
;     LDS_WAIT(); asm volatile("" ::: "memory");
	ds_read2_b32 v[28:29], v36 offset1:8
	ds_read2_b32 v[54:55], v36 offset0:33 offset1:41
	ds_read2_b32 v[56:57], v36 offset0:66 offset1:74
	ds_read2_b32 v[58:59], v36 offset0:99 offset1:107
	ds_read2_b32 v[60:61], v36 offset0:132 offset1:140
	s_waitcnt lgkmcnt(4)
	v_bfe_u32 v48, v28, 16, 1
	v_add3_u32 v28, v28, v48, s46
	s_waitcnt lgkmcnt(3)
	v_bfe_u32 v48, v54, 16, 1
	v_lshrrev_b32_e32 v28, 16, v28
	v_add3_u32 v48, v54, v48, s46
	ds_read2_b32 v[62:63], v36 offset0:165 offset1:173
	v_and_or_b32 v48, v48, s47, v28
	s_waitcnt lgkmcnt(3)
	v_bfe_u32 v28, v56, 16, 1
	v_add3_u32 v28, v56, v28, s46
	s_waitcnt lgkmcnt(2)
	v_bfe_u32 v49, v58, 16, 1
	ds_read2_b32 v[64:65], v36 offset0:198 offset1:206
	v_lshrrev_b32_e32 v28, 16, v28
	v_add3_u32 v49, v58, v49, s46
	ds_read2_b32 v[66:67], v36 offset0:231 offset1:239
	v_and_or_b32 v49, v49, s47, v28
	s_waitcnt lgkmcnt(3)
	v_bfe_u32 v28, v60, 16, 1
	v_add3_u32 v28, v60, v28, s46
	s_waitcnt lgkmcnt(2)
	v_bfe_u32 v50, v62, 16, 1
	v_lshrrev_b32_e32 v28, 16, v28
	v_add3_u32 v50, v62, v50, s46
	v_and_or_b32 v50, v50, s47, v28
	s_waitcnt lgkmcnt(1)
	v_bfe_u32 v28, v64, 16, 1
	v_add3_u32 v28, v64, v28, s46
	s_waitcnt lgkmcnt(0)
	v_bfe_u32 v51, v66, 16, 1
	v_lshrrev_b32_e32 v28, 16, v28
	v_add3_u32 v51, v66, v51, s46
	v_add_u32_e32 v68, s24, v35
	s_ashr_i32 s27, s26, 31
	v_and_or_b32 v51, v51, s47, v28
	v_ashrrev_i32_e32 v69, 31, v68
	v_bfe_u32 v28, v29, 16, 1
	v_lshl_add_u64 v[52:53], s[26:27], 1, v[26:27]
	v_lshlrev_b64 v[70:71], 11, v[68:69]
	v_add3_u32 v28, v29, v28, s46
	v_bfe_u32 v29, v55, 16, 1
	v_lshl_add_u64 v[70:71], v[52:53], 0, v[70:71]
	v_lshrrev_b32_e32 v28, 16, v28
	v_add3_u32 v29, v55, v29, s46
	global_store_dwordx4 v[70:71], v[48:51], off sc1 nt
	ds_read2_b32 v[54:55], v36 offset0:16 offset1:24
	v_add_u32_e32 v70, 16, v68
	v_and_or_b32 v48, v29, s47, v28
	v_bfe_u32 v28, v57, 16, 1
	v_add3_u32 v28, v57, v28, s46
	v_bfe_u32 v29, v59, 16, 1
	v_lshrrev_b32_e32 v28, 16, v28
	v_add3_u32 v29, v59, v29, s46
	v_and_or_b32 v49, v29, s47, v28
	v_bfe_u32 v28, v61, 16, 1
	v_add3_u32 v28, v61, v28, s46
	v_bfe_u32 v29, v63, 16, 1
	v_lshrrev_b32_e32 v28, 16, v28
	v_add3_u32 v29, v63, v29, s46
	v_and_or_b32 v50, v29, s47, v28
	v_bfe_u32 v28, v65, 16, 1
	v_add3_u32 v28, v65, v28, s46
	v_bfe_u32 v29, v67, 16, 1
	v_lshrrev_b32_e32 v28, 16, v28
	v_add3_u32 v29, v67, v29, s46
	v_and_or_b32 v51, v29, s47, v28
	v_add_u32_e32 v28, 8, v68
	v_ashrrev_i32_e32 v29, 31, v28
	v_lshlrev_b64 v[28:29], 11, v[28:29]
	v_lshl_add_u64 v[28:29], v[52:53], 0, v[28:29]
	global_store_dwordx4 v[28:29], v[48:51], off sc1 nt
	ds_read2_b32 v[28:29], v36 offset0:49 offset1:57
	ds_read2_b32 v[56:57], v36 offset0:82 offset1:90
	ds_read2_b32 v[58:59], v36 offset0:115 offset1:123
	s_waitcnt lgkmcnt(3)
	v_bfe_u32 v48, v54, 16, 1
	v_add3_u32 v48, v54, v48, s46
	s_waitcnt lgkmcnt(2)
	v_bfe_u32 v49, v28, 16, 1
	ds_read2_b32 v[60:61], v36 offset0:148 offset1:156
	v_lshrrev_b32_e32 v48, 16, v48
	v_add3_u32 v28, v28, v49, s46
	ds_read2_b32 v[62:63], v36 offset0:181 offset1:189
	v_and_or_b32 v48, v28, s47, v48
	s_waitcnt lgkmcnt(3)
	v_bfe_u32 v28, v56, 16, 1
	v_add3_u32 v28, v56, v28, s46
	s_waitcnt lgkmcnt(2)
	v_bfe_u32 v49, v58, 16, 1
	ds_read2_b32 v[64:65], v36 offset0:214 offset1:222
	v_lshrrev_b32_e32 v28, 16, v28
	v_add3_u32 v49, v58, v49, s46
	ds_read2_b32 v[66:67], v36 offset0:247 offset1:255
	v_and_or_b32 v49, v49, s47, v28
	s_waitcnt lgkmcnt(3)
	v_bfe_u32 v28, v60, 16, 1
	v_add3_u32 v28, v60, v28, s46
	s_waitcnt lgkmcnt(2)
	v_bfe_u32 v50, v62, 16, 1
	v_lshrrev_b32_e32 v28, 16, v28
	v_add3_u32 v50, v62, v50, s46
	v_and_or_b32 v50, v50, s47, v28
	s_waitcnt lgkmcnt(1)
	v_bfe_u32 v28, v64, 16, 1
	v_add3_u32 v28, v64, v28, s46
	s_waitcnt lgkmcnt(0)
	v_bfe_u32 v51, v66, 16, 1
	v_ashrrev_i32_e32 v71, 31, v70
	v_lshrrev_b32_e32 v28, 16, v28
	v_add3_u32 v51, v66, v51, s46
	v_lshlrev_b64 v[70:71], 11, v[70:71]
	v_and_or_b32 v51, v51, s47, v28
	v_lshl_add_u64 v[70:71], v[52:53], 0, v[70:71]
	v_bfe_u32 v28, v55, 16, 1
	global_store_dwordx4 v[70:71], v[48:51], off sc1 nt
	v_add3_u32 v28, v55, v28, s46
	v_lshrrev_b32_e32 v28, 16, v28
	v_bfe_u32 v48, v29, 16, 1
	v_add3_u32 v29, v29, v48, s46
	v_and_or_b32 v48, v29, s47, v28
	v_bfe_u32 v28, v57, 16, 1
	v_add3_u32 v28, v57, v28, s46
	v_bfe_u32 v29, v59, 16, 1
	v_lshrrev_b32_e32 v28, 16, v28
	v_add3_u32 v29, v59, v29, s46
	v_and_or_b32 v49, v29, s47, v28
	v_bfe_u32 v28, v61, 16, 1
	v_add3_u32 v28, v61, v28, s46
	v_bfe_u32 v29, v63, 16, 1
	v_lshrrev_b32_e32 v28, 16, v28
	v_add3_u32 v29, v63, v29, s46
	v_and_or_b32 v50, v29, s47, v28
	v_bfe_u32 v28, v65, 16, 1
	v_add3_u32 v28, v65, v28, s46
	v_bfe_u32 v29, v67, 16, 1
	v_lshrrev_b32_e32 v28, 16, v28
	v_add3_u32 v29, v67, v29, s46
	v_and_or_b32 v51, v29, s47, v28
	v_add_u32_e32 v28, 24, v68
	v_ashrrev_i32_e32 v29, 31, v28
	v_lshlrev_b64 v[28:29], 11, v[28:29]
	v_lshl_add_u64 v[28:29], v[52:53], 0, v[28:29]
	global_store_dwordx4 v[28:29], v[48:51], off sc1 nt
	s_waitcnt lgkmcnt(0)
	s_branch .LBB0_1131

; #define LAS __attribute__((address_space(3)))
; __device__ __forceinline__ void tr_item8(const float* W, int ld, int K, int nblk, int item, unsigned char* WT, bool gu, float scale, LAS float* scr, int lane) {
;     const int kb = item / nblk, nb = item % nblk, k0 = 64 * kb, n0 = 32 * nb;
;     int drow0 = n0;
;     if (gu) { const int bj = n0 / FF, j = n0 - bj * FF; drow0 = 256 * (j / 128) + 128 * bj + (j % 128); }
;     { float t_[32];
; #pragma unroll
;       for (int i = 0; i < 32; ++i) t_[i] = W[(size_t)(k0 + 2 * i + (lane >> 5)) * ld + n0 + (lane & 31)];
; #pragma unroll
;       for (int i = 0; i < 32; ++i) scr[(2 * i + (lane >> 5)) * 33 + (lane & 31)] = t_[i] * scale; }
; __device__ __forceinline__ void convert_items(Frame& F, const Args& a, int lo, int hi, int w, int nw) {
;     ...
;         if (r < NE * I_GU) { const int e = r / I_GU, rr = r % I_GU; tr_item8(a.in[18] + (size_t)e * D * 2 * FF, 2 * FF, D, 224, rr, F.ws + WS_WMGU + (size_t)e * 2 * FF * D, true, WSC_GU, scr, lane); continue; } r -= NE * I_GU;
.LBB0_1161:
	s_cmpk_gt_i32 s16, 0x5ff
	s_mov_b64 s[6:7], -1
	s_cbranch_scc0 .LBB0_1183
	s_cmpk_gt_u32 s16, 0x7ff
	s_cbranch_scc0 .LBB0_1180
	s_cmpk_gt_u32 s16, 0xaff
	s_cbranch_scc0 .LBB0_1177
	s_cmpk_gt_u32 s16, 0xcff
	s_cbranch_scc0 .LBB0_1174
	s_cmpk_gt_u32 s16, 0x1aff
	s_cbranch_scc0 .LBB0_1171
	s_cmpk_gt_u32 s16, 0x21ff
	s_cbranch_scc0 .LBB0_1168
	s_add_i32 s4, s16, 0xde00
	s_bfe_u32 s6, s4, 0x70009
	s_mulk_i32 s6, 0x2493
	s_lshr_b32 s6, s6, 16
	s_mul_i32 s7, s6, 0xe00
	s_sub_i32 s4, s4, s7
	s_mul_i32 s7, s6, 0x1c00000
	s_add_u32 s8, s72, s7
	s_addc_u32 s9, s73, 0
	s_mul_i32 s6, s6, 0x700000
	s_add_u32 s6, s3, s6
	s_addc_u32 s7, s30, 0
	s_bfe_u32 s25, s4, 0xb0005
	s_mulk_i32 s25, 0x2493
	s_lshr_b32 s25, s25, 16
	s_mul_i32 s26, s25, 0xe0
	s_sub_i32 s26, s4, s26
	s_lshl_b32 s4, s26, 5
	s_and_b32 s27, s26, 0xffff
	s_cmpk_gt_u32 s27, 0x6f
	s_cselect_b32 s27, 0xfffff200, 0
	s_cselect_b32 s31, 0x80, 0
	s_add_i32 s4, s27, s4
	s_sext_i32_i16 s27, s4
	s_bfe_u32 s27, s27, 0x70018
	s_add_i32 s27, s4, s27
	s_sext_i32_i16 s36, s27
	s_and_b32 s27, s27, 0xff80
	s_sub_i32 s4, s4, s27
	s_lshl_b32 s36, s36, 1
	s_sext_i32_i16 s4, s4
	s_and_b32 s36, s36, 0xffffff00
	s_add_i32 s4, s31, s4
	s_lshl_b32 s26, s26, 7
	s_add_i32 s4, s4, s36
	s_lshl_b32 s25, s25, 6
	s_and_b32 s26, s26, 0x3ff80
	s_add_u32 s8, s8, s26
	s_addc_u32 s9, s9, 0
	v_add_u32_e32 v64, s25, v28
	v_lshl_add_u64 v[46:47], s[8:9], 0, v[0:1]
	v_mad_i64_i32 v[48:49], s[8:9], v64, s13, v[46:47]
	v_add_u32_e32 v50, 2, v64
	v_add_u32_e32 v52, 4, v64
	v_add_u32_e32 v54, 6, v64
	v_add_u32_e32 v56, 8, v64
	v_add_u32_e32 v58, 10, v64
	v_add_u32_e32 v60, 12, v64
	v_add_u32_e32 v62, 14, v64
	v_mad_i64_i32 v[50:51], s[8:9], v50, s13, v[46:47]
	v_mad_i64_i32 v[52:53], s[8:9], v52, s13, v[46:47]
	v_mad_i64_i32 v[54:55], s[8:9], v54, s13, v[46:47]
	v_mad_i64_i32 v[56:57], s[8:9], v56, s13, v[46:47]
	v_mad_i64_i32 v[58:59], s[8:9], v58, s13, v[46:47]
	v_mad_i64_i32 v[60:61], s[8:9], v60, s13, v[46:47]
	v_mad_i64_i32 v[62:63], s[8:9], v62, s13, v[46:47]
	global_load_dword v65, v[48:49], off nt
	global_load_dword v66, v[50:51], off nt
	global_load_dword v67, v[52:53], off nt
	global_load_dword v68, v[54:55], off nt
	global_load_dword v69, v[56:57], off nt
	global_load_dword v70, v[58:59], off nt
	global_load_dword v71, v[60:61], off nt
	global_load_dword v72, v[62:63], off nt
	v_add_u32_e32 v48, 16, v64
	v_mad_i64_i32 v[48:49], s[8:9], v48, s13, v[46:47]
	v_add_u32_e32 v50, 18, v64
	v_add_u32_e32 v52, 20, v64
	v_add_u32_e32 v54, 22, v64
	v_add_u32_e32 v56, 24, v64
	v_add_u32_e32 v58, 26, v64
	v_add_u32_e32 v60, 28, v64
	v_add_u32_e32 v62, 30, v64
	v_mad_i64_i32 v[50:51], s[8:9], v50, s13, v[46:47]
	v_mad_i64_i32 v[52:53], s[8:9], v52, s13, v[46:47]
	v_mad_i64_i32 v[54:55], s[8:9], v54, s13, v[46:47]
	v_mad_i64_i32 v[56:57], s[8:9], v56, s13, v[46:47]
	v_mad_i64_i32 v[58:59], s[8:9], v58, s13, v[46:47]
	v_mad_i64_i32 v[60:61], s[8:9], v60, s13, v[46:47]
	v_mad_i64_i32 v[62:63], s[8:9], v62, s13, v[46:47]
	global_load_dword v73, v[48:49], off nt
	global_load_dword v74, v[50:51], off nt
	global_load_dword v75, v[52:53], off nt
	global_load_dword v76, v[54:55], off nt
	global_load_dword v77, v[56:57], off nt
	global_load_dword v78, v[58:59], off nt
	global_load_dword v79, v[60:61], off nt
	global_load_dword v80, v[62:63], off nt
	v_add_u32_e32 v48, 32, v64
	v_add_u32_e32 v50, 34, v64
	v_add_u32_e32 v52, 36, v64
	v_add_u32_e32 v54, 38, v64
	v_add_u32_e32 v60, 44, v64
	v_mad_i64_i32 v[48:49], s[8:9], v48, s13, v[46:47]
	v_mad_i64_i32 v[50:51], s[8:9], v50, s13, v[46:47]
	v_mad_i64_i32 v[52:53], s[8:9], v52, s13, v[46:47]
	v_mad_i64_i32 v[54:55], s[8:9], v54, s13, v[46:47]
	v_add_u32_e32 v56, 40, v64
	v_add_u32_e32 v58, 42, v64
	v_mad_i64_i32 v[60:61], s[8:9], v60, s13, v[46:47]
	v_add_u32_e32 v62, 46, v64
	v_mad_i64_i32 v[56:57], s[8:9], v56, s13, v[46:47]
	v_mad_i64_i32 v[58:59], s[8:9], v58, s13, v[46:47]
	v_mad_i64_i32 v[62:63], s[8:9], v62, s13, v[46:47]
	global_load_dword v81, v[48:49], off nt
	global_load_dword v82, v[50:51], off nt
	global_load_dword v83, v[52:53], off nt
	global_load_dword v84, v[54:55], off nt
	global_load_dword v85, v[56:57], off nt
	global_load_dword v86, v[58:59], off nt
	s_nop 0
	global_load_dword v60, v[60:61], off nt
	s_nop 0
	global_load_dword v61, v[62:63], off nt
	v_add_u32_e32 v48, 48, v64
	v_add_u32_e32 v50, 50, v64
	v_add_u32_e32 v52, 52, v64
	v_add_u32_e32 v54, 54, v64
	v_mad_i64_i32 v[48:49], s[8:9], v48, s13, v[46:47]
	v_mad_i64_i32 v[50:51], s[8:9], v50, s13, v[46:47]
	v_mad_i64_i32 v[52:53], s[8:9], v52, s13, v[46:47]
	v_mad_i64_i32 v[54:55], s[8:9], v54, s13, v[46:47]
	v_add_u32_e32 v56, 56, v64
	v_add_u32_e32 v58, 58, v64
	v_mad_i64_i32 v[56:57], s[8:9], v56, s13, v[46:47]
	v_mad_i64_i32 v[58:59], s[8:9], v58, s13, v[46:47]
	global_load_dword v62, v[48:49], off nt
	s_nop 0
	global_load_dword v50, v[50:51], off nt
	s_nop 0
	global_load_dword v51, v[52:53], off nt
	s_nop 0
	global_load_dword v52, v[54:55], off nt
	global_load_dword v53, v[56:57], off nt
	s_nop 0
	global_load_dword v54, v[58:59], off nt
	v_add_u32_e32 v48, 60, v64
	v_add_u32_e32 v55, 62, v64
	v_mad_i64_i32 v[48:49], s[8:9], v48, s13, v[46:47]
	v_mad_i64_i32 v[46:47], s[8:9], v55, s13, v[46:47]
	global_load_dword v48, v[48:49], off nt
	s_nop 0
	global_load_dword v46, v[46:47], off nt
	s_waitcnt vmcnt(0)
; __device__ __forceinline__ unsigned cvt_pk4_fp8(float a, float b, float c, float d) { int w = 0; w = __builtin_amdgcn_cvt_pk_fp8_f32(a, b, w, false); w = __builtin_amdgcn_cvt_pk_fp8_f32(c, d, w, true); return (unsigned)w; }
; #define GAS __attribute__((address_space(1)))
; #define LAS __attribute__((address_space(3)))
; #define LDS_WAIT() asm volatile("s_waitcnt lgkmcnt(0)" ::: "memory")
; __device__ __forceinline__ void tr_item8(const float* W, int ld, int K, int nblk, int item, unsigned char* WT, bool gu, float scale, LAS float* scr, int lane) {
;     ...
;       for (int i = 0; i < 32; ++i) scr[(2 * i + (lane >> 5)) * 33 + (lane & 31)] = t_[i] * scale; }
;     LDS_WAIT(); asm volatile("" ::: "memory");
;     const int c = lane & 3;
; #pragma unroll
;     for (int j = 0; j < 2; ++j) { const int n = (lane >> 2) + 16 * j; const LAS float* sp = scr + (16 * c) * 33 + n;
;         v4u o; o.x = pg8::cvt_pk4_fp8(sp[0 * 33], sp[1 * 33], sp[2 * 33], sp[3 * 33]); o.y = pg8::cvt_pk4_fp8(sp[4 * 33], sp[5 * 33], sp[6 * 33], sp[7 * 33]);
;         o.z = pg8::cvt_pk4_fp8(sp[8 * 33], sp[9 * 33], sp[10 * 33], sp[11 * 33]); o.w = pg8::cvt_pk4_fp8(sp[12 * 33], sp[13 * 33], sp[14 * 33], sp[15 * 33]);
;         *(GAS v4u*)(WT + (size_t)(drow0 + n) * K + k0 + 16 * c) = o; }
;     LDS_WAIT(); asm volatile("" ::: "memory");
	v_mul_f32_e32 v47, 0x42800000, v65
	v_mul_f32_e32 v49, 0x42800000, v66
	ds_write2_b32 v29, v47, v49 offset1:66
	v_mul_f32_e32 v47, 0x42800000, v67
	v_mul_f32_e32 v49, 0x42800000, v68
	ds_write2_b32 v29, v47, v49 offset0:132 offset1:198
	v_mul_f32_e32 v47, 0x42800000, v69
	v_mul_f32_e32 v49, 0x42800000, v70
	ds_write2_b32 v38, v47, v49 offset0:8 offset1:74
	v_mul_f32_e32 v47, 0x42800000, v71
	v_mul_f32_e32 v49, 0x42800000, v72
	ds_write2_b32 v38, v47, v49 offset0:140 offset1:206
	s_add_u32 s6, s6, s25
	s_addc_u32 s7, s7, 0
	v_mul_f32_e32 v47, 0x42800000, v73
	v_mul_f32_e32 v49, 0x42800000, v74
	ds_write2_b32 v39, v47, v49 offset0:16 offset1:82
	v_mul_f32_e32 v47, 0x42800000, v75
	v_mul_f32_e32 v49, 0x42800000, v76
	ds_write2_b32 v39, v47, v49 offset0:148 offset1:214
	v_mul_f32_e32 v47, 0x42800000, v77
	v_mul_f32_e32 v49, 0x42800000, v78
	ds_write2_b32 v40, v47, v49 offset0:24 offset1:90
	v_mul_f32_e32 v47, 0x42800000, v79
	v_mul_f32_e32 v49, 0x42800000, v80
	ds_write2_b32 v40, v47, v49 offset0:156 offset1:222
	v_mul_f32_e32 v47, 0x42800000, v81
	v_mul_f32_e32 v49, 0x42800000, v82
	ds_write2_b32 v41, v47, v49 offset0:32 offset1:98
	v_mul_f32_e32 v47, 0x42800000, v83
	v_mul_f32_e32 v49, 0x42800000, v84
	ds_write2_b32 v41, v47, v49 offset0:164 offset1:230
	v_mul_f32_e32 v47, 0x42800000, v85
	v_mul_f32_e32 v49, 0x42800000, v86
	ds_write2_b32 v42, v47, v49 offset0:40 offset1:106
	v_mul_f32_e32 v47, 0x42800000, v60
	v_mul_f32_e32 v49, 0x42800000, v61
	ds_write2_b32 v42, v47, v49 offset0:172 offset1:238
	v_add_u32_e32 v84, s4, v30
	v_ashrrev_i32_e32 v85, 31, v84
	v_lshlrev_b64 v[84:85], 10, v[84:85]
	v_mul_f32_e32 v47, 0x42800000, v62
	v_mul_f32_e32 v49, 0x42800000, v50
	ds_write2_b32 v43, v47, v49 offset0:48 offset1:114
	v_mul_f32_e32 v47, 0x42800000, v51
	v_mul_f32_e32 v49, 0x42800000, v52
	ds_write2_b32 v43, v47, v49 offset0:180 offset1:246
	v_mul_f32_e32 v47, 0x42800000, v53
	v_mul_f32_e32 v49, 0x42800000, v54
	ds_write2_b32 v44, v47, v49 offset0:56 offset1:122
	v_mov_b32_e32 v49, v1
	v_lshl_add_u64 v[50:51], s[6:7], 0, v[2:3]
	v_mul_f32_e32 v47, 0x42800000, v48
	v_mul_f32_e32 v46, 0x42800000, v46
	ds_write2_b32 v44, v47, v46 offset0:188 offset1:254
	s_waitcnt lgkmcnt(0)
	ds_read2_b32 v[52:53], v31 offset1:16
	ds_read2_b32 v[54:55], v31 offset0:33 offset1:49
	ds_read2_b32 v[56:57], v31 offset0:66 offset1:82
	ds_read2_b32 v[58:59], v31 offset0:99 offset1:115
	ds_read2_b32 v[60:61], v31 offset0:132 offset1:148
	ds_read2_b32 v[62:63], v31 offset0:165 offset1:181
	ds_read2_b32 v[64:65], v31 offset0:198 offset1:214
	ds_read2_b32 v[66:67], v31 offset0:231 offset1:247
	ds_read2_b32 v[68:69], v45 offset0:8 offset1:24
	ds_read2_b32 v[70:71], v45 offset0:41 offset1:57
	ds_read2_b32 v[72:73], v45 offset0:74 offset1:90
	ds_read2_b32 v[74:75], v45 offset0:107 offset1:123
	ds_read2_b32 v[76:77], v45 offset0:140 offset1:156
	ds_read2_b32 v[78:79], v45 offset0:173 offset1:189
	v_mov_b32_e32 v46, v1
	v_mov_b32_e32 v47, v1
	v_mov_b32_e32 v48, v1
	ds_read2_b32 v[80:81], v45 offset0:206 offset1:222
	ds_read2_b32 v[82:83], v45 offset0:239 offset1:255
	s_waitcnt lgkmcnt(14)
	v_cvt_pk_fp8_f32 v46, v52, v54
	s_waitcnt lgkmcnt(10)
	v_cvt_pk_fp8_f32 v47, v60, v62
	s_waitcnt lgkmcnt(6)
	v_cvt_pk_fp8_f32 v48, v68, v70
	s_waitcnt lgkmcnt(2)
	v_cvt_pk_fp8_f32 v49, v76, v78
	v_cvt_pk_fp8_f32 v46, v56, v58 op_sel:[0,0,1]
	v_cvt_pk_fp8_f32 v47, v64, v66 op_sel:[0,0,1]
	v_cvt_pk_fp8_f32 v48, v72, v74 op_sel:[0,0,1]
	s_waitcnt lgkmcnt(0)
	v_cvt_pk_fp8_f32 v49, v80, v82 op_sel:[0,0,1]
	v_lshl_add_u64 v[84:85], v[50:51], 0, v[84:85]
	v_add_u32_e32 v52, s4, v32
	s_mov_b64 s[6:7], 0
	global_store_dwordx4 v[84:85], v[46:49], off sc1 nt
	s_nop 1
	v_mov_b32_e32 v46, v1
	v_mov_b32_e32 v47, v1
	v_mov_b32_e32 v48, v1
	v_mov_b32_e32 v49, v1
	v_cvt_pk_fp8_f32 v46, v53, v55
	v_cvt_pk_fp8_f32 v47, v61, v63
	v_cvt_pk_fp8_f32 v48, v69, v71
	v_cvt_pk_fp8_f32 v49, v77, v79
	v_cvt_pk_fp8_f32 v46, v57, v59 op_sel:[0,0,1]
	v_cvt_pk_fp8_f32 v47, v65, v67 op_sel:[0,0,1]
	v_cvt_pk_fp8_f32 v48, v73, v75 op_sel:[0,0,1]
	v_cvt_pk_fp8_f32 v49, v81, v83 op_sel:[0,0,1]
	v_ashrrev_i32_e32 v53, 31, v52
	v_lshlrev_b64 v[52:53], 10, v[52:53]
	v_lshl_add_u64 v[50:51], v[50:51], 0, v[52:53]
	global_store_dwordx4 v[50:51], v[46:49], off sc1 nt
	s_waitcnt lgkmcnt(0)
; #define LAS __attribute__((address_space(3)))
; __device__ __forceinline__ void tr_item8(const float* W, int ld, int K, int nblk, int item, unsigned char* WT, bool gu, float scale, LAS float* scr, int lane) {
;     const int kb = item / nblk, nb = item % nblk, k0 = 64 * kb, n0 = 32 * nb;
;     int drow0 = n0;
;     if (gu) { const int bj = n0 / FF, j = n0 - bj * FF; drow0 = 256 * (j / 128) + 128 * bj + (j % 128); }
;     { float t_[32];
; #pragma unroll
;       for (int i = 0; i < 32; ++i) t_[i] = W[(size_t)(k0 + 2 * i + (lane >> 5)) * ld + n0 + (lane & 31)];
; #pragma unroll
;       for (int i = 0; i < 32; ++i) scr[(2 * i + (lane >> 5)) * 33 + (lane & 31)] = t_[i] * scale; }
; __device__ __forceinline__ void convert_items(Frame& F, const Args& a, int lo, int hi, int w, int nw) {
;     ...
;         if (r < I_DN) { tr_item8(a.in[15], D, FF, 32, r, F.ws + WS_WDN, false, WSC_DN, scr, lane); continue; } r -= I_DN;
.LBB0_1168:
	s_andn2_b64 vcc, exec, s[6:7]
	s_cbranch_vccnz .LBB0_1170
	s_lshl_b32 s4, s16, 5
	s_and_b32 s6, s11, 0x1ffc0
	s_and_b32 s8, s4, 0x3e0
	v_add_u32_e32 v46, s6, v28
	s_lshl_b32 s4, s8, 2
	v_ashrrev_i32_e32 v47, 31, v46
	v_lshl_add_u64 v[48:49], v[4:5], 0, s[4:5]
	v_lshlrev_b64 v[46:47], 12, v[46:47]
	v_lshl_add_u64 v[46:47], v[48:49], 0, v[46:47]
	v_add_co_u32_e32 v48, vcc, 0x2000, v46
	s_mov_b32 s7, s5
	s_nop 0
	v_addc_co_u32_e32 v49, vcc, 0, v47, vcc
	v_add_co_u32_e32 v50, vcc, 0x4000, v46
	s_nop 1
	v_addc_co_u32_e32 v51, vcc, 0, v47, vcc
	v_add_co_u32_e32 v52, vcc, 0x6000, v46
	s_nop 1
	v_addc_co_u32_e32 v53, vcc, 0, v47, vcc
	v_add_co_u32_e32 v54, vcc, 0x8000, v46
	s_nop 1
	v_addc_co_u32_e32 v55, vcc, 0, v47, vcc
	v_add_co_u32_e32 v56, vcc, 0xa000, v46
	s_nop 1
	v_addc_co_u32_e32 v57, vcc, 0, v47, vcc
	v_add_co_u32_e32 v58, vcc, 0xc000, v46
	s_nop 1
	v_addc_co_u32_e32 v59, vcc, 0, v47, vcc
	v_add_co_u32_e32 v60, vcc, 0xe000, v46
	s_nop 1
	v_addc_co_u32_e32 v61, vcc, 0, v47, vcc
	global_load_dword v64, v[46:47], off nt
	global_load_dword v65, v[48:49], off nt
	global_load_dword v66, v[50:51], off nt
	global_load_dword v67, v[52:53], off nt
	global_load_dword v68, v[54:55], off nt
	global_load_dword v69, v[56:57], off nt
	global_load_dword v70, v[58:59], off nt
	global_load_dword v71, v[60:61], off nt
	v_add_co_u32_e32 v48, vcc, 0x10000, v46
	s_nop 1
	v_addc_co_u32_e32 v49, vcc, 0, v47, vcc
	v_add_co_u32_e32 v50, vcc, 0x12000, v46
	s_nop 1
	v_addc_co_u32_e32 v51, vcc, 0, v47, vcc
	v_add_co_u32_e32 v52, vcc, 0x14000, v46
	s_nop 1
	v_addc_co_u32_e32 v53, vcc, 0, v47, vcc
	v_add_co_u32_e32 v54, vcc, 0x16000, v46
	s_nop 1
	v_addc_co_u32_e32 v55, vcc, 0, v47, vcc
	v_add_co_u32_e32 v56, vcc, 0x18000, v46
	s_nop 1
	v_addc_co_u32_e32 v57, vcc, 0, v47, vcc
	v_add_co_u32_e32 v58, vcc, 0x1a000, v46
	s_nop 1
	v_addc_co_u32_e32 v59, vcc, 0, v47, vcc
	v_add_co_u32_e32 v60, vcc, 0x1c000, v46
	s_nop 1
	v_addc_co_u32_e32 v61, vcc, 0, v47, vcc
	v_add_co_u32_e32 v62, vcc, 0x1e000, v46
	s_nop 1
	v_addc_co_u32_e32 v63, vcc, 0, v47, vcc
	global_load_dword v72, v[48:49], off nt
	global_load_dword v73, v[50:51], off nt
	global_load_dword v74, v[52:53], off nt
	global_load_dword v75, v[54:55], off nt
	global_load_dword v76, v[56:57], off nt
	global_load_dword v77, v[58:59], off nt
	global_load_dword v78, v[60:61], off nt
	global_load_dword v79, v[62:63], off nt
	v_add_co_u32_e32 v48, vcc, 0x20000, v46
	s_nop 1
	v_addc_co_u32_e32 v49, vcc, 0, v47, vcc
	v_add_co_u32_e32 v50, vcc, 0x22000, v46
	s_nop 1
	v_addc_co_u32_e32 v51, vcc, 0, v47, vcc
	v_add_co_u32_e32 v52, vcc, 0x24000, v46
	s_nop 1
	v_addc_co_u32_e32 v53, vcc, 0, v47, vcc
	v_add_co_u32_e32 v54, vcc, 0x26000, v46
	s_nop 1
	v_addc_co_u32_e32 v55, vcc, 0, v47, vcc
	v_add_co_u32_e32 v56, vcc, 0x28000, v46
	s_nop 1
	v_addc_co_u32_e32 v57, vcc, 0, v47, vcc
	v_add_co_u32_e32 v58, vcc, 0x2a000, v46
	s_nop 1
	v_addc_co_u32_e32 v59, vcc, 0, v47, vcc
	v_add_co_u32_e32 v60, vcc, 0x2c000, v46
	s_nop 1
	v_addc_co_u32_e32 v61, vcc, 0, v47, vcc
	v_add_co_u32_e32 v62, vcc, 0x2e000, v46
	s_nop 1
	v_addc_co_u32_e32 v63, vcc, 0, v47, vcc
	global_load_dword v80, v[48:49], off nt
	global_load_dword v81, v[50:51], off nt
	global_load_dword v82, v[52:53], off nt
	global_load_dword v83, v[54:55], off nt
	global_load_dword v84, v[56:57], off nt
	global_load_dword v85, v[58:59], off nt
	s_nop 0
	global_load_dword v60, v[60:61], off nt
	s_nop 0
	global_load_dword v61, v[62:63], off nt
	v_add_co_u32_e32 v48, vcc, 0x30000, v46
	s_nop 1
	v_addc_co_u32_e32 v49, vcc, 0, v47, vcc
	v_add_co_u32_e32 v50, vcc, 0x32000, v46
	s_nop 1
	v_addc_co_u32_e32 v51, vcc, 0, v47, vcc
	v_add_co_u32_e32 v52, vcc, 0x34000, v46
	s_nop 1
	v_addc_co_u32_e32 v53, vcc, 0, v47, vcc
	v_add_co_u32_e32 v54, vcc, 0x36000, v46
	s_nop 1
	v_addc_co_u32_e32 v55, vcc, 0, v47, vcc
	v_add_co_u32_e32 v56, vcc, 0x38000, v46
	s_nop 1
	v_addc_co_u32_e32 v57, vcc, 0, v47, vcc
	v_add_co_u32_e32 v58, vcc, 0x3a000, v46
	s_nop 1
	v_addc_co_u32_e32 v59, vcc, 0, v47, vcc
	global_load_dword v62, v[48:49], off nt
	s_nop 0
	global_load_dword v50, v[50:51], off nt
	s_nop 0
	global_load_dword v51, v[52:53], off nt
	s_nop 0
	global_load_dword v52, v[54:55], off nt
	global_load_dword v53, v[56:57], off nt
	s_nop 0
	global_load_dword v54, v[58:59], off nt
	v_add_co_u32_e32 v48, vcc, 0x3c000, v46
	s_nop 1
	v_addc_co_u32_e32 v49, vcc, 0, v47, vcc
	v_add_co_u32_e32 v46, vcc, 0x3e000, v46
	s_nop 1
	v_addc_co_u32_e32 v47, vcc, 0, v47, vcc
	global_load_dword v48, v[48:49], off nt
	s_nop 0
	global_load_dword v46, v[46:47], off nt
	s_waitcnt vmcnt(0)
; __device__ __forceinline__ unsigned cvt_pk4_fp8(float a, float b, float c, float d) { int w = 0; w = __builtin_amdgcn_cvt_pk_fp8_f32(a, b, w, false); w = __builtin_amdgcn_cvt_pk_fp8_f32(c, d, w, true); return (unsigned)w; }
; #define GAS __attribute__((address_space(1)))
; #define LAS __attribute__((address_space(3)))
; #define LDS_WAIT() asm volatile("s_waitcnt lgkmcnt(0)" ::: "memory")
; __device__ __forceinline__ void tr_item8(const float* W, int ld, int K, int nblk, int item, unsigned char* WT, bool gu, float scale, LAS float* scr, int lane) {
;     ...
;       for (int i = 0; i < 32; ++i) scr[(2 * i + (lane >> 5)) * 33 + (lane & 31)] = t_[i] * scale; }
;     LDS_WAIT(); asm volatile("" ::: "memory");
;     const int c = lane & 3;
; #pragma unroll
;     for (int j = 0; j < 2; ++j) { const int n = (lane >> 2) + 16 * j; const LAS float* sp = scr + (16 * c) * 33 + n;
;         v4u o; o.x = pg8::cvt_pk4_fp8(sp[0 * 33], sp[1 * 33], sp[2 * 33], sp[3 * 33]); o.y = pg8::cvt_pk4_fp8(sp[4 * 33], sp[5 * 33], sp[6 * 33], sp[7 * 33]);
;         o.z = pg8::cvt_pk4_fp8(sp[8 * 33], sp[9 * 33], sp[10 * 33], sp[11 * 33]); o.w = pg8::cvt_pk4_fp8(sp[12 * 33], sp[13 * 33], sp[14 * 33], sp[15 * 33]);
;         *(GAS v4u*)(WT + (size_t)(drow0 + n) * K + k0 + 16 * c) = o; }
;     LDS_WAIT(); asm volatile("" ::: "memory");
	v_mul_f32_e32 v47, 0x43000000, v64
	v_mul_f32_e32 v49, 0x43000000, v65
	ds_write2_b32 v29, v47, v49 offset1:66
	v_mul_f32_e32 v47, 0x43000000, v66
	v_mul_f32_e32 v49, 0x43000000, v67
	ds_write2_b32 v29, v47, v49 offset0:132 offset1:198
	v_mul_f32_e32 v47, 0x43000000, v68
	v_mul_f32_e32 v49, 0x43000000, v69
	ds_write2_b32 v38, v47, v49 offset0:8 offset1:74
	v_mul_f32_e32 v47, 0x43000000, v70
	v_mul_f32_e32 v49, 0x43000000, v71
	ds_write2_b32 v38, v47, v49 offset0:140 offset1:206
	v_mul_f32_e32 v47, 0x43000000, v72
	v_mul_f32_e32 v49, 0x43000000, v73
	ds_write2_b32 v39, v47, v49 offset0:16 offset1:82
	v_mul_f32_e32 v47, 0x43000000, v74
	v_mul_f32_e32 v49, 0x43000000, v75
	ds_write2_b32 v39, v47, v49 offset0:148 offset1:214
	v_mul_f32_e32 v47, 0x43000000, v76
	v_mul_f32_e32 v49, 0x43000000, v77
	ds_write2_b32 v40, v47, v49 offset0:24 offset1:90
	v_mul_f32_e32 v47, 0x43000000, v78
	v_mul_f32_e32 v49, 0x43000000, v79
	ds_write2_b32 v40, v47, v49 offset0:156 offset1:222
	v_mul_f32_e32 v47, 0x43000000, v80
	v_mul_f32_e32 v49, 0x43000000, v81
	ds_write2_b32 v41, v47, v49 offset0:32 offset1:98
	v_mul_f32_e32 v47, 0x43000000, v82
	v_mul_f32_e32 v49, 0x43000000, v83
	ds_write2_b32 v41, v47, v49 offset0:164 offset1:230
	v_mul_f32_e32 v47, 0x43000000, v84
	v_mul_f32_e32 v49, 0x43000000, v85
	ds_write2_b32 v42, v47, v49 offset0:40 offset1:106
	v_mul_f32_e32 v47, 0x43000000, v60
	v_mul_f32_e32 v49, 0x43000000, v61
	ds_write2_b32 v42, v47, v49 offset0:172 offset1:238
	v_mul_f32_e32 v47, 0x43000000, v62
	v_mul_f32_e32 v49, 0x43000000, v50
	ds_write2_b32 v43, v47, v49 offset0:48 offset1:114
	v_mul_f32_e32 v47, 0x43000000, v51
	v_mul_f32_e32 v49, 0x43000000, v52
	ds_write2_b32 v43, v47, v49 offset0:180 offset1:246
	v_mul_f32_e32 v47, 0x43000000, v53
	v_mul_f32_e32 v49, 0x43000000, v54
	ds_write2_b32 v44, v47, v49 offset0:56 offset1:122
	v_mov_b32_e32 v49, 0
	v_lshl_add_u64 v[50:51], v[18:19], 0, s[6:7]
	v_mul_f32_e32 v47, 0x43000000, v48
	v_mul_f32_e32 v46, 0x43000000, v46
	ds_write2_b32 v44, v47, v46 offset0:188 offset1:254
	s_waitcnt lgkmcnt(0)
	ds_read2_b32 v[52:53], v31 offset1:16
	ds_read2_b32 v[54:55], v31 offset0:33 offset1:49
	ds_read2_b32 v[56:57], v31 offset0:66 offset1:82
	ds_read2_b32 v[58:59], v31 offset0:99 offset1:115
	ds_read2_b32 v[60:61], v31 offset0:132 offset1:148
	ds_read2_b32 v[62:63], v31 offset0:165 offset1:181
	ds_read2_b32 v[64:65], v31 offset0:198 offset1:214
	ds_read2_b32 v[66:67], v31 offset0:231 offset1:247
	ds_read2_b32 v[68:69], v45 offset0:8 offset1:24
	ds_read2_b32 v[70:71], v45 offset0:41 offset1:57
	ds_read2_b32 v[72:73], v45 offset0:74 offset1:90
	ds_read2_b32 v[74:75], v45 offset0:107 offset1:123
	ds_read2_b32 v[76:77], v45 offset0:140 offset1:156
	ds_read2_b32 v[78:79], v45 offset0:173 offset1:189
	v_mov_b32_e32 v46, 0
	v_mov_b32_e32 v47, 0
	v_mov_b32_e32 v48, 0
	ds_read2_b32 v[80:81], v45 offset0:206 offset1:222
	ds_read2_b32 v[82:83], v45 offset0:239 offset1:255
	s_waitcnt lgkmcnt(14)
	v_cvt_pk_fp8_f32 v46, v52, v54
	s_waitcnt lgkmcnt(10)
	v_cvt_pk_fp8_f32 v47, v60, v62
	s_waitcnt lgkmcnt(6)
	v_cvt_pk_fp8_f32 v48, v68, v70
	s_waitcnt lgkmcnt(2)
	v_cvt_pk_fp8_f32 v49, v76, v78
	v_cvt_pk_fp8_f32 v46, v56, v58 op_sel:[0,0,1]
	v_cvt_pk_fp8_f32 v47, v64, v66 op_sel:[0,0,1]
	v_cvt_pk_fp8_f32 v48, v72, v74 op_sel:[0,0,1]
	s_waitcnt lgkmcnt(0)
	v_cvt_pk_fp8_f32 v49, v80, v82 op_sel:[0,0,1]
	v_add_u32_e32 v52, s8, v30
	v_mad_i64_i32 v[84:85], s[6:7], v52, s12, v[50:51]
	global_store_dwordx4 v[84:85], v[46:49], off sc1 nt
	v_add_u32_e32 v52, s8, v32
	v_mad_i64_i32 v[50:51], s[6:7], v52, s12, v[50:51]
	v_mov_b32_e32 v46, 0
	v_mov_b32_e32 v47, 0
	v_mov_b32_e32 v48, 0
	v_mov_b32_e32 v49, 0
	v_cvt_pk_fp8_f32 v46, v53, v55
	v_cvt_pk_fp8_f32 v47, v61, v63
	v_cvt_pk_fp8_f32 v48, v69, v71
	v_cvt_pk_fp8_f32 v49, v77, v79
	v_cvt_pk_fp8_f32 v46, v57, v59 op_sel:[0,0,1]
	v_cvt_pk_fp8_f32 v47, v65, v67 op_sel:[0,0,1]
	v_cvt_pk_fp8_f32 v48, v73, v75 op_sel:[0,0,1]
	v_cvt_pk_fp8_f32 v49, v81, v83 op_sel:[0,0,1]
	global_store_dwordx4 v[50:51], v[46:49], off sc1 nt
	s_waitcnt lgkmcnt(0)

; #define LAS __attribute__((address_space(3)))
; __device__ __forceinline__ void tr_item8(const float* W, int ld, int K, int nblk, int item, unsigned char* WT, bool gu, float scale, LAS float* scr, int lane) {
;     const int kb = item / nblk, nb = item % nblk, k0 = 64 * kb, n0 = 32 * nb;
;     int drow0 = n0;
;     if (gu) { const int bj = n0 / FF, j = n0 - bj * FF; drow0 = 256 * (j / 128) + 128 * bj + (j % 128); }
;     { float t_[32];
; #pragma unroll
;       for (int i = 0; i < 32; ++i) t_[i] = W[(size_t)(k0 + 2 * i + (lane >> 5)) * ld + n0 + (lane & 31)];
; #pragma unroll
;       for (int i = 0; i < 32; ++i) scr[(2 * i + (lane >> 5)) * 33 + (lane & 31)] = t_[i] * scale; }
; __device__ __forceinline__ void convert_items(Frame& F, const Args& a, int lo, int hi, int w, int nw) {
;     ...
;         if (r < I_GU) { tr_item8(a.in[14], 2 * FF, D, 224, r, F.ws + WS_WGU, true, WSC_GU, scr, lane); continue; } r -= I_GU;
.LBB0_1171:
	s_andn2_b64 vcc, exec, s[6:7]
	s_cbranch_vccnz .LBB0_1173
	s_add_i32 s4, s16, 0xf300
	s_bfe_u32 s6, s4, 0xb0005
	s_mulk_i32 s6, 0x2493
	s_lshr_b32 s6, s6, 16
	s_mul_i32 s7, s6, 0xe0
	s_sub_i32 s4, s4, s7
	s_lshl_b32 s7, s4, 5
	s_and_b32 s8, s4, 0xffff
	s_cmpk_gt_u32 s8, 0x6f
	s_cselect_b32 s25, 0xfffff200, 0
	s_cselect_b32 s26, 0x80, 0
	s_lshl_b32 s4, s4, 7
	s_lshl_b32 s6, s6, 6
	s_and_b32 s4, s4, 0x3ff80
	v_add_u32_e32 v64, s6, v28
	v_lshl_add_u64 v[46:47], v[6:7], 0, s[4:5]
	v_mad_i64_i32 v[48:49], s[8:9], v64, s13, v[46:47]
	v_add_u32_e32 v50, 2, v64
	v_add_u32_e32 v52, 4, v64
	v_add_u32_e32 v54, 6, v64
	v_add_u32_e32 v56, 8, v64
	v_add_u32_e32 v58, 10, v64
	v_add_u32_e32 v60, 12, v64
	v_add_u32_e32 v62, 14, v64
	v_mad_i64_i32 v[50:51], s[8:9], v50, s13, v[46:47]
	v_mad_i64_i32 v[52:53], s[8:9], v52, s13, v[46:47]
	v_mad_i64_i32 v[54:55], s[8:9], v54, s13, v[46:47]
	v_mad_i64_i32 v[56:57], s[8:9], v56, s13, v[46:47]
	v_mad_i64_i32 v[58:59], s[8:9], v58, s13, v[46:47]
	v_mad_i64_i32 v[60:61], s[8:9], v60, s13, v[46:47]
	v_mad_i64_i32 v[62:63], s[8:9], v62, s13, v[46:47]
	global_load_dword v65, v[48:49], off nt
	global_load_dword v66, v[50:51], off nt
	global_load_dword v67, v[52:53], off nt
	global_load_dword v68, v[54:55], off nt
	global_load_dword v69, v[56:57], off nt
	global_load_dword v70, v[58:59], off nt
	global_load_dword v71, v[60:61], off nt
	global_load_dword v72, v[62:63], off nt
	v_add_u32_e32 v48, 16, v64
	v_mad_i64_i32 v[48:49], s[8:9], v48, s13, v[46:47]
	v_add_u32_e32 v50, 18, v64
	v_add_u32_e32 v52, 20, v64
	v_add_u32_e32 v54, 22, v64
	v_add_u32_e32 v56, 24, v64
	v_add_u32_e32 v58, 26, v64
	v_add_u32_e32 v60, 28, v64
	v_add_u32_e32 v62, 30, v64
	v_mad_i64_i32 v[50:51], s[8:9], v50, s13, v[46:47]
	v_mad_i64_i32 v[52:53], s[8:9], v52, s13, v[46:47]
	v_mad_i64_i32 v[54:55], s[8:9], v54, s13, v[46:47]
	v_mad_i64_i32 v[56:57], s[8:9], v56, s13, v[46:47]
	v_mad_i64_i32 v[58:59], s[8:9], v58, s13, v[46:47]
	v_mad_i64_i32 v[60:61], s[8:9], v60, s13, v[46:47]
	v_mad_i64_i32 v[62:63], s[8:9], v62, s13, v[46:47]
	global_load_dword v73, v[48:49], off nt
	global_load_dword v74, v[50:51], off nt
	global_load_dword v75, v[52:53], off nt
	global_load_dword v76, v[54:55], off nt
	global_load_dword v77, v[56:57], off nt
	global_load_dword v78, v[58:59], off nt
	global_load_dword v79, v[60:61], off nt
	global_load_dword v80, v[62:63], off nt
	v_add_u32_e32 v48, 32, v64
	v_add_u32_e32 v50, 34, v64
	v_add_u32_e32 v52, 36, v64
	v_add_u32_e32 v54, 38, v64
	v_add_u32_e32 v60, 44, v64
	v_mad_i64_i32 v[48:49], s[8:9], v48, s13, v[46:47]
	v_mad_i64_i32 v[50:51], s[8:9], v50, s13, v[46:47]
	v_mad_i64_i32 v[52:53], s[8:9], v52, s13, v[46:47]
	v_mad_i64_i32 v[54:55], s[8:9], v54, s13, v[46:47]
	v_add_u32_e32 v56, 40, v64
	v_add_u32_e32 v58, 42, v64
	v_mad_i64_i32 v[60:61], s[8:9], v60, s13, v[46:47]
	v_add_u32_e32 v62, 46, v64
	v_mad_i64_i32 v[56:57], s[8:9], v56, s13, v[46:47]
	v_mad_i64_i32 v[58:59], s[8:9], v58, s13, v[46:47]
	v_mad_i64_i32 v[62:63], s[8:9], v62, s13, v[46:47]
	global_load_dword v81, v[48:49], off nt
	global_load_dword v82, v[50:51], off nt
	global_load_dword v83, v[52:53], off nt
	global_load_dword v84, v[54:55], off nt
	global_load_dword v85, v[56:57], off nt
	global_load_dword v86, v[58:59], off nt
	s_nop 0
	global_load_dword v60, v[60:61], off nt
	s_nop 0
	global_load_dword v61, v[62:63], off nt
	v_add_u32_e32 v48, 48, v64
	v_add_u32_e32 v50, 50, v64
	v_add_u32_e32 v52, 52, v64
	v_add_u32_e32 v54, 54, v64
	v_mad_i64_i32 v[48:49], s[8:9], v48, s13, v[46:47]
	v_mad_i64_i32 v[50:51], s[8:9], v50, s13, v[46:47]
	v_mad_i64_i32 v[52:53], s[8:9], v52, s13, v[46:47]
	v_mad_i64_i32 v[54:55], s[8:9], v54, s13, v[46:47]
	v_add_u32_e32 v56, 56, v64
	v_add_u32_e32 v58, 58, v64
	v_mad_i64_i32 v[56:57], s[8:9], v56, s13, v[46:47]
	v_mad_i64_i32 v[58:59], s[8:9], v58, s13, v[46:47]
	global_load_dword v62, v[48:49], off nt
	s_nop 0
	global_load_dword v50, v[50:51], off nt
	s_nop 0
	global_load_dword v51, v[52:53], off nt
	s_nop 0
	global_load_dword v52, v[54:55], off nt
	global_load_dword v53, v[56:57], off nt
	s_nop 0
	global_load_dword v54, v[58:59], off nt
	v_add_u32_e32 v48, 60, v64
	v_add_u32_e32 v55, 62, v64
	v_mad_i64_i32 v[48:49], s[8:9], v48, s13, v[46:47]
	v_mad_i64_i32 v[46:47], s[8:9], v55, s13, v[46:47]
	global_load_dword v48, v[48:49], off nt
	s_nop 0
	global_load_dword v46, v[46:47], off nt
	s_waitcnt vmcnt(0)
; __device__ __forceinline__ unsigned cvt_pk4_fp8(float a, float b, float c, float d) { int w = 0; w = __builtin_amdgcn_cvt_pk_fp8_f32(a, b, w, false); w = __builtin_amdgcn_cvt_pk_fp8_f32(c, d, w, true); return (unsigned)w; }
; #define GAS __attribute__((address_space(1)))
; #define LAS __attribute__((address_space(3)))
; #define LDS_WAIT() asm volatile("s_waitcnt lgkmcnt(0)" ::: "memory")
; __device__ __forceinline__ void tr_item8(const float* W, int ld, int K, int nblk, int item, unsigned char* WT, bool gu, float scale, LAS float* scr, int lane) {
;     ...
;       for (int i = 0; i < 32; ++i) scr[(2 * i + (lane >> 5)) * 33 + (lane & 31)] = t_[i] * scale; }
;     LDS_WAIT(); asm volatile("" ::: "memory");
;     const int c = lane & 3;
; #pragma unroll
;     for (int j = 0; j < 2; ++j) { const int n = (lane >> 2) + 16 * j; const LAS float* sp = scr + (16 * c) * 33 + n;
;         v4u o; o.x = pg8::cvt_pk4_fp8(sp[0 * 33], sp[1 * 33], sp[2 * 33], sp[3 * 33]); o.y = pg8::cvt_pk4_fp8(sp[4 * 33], sp[5 * 33], sp[6 * 33], sp[7 * 33]);
;         o.z = pg8::cvt_pk4_fp8(sp[8 * 33], sp[9 * 33], sp[10 * 33], sp[11 * 33]); o.w = pg8::cvt_pk4_fp8(sp[12 * 33], sp[13 * 33], sp[14 * 33], sp[15 * 33]);
;         *(GAS v4u*)(WT + (size_t)(drow0 + n) * K + k0 + 16 * c) = o; }
;     LDS_WAIT(); asm volatile("" ::: "memory");
	v_mul_f32_e32 v47, 0x42800000, v65
	v_mul_f32_e32 v49, 0x42800000, v66
	ds_write2_b32 v29, v47, v49 offset1:66
	v_mul_f32_e32 v47, 0x42800000, v67
	v_mul_f32_e32 v49, 0x42800000, v68
	ds_write2_b32 v29, v47, v49 offset0:132 offset1:198
	v_mul_f32_e32 v47, 0x42800000, v69
	v_mul_f32_e32 v49, 0x42800000, v70
	ds_write2_b32 v38, v47, v49 offset0:8 offset1:74
	v_mul_f32_e32 v47, 0x42800000, v71
	v_mul_f32_e32 v49, 0x42800000, v72
	ds_write2_b32 v38, v47, v49 offset0:140 offset1:206
	s_add_i32 s4, s25, s7
	s_sext_i32_i16 s7, s4
	s_bfe_u32 s7, s7, 0x70018
	s_add_i32 s7, s4, s7
	s_sext_i32_i16 s8, s7
	s_and_b32 s7, s7, 0xff80
	s_sub_i32 s4, s4, s7
	s_lshl_b32 s8, s8, 1
	s_sext_i32_i16 s4, s4
	v_mul_f32_e32 v47, 0x42800000, v73
	v_mul_f32_e32 v49, 0x42800000, v74
	ds_write2_b32 v39, v47, v49 offset0:16 offset1:82
	v_mul_f32_e32 v47, 0x42800000, v75
	v_mul_f32_e32 v49, 0x42800000, v76
	ds_write2_b32 v39, v47, v49 offset0:148 offset1:214
	v_mul_f32_e32 v47, 0x42800000, v77
	v_mul_f32_e32 v49, 0x42800000, v78
	ds_write2_b32 v40, v47, v49 offset0:24 offset1:90
	v_mul_f32_e32 v47, 0x42800000, v79
	v_mul_f32_e32 v49, 0x42800000, v80
	ds_write2_b32 v40, v47, v49 offset0:156 offset1:222
	s_and_b32 s8, s8, 0xffffff00
	s_add_i32 s4, s26, s4
	s_add_i32 s4, s4, s8
	s_mov_b32 s7, s5
	v_mul_f32_e32 v47, 0x42800000, v81
	v_mul_f32_e32 v49, 0x42800000, v82
	ds_write2_b32 v41, v47, v49 offset0:32 offset1:98
	v_mul_f32_e32 v47, 0x42800000, v83
	v_mul_f32_e32 v49, 0x42800000, v84
	ds_write2_b32 v41, v47, v49 offset0:164 offset1:230
	v_mul_f32_e32 v47, 0x42800000, v85
	v_mul_f32_e32 v49, 0x42800000, v86
	ds_write2_b32 v42, v47, v49 offset0:40 offset1:106
	v_mul_f32_e32 v47, 0x42800000, v60
	v_mul_f32_e32 v49, 0x42800000, v61
	ds_write2_b32 v42, v47, v49 offset0:172 offset1:238
	v_add_u32_e32 v84, s4, v30
	v_ashrrev_i32_e32 v85, 31, v84
	v_lshlrev_b64 v[84:85], 10, v[84:85]
	v_mul_f32_e32 v47, 0x42800000, v62
	v_mul_f32_e32 v49, 0x42800000, v50
	ds_write2_b32 v43, v47, v49 offset0:48 offset1:114
	v_mul_f32_e32 v47, 0x42800000, v51
	v_mul_f32_e32 v49, 0x42800000, v52
	ds_write2_b32 v43, v47, v49 offset0:180 offset1:246
	v_mul_f32_e32 v47, 0x42800000, v53
	v_mul_f32_e32 v49, 0x42800000, v54
	ds_write2_b32 v44, v47, v49 offset0:56 offset1:122
	v_mov_b32_e32 v49, 0
	v_lshl_add_u64 v[50:51], v[20:21], 0, s[6:7]
	v_mul_f32_e32 v47, 0x42800000, v48
	v_mul_f32_e32 v46, 0x42800000, v46
	ds_write2_b32 v44, v47, v46 offset0:188 offset1:254
	s_waitcnt lgkmcnt(0)
	ds_read2_b32 v[52:53], v31 offset1:16
	ds_read2_b32 v[54:55], v31 offset0:33 offset1:49
	ds_read2_b32 v[56:57], v31 offset0:66 offset1:82
	ds_read2_b32 v[58:59], v31 offset0:99 offset1:115
	ds_read2_b32 v[60:61], v31 offset0:132 offset1:148
	ds_read2_b32 v[62:63], v31 offset0:165 offset1:181
	ds_read2_b32 v[64:65], v31 offset0:198 offset1:214
	ds_read2_b32 v[66:67], v31 offset0:231 offset1:247
	ds_read2_b32 v[68:69], v45 offset0:8 offset1:24
	ds_read2_b32 v[70:71], v45 offset0:41 offset1:57
	ds_read2_b32 v[72:73], v45 offset0:74 offset1:90
	ds_read2_b32 v[74:75], v45 offset0:107 offset1:123
	ds_read2_b32 v[76:77], v45 offset0:140 offset1:156
	ds_read2_b32 v[78:79], v45 offset0:173 offset1:189
	v_mov_b32_e32 v46, 0
	v_mov_b32_e32 v47, 0
	v_mov_b32_e32 v48, 0
	ds_read2_b32 v[80:81], v45 offset0:206 offset1:222
	ds_read2_b32 v[82:83], v45 offset0:239 offset1:255
	s_waitcnt lgkmcnt(14)
	v_cvt_pk_fp8_f32 v46, v52, v54
	s_waitcnt lgkmcnt(10)
	v_cvt_pk_fp8_f32 v47, v60, v62
	s_waitcnt lgkmcnt(6)
	v_cvt_pk_fp8_f32 v48, v68, v70
	s_waitcnt lgkmcnt(2)
	v_cvt_pk_fp8_f32 v49, v76, v78
	v_cvt_pk_fp8_f32 v46, v56, v58 op_sel:[0,0,1]
	v_cvt_pk_fp8_f32 v47, v64, v66 op_sel:[0,0,1]
	v_cvt_pk_fp8_f32 v48, v72, v74 op_sel:[0,0,1]
	s_waitcnt lgkmcnt(0)
	v_cvt_pk_fp8_f32 v49, v80, v82 op_sel:[0,0,1]
	v_lshl_add_u64 v[84:85], v[50:51], 0, v[84:85]
	v_add_u32_e32 v52, s4, v32
	global_store_dwordx4 v[84:85], v[46:49], off sc1 nt
	s_nop 1
	v_mov_b32_e32 v46, 0
	v_mov_b32_e32 v47, 0
	v_mov_b32_e32 v48, 0
	v_mov_b32_e32 v49, 0
	v_cvt_pk_fp8_f32 v46, v53, v55
	v_cvt_pk_fp8_f32 v47, v61, v63
	v_cvt_pk_fp8_f32 v48, v69, v71
	v_cvt_pk_fp8_f32 v49, v77, v79
	v_cvt_pk_fp8_f32 v46, v57, v59 op_sel:[0,0,1]
	v_cvt_pk_fp8_f32 v47, v65, v67 op_sel:[0,0,1]
	v_cvt_pk_fp8_f32 v48, v73, v75 op_sel:[0,0,1]
	v_cvt_pk_fp8_f32 v49, v81, v83 op_sel:[0,0,1]
	v_ashrrev_i32_e32 v53, 31, v52
	v_lshlrev_b64 v[52:53], 10, v[52:53]
	v_lshl_add_u64 v[50:51], v[50:51], 0, v[52:53]
	global_store_dwordx4 v[50:51], v[46:49], off sc1 nt
	s_waitcnt lgkmcnt(0)

; #define LAS __attribute__((address_space(3)))
; #define LDS_WAIT() asm volatile("s_waitcnt lgkmcnt(0)" ::: "memory")
; __device__ __forceinline__ void tr_item(const float* W, int ld, int K, int nblk, int item, bf16* WT, bool gu, LAS float* scr, int lane) {
;     const int kb = item / nblk, nb = item % nblk, k0 = 64 * kb, n0 = 32 * nb;
;     int drow0 = n0;
;     if (gu) { const int bj = n0 / FF, j = n0 - bj * FF; drow0 = 256 * (j / 128) + 128 * bj + (j % 128); }
;     { float t_[32];
; #pragma unroll
;       for (int i = 0; i < 32; ++i) t_[i] = W[(size_t)(k0 + 2 * i + (lane >> 5)) * ld + n0 + (lane & 31)];
; #pragma unroll
;       for (int i = 0; i < 32; ++i) scr[(2 * i + (lane >> 5)) * 33 + (lane & 31)] = t_[i]; }
;     LDS_WAIT(); asm volatile("" ::: "memory");
; __device__ __forceinline__ void convert_items(Frame& F, const Args& a, int lo, int hi, int w, int nw) {
;     ...
;         if (r < I_SO) { tr_item(a.in[12], D, D, 32, r, (bf16*)(F.ws + WS_WSWAOUT), false, scr, lane); continue; } r -= I_SO;
.LBB0_1174:
	s_andn2_b64 vcc, exec, s[6:7]
	s_cbranch_vccnz .LBB0_1176
	s_add_i32 s4, s11, 0x2000
	s_and_b32 s7, s4, 0x1ffc0
	s_and_b32 s6, s10, 0x3e0
	v_add_u32_e32 v46, s7, v28
	s_lshl_b32 s4, s6, 2
	v_ashrrev_i32_e32 v47, 31, v46
	v_lshl_add_u64 v[48:49], v[8:9], 0, s[4:5]
	v_lshlrev_b64 v[46:47], 12, v[46:47]
	v_lshl_add_u64 v[46:47], v[48:49], 0, v[46:47]
	v_add_co_u32_e32 v48, vcc, 0x2000, v46
	s_lshl_b32 s4, s7, 1
	s_nop 0
	v_addc_co_u32_e32 v49, vcc, 0, v47, vcc
	v_add_co_u32_e32 v50, vcc, 0x4000, v46
	s_nop 1
	v_addc_co_u32_e32 v51, vcc, 0, v47, vcc
	v_add_co_u32_e32 v52, vcc, 0x6000, v46
	s_nop 1
	v_addc_co_u32_e32 v53, vcc, 0, v47, vcc
	v_add_co_u32_e32 v54, vcc, 0x8000, v46
	s_nop 1
	v_addc_co_u32_e32 v55, vcc, 0, v47, vcc
	v_add_co_u32_e32 v56, vcc, 0xa000, v46
	s_nop 1
	v_addc_co_u32_e32 v57, vcc, 0, v47, vcc
	v_add_co_u32_e32 v58, vcc, 0xc000, v46
	s_nop 1
	v_addc_co_u32_e32 v59, vcc, 0, v47, vcc
	v_add_co_u32_e32 v60, vcc, 0xe000, v46
	s_nop 1
	v_addc_co_u32_e32 v61, vcc, 0, v47, vcc
	global_load_dword v64, v[46:47], off nt
	global_load_dword v65, v[48:49], off nt
	global_load_dword v66, v[50:51], off nt
	global_load_dword v67, v[52:53], off nt
	global_load_dword v68, v[54:55], off nt
	global_load_dword v69, v[56:57], off nt
	global_load_dword v70, v[58:59], off nt
	global_load_dword v71, v[60:61], off nt
	v_add_co_u32_e32 v48, vcc, 0x10000, v46
	s_nop 1
	v_addc_co_u32_e32 v49, vcc, 0, v47, vcc
	v_add_co_u32_e32 v50, vcc, 0x12000, v46
	s_nop 1
	v_addc_co_u32_e32 v51, vcc, 0, v47, vcc
	v_add_co_u32_e32 v52, vcc, 0x14000, v46
	s_nop 1
	v_addc_co_u32_e32 v53, vcc, 0, v47, vcc
	v_add_co_u32_e32 v54, vcc, 0x16000, v46
	s_nop 1
	v_addc_co_u32_e32 v55, vcc, 0, v47, vcc
	v_add_co_u32_e32 v56, vcc, 0x18000, v46
	s_nop 1
	v_addc_co_u32_e32 v57, vcc, 0, v47, vcc
	v_add_co_u32_e32 v58, vcc, 0x1a000, v46
	s_nop 1
	v_addc_co_u32_e32 v59, vcc, 0, v47, vcc
	v_add_co_u32_e32 v60, vcc, 0x1c000, v46
	s_nop 1
	v_addc_co_u32_e32 v61, vcc, 0, v47, vcc
	v_add_co_u32_e32 v62, vcc, 0x1e000, v46
	s_nop 1
	v_addc_co_u32_e32 v63, vcc, 0, v47, vcc
	global_load_dword v72, v[48:49], off nt
	global_load_dword v73, v[50:51], off nt
	global_load_dword v74, v[52:53], off nt
	global_load_dword v75, v[54:55], off nt
	global_load_dword v76, v[56:57], off nt
	global_load_dword v77, v[58:59], off nt
	global_load_dword v78, v[60:61], off nt
	global_load_dword v79, v[62:63], off nt
	v_add_co_u32_e32 v48, vcc, 0x20000, v46
	s_nop 1
	v_addc_co_u32_e32 v49, vcc, 0, v47, vcc
	v_add_co_u32_e32 v50, vcc, 0x22000, v46
	s_nop 1
	v_addc_co_u32_e32 v51, vcc, 0, v47, vcc
	v_add_co_u32_e32 v52, vcc, 0x24000, v46
	s_nop 1
	v_addc_co_u32_e32 v53, vcc, 0, v47, vcc
	v_add_co_u32_e32 v54, vcc, 0x26000, v46
	s_nop 1
	v_addc_co_u32_e32 v55, vcc, 0, v47, vcc
	v_add_co_u32_e32 v56, vcc, 0x28000, v46
	s_nop 1
	v_addc_co_u32_e32 v57, vcc, 0, v47, vcc
	v_add_co_u32_e32 v58, vcc, 0x2a000, v46
	s_nop 1
	v_addc_co_u32_e32 v59, vcc, 0, v47, vcc
	v_add_co_u32_e32 v60, vcc, 0x2c000, v46
	s_nop 1
	v_addc_co_u32_e32 v61, vcc, 0, v47, vcc
	v_add_co_u32_e32 v62, vcc, 0x2e000, v46
	s_nop 1
	v_addc_co_u32_e32 v63, vcc, 0, v47, vcc
	global_load_dword v80, v[48:49], off nt
	global_load_dword v81, v[50:51], off nt
	global_load_dword v82, v[52:53], off nt
	global_load_dword v83, v[54:55], off nt
	global_load_dword v84, v[56:57], off nt
	global_load_dword v85, v[58:59], off nt
	global_load_dword v86, v[60:61], off nt
	s_nop 0
	global_load_dword v62, v[62:63], off nt
	v_add_co_u32_e32 v48, vcc, 0x30000, v46
	s_nop 1
	v_addc_co_u32_e32 v49, vcc, 0, v47, vcc
	v_add_co_u32_e32 v50, vcc, 0x32000, v46
	s_nop 1
	v_addc_co_u32_e32 v51, vcc, 0, v47, vcc
	v_add_co_u32_e32 v52, vcc, 0x34000, v46
	s_nop 1
	v_addc_co_u32_e32 v53, vcc, 0, v47, vcc
	v_add_co_u32_e32 v54, vcc, 0x36000, v46
	s_nop 1
	v_addc_co_u32_e32 v55, vcc, 0, v47, vcc
	v_add_co_u32_e32 v56, vcc, 0x38000, v46
	s_nop 1
	v_addc_co_u32_e32 v57, vcc, 0, v47, vcc
	v_add_co_u32_e32 v58, vcc, 0x3a000, v46
	s_nop 1
	v_addc_co_u32_e32 v59, vcc, 0, v47, vcc
	v_add_co_u32_e32 v60, vcc, 0x3c000, v46
	s_nop 1
	v_addc_co_u32_e32 v61, vcc, 0, v47, vcc
	v_add_co_u32_e32 v46, vcc, 0x3e000, v46
	s_nop 1
	v_addc_co_u32_e32 v47, vcc, 0, v47, vcc
	global_load_dword v48, v[48:49], off nt
	s_nop 0
	global_load_dword v49, v[50:51], off nt
	s_nop 0
	global_load_dword v50, v[52:53], off nt
	global_load_dword v51, v[54:55], off nt
	s_nop 0
	global_load_dword v52, v[56:57], off nt
	global_load_dword v53, v[58:59], off nt
	global_load_dword v54, v[60:61], off nt
	s_nop 0
	global_load_dword v46, v[46:47], off nt
	s_waitcnt vmcnt(0)
	ds_write2_b32 v29, v64, v65 offset1:66
	ds_write2_b32 v29, v66, v67 offset0:132 offset1:198
	ds_write2_b32 v38, v68, v69 offset0:8 offset1:74
	ds_write2_b32 v38, v70, v71 offset0:140 offset1:206
	ds_write2_b32 v39, v72, v73 offset0:16 offset1:82
	ds_write2_b32 v39, v74, v75 offset0:148 offset1:214
	ds_write2_b32 v40, v76, v77 offset0:24 offset1:90
	ds_write2_b32 v40, v78, v79 offset0:156 offset1:222
	ds_write2_b32 v41, v80, v81 offset0:32 offset1:98
	ds_write2_b32 v41, v82, v83 offset0:164 offset1:230
	ds_write2_b32 v42, v84, v85 offset0:40 offset1:106
	ds_write2_b32 v42, v86, v62 offset0:172 offset1:238
	ds_write2_b32 v43, v48, v49 offset0:48 offset1:114
	ds_write2_b32 v43, v50, v51 offset0:180 offset1:246
	ds_write2_b32 v44, v52, v53 offset0:56 offset1:122
	ds_write2_b32 v44, v54, v46 offset0:188 offset1:254
	s_waitcnt lgkmcnt(0)
; #define GAS __attribute__((address_space(1)))
; #define LAS __attribute__((address_space(3)))
; #define LDS_WAIT() asm volatile("s_waitcnt lgkmcnt(0)" ::: "memory")
; __device__ __forceinline__ unsigned pk2(float lo, float hi) { return f2bf(lo) | (f2bf(hi) << 16); }
; __device__ __forceinline__ void tr_item(const float* W, int ld, int K, int nblk, int item, bf16* WT, bool gu, LAS float* scr, int lane) {
;     ...
;     const int c = lane & 7;
; #pragma unroll
;     for (int j = 0; j < 4; ++j) { const int n = (lane >> 3) + 8 * j; const LAS float* s = scr + (8 * c) * 33 + n;
;         v4u o; o.x = pk2(s[0 * 33], s[1 * 33]); o.y = pk2(s[2 * 33], s[3 * 33]); o.z = pk2(s[4 * 33], s[5 * 33]); o.w = pk2(s[6 * 33], s[7 * 33]);
;         *(GAS v4u*)(WT + (size_t)(drow0 + n) * K + k0 + 8 * c) = o; }
;     LDS_WAIT(); asm volatile("" ::: "memory");
	ds_read2_b32 v[50:51], v34 offset1:8
	ds_read2_b32 v[54:55], v34 offset0:33 offset1:41
	ds_read2_b32 v[56:57], v34 offset0:66 offset1:74
	ds_read2_b32 v[58:59], v34 offset0:99 offset1:107
	ds_read2_b32 v[60:61], v34 offset0:132 offset1:140
	s_waitcnt lgkmcnt(4)
	v_bfe_u32 v46, v50, 16, 1
	v_add3_u32 v46, v50, v46, s14
	s_waitcnt lgkmcnt(3)
	v_bfe_u32 v47, v54, 16, 1
	v_lshrrev_b32_e32 v46, 16, v46
	v_add3_u32 v47, v54, v47, s14
	ds_read2_b32 v[62:63], v34 offset0:165 offset1:173
	v_and_or_b32 v46, v47, s15, v46
	s_waitcnt lgkmcnt(3)
	v_bfe_u32 v47, v56, 16, 1
	v_add3_u32 v47, v56, v47, s14
	s_waitcnt lgkmcnt(2)
	v_bfe_u32 v48, v58, 16, 1
	ds_read2_b32 v[64:65], v34 offset0:198 offset1:206
	v_lshrrev_b32_e32 v47, 16, v47
	v_add3_u32 v48, v58, v48, s14
	ds_read2_b32 v[66:67], v34 offset0:231 offset1:239
	v_and_or_b32 v47, v48, s15, v47
	s_waitcnt lgkmcnt(3)
	v_bfe_u32 v48, v60, 16, 1
	v_add3_u32 v48, v60, v48, s14
	s_waitcnt lgkmcnt(2)
	v_bfe_u32 v49, v62, 16, 1
	v_lshrrev_b32_e32 v48, 16, v48
	v_add3_u32 v49, v62, v49, s14
	v_and_or_b32 v48, v49, s15, v48
	s_waitcnt lgkmcnt(1)
	v_bfe_u32 v49, v64, 16, 1
	v_add_u32_e32 v68, s6, v33
	v_add3_u32 v49, v64, v49, s14
	s_waitcnt lgkmcnt(0)
	v_bfe_u32 v50, v66, 16, 1
	v_ashrrev_i32_e32 v69, 31, v68
	v_lshl_add_u64 v[52:53], v[22:23], 0, s[4:5]
	v_lshrrev_b32_e32 v49, 16, v49
	v_add3_u32 v50, v66, v50, s14
	v_lshlrev_b64 v[68:69], 11, v[68:69]
	v_and_or_b32 v49, v50, s15, v49
	v_lshl_add_u64 v[68:69], v[52:53], 0, v[68:69]
	global_store_dwordx4 v[68:69], v[46:49], off sc1 nt
	v_bfe_u32 v50, v67, 16, 1
	v_add3_u32 v50, v67, v50, s14
	v_bfe_u32 v46, v51, 16, 1
	v_add3_u32 v46, v51, v46, s14
	v_bfe_u32 v47, v55, 16, 1
	v_lshrrev_b32_e32 v46, 16, v46
	v_add3_u32 v47, v55, v47, s14
	v_and_or_b32 v46, v47, s15, v46
	v_bfe_u32 v47, v57, 16, 1
	v_add3_u32 v47, v57, v47, s14
	v_bfe_u32 v48, v59, 16, 1
	v_lshrrev_b32_e32 v47, 16, v47
	v_add3_u32 v48, v59, v48, s14
	v_and_or_b32 v47, v48, s15, v47
	v_bfe_u32 v48, v61, 16, 1
	v_add3_u32 v48, v61, v48, s14
	v_bfe_u32 v49, v63, 16, 1
	v_lshrrev_b32_e32 v48, 16, v48
	v_add3_u32 v49, v63, v49, s14
	v_and_or_b32 v48, v49, s15, v48
	v_bfe_u32 v49, v65, 16, 1
	v_add3_u32 v49, v65, v49, s14
	v_lshrrev_b32_e32 v49, 16, v49
	v_and_or_b32 v49, v50, s15, v49
	v_add_u32_e32 v50, s6, v35
	v_ashrrev_i32_e32 v51, 31, v50
	v_lshlrev_b64 v[50:51], 11, v[50:51]
	ds_read2_b32 v[54:55], v34 offset0:16 offset1:24
	v_lshl_add_u64 v[50:51], v[52:53], 0, v[50:51]
	global_store_dwordx4 v[50:51], v[46:49], off sc1 nt
	ds_read2_b32 v[50:51], v34 offset0:49 offset1:57
	ds_read2_b32 v[56:57], v34 offset0:82 offset1:90
	ds_read2_b32 v[58:59], v34 offset0:115 offset1:123
	s_waitcnt lgkmcnt(3)
	v_bfe_u32 v46, v54, 16, 1
	v_add3_u32 v46, v54, v46, s14
	s_waitcnt lgkmcnt(2)
	v_bfe_u32 v47, v50, 16, 1
	ds_read2_b32 v[60:61], v34 offset0:148 offset1:156
	v_lshrrev_b32_e32 v46, 16, v46
	v_add3_u32 v47, v50, v47, s14
	ds_read2_b32 v[62:63], v34 offset0:181 offset1:189
	v_and_or_b32 v46, v47, s15, v46
	s_waitcnt lgkmcnt(3)
	v_bfe_u32 v47, v56, 16, 1
	v_add3_u32 v47, v56, v47, s14
	s_waitcnt lgkmcnt(2)
	v_bfe_u32 v48, v58, 16, 1
	ds_read2_b32 v[64:65], v34 offset0:214 offset1:222
	v_lshrrev_b32_e32 v47, 16, v47
	v_add3_u32 v48, v58, v48, s14
	ds_read2_b32 v[66:67], v34 offset0:247 offset1:255
	v_and_or_b32 v47, v48, s15, v47
	s_waitcnt lgkmcnt(3)
	v_bfe_u32 v48, v60, 16, 1
	v_add3_u32 v48, v60, v48, s14
	s_waitcnt lgkmcnt(2)
	v_bfe_u32 v49, v62, 16, 1
	v_lshrrev_b32_e32 v48, 16, v48
	v_add3_u32 v49, v62, v49, s14
	v_and_or_b32 v48, v49, s15, v48
	s_waitcnt lgkmcnt(1)
	v_bfe_u32 v49, v64, 16, 1
	v_add_u32_e32 v68, s6, v36
	v_add3_u32 v49, v64, v49, s14
	s_waitcnt lgkmcnt(0)
	v_bfe_u32 v50, v66, 16, 1
	v_ashrrev_i32_e32 v69, 31, v68
	v_lshrrev_b32_e32 v49, 16, v49
	v_add3_u32 v50, v66, v50, s14
	v_lshlrev_b64 v[68:69], 11, v[68:69]
	v_and_or_b32 v49, v50, s15, v49
	v_lshl_add_u64 v[68:69], v[52:53], 0, v[68:69]
	global_store_dwordx4 v[68:69], v[46:49], off sc1 nt
	v_bfe_u32 v50, v67, 16, 1
	v_add3_u32 v50, v67, v50, s14
	v_bfe_u32 v46, v55, 16, 1
	v_add3_u32 v46, v55, v46, s14
	v_bfe_u32 v47, v51, 16, 1
	v_lshrrev_b32_e32 v46, 16, v46
	v_add3_u32 v47, v51, v47, s14
	v_and_or_b32 v46, v47, s15, v46
	v_bfe_u32 v47, v57, 16, 1
	v_add3_u32 v47, v57, v47, s14
	v_bfe_u32 v48, v59, 16, 1
	v_lshrrev_b32_e32 v47, 16, v47
	v_add3_u32 v48, v59, v48, s14
	v_and_or_b32 v47, v48, s15, v47
	v_bfe_u32 v48, v61, 16, 1
	v_add3_u32 v48, v61, v48, s14
	v_bfe_u32 v49, v63, 16, 1
	v_lshrrev_b32_e32 v48, 16, v48
	v_add3_u32 v49, v63, v49, s14
	v_and_or_b32 v48, v49, s15, v48
	v_bfe_u32 v49, v65, 16, 1
	v_add3_u32 v49, v65, v49, s14
	v_lshrrev_b32_e32 v49, 16, v49
	v_and_or_b32 v49, v50, s15, v49
	v_add_u32_e32 v50, s6, v37
	v_ashrrev_i32_e32 v51, 31, v50
	v_lshlrev_b64 v[50:51], 11, v[50:51]
	v_lshl_add_u64 v[50:51], v[52:53], 0, v[50:51]
	global_store_dwordx4 v[50:51], v[46:49], off sc1 nt
	s_waitcnt lgkmcnt(0)

; #define LAS __attribute__((address_space(3)))
; #define LDS_WAIT() asm volatile("s_waitcnt lgkmcnt(0)" ::: "memory")
; __device__ __forceinline__ void tr_item(const float* W, int ld, int K, int nblk, int item, bf16* WT, bool gu, LAS float* scr, int lane) {
;     const int kb = item / nblk, nb = item % nblk, k0 = 64 * kb, n0 = 32 * nb;
;     int drow0 = n0;
;     if (gu) { const int bj = n0 / FF, j = n0 - bj * FF; drow0 = 256 * (j / 128) + 128 * bj + (j % 128); }
;     { float t_[32];
; #pragma unroll
;       for (int i = 0; i < 32; ++i) t_[i] = W[(size_t)(k0 + 2 * i + (lane >> 5)) * ld + n0 + (lane & 31)];
; #pragma unroll
;       for (int i = 0; i < 32; ++i) scr[(2 * i + (lane >> 5)) * 33 + (lane & 31)] = t_[i]; }
;     LDS_WAIT(); asm volatile("" ::: "memory");
; __device__ __forceinline__ void convert_items(Frame& F, const Args& a, int lo, int hi, int w, int nw) {
;     ...
;         if (r < I_SI) { tr_item(a.in[10], D + 512, D, 48, r, (bf16*)(F.ws + WS_WSWAIN), false, scr, lane); continue; } r -= I_SI;
.LBB0_1177:
	s_andn2_b64 vcc, exec, s[6:7]
	s_cbranch_vccnz .LBB0_1179
	s_add_i32 s4, s16, 0xf800
	s_and_b32 s6, s4, 0xffff
	s_mul_i32 s6, s6, 0xaaab
	s_lshr_b32 s7, s6, 21
	s_mul_i32 s6, s7, 48
	s_sub_i32 s4, s4, s6
	s_lshl_b32 s4, s4, 5
	s_and_b32 s6, s4, 0xffe0
	v_lshl_add_u32 v64, s7, 6, v28
	s_lshl_b32 s4, s6, 2
	v_lshl_add_u64 v[46:47], v[10:11], 0, s[4:5]
	v_add_u32_e32 v50, 2, v64
	v_add_u32_e32 v52, 4, v64
	v_add_u32_e32 v54, 6, v64
	v_add_u32_e32 v56, 8, v64
	v_add_u32_e32 v58, 10, v64
	v_add_u32_e32 v60, 12, v64
	v_add_u32_e32 v62, 14, v64
	v_mad_i64_i32 v[48:49], s[8:9], v64, s17, v[46:47]
	v_mad_i64_i32 v[50:51], s[8:9], v50, s17, v[46:47]
	v_mad_i64_i32 v[52:53], s[8:9], v52, s17, v[46:47]
	v_mad_i64_i32 v[54:55], s[8:9], v54, s17, v[46:47]
	v_mad_i64_i32 v[56:57], s[8:9], v56, s17, v[46:47]
	v_mad_i64_i32 v[58:59], s[8:9], v58, s17, v[46:47]
	v_mad_i64_i32 v[60:61], s[8:9], v60, s17, v[46:47]
	v_mad_i64_i32 v[62:63], s[8:9], v62, s17, v[46:47]
	global_load_dword v65, v[48:49], off nt
	global_load_dword v66, v[50:51], off nt
	global_load_dword v67, v[52:53], off nt
	global_load_dword v68, v[54:55], off nt
	global_load_dword v69, v[56:57], off nt
	global_load_dword v70, v[58:59], off nt
	global_load_dword v71, v[60:61], off nt
	global_load_dword v72, v[62:63], off nt
	v_add_u32_e32 v48, 16, v64
	v_add_u32_e32 v50, 18, v64
	v_add_u32_e32 v52, 20, v64
	v_add_u32_e32 v54, 22, v64
	v_add_u32_e32 v56, 24, v64
	v_add_u32_e32 v58, 26, v64
	v_add_u32_e32 v60, 28, v64
	v_add_u32_e32 v62, 30, v64
	v_mad_i64_i32 v[48:49], s[8:9], v48, s17, v[46:47]
	v_mad_i64_i32 v[50:51], s[8:9], v50, s17, v[46:47]
	v_mad_i64_i32 v[52:53], s[8:9], v52, s17, v[46:47]
	v_mad_i64_i32 v[54:55], s[8:9], v54, s17, v[46:47]
	v_mad_i64_i32 v[56:57], s[8:9], v56, s17, v[46:47]
	v_mad_i64_i32 v[58:59], s[8:9], v58, s17, v[46:47]
	v_mad_i64_i32 v[60:61], s[8:9], v60, s17, v[46:47]
	v_mad_i64_i32 v[62:63], s[8:9], v62, s17, v[46:47]
	global_load_dword v73, v[48:49], off nt
	global_load_dword v74, v[50:51], off nt
	global_load_dword v75, v[52:53], off nt
	global_load_dword v76, v[54:55], off nt
	global_load_dword v77, v[56:57], off nt
	global_load_dword v78, v[58:59], off nt
	global_load_dword v79, v[60:61], off nt
	global_load_dword v80, v[62:63], off nt
	v_add_u32_e32 v48, 32, v64
	v_add_u32_e32 v50, 34, v64
	v_add_u32_e32 v52, 36, v64
	v_add_u32_e32 v54, 38, v64
	v_add_u32_e32 v56, 40, v64
	v_add_u32_e32 v58, 42, v64
	v_add_u32_e32 v60, 44, v64
	v_add_u32_e32 v62, 46, v64
	v_mad_i64_i32 v[48:49], s[8:9], v48, s17, v[46:47]
	v_mad_i64_i32 v[50:51], s[8:9], v50, s17, v[46:47]
	v_mad_i64_i32 v[52:53], s[8:9], v52, s17, v[46:47]
	v_mad_i64_i32 v[54:55], s[8:9], v54, s17, v[46:47]
	v_mad_i64_i32 v[56:57], s[8:9], v56, s17, v[46:47]
	v_mad_i64_i32 v[58:59], s[8:9], v58, s17, v[46:47]
	v_mad_i64_i32 v[60:61], s[8:9], v60, s17, v[46:47]
	v_mad_i64_i32 v[62:63], s[8:9], v62, s17, v[46:47]
	global_load_dword v81, v[48:49], off nt
	global_load_dword v82, v[50:51], off nt
	global_load_dword v83, v[52:53], off nt
	global_load_dword v84, v[54:55], off nt
	global_load_dword v85, v[56:57], off nt
	global_load_dword v86, v[58:59], off nt
	global_load_dword v87, v[60:61], off nt
	s_nop 0
	global_load_dword v62, v[62:63], off nt
	v_add_u32_e32 v48, 48, v64
	v_add_u32_e32 v50, 50, v64
	v_add_u32_e32 v52, 52, v64
	v_add_u32_e32 v54, 54, v64
	v_add_u32_e32 v56, 56, v64
	v_add_u32_e32 v58, 58, v64
	v_add_u32_e32 v60, 60, v64
	v_add_u32_e32 v63, 62, v64
	v_mad_i64_i32 v[48:49], s[8:9], v48, s17, v[46:47]
	v_mad_i64_i32 v[50:51], s[8:9], v50, s17, v[46:47]
	v_mad_i64_i32 v[52:53], s[8:9], v52, s17, v[46:47]
	v_mad_i64_i32 v[54:55], s[8:9], v54, s17, v[46:47]
	v_mad_i64_i32 v[56:57], s[8:9], v56, s17, v[46:47]
	v_mad_i64_i32 v[58:59], s[8:9], v58, s17, v[46:47]
	v_mad_i64_i32 v[60:61], s[8:9], v60, s17, v[46:47]
	v_mad_i64_i32 v[46:47], s[8:9], v63, s17, v[46:47]
	global_load_dword v48, v[48:49], off nt
	s_nop 0
	global_load_dword v49, v[50:51], off nt
	s_nop 0
	global_load_dword v50, v[52:53], off nt
	global_load_dword v51, v[54:55], off nt
	s_nop 0
	global_load_dword v52, v[56:57], off nt
	global_load_dword v53, v[58:59], off nt
	global_load_dword v54, v[60:61], off nt
	s_nop 0
	global_load_dword v46, v[46:47], off nt
	s_waitcnt vmcnt(0)
	ds_write2_b32 v29, v65, v66 offset1:66
	ds_write2_b32 v29, v67, v68 offset0:132 offset1:198
	ds_write2_b32 v38, v69, v70 offset0:8 offset1:74
	ds_write2_b32 v38, v71, v72 offset0:140 offset1:206
	ds_write2_b32 v39, v73, v74 offset0:16 offset1:82
	ds_write2_b32 v39, v75, v76 offset0:148 offset1:214
	ds_write2_b32 v40, v77, v78 offset0:24 offset1:90
	ds_write2_b32 v40, v79, v80 offset0:156 offset1:222
	ds_write2_b32 v41, v81, v82 offset0:32 offset1:98
	ds_write2_b32 v41, v83, v84 offset0:164 offset1:230
	ds_write2_b32 v42, v85, v86 offset0:40 offset1:106
	ds_write2_b32 v42, v87, v62 offset0:172 offset1:238
	ds_write2_b32 v43, v48, v49 offset0:48 offset1:114
	ds_write2_b32 v43, v50, v51 offset0:180 offset1:246
	ds_write2_b32 v44, v52, v53 offset0:56 offset1:122
	ds_write2_b32 v44, v54, v46 offset0:188 offset1:254
	s_waitcnt lgkmcnt(0)
; #define GAS __attribute__((address_space(1)))
; #define LAS __attribute__((address_space(3)))
; #define LDS_WAIT() asm volatile("s_waitcnt lgkmcnt(0)" ::: "memory")
; __device__ __forceinline__ unsigned pk2(float lo, float hi) { return f2bf(lo) | (f2bf(hi) << 16); }
; __device__ __forceinline__ void tr_item(const float* W, int ld, int K, int nblk, int item, bf16* WT, bool gu, LAS float* scr, int lane) {
;     ...
;     const int c = lane & 7;
; #pragma unroll
;     for (int j = 0; j < 4; ++j) { const int n = (lane >> 3) + 8 * j; const LAS float* s = scr + (8 * c) * 33 + n;
;         v4u o; o.x = pk2(s[0 * 33], s[1 * 33]); o.y = pk2(s[2 * 33], s[3 * 33]); o.z = pk2(s[4 * 33], s[5 * 33]); o.w = pk2(s[6 * 33], s[7 * 33]);
;         *(GAS v4u*)(WT + (size_t)(drow0 + n) * K + k0 + 8 * c) = o; }
;     LDS_WAIT(); asm volatile("" ::: "memory");
	ds_read2_b32 v[50:51], v34 offset1:8
	ds_read2_b32 v[54:55], v34 offset0:33 offset1:41
	ds_read2_b32 v[56:57], v34 offset0:66 offset1:74
	ds_read2_b32 v[58:59], v34 offset0:99 offset1:107
	ds_read2_b32 v[60:61], v34 offset0:132 offset1:140
	s_waitcnt lgkmcnt(4)
	v_bfe_u32 v46, v50, 16, 1
	v_add3_u32 v46, v50, v46, s14
	s_waitcnt lgkmcnt(3)
	v_bfe_u32 v47, v54, 16, 1
	v_lshrrev_b32_e32 v46, 16, v46
	v_add3_u32 v47, v54, v47, s14
	ds_read2_b32 v[62:63], v34 offset0:165 offset1:173
	v_and_or_b32 v46, v47, s15, v46
	s_waitcnt lgkmcnt(3)
	v_bfe_u32 v47, v56, 16, 1
	v_add3_u32 v47, v56, v47, s14
	s_waitcnt lgkmcnt(2)
	v_bfe_u32 v48, v58, 16, 1
	ds_read2_b32 v[64:65], v34 offset0:198 offset1:206
	v_lshrrev_b32_e32 v47, 16, v47
	v_add3_u32 v48, v58, v48, s14
	ds_read2_b32 v[66:67], v34 offset0:231 offset1:239
	v_and_or_b32 v47, v48, s15, v47
	s_waitcnt lgkmcnt(3)
	v_bfe_u32 v48, v60, 16, 1
	v_add3_u32 v48, v60, v48, s14
	s_waitcnt lgkmcnt(2)
	v_bfe_u32 v49, v62, 16, 1
	v_lshrrev_b32_e32 v48, 16, v48
	v_add3_u32 v49, v62, v49, s14
	v_and_or_b32 v48, v49, s15, v48
	s_waitcnt lgkmcnt(1)
	v_bfe_u32 v49, v64, 16, 1
	v_add_u32_e32 v68, s6, v33
	s_lshl_b32 s4, s7, 7
	v_add3_u32 v49, v64, v49, s14
	s_waitcnt lgkmcnt(0)
	v_bfe_u32 v50, v66, 16, 1
	v_ashrrev_i32_e32 v69, 31, v68
	v_lshl_add_u64 v[52:53], v[12:13], 0, s[4:5]
	v_lshrrev_b32_e32 v49, 16, v49
	v_add3_u32 v50, v66, v50, s14
	v_lshlrev_b64 v[68:69], 11, v[68:69]
	v_and_or_b32 v49, v50, s15, v49
	v_lshl_add_u64 v[68:69], v[52:53], 0, v[68:69]
	global_store_dwordx4 v[68:69], v[46:49], off sc1 nt
	v_bfe_u32 v50, v67, 16, 1
	v_add3_u32 v50, v67, v50, s14
	v_bfe_u32 v46, v51, 16, 1
	v_add3_u32 v46, v51, v46, s14
	v_bfe_u32 v47, v55, 16, 1
	v_lshrrev_b32_e32 v46, 16, v46
	v_add3_u32 v47, v55, v47, s14
	v_and_or_b32 v46, v47, s15, v46
	v_bfe_u32 v47, v57, 16, 1
	v_add3_u32 v47, v57, v47, s14
	v_bfe_u32 v48, v59, 16, 1
	v_lshrrev_b32_e32 v47, 16, v47
	v_add3_u32 v48, v59, v48, s14
	v_and_or_b32 v47, v48, s15, v47
	v_bfe_u32 v48, v61, 16, 1
	v_add3_u32 v48, v61, v48, s14
	v_bfe_u32 v49, v63, 16, 1
	v_lshrrev_b32_e32 v48, 16, v48
	v_add3_u32 v49, v63, v49, s14
	v_and_or_b32 v48, v49, s15, v48
	v_bfe_u32 v49, v65, 16, 1
	v_add3_u32 v49, v65, v49, s14
	v_lshrrev_b32_e32 v49, 16, v49
	v_and_or_b32 v49, v50, s15, v49
	v_add_u32_e32 v50, s6, v35
	v_ashrrev_i32_e32 v51, 31, v50
	v_lshlrev_b64 v[50:51], 11, v[50:51]
	ds_read2_b32 v[54:55], v34 offset0:16 offset1:24
	v_lshl_add_u64 v[50:51], v[52:53], 0, v[50:51]
	global_store_dwordx4 v[50:51], v[46:49], off sc1 nt
	ds_read2_b32 v[50:51], v34 offset0:49 offset1:57
	ds_read2_b32 v[56:57], v34 offset0:82 offset1:90
	ds_read2_b32 v[58:59], v34 offset0:115 offset1:123
	s_waitcnt lgkmcnt(3)
	v_bfe_u32 v46, v54, 16, 1
	v_add3_u32 v46, v54, v46, s14
	s_waitcnt lgkmcnt(2)
	v_bfe_u32 v47, v50, 16, 1
	ds_read2_b32 v[60:61], v34 offset0:148 offset1:156
	v_lshrrev_b32_e32 v46, 16, v46
	v_add3_u32 v47, v50, v47, s14
	ds_read2_b32 v[62:63], v34 offset0:181 offset1:189
	v_and_or_b32 v46, v47, s15, v46
	s_waitcnt lgkmcnt(3)
	v_bfe_u32 v47, v56, 16, 1
	v_add3_u32 v47, v56, v47, s14
	s_waitcnt lgkmcnt(2)
	v_bfe_u32 v48, v58, 16, 1
	ds_read2_b32 v[64:65], v34 offset0:214 offset1:222
	v_lshrrev_b32_e32 v47, 16, v47
	v_add3_u32 v48, v58, v48, s14
	ds_read2_b32 v[66:67], v34 offset0:247 offset1:255
	v_and_or_b32 v47, v48, s15, v47
	s_waitcnt lgkmcnt(3)
	v_bfe_u32 v48, v60, 16, 1
	v_add3_u32 v48, v60, v48, s14
	s_waitcnt lgkmcnt(2)
	v_bfe_u32 v49, v62, 16, 1
	v_lshrrev_b32_e32 v48, 16, v48
	v_add3_u32 v49, v62, v49, s14
	v_and_or_b32 v48, v49, s15, v48
	s_waitcnt lgkmcnt(1)
	v_bfe_u32 v49, v64, 16, 1
	v_add_u32_e32 v68, s6, v36
	v_add3_u32 v49, v64, v49, s14
	s_waitcnt lgkmcnt(0)
	v_bfe_u32 v50, v66, 16, 1
	v_ashrrev_i32_e32 v69, 31, v68
	v_lshrrev_b32_e32 v49, 16, v49
	v_add3_u32 v50, v66, v50, s14
	v_lshlrev_b64 v[68:69], 11, v[68:69]
	v_and_or_b32 v49, v50, s15, v49
	v_lshl_add_u64 v[68:69], v[52:53], 0, v[68:69]
	global_store_dwordx4 v[68:69], v[46:49], off sc1 nt
	v_bfe_u32 v50, v67, 16, 1
	v_add3_u32 v50, v67, v50, s14
	v_bfe_u32 v46, v55, 16, 1
	v_add3_u32 v46, v55, v46, s14
	v_bfe_u32 v47, v51, 16, 1
	v_lshrrev_b32_e32 v46, 16, v46
	v_add3_u32 v47, v51, v47, s14
	v_and_or_b32 v46, v47, s15, v46
	v_bfe_u32 v47, v57, 16, 1
	v_add3_u32 v47, v57, v47, s14
	v_bfe_u32 v48, v59, 16, 1
	v_lshrrev_b32_e32 v47, 16, v47
	v_add3_u32 v48, v59, v48, s14
	v_and_or_b32 v47, v48, s15, v47
	v_bfe_u32 v48, v61, 16, 1
	v_add3_u32 v48, v61, v48, s14
	v_bfe_u32 v49, v63, 16, 1
	v_lshrrev_b32_e32 v48, 16, v48
	v_add3_u32 v49, v63, v49, s14
	v_and_or_b32 v48, v49, s15, v48
	v_bfe_u32 v49, v65, 16, 1
	v_add3_u32 v49, v65, v49, s14
	v_lshrrev_b32_e32 v49, 16, v49
	v_and_or_b32 v49, v50, s15, v49
	v_add_u32_e32 v50, s6, v37
	v_ashrrev_i32_e32 v51, 31, v50
	v_lshlrev_b64 v[50:51], 11, v[50:51]
	v_lshl_add_u64 v[50:51], v[52:53], 0, v[50:51]
	global_store_dwordx4 v[50:51], v[46:49], off sc1 nt
	s_waitcnt lgkmcnt(0)

; #define LDS_WAIT() asm volatile("s_waitcnt lgkmcnt(0)" ::: "memory")
; __device__ __forceinline__ void tr_item(const float* W, int ld, int K, int nblk, int item, bf16* WT, bool gu, LAS float* scr, int lane) {
;     const int kb = item / nblk, nb = item % nblk, k0 = 64 * kb, n0 = 32 * nb;
;     int drow0 = n0;
;     if (gu) { const int bj = n0 / FF, j = n0 - bj * FF; drow0 = 256 * (j / 128) + 128 * bj + (j % 128); }
;     { float t_[32];
; #pragma unroll
;       for (int i = 0; i < 32; ++i) t_[i] = W[(size_t)(k0 + 2 * i + (lane >> 5)) * ld + n0 + (lane & 31)];
; #pragma unroll
;       for (int i = 0; i < 32; ++i) scr[(2 * i + (lane >> 5)) * 33 + (lane & 31)] = t_[i]; }
;     LDS_WAIT(); asm volatile("" ::: "memory");
; __device__ __forceinline__ void convert_items(Frame& F, const Args& a, int lo, int hi, int w, int nw) {
;     ...
;         if (r < I_FO) { tr_item(a.in[9], D, D, 32, r, (bf16*)(F.ws + WS_WFOXOUT), false, scr, lane); continue; } r -= I_FO;
.LBB0_1180:
	s_andn2_b64 vcc, exec, s[6:7]
	s_cbranch_vccnz .LBB0_1182
	s_add_i32 s4, s11, 0x2a00
	s_and_b32 s7, s4, 0x1ffc0
	s_and_b32 s6, s10, 0x3e0
	v_add_u32_e32 v46, s7, v28
	s_lshl_b32 s4, s6, 2
	v_ashrrev_i32_e32 v47, 31, v46
	v_lshl_add_u64 v[48:49], v[14:15], 0, s[4:5]
	v_lshlrev_b64 v[46:47], 12, v[46:47]
	v_lshl_add_u64 v[46:47], v[48:49], 0, v[46:47]
	v_add_co_u32_e32 v48, vcc, 0x2000, v46
	s_lshl_b32 s4, s7, 1
	s_nop 0
	v_addc_co_u32_e32 v49, vcc, 0, v47, vcc
	v_add_co_u32_e32 v50, vcc, 0x4000, v46
	s_nop 1
	v_addc_co_u32_e32 v51, vcc, 0, v47, vcc
	v_add_co_u32_e32 v52, vcc, 0x6000, v46
	s_nop 1
	v_addc_co_u32_e32 v53, vcc, 0, v47, vcc
	v_add_co_u32_e32 v54, vcc, 0x8000, v46
	s_nop 1
	v_addc_co_u32_e32 v55, vcc, 0, v47, vcc
	v_add_co_u32_e32 v56, vcc, 0xa000, v46
	s_nop 1
	v_addc_co_u32_e32 v57, vcc, 0, v47, vcc
	v_add_co_u32_e32 v58, vcc, 0xc000, v46
	s_nop 1
	v_addc_co_u32_e32 v59, vcc, 0, v47, vcc
	v_add_co_u32_e32 v60, vcc, 0xe000, v46
	s_nop 1
	v_addc_co_u32_e32 v61, vcc, 0, v47, vcc
	global_load_dword v64, v[46:47], off nt
	global_load_dword v65, v[48:49], off nt
	global_load_dword v66, v[50:51], off nt
	global_load_dword v67, v[52:53], off nt
	global_load_dword v68, v[54:55], off nt
	global_load_dword v69, v[56:57], off nt
	global_load_dword v70, v[58:59], off nt
	global_load_dword v71, v[60:61], off nt
	v_add_co_u32_e32 v48, vcc, 0x10000, v46
	s_nop 1
	v_addc_co_u32_e32 v49, vcc, 0, v47, vcc
	v_add_co_u32_e32 v50, vcc, 0x12000, v46
	s_nop 1
	v_addc_co_u32_e32 v51, vcc, 0, v47, vcc
	v_add_co_u32_e32 v52, vcc, 0x14000, v46
	s_nop 1
	v_addc_co_u32_e32 v53, vcc, 0, v47, vcc
	v_add_co_u32_e32 v54, vcc, 0x16000, v46
	s_nop 1
	v_addc_co_u32_e32 v55, vcc, 0, v47, vcc
	v_add_co_u32_e32 v56, vcc, 0x18000, v46
	s_nop 1
	v_addc_co_u32_e32 v57, vcc, 0, v47, vcc
	v_add_co_u32_e32 v58, vcc, 0x1a000, v46
	s_nop 1
	v_addc_co_u32_e32 v59, vcc, 0, v47, vcc
	v_add_co_u32_e32 v60, vcc, 0x1c000, v46
	s_nop 1
	v_addc_co_u32_e32 v61, vcc, 0, v47, vcc
	v_add_co_u32_e32 v62, vcc, 0x1e000, v46
	s_nop 1
	v_addc_co_u32_e32 v63, vcc, 0, v47, vcc
	global_load_dword v72, v[48:49], off nt
	global_load_dword v73, v[50:51], off nt
	global_load_dword v74, v[52:53], off nt
	global_load_dword v75, v[54:55], off nt
	global_load_dword v76, v[56:57], off nt
	global_load_dword v77, v[58:59], off nt
	global_load_dword v78, v[60:61], off nt
	global_load_dword v79, v[62:63], off nt
	v_add_co_u32_e32 v48, vcc, 0x20000, v46
	s_nop 1
	v_addc_co_u32_e32 v49, vcc, 0, v47, vcc
	v_add_co_u32_e32 v50, vcc, 0x22000, v46
	s_nop 1
	v_addc_co_u32_e32 v51, vcc, 0, v47, vcc
	v_add_co_u32_e32 v52, vcc, 0x24000, v46
	s_nop 1
	v_addc_co_u32_e32 v53, vcc, 0, v47, vcc
	v_add_co_u32_e32 v54, vcc, 0x26000, v46
	s_nop 1
	v_addc_co_u32_e32 v55, vcc, 0, v47, vcc
	v_add_co_u32_e32 v56, vcc, 0x28000, v46
	s_nop 1
	v_addc_co_u32_e32 v57, vcc, 0, v47, vcc
	v_add_co_u32_e32 v58, vcc, 0x2a000, v46
	s_nop 1
	v_addc_co_u32_e32 v59, vcc, 0, v47, vcc
	v_add_co_u32_e32 v60, vcc, 0x2c000, v46
	s_nop 1
	v_addc_co_u32_e32 v61, vcc, 0, v47, vcc
	v_add_co_u32_e32 v62, vcc, 0x2e000, v46
	s_nop 1
	v_addc_co_u32_e32 v63, vcc, 0, v47, vcc
	global_load_dword v80, v[48:49], off nt
	global_load_dword v81, v[50:51], off nt
	global_load_dword v82, v[52:53], off nt
	global_load_dword v83, v[54:55], off nt
	global_load_dword v84, v[56:57], off nt
	global_load_dword v85, v[58:59], off nt
	global_load_dword v86, v[60:61], off nt
	s_nop 0
	global_load_dword v62, v[62:63], off nt
	v_add_co_u32_e32 v48, vcc, 0x30000, v46
	s_nop 1
	v_addc_co_u32_e32 v49, vcc, 0, v47, vcc
	v_add_co_u32_e32 v50, vcc, 0x32000, v46
	s_nop 1
	v_addc_co_u32_e32 v51, vcc, 0, v47, vcc
	v_add_co_u32_e32 v52, vcc, 0x34000, v46
	s_nop 1
	v_addc_co_u32_e32 v53, vcc, 0, v47, vcc
	v_add_co_u32_e32 v54, vcc, 0x36000, v46
	s_nop 1
	v_addc_co_u32_e32 v55, vcc, 0, v47, vcc
	v_add_co_u32_e32 v56, vcc, 0x38000, v46
	s_nop 1
	v_addc_co_u32_e32 v57, vcc, 0, v47, vcc
	v_add_co_u32_e32 v58, vcc, 0x3a000, v46
	s_nop 1
	v_addc_co_u32_e32 v59, vcc, 0, v47, vcc
	v_add_co_u32_e32 v60, vcc, 0x3c000, v46
	s_nop 1
	v_addc_co_u32_e32 v61, vcc, 0, v47, vcc
	v_add_co_u32_e32 v46, vcc, 0x3e000, v46
	s_nop 1
	v_addc_co_u32_e32 v47, vcc, 0, v47, vcc
	global_load_dword v48, v[48:49], off nt
	s_nop 0
	global_load_dword v49, v[50:51], off nt
	s_nop 0
	global_load_dword v50, v[52:53], off nt
	global_load_dword v51, v[54:55], off nt
	s_nop 0
	global_load_dword v52, v[56:57], off nt
	global_load_dword v53, v[58:59], off nt
	global_load_dword v54, v[60:61], off nt
	s_nop 0
	global_load_dword v46, v[46:47], off nt
	s_waitcnt vmcnt(0)
	ds_write2_b32 v29, v64, v65 offset1:66
	ds_write2_b32 v29, v66, v67 offset0:132 offset1:198
	ds_write2_b32 v38, v68, v69 offset0:8 offset1:74
	ds_write2_b32 v38, v70, v71 offset0:140 offset1:206
	ds_write2_b32 v39, v72, v73 offset0:16 offset1:82
	ds_write2_b32 v39, v74, v75 offset0:148 offset1:214
	ds_write2_b32 v40, v76, v77 offset0:24 offset1:90
	ds_write2_b32 v40, v78, v79 offset0:156 offset1:222
	ds_write2_b32 v41, v80, v81 offset0:32 offset1:98
	ds_write2_b32 v41, v82, v83 offset0:164 offset1:230
	ds_write2_b32 v42, v84, v85 offset0:40 offset1:106
	ds_write2_b32 v42, v86, v62 offset0:172 offset1:238
	ds_write2_b32 v43, v48, v49 offset0:48 offset1:114
	ds_write2_b32 v43, v50, v51 offset0:180 offset1:246
	ds_write2_b32 v44, v52, v53 offset0:56 offset1:122
	ds_write2_b32 v44, v54, v46 offset0:188 offset1:254
	s_waitcnt lgkmcnt(0)
; #define GAS __attribute__((address_space(1)))
; #define LAS __attribute__((address_space(3)))
; #define LDS_WAIT() asm volatile("s_waitcnt lgkmcnt(0)" ::: "memory")
; __device__ __forceinline__ unsigned pk2(float lo, float hi) { return f2bf(lo) | (f2bf(hi) << 16); }
; __device__ __forceinline__ void tr_item(const float* W, int ld, int K, int nblk, int item, bf16* WT, bool gu, LAS float* scr, int lane) {
;     ...
;     const int c = lane & 7;
; #pragma unroll
;     for (int j = 0; j < 4; ++j) { const int n = (lane >> 3) + 8 * j; const LAS float* s = scr + (8 * c) * 33 + n;
;         v4u o; o.x = pk2(s[0 * 33], s[1 * 33]); o.y = pk2(s[2 * 33], s[3 * 33]); o.z = pk2(s[4 * 33], s[5 * 33]); o.w = pk2(s[6 * 33], s[7 * 33]);
;         *(GAS v4u*)(WT + (size_t)(drow0 + n) * K + k0 + 8 * c) = o; }
;     LDS_WAIT(); asm volatile("" ::: "memory");
	ds_read2_b32 v[50:51], v34 offset1:8
	ds_read2_b32 v[54:55], v34 offset0:33 offset1:41
	ds_read2_b32 v[56:57], v34 offset0:66 offset1:74
	ds_read2_b32 v[58:59], v34 offset0:99 offset1:107
	ds_read2_b32 v[60:61], v34 offset0:132 offset1:140
	s_waitcnt lgkmcnt(4)
	v_bfe_u32 v46, v50, 16, 1
	v_add3_u32 v46, v50, v46, s14
	s_waitcnt lgkmcnt(3)
	v_bfe_u32 v47, v54, 16, 1
	v_lshrrev_b32_e32 v46, 16, v46
	v_add3_u32 v47, v54, v47, s14
	ds_read2_b32 v[62:63], v34 offset0:165 offset1:173
	v_and_or_b32 v46, v47, s15, v46
	s_waitcnt lgkmcnt(3)
	v_bfe_u32 v47, v56, 16, 1
	v_add3_u32 v47, v56, v47, s14
	s_waitcnt lgkmcnt(2)
	v_bfe_u32 v48, v58, 16, 1
	ds_read2_b32 v[64:65], v34 offset0:198 offset1:206
	v_lshrrev_b32_e32 v47, 16, v47
	v_add3_u32 v48, v58, v48, s14
	ds_read2_b32 v[66:67], v34 offset0:231 offset1:239
	v_and_or_b32 v47, v48, s15, v47
	s_waitcnt lgkmcnt(3)
	v_bfe_u32 v48, v60, 16, 1
	v_add3_u32 v48, v60, v48, s14
	s_waitcnt lgkmcnt(2)
	v_bfe_u32 v49, v62, 16, 1
	v_lshrrev_b32_e32 v48, 16, v48
	v_add3_u32 v49, v62, v49, s14
	v_and_or_b32 v48, v49, s15, v48
	s_waitcnt lgkmcnt(1)
	v_bfe_u32 v49, v64, 16, 1
	v_add_u32_e32 v68, s6, v33
	v_add3_u32 v49, v64, v49, s14
	s_waitcnt lgkmcnt(0)
	v_bfe_u32 v50, v66, 16, 1
	v_ashrrev_i32_e32 v69, 31, v68
	v_lshl_add_u64 v[52:53], v[24:25], 0, s[4:5]
	v_lshrrev_b32_e32 v49, 16, v49
	v_add3_u32 v50, v66, v50, s14
	v_lshlrev_b64 v[68:69], 11, v[68:69]
	v_and_or_b32 v49, v50, s15, v49
	v_lshl_add_u64 v[68:69], v[52:53], 0, v[68:69]
	global_store_dwordx4 v[68:69], v[46:49], off sc1 nt
	v_bfe_u32 v50, v67, 16, 1
	v_add3_u32 v50, v67, v50, s14
	v_bfe_u32 v46, v51, 16, 1
	v_add3_u32 v46, v51, v46, s14
	v_bfe_u32 v47, v55, 16, 1
	v_lshrrev_b32_e32 v46, 16, v46
	v_add3_u32 v47, v55, v47, s14
	v_and_or_b32 v46, v47, s15, v46
	v_bfe_u32 v47, v57, 16, 1
	v_add3_u32 v47, v57, v47, s14
	v_bfe_u32 v48, v59, 16, 1
	v_lshrrev_b32_e32 v47, 16, v47
	v_add3_u32 v48, v59, v48, s14
	v_and_or_b32 v47, v48, s15, v47
	v_bfe_u32 v48, v61, 16, 1
	v_add3_u32 v48, v61, v48, s14
	v_bfe_u32 v49, v63, 16, 1
	v_lshrrev_b32_e32 v48, 16, v48
	v_add3_u32 v49, v63, v49, s14
	v_and_or_b32 v48, v49, s15, v48
	v_bfe_u32 v49, v65, 16, 1
	v_add3_u32 v49, v65, v49, s14
	v_lshrrev_b32_e32 v49, 16, v49
	v_and_or_b32 v49, v50, s15, v49
	v_add_u32_e32 v50, s6, v35
	v_ashrrev_i32_e32 v51, 31, v50
	v_lshlrev_b64 v[50:51], 11, v[50:51]
	ds_read2_b32 v[54:55], v34 offset0:16 offset1:24
	v_lshl_add_u64 v[50:51], v[52:53], 0, v[50:51]
	global_store_dwordx4 v[50:51], v[46:49], off sc1 nt
	ds_read2_b32 v[50:51], v34 offset0:49 offset1:57
	ds_read2_b32 v[56:57], v34 offset0:82 offset1:90
	ds_read2_b32 v[58:59], v34 offset0:115 offset1:123
	s_waitcnt lgkmcnt(3)
	v_bfe_u32 v46, v54, 16, 1
	v_add3_u32 v46, v54, v46, s14
	s_waitcnt lgkmcnt(2)
	v_bfe_u32 v47, v50, 16, 1
	ds_read2_b32 v[60:61], v34 offset0:148 offset1:156
	v_lshrrev_b32_e32 v46, 16, v46
	v_add3_u32 v47, v50, v47, s14
	ds_read2_b32 v[62:63], v34 offset0:181 offset1:189
	v_and_or_b32 v46, v47, s15, v46
	s_waitcnt lgkmcnt(3)
	v_bfe_u32 v47, v56, 16, 1
	v_add3_u32 v47, v56, v47, s14
	s_waitcnt lgkmcnt(2)
	v_bfe_u32 v48, v58, 16, 1
	ds_read2_b32 v[64:65], v34 offset0:214 offset1:222
	v_lshrrev_b32_e32 v47, 16, v47
	v_add3_u32 v48, v58, v48, s14
	ds_read2_b32 v[66:67], v34 offset0:247 offset1:255
	v_and_or_b32 v47, v48, s15, v47
	s_waitcnt lgkmcnt(3)
	v_bfe_u32 v48, v60, 16, 1
	v_add3_u32 v48, v60, v48, s14
	s_waitcnt lgkmcnt(2)
	v_bfe_u32 v49, v62, 16, 1
	v_lshrrev_b32_e32 v48, 16, v48
	v_add3_u32 v49, v62, v49, s14
	v_and_or_b32 v48, v49, s15, v48
	s_waitcnt lgkmcnt(1)
	v_bfe_u32 v49, v64, 16, 1
	v_add_u32_e32 v68, s6, v36
	v_add3_u32 v49, v64, v49, s14
	s_waitcnt lgkmcnt(0)
	v_bfe_u32 v50, v66, 16, 1
	v_ashrrev_i32_e32 v69, 31, v68
	v_lshrrev_b32_e32 v49, 16, v49
	v_add3_u32 v50, v66, v50, s14
	v_lshlrev_b64 v[68:69], 11, v[68:69]
	v_and_or_b32 v49, v50, s15, v49
	v_lshl_add_u64 v[68:69], v[52:53], 0, v[68:69]
	global_store_dwordx4 v[68:69], v[46:49], off sc1 nt
	v_bfe_u32 v50, v67, 16, 1
	v_add3_u32 v50, v67, v50, s14
	v_bfe_u32 v46, v55, 16, 1
	v_add3_u32 v46, v55, v46, s14
	v_bfe_u32 v47, v51, 16, 1
	v_lshrrev_b32_e32 v46, 16, v46
	v_add3_u32 v47, v51, v47, s14
	v_and_or_b32 v46, v47, s15, v46
	v_bfe_u32 v47, v57, 16, 1
	v_add3_u32 v47, v57, v47, s14
	v_bfe_u32 v48, v59, 16, 1
	v_lshrrev_b32_e32 v47, 16, v47
	v_add3_u32 v48, v59, v48, s14
	v_and_or_b32 v47, v48, s15, v47
	v_bfe_u32 v48, v61, 16, 1
	v_add3_u32 v48, v61, v48, s14
	v_bfe_u32 v49, v63, 16, 1
	v_lshrrev_b32_e32 v48, 16, v48
	v_add3_u32 v49, v63, v49, s14
	v_and_or_b32 v48, v49, s15, v48
	v_bfe_u32 v49, v65, 16, 1
	v_add3_u32 v49, v65, v49, s14
	v_lshrrev_b32_e32 v49, 16, v49
	v_and_or_b32 v49, v50, s15, v49
	v_add_u32_e32 v50, s6, v37
	v_ashrrev_i32_e32 v51, 31, v50
	v_lshlrev_b64 v[50:51], 11, v[50:51]
	v_lshl_add_u64 v[50:51], v[52:53], 0, v[50:51]
	global_store_dwordx4 v[50:51], v[46:49], off sc1 nt
	s_waitcnt lgkmcnt(0)

; #define LDS_WAIT() asm volatile("s_waitcnt lgkmcnt(0)" ::: "memory")
; __device__ __forceinline__ void tr_item(const float* W, int ld, int K, int nblk, int item, bf16* WT, bool gu, LAS float* scr, int lane) {
;     const int kb = item / nblk, nb = item % nblk, k0 = 64 * kb, n0 = 32 * nb;
;     int drow0 = n0;
;     if (gu) { const int bj = n0 / FF, j = n0 - bj * FF; drow0 = 256 * (j / 128) + 128 * bj + (j % 128); }
;     { float t_[32];
; #pragma unroll
;       for (int i = 0; i < 32; ++i) t_[i] = W[(size_t)(k0 + 2 * i + (lane >> 5)) * ld + n0 + (lane & 31)];
; #pragma unroll
;       for (int i = 0; i < 32; ++i) scr[(2 * i + (lane >> 5)) * 33 + (lane & 31)] = t_[i]; }
;     LDS_WAIT(); asm volatile("" ::: "memory");
; __device__ __forceinline__ void convert_items(Frame& F, const Args& a, int lo, int hi, int w, int nw) {
;     ...
;     for (int it = lo + w; it < hi; it += nw) {
;         int r = it;
;         if (r < I_FI) { tr_item(a.in[7], 3 * D + 16, D, 96, r, (bf16*)(F.ws + WS_WFOXIN), false, scr, lane); continue; } r -= I_FI;
.LBB0_1183:
	s_andn2_b64 vcc, exec, s[6:7]
	s_cbranch_vccnz .LBB0_1160
	s_mul_hi_i32 s4, s16, 0x2aaaaaab
	s_lshr_b32 s6, s4, 31
	s_ashr_i32 s4, s4, 4
	s_add_i32 s4, s4, s6
	s_lshl_b32 s8, s4, 6
	s_mulk_i32 s4, 0xf400
	s_add_i32 s6, s10, s4
	v_add_u32_e32 v64, s8, v28
	s_ashr_i32 s7, s6, 31
	v_lshl_add_u64 v[46:47], s[6:7], 2, v[16:17]
	v_add_u32_e32 v50, 2, v64
	v_add_u32_e32 v52, 4, v64
	v_add_u32_e32 v54, 6, v64
	v_add_u32_e32 v56, 8, v64
	v_add_u32_e32 v58, 10, v64
	v_add_u32_e32 v60, 12, v64
	v_add_u32_e32 v62, 14, v64
	v_mad_i64_i32 v[48:49], s[26:27], v64, s24, v[46:47]
	v_mad_i64_i32 v[50:51], s[26:27], v50, s24, v[46:47]
	v_mad_i64_i32 v[52:53], s[26:27], v52, s24, v[46:47]
	v_mad_i64_i32 v[54:55], s[26:27], v54, s24, v[46:47]
	v_mad_i64_i32 v[56:57], s[26:27], v56, s24, v[46:47]
	v_mad_i64_i32 v[58:59], s[26:27], v58, s24, v[46:47]
	v_mad_i64_i32 v[60:61], s[26:27], v60, s24, v[46:47]
	v_mad_i64_i32 v[62:63], s[26:27], v62, s24, v[46:47]
	global_load_dword v65, v[48:49], off nt
	global_load_dword v66, v[50:51], off nt
	global_load_dword v67, v[52:53], off nt
	global_load_dword v68, v[54:55], off nt
	global_load_dword v69, v[56:57], off nt
	global_load_dword v70, v[58:59], off nt
	global_load_dword v71, v[60:61], off nt
	global_load_dword v72, v[62:63], off nt
	v_add_u32_e32 v48, 16, v64
	v_add_u32_e32 v50, 18, v64
	v_add_u32_e32 v52, 20, v64
	v_add_u32_e32 v54, 22, v64
	v_add_u32_e32 v56, 24, v64
	v_add_u32_e32 v58, 26, v64
	v_add_u32_e32 v60, 28, v64
	v_add_u32_e32 v62, 30, v64
	v_mad_i64_i32 v[48:49], s[26:27], v48, s24, v[46:47]
	v_mad_i64_i32 v[50:51], s[26:27], v50, s24, v[46:47]
	v_mad_i64_i32 v[52:53], s[26:27], v52, s24, v[46:47]
	v_mad_i64_i32 v[54:55], s[26:27], v54, s24, v[46:47]
	v_mad_i64_i32 v[56:57], s[26:27], v56, s24, v[46:47]
	v_mad_i64_i32 v[58:59], s[26:27], v58, s24, v[46:47]
	v_mad_i64_i32 v[60:61], s[26:27], v60, s24, v[46:47]
	v_mad_i64_i32 v[62:63], s[26:27], v62, s24, v[46:47]
	global_load_dword v73, v[48:49], off nt
	global_load_dword v74, v[50:51], off nt
	global_load_dword v75, v[52:53], off nt
	global_load_dword v76, v[54:55], off nt
	global_load_dword v77, v[56:57], off nt
	global_load_dword v78, v[58:59], off nt
	global_load_dword v79, v[60:61], off nt
	global_load_dword v80, v[62:63], off nt
	v_add_u32_e32 v48, 32, v64
	v_add_u32_e32 v50, 34, v64
	v_add_u32_e32 v52, 36, v64
	v_add_u32_e32 v54, 38, v64
	v_add_u32_e32 v56, 40, v64
	v_add_u32_e32 v58, 42, v64
	v_add_u32_e32 v60, 44, v64
	v_add_u32_e32 v62, 46, v64
	v_mad_i64_i32 v[48:49], s[26:27], v48, s24, v[46:47]
	v_mad_i64_i32 v[50:51], s[26:27], v50, s24, v[46:47]
	v_mad_i64_i32 v[52:53], s[26:27], v52, s24, v[46:47]
	v_mad_i64_i32 v[54:55], s[26:27], v54, s24, v[46:47]
	v_mad_i64_i32 v[56:57], s[26:27], v56, s24, v[46:47]
	v_mad_i64_i32 v[58:59], s[26:27], v58, s24, v[46:47]
	v_mad_i64_i32 v[60:61], s[26:27], v60, s24, v[46:47]
	v_mad_i64_i32 v[62:63], s[26:27], v62, s24, v[46:47]
	global_load_dword v81, v[48:49], off nt
	global_load_dword v82, v[50:51], off nt
	global_load_dword v83, v[52:53], off nt
	global_load_dword v84, v[54:55], off nt
	global_load_dword v85, v[56:57], off nt
	global_load_dword v86, v[58:59], off nt
	global_load_dword v87, v[60:61], off nt
	s_nop 0
	global_load_dword v62, v[62:63], off nt
	v_add_u32_e32 v48, 48, v64
	v_add_u32_e32 v50, 50, v64
	v_add_u32_e32 v52, 52, v64
	v_add_u32_e32 v54, 54, v64
	v_add_u32_e32 v56, 56, v64
	v_add_u32_e32 v58, 58, v64
	v_add_u32_e32 v60, 60, v64
	v_add_u32_e32 v63, 62, v64
	v_mad_i64_i32 v[48:49], s[26:27], v48, s24, v[46:47]
	v_mad_i64_i32 v[50:51], s[26:27], v50, s24, v[46:47]
	v_mad_i64_i32 v[52:53], s[26:27], v52, s24, v[46:47]
	v_mad_i64_i32 v[54:55], s[26:27], v54, s24, v[46:47]
	v_mad_i64_i32 v[56:57], s[26:27], v56, s24, v[46:47]
	v_mad_i64_i32 v[58:59], s[26:27], v58, s24, v[46:47]
	v_mad_i64_i32 v[60:61], s[26:27], v60, s24, v[46:47]
	v_mad_i64_i32 v[46:47], s[26:27], v63, s24, v[46:47]
	global_load_dword v48, v[48:49], off nt
	s_nop 0
	global_load_dword v49, v[50:51], off nt
	s_nop 0
	global_load_dword v50, v[52:53], off nt
	global_load_dword v51, v[54:55], off nt
	s_nop 0
	global_load_dword v52, v[56:57], off nt
	global_load_dword v53, v[58:59], off nt
	global_load_dword v54, v[60:61], off nt
	s_nop 0
	global_load_dword v46, v[46:47], off nt
	s_waitcnt vmcnt(0)
	ds_write2_b32 v29, v65, v66 offset1:66
	ds_write2_b32 v29, v67, v68 offset0:132 offset1:198
	ds_write2_b32 v38, v69, v70 offset0:8 offset1:74
	ds_write2_b32 v38, v71, v72 offset0:140 offset1:206
	ds_write2_b32 v39, v73, v74 offset0:16 offset1:82
	ds_write2_b32 v39, v75, v76 offset0:148 offset1:214
	ds_write2_b32 v40, v77, v78 offset0:24 offset1:90
	ds_write2_b32 v40, v79, v80 offset0:156 offset1:222
	ds_write2_b32 v41, v81, v82 offset0:32 offset1:98
	ds_write2_b32 v41, v83, v84 offset0:164 offset1:230
	ds_write2_b32 v42, v85, v86 offset0:40 offset1:106
	ds_write2_b32 v42, v87, v62 offset0:172 offset1:238
	ds_write2_b32 v43, v48, v49 offset0:48 offset1:114
	ds_write2_b32 v43, v50, v51 offset0:180 offset1:246
	ds_write2_b32 v44, v52, v53 offset0:56 offset1:122
	ds_write2_b32 v44, v54, v46 offset0:188 offset1:254
	s_waitcnt lgkmcnt(0)
; #define GAS __attribute__((address_space(1)))
; #define LAS __attribute__((address_space(3)))
; #define LDS_WAIT() asm volatile("s_waitcnt lgkmcnt(0)" ::: "memory")
; __device__ __forceinline__ unsigned pk2(float lo, float hi) { return f2bf(lo) | (f2bf(hi) << 16); }
; __device__ __forceinline__ void tr_item(const float* W, int ld, int K, int nblk, int item, bf16* WT, bool gu, LAS float* scr, int lane) {
;     ...
;     const int c = lane & 7;
; #pragma unroll
;     for (int j = 0; j < 4; ++j) { const int n = (lane >> 3) + 8 * j; const LAS float* s = scr + (8 * c) * 33 + n;
;         v4u o; o.x = pk2(s[0 * 33], s[1 * 33]); o.y = pk2(s[2 * 33], s[3 * 33]); o.z = pk2(s[4 * 33], s[5 * 33]); o.w = pk2(s[6 * 33], s[7 * 33]);
;         *(GAS v4u*)(WT + (size_t)(drow0 + n) * K + k0 + 8 * c) = o; }
;     LDS_WAIT(); asm volatile("" ::: "memory");
	ds_read2_b32 v[50:51], v34 offset1:8
	ds_read2_b32 v[54:55], v34 offset0:33 offset1:41
	ds_read2_b32 v[56:57], v34 offset0:66 offset1:74
	ds_read2_b32 v[58:59], v34 offset0:99 offset1:107
	ds_read2_b32 v[60:61], v34 offset0:132 offset1:140
	s_waitcnt lgkmcnt(4)
	v_bfe_u32 v46, v50, 16, 1
	v_add3_u32 v46, v50, v46, s14
	s_waitcnt lgkmcnt(3)
	v_bfe_u32 v47, v54, 16, 1
	v_lshrrev_b32_e32 v46, 16, v46
	v_add3_u32 v47, v54, v47, s14
	ds_read2_b32 v[62:63], v34 offset0:165 offset1:173
	v_and_or_b32 v46, v47, s15, v46
	s_waitcnt lgkmcnt(3)
	v_bfe_u32 v47, v56, 16, 1
	v_add3_u32 v47, v56, v47, s14
	s_waitcnt lgkmcnt(2)
	v_bfe_u32 v48, v58, 16, 1
	ds_read2_b32 v[64:65], v34 offset0:198 offset1:206
	v_lshrrev_b32_e32 v47, 16, v47
	v_add3_u32 v48, v58, v48, s14
	ds_read2_b32 v[66:67], v34 offset0:231 offset1:239
	v_and_or_b32 v47, v48, s15, v47
	s_waitcnt lgkmcnt(3)
	v_bfe_u32 v48, v60, 16, 1
	v_add3_u32 v48, v60, v48, s14
	s_waitcnt lgkmcnt(2)
	v_bfe_u32 v49, v62, 16, 1
	v_lshrrev_b32_e32 v48, 16, v48
	v_add3_u32 v49, v62, v49, s14
	v_and_or_b32 v48, v49, s15, v48
	s_waitcnt lgkmcnt(1)
	v_bfe_u32 v49, v64, 16, 1
	v_add_u32_e32 v68, s6, v33
	s_ashr_i32 s9, s8, 31
	v_add3_u32 v49, v64, v49, s14
	s_waitcnt lgkmcnt(0)
	v_bfe_u32 v50, v66, 16, 1
	v_ashrrev_i32_e32 v69, 31, v68
	v_lshl_add_u64 v[52:53], s[8:9], 1, v[26:27]
	v_lshrrev_b32_e32 v49, 16, v49
	v_add3_u32 v50, v66, v50, s14
	v_lshlrev_b64 v[70:71], 11, v[68:69]
	v_and_or_b32 v49, v50, s15, v49
	v_lshl_add_u64 v[70:71], v[52:53], 0, v[70:71]
	global_store_dwordx4 v[70:71], v[46:49], off sc1 nt
	v_bfe_u32 v50, v67, 16, 1
	v_add3_u32 v50, v67, v50, s14
	v_bfe_u32 v46, v51, 16, 1
	v_add3_u32 v46, v51, v46, s14
	v_bfe_u32 v47, v55, 16, 1
	v_lshrrev_b32_e32 v46, 16, v46
	v_add3_u32 v47, v55, v47, s14
	v_and_or_b32 v46, v47, s15, v46
	v_bfe_u32 v47, v57, 16, 1
	v_add3_u32 v47, v57, v47, s14
	v_bfe_u32 v48, v59, 16, 1
	v_lshrrev_b32_e32 v47, 16, v47
	v_add3_u32 v48, v59, v48, s14
	v_and_or_b32 v47, v48, s15, v47
	v_bfe_u32 v48, v61, 16, 1
	v_add3_u32 v48, v61, v48, s14
	v_bfe_u32 v49, v63, 16, 1
	v_lshrrev_b32_e32 v48, 16, v48
	v_add3_u32 v49, v63, v49, s14
	v_and_or_b32 v48, v49, s15, v48
	v_bfe_u32 v49, v65, 16, 1
	v_add3_u32 v49, v65, v49, s14
	v_lshrrev_b32_e32 v49, 16, v49
	v_and_or_b32 v49, v50, s15, v49
	v_add_u32_e32 v50, 8, v68
	v_ashrrev_i32_e32 v51, 31, v50
	v_lshlrev_b64 v[50:51], 11, v[50:51]
	ds_read2_b32 v[54:55], v34 offset0:16 offset1:24
	v_lshl_add_u64 v[50:51], v[52:53], 0, v[50:51]
	global_store_dwordx4 v[50:51], v[46:49], off sc1 nt
	ds_read2_b32 v[50:51], v34 offset0:49 offset1:57
	ds_read2_b32 v[56:57], v34 offset0:82 offset1:90
	ds_read2_b32 v[58:59], v34 offset0:115 offset1:123
	s_waitcnt lgkmcnt(3)
	v_bfe_u32 v46, v54, 16, 1
	v_add3_u32 v46, v54, v46, s14
	s_waitcnt lgkmcnt(2)
	v_bfe_u32 v47, v50, 16, 1
	ds_read2_b32 v[60:61], v34 offset0:148 offset1:156
	v_lshrrev_b32_e32 v46, 16, v46
	v_add3_u32 v47, v50, v47, s14
	ds_read2_b32 v[62:63], v34 offset0:181 offset1:189
	v_and_or_b32 v46, v47, s15, v46
	s_waitcnt lgkmcnt(3)
	v_bfe_u32 v47, v56, 16, 1
	v_add3_u32 v47, v56, v47, s14
	s_waitcnt lgkmcnt(2)
	v_bfe_u32 v48, v58, 16, 1
	ds_read2_b32 v[64:65], v34 offset0:214 offset1:222
	v_lshrrev_b32_e32 v47, 16, v47
	v_add3_u32 v48, v58, v48, s14
	ds_read2_b32 v[66:67], v34 offset0:247 offset1:255
	v_and_or_b32 v47, v48, s15, v47
	s_waitcnt lgkmcnt(3)
	v_bfe_u32 v48, v60, 16, 1
	v_add3_u32 v48, v60, v48, s14
	s_waitcnt lgkmcnt(2)
	v_bfe_u32 v49, v62, 16, 1
	v_lshrrev_b32_e32 v48, 16, v48
	v_add3_u32 v49, v62, v49, s14
	v_and_or_b32 v48, v49, s15, v48
	s_waitcnt lgkmcnt(1)
	v_bfe_u32 v49, v64, 16, 1
	v_add_u32_e32 v70, 16, v68
	v_add3_u32 v49, v64, v49, s14
	s_waitcnt lgkmcnt(0)
	v_bfe_u32 v50, v66, 16, 1
	v_ashrrev_i32_e32 v71, 31, v70
	v_lshrrev_b32_e32 v49, 16, v49
	v_add3_u32 v50, v66, v50, s14
	v_lshlrev_b64 v[70:71], 11, v[70:71]
	v_and_or_b32 v49, v50, s15, v49
	v_lshl_add_u64 v[70:71], v[52:53], 0, v[70:71]
	global_store_dwordx4 v[70:71], v[46:49], off sc1 nt
	v_bfe_u32 v50, v67, 16, 1
	v_add3_u32 v50, v67, v50, s14
	v_bfe_u32 v46, v55, 16, 1
	v_add3_u32 v46, v55, v46, s14
	v_bfe_u32 v47, v51, 16, 1
	v_lshrrev_b32_e32 v46, 16, v46
	v_add3_u32 v47, v51, v47, s14
	v_and_or_b32 v46, v47, s15, v46
	v_bfe_u32 v47, v57, 16, 1
	v_add3_u32 v47, v57, v47, s14
	v_bfe_u32 v48, v59, 16, 1
	v_lshrrev_b32_e32 v47, 16, v47
	v_add3_u32 v48, v59, v48, s14
	v_and_or_b32 v47, v48, s15, v47
	v_bfe_u32 v48, v61, 16, 1
	v_add3_u32 v48, v61, v48, s14
	v_bfe_u32 v49, v63, 16, 1
	v_lshrrev_b32_e32 v48, 16, v48
	v_add3_u32 v49, v63, v49, s14
	v_and_or_b32 v48, v49, s15, v48
	v_bfe_u32 v49, v65, 16, 1
	v_add3_u32 v49, v65, v49, s14
	v_lshrrev_b32_e32 v49, 16, v49
	v_and_or_b32 v49, v50, s15, v49
	v_add_u32_e32 v50, 24, v68
	v_ashrrev_i32_e32 v51, 31, v50
	v_lshlrev_b64 v[50:51], 11, v[50:51]
	v_lshl_add_u64 v[50:51], v[52:53], 0, v[50:51]
	global_store_dwordx4 v[50:51], v[46:49], off sc1 nt
	s_waitcnt lgkmcnt(0)
	s_branch .LBB0_1160

; #define LAS __attribute__((address_space(3)))
; __device__ __forceinline__ void tr_item8(const float* W, int ld, int K, int nblk, int item, unsigned char* WT, bool gu, float scale, LAS float* scr, int lane) {
;     const int kb = item / nblk, nb = item % nblk, k0 = 64 * kb, n0 = 32 * nb;
;     int drow0 = n0;
;     if (gu) { const int bj = n0 / FF, j = n0 - bj * FF; drow0 = 256 * (j / 128) + 128 * bj + (j % 128); }
;     { float t_[32];
; #pragma unroll
;       for (int i = 0; i < 32; ++i) t_[i] = W[(size_t)(k0 + 2 * i + (lane >> 5)) * ld + n0 + (lane & 31)];
; #pragma unroll
;       for (int i = 0; i < 32; ++i) scr[(2 * i + (lane >> 5)) * 33 + (lane & 31)] = t_[i] * scale; }
; __device__ __forceinline__ void convert_items(Frame& F, const Args& a, int lo, int hi, int w, int nw) {
;     ...
;         if (r < NE * I_GU) { const int e = r / I_GU, rr = r % I_GU; tr_item8(a.in[18] + (size_t)e * D * 2 * FF, 2 * FF, D, 224, rr, F.ws + WS_WMGU + (size_t)e * 2 * FF * D, true, WSC_GU, scr, lane); continue; } r -= NE * I_GU;
;         { const int e = r / I_DN, rr = r % I_DN; tr_item8(a.in[19] + (size_t)e * FF * D, D, FF, 32, rr, F.ws + WS_WMDN + (size_t)e * D * FF, false, WSC_DN, scr, lane); }
.LBB0_1296:
	s_cmpk_gt_i32 s8, 0x5ff
	s_mov_b64 s[4:5], -1
	s_cbranch_scc0 .LBB0_1322
	s_cmpk_gt_u32 s8, 0x7ff
	s_cbranch_scc0 .LBB0_1319
	s_cmpk_gt_u32 s8, 0xaff
	s_cbranch_scc0 .LBB0_1316
	s_cmpk_gt_u32 s8, 0xcff
	s_cbranch_scc0 .LBB0_1313
	s_cmpk_gt_u32 s8, 0x1aff
	s_cbranch_scc0 .LBB0_1310
	s_cmpk_gt_u32 s8, 0x21ff
	s_cbranch_scc0 .LBB0_1307
	s_cmpk_gt_u32 s8, 0x91ff
	s_cbranch_scc0 .LBB0_1304
	s_add_i32 s0, s8, 0x6e00
	s_bfe_u32 s4, s0, 0x80008
	s_mulk_i32 s4, 0x2493
	s_lshr_b32 s4, s4, 16
	s_mul_i32 s5, s4, 0x700
	v_readlane_b32 s40, v254, 28
	s_sub_i32 s6, s0, s5
	s_mul_i32 s0, s4, 0xe00000
	v_readlane_b32 s46, v254, 34
	v_readlane_b32 s47, v254, 35
	s_add_u32 s7, s46, s0
	s_addc_u32 s31, s47, 0
	s_mul_i32 s4, s4, 0x380000
	s_add_u32 s4, s66, s4
	s_addc_u32 s5, s58, 0
	s_lshl_b32 s0, s6, 5
	s_and_b32 s0, s0, 0x3e0
	s_lshl_b32 s6, s6, 1
	s_and_b32 s6, s6, 0xfc0
	s_lshl_b32 s40, s0, 2
	v_readlane_b32 s41, v254, 29
	v_add_u32_e32 v28, s6, v30
	s_add_u32 s40, s7, s40
	s_addc_u32 s41, s31, 0
	v_ashrrev_i32_e32 v29, 31, v28
	v_lshl_add_u64 v[48:49], s[40:41], 0, v[0:1]
	v_lshlrev_b64 v[28:29], 12, v[28:29]
	v_lshl_add_u64 v[28:29], v[48:49], 0, v[28:29]
	s_movk_i32 s7, 0x2000
	v_add_co_u32_e32 v48, vcc, s7, v28
	s_movk_i32 s7, 0x4000
	s_nop 0
	v_addc_co_u32_e32 v49, vcc, 0, v29, vcc
	global_load_dword v50, v[28:29], off nt
	global_load_dword v51, v[48:49], off nt
	v_add_co_u32_e32 v48, vcc, s7, v28
	s_movk_i32 s7, 0x6000
	s_nop 0
	v_addc_co_u32_e32 v49, vcc, 0, v29, vcc
	global_load_dword v52, v[48:49], off nt
	v_add_co_u32_e32 v48, vcc, s7, v28
	s_mov_b32 s7, 0x8000
	s_nop 0
	v_addc_co_u32_e32 v49, vcc, 0, v29, vcc
	global_load_dword v53, v[48:49], off nt
	v_add_co_u32_e32 v48, vcc, s7, v28
	s_mov_b32 s7, 0xa000
	s_nop 0
	v_addc_co_u32_e32 v49, vcc, 0, v29, vcc
	global_load_dword v54, v[48:49], off nt
	v_add_co_u32_e32 v48, vcc, s7, v28
	s_mov_b32 s7, 0xc000
	s_nop 0
	v_addc_co_u32_e32 v49, vcc, 0, v29, vcc
	global_load_dword v55, v[48:49], off nt
	v_add_co_u32_e32 v48, vcc, s7, v28
	s_mov_b32 s7, 0xe000
	s_nop 0
	v_addc_co_u32_e32 v49, vcc, 0, v29, vcc
	global_load_dword v56, v[48:49], off nt
	v_add_co_u32_e32 v48, vcc, s7, v28
	s_mov_b32 s7, 0x10000
	s_nop 0
	v_addc_co_u32_e32 v49, vcc, 0, v29, vcc
	global_load_dword v57, v[48:49], off nt
	v_add_co_u32_e32 v48, vcc, s7, v28
	s_mov_b32 s7, 0x12000
	s_nop 0
	v_addc_co_u32_e32 v49, vcc, 0, v29, vcc
	global_load_dword v58, v[48:49], off nt
	v_add_co_u32_e32 v48, vcc, s7, v28
	s_mov_b32 s7, 0x14000
	s_nop 0
	v_addc_co_u32_e32 v49, vcc, 0, v29, vcc
	global_load_dword v59, v[48:49], off nt
	v_add_co_u32_e32 v48, vcc, s7, v28
	s_mov_b32 s7, 0x16000
	s_nop 0
	v_addc_co_u32_e32 v49, vcc, 0, v29, vcc
	global_load_dword v60, v[48:49], off nt
	v_add_co_u32_e32 v48, vcc, s7, v28
	s_mov_b32 s7, 0x18000
	s_nop 0
	v_addc_co_u32_e32 v49, vcc, 0, v29, vcc
	global_load_dword v61, v[48:49], off nt
	v_add_co_u32_e32 v48, vcc, s7, v28
	s_mov_b32 s7, 0x1a000
	s_nop 0
	v_addc_co_u32_e32 v49, vcc, 0, v29, vcc
	global_load_dword v62, v[48:49], off nt
	v_add_co_u32_e32 v48, vcc, s7, v28
	s_mov_b32 s7, 0x1c000
	s_nop 0
	v_addc_co_u32_e32 v49, vcc, 0, v29, vcc
	global_load_dword v63, v[48:49], off nt
	v_add_co_u32_e32 v48, vcc, s7, v28
	s_mov_b32 s7, 0x1e000
	s_nop 0
	v_addc_co_u32_e32 v49, vcc, 0, v29, vcc
	global_load_dword v64, v[48:49], off nt
	v_add_co_u32_e32 v48, vcc, s7, v28
	s_mov_b32 s7, 0x20000
	s_nop 0
	v_addc_co_u32_e32 v49, vcc, 0, v29, vcc
	global_load_dword v65, v[48:49], off nt
	v_add_co_u32_e32 v48, vcc, s7, v28
	s_mov_b32 s7, 0x22000
	s_nop 0
	v_addc_co_u32_e32 v49, vcc, 0, v29, vcc
	global_load_dword v66, v[48:49], off nt
	v_add_co_u32_e32 v48, vcc, s7, v28
	s_mov_b32 s7, 0x24000
	s_nop 0
	v_addc_co_u32_e32 v49, vcc, 0, v29, vcc
	global_load_dword v67, v[48:49], off nt
	v_add_co_u32_e32 v48, vcc, s7, v28
	s_mov_b32 s7, 0x26000
	s_nop 0
	v_addc_co_u32_e32 v49, vcc, 0, v29, vcc
	global_load_dword v68, v[48:49], off nt
	v_add_co_u32_e32 v48, vcc, s7, v28
	s_mov_b32 s7, 0x28000
	s_nop 0
	v_addc_co_u32_e32 v49, vcc, 0, v29, vcc
	global_load_dword v69, v[48:49], off nt
	v_add_co_u32_e32 v48, vcc, s7, v28
	s_mov_b32 s7, 0x2a000
	s_nop 0
	v_addc_co_u32_e32 v49, vcc, 0, v29, vcc
	global_load_dword v70, v[48:49], off nt
	v_add_co_u32_e32 v48, vcc, s7, v28
	s_mov_b32 s7, 0x2c000
	s_nop 0
	v_addc_co_u32_e32 v49, vcc, 0, v29, vcc
	global_load_dword v71, v[48:49], off nt
	v_add_co_u32_e32 v48, vcc, s7, v28
	s_mov_b32 s7, 0x2e000
	s_nop 0
	v_addc_co_u32_e32 v49, vcc, 0, v29, vcc
	global_load_dword v72, v[48:49], off nt
	v_add_co_u32_e32 v48, vcc, s7, v28
	s_mov_b32 s7, 0x30000
	s_nop 0
	v_addc_co_u32_e32 v49, vcc, 0, v29, vcc
	global_load_dword v73, v[48:49], off nt
	v_add_co_u32_e32 v48, vcc, s7, v28
	s_mov_b32 s7, 0x32000
	s_nop 0
	v_addc_co_u32_e32 v49, vcc, 0, v29, vcc
	global_load_dword v74, v[48:49], off nt
	v_add_co_u32_e32 v48, vcc, s7, v28
	s_mov_b32 s7, 0x34000
	s_nop 0
	v_addc_co_u32_e32 v49, vcc, 0, v29, vcc
	global_load_dword v75, v[48:49], off nt
	v_add_co_u32_e32 v48, vcc, s7, v28
	s_mov_b32 s7, 0x36000
	s_nop 0
	v_addc_co_u32_e32 v49, vcc, 0, v29, vcc
	global_load_dword v76, v[48:49], off nt
	v_add_co_u32_e32 v48, vcc, s7, v28
	s_mov_b32 s7, 0x38000
	s_nop 0
	v_addc_co_u32_e32 v49, vcc, 0, v29, vcc
	global_load_dword v77, v[48:49], off nt
	v_add_co_u32_e32 v48, vcc, s7, v28
	s_mov_b32 s7, 0x3a000
	s_nop 0
	v_addc_co_u32_e32 v49, vcc, 0, v29, vcc
	global_load_dword v78, v[48:49], off nt
	v_add_co_u32_e32 v48, vcc, s7, v28
	s_mov_b32 s7, 0x3c000
	s_nop 0
	v_addc_co_u32_e32 v49, vcc, 0, v29, vcc
	global_load_dword v79, v[48:49], off nt
	v_add_co_u32_e32 v48, vcc, s7, v28
	s_mov_b32 s7, 0x3e000
	s_nop 0
	v_addc_co_u32_e32 v49, vcc, 0, v29, vcc
	v_add_co_u32_e32 v28, vcc, s7, v28
	global_load_dword v48, v[48:49], off nt
	s_nop 0
	v_addc_co_u32_e32 v29, vcc, 0, v29, vcc
	global_load_dword v28, v[28:29], off nt
	s_waitcnt vmcnt(31)
; __device__ __forceinline__ unsigned cvt_pk4_fp8(float a, float b, float c, float d) { int w = 0; w = __builtin_amdgcn_cvt_pk_fp8_f32(a, b, w, false); w = __builtin_amdgcn_cvt_pk_fp8_f32(c, d, w, true); return (unsigned)w; }
; #define GAS __attribute__((address_space(1)))
; #define LAS __attribute__((address_space(3)))
; #define LDS_WAIT() asm volatile("s_waitcnt lgkmcnt(0)" ::: "memory")
; __device__ __forceinline__ void tr_item8(const float* W, int ld, int K, int nblk, int item, unsigned char* WT, bool gu, float scale, LAS float* scr, int lane) {
;     ...
; #pragma unroll
;       for (int i = 0; i < 32; ++i) scr[(2 * i + (lane >> 5)) * 33 + (lane & 31)] = t_[i] * scale; }
;     LDS_WAIT(); asm volatile("" ::: "memory");
;     const int c = lane & 3;
; #pragma unroll
;     for (int j = 0; j < 2; ++j) { const int n = (lane >> 2) + 16 * j; const LAS float* sp = scr + (16 * c) * 33 + n;
;         v4u o; o.x = pg8::cvt_pk4_fp8(sp[0 * 33], sp[1 * 33], sp[2 * 33], sp[3 * 33]); o.y = pg8::cvt_pk4_fp8(sp[4 * 33], sp[5 * 33], sp[6 * 33], sp[7 * 33]);
;         o.z = pg8::cvt_pk4_fp8(sp[8 * 33], sp[9 * 33], sp[10 * 33], sp[11 * 33]); o.w = pg8::cvt_pk4_fp8(sp[12 * 33], sp[13 * 33], sp[14 * 33], sp[15 * 33]);
;         *(GAS v4u*)(WT + (size_t)(drow0 + n) * K + k0 + 16 * c) = o; }
;     LDS_WAIT(); asm volatile("" ::: "memory");
	v_mul_f32_e32 v29, 0x43000000, v50
	s_waitcnt vmcnt(30)
	v_mul_f32_e32 v49, 0x43000000, v51
	ds_write2_b32 v31, v29, v49 offset1:66
	s_waitcnt vmcnt(29)
	v_mul_f32_e32 v29, 0x43000000, v52
	s_waitcnt vmcnt(28)
	v_mul_f32_e32 v49, 0x43000000, v53
	ds_write2_b32 v31, v29, v49 offset0:132 offset1:198
	s_waitcnt vmcnt(27)
	v_mul_f32_e32 v29, 0x43000000, v54
	s_waitcnt vmcnt(26)
	v_mul_f32_e32 v49, 0x43000000, v55
	ds_write2_b32 v40, v29, v49 offset0:8 offset1:74
	s_waitcnt vmcnt(25)
	v_mul_f32_e32 v29, 0x43000000, v56
	s_waitcnt vmcnt(24)
	v_mul_f32_e32 v49, 0x43000000, v57
	ds_write2_b32 v40, v29, v49 offset0:140 offset1:206
	s_waitcnt vmcnt(23)
	v_mul_f32_e32 v29, 0x43000000, v58
	s_waitcnt vmcnt(22)
	v_mul_f32_e32 v49, 0x43000000, v59
	ds_write2_b32 v41, v29, v49 offset0:16 offset1:82
	s_waitcnt vmcnt(21)
	v_mul_f32_e32 v29, 0x43000000, v60
	s_waitcnt vmcnt(20)
	v_mul_f32_e32 v49, 0x43000000, v61
	ds_write2_b32 v41, v29, v49 offset0:148 offset1:214
	s_waitcnt vmcnt(19)
	v_mul_f32_e32 v29, 0x43000000, v62
	s_waitcnt vmcnt(18)
	v_mul_f32_e32 v49, 0x43000000, v63
	ds_write2_b32 v42, v29, v49 offset0:24 offset1:90
	s_waitcnt vmcnt(17)
	v_mul_f32_e32 v29, 0x43000000, v64
	s_waitcnt vmcnt(16)
	v_mul_f32_e32 v49, 0x43000000, v65
	ds_write2_b32 v42, v29, v49 offset0:156 offset1:222
	s_waitcnt vmcnt(15)
	v_mul_f32_e32 v29, 0x43000000, v66
	s_waitcnt vmcnt(14)
	v_mul_f32_e32 v49, 0x43000000, v67
	ds_write2_b32 v43, v29, v49 offset0:32 offset1:98
	s_waitcnt vmcnt(13)
	v_mul_f32_e32 v29, 0x43000000, v68
	s_waitcnt vmcnt(12)
	v_mul_f32_e32 v49, 0x43000000, v69
	ds_write2_b32 v43, v29, v49 offset0:164 offset1:230
	s_waitcnt vmcnt(11)
	v_mul_f32_e32 v29, 0x43000000, v70
	s_waitcnt vmcnt(10)
	v_mul_f32_e32 v49, 0x43000000, v71
	ds_write2_b32 v44, v29, v49 offset0:40 offset1:106
	s_waitcnt vmcnt(9)
	v_mul_f32_e32 v29, 0x43000000, v72
	s_waitcnt vmcnt(8)
	v_mul_f32_e32 v49, 0x43000000, v73
	ds_write2_b32 v44, v29, v49 offset0:172 offset1:238
	v_mov_b32_e32 v50, v1
	v_mov_b32_e32 v51, v1
	s_waitcnt vmcnt(7)
	v_mul_f32_e32 v29, 0x43000000, v74
	s_add_u32 s4, s4, s6
	s_addc_u32 s5, s5, 0
	v_readlane_b32 s42, v254, 30
	v_readlane_b32 s43, v254, 31
	v_readlane_b32 s44, v254, 32
	s_waitcnt vmcnt(6)
	v_mul_f32_e32 v49, 0x43000000, v75
	ds_write2_b32 v45, v29, v49 offset0:48 offset1:114
	v_readlane_b32 s45, v254, 33
	s_waitcnt vmcnt(5)
	v_mul_f32_e32 v29, 0x43000000, v76
	s_waitcnt vmcnt(4)
	v_mul_f32_e32 v49, 0x43000000, v77
	ds_write2_b32 v45, v29, v49 offset0:180 offset1:246
	s_waitcnt vmcnt(3)
	v_mul_f32_e32 v29, 0x43000000, v78
	s_waitcnt vmcnt(2)
	v_mul_f32_e32 v49, 0x43000000, v79
	ds_write2_b32 v46, v29, v49 offset0:56 offset1:122
	v_mov_b32_e32 v49, v1
	s_waitcnt vmcnt(1)
	v_mul_f32_e32 v29, 0x43000000, v48
	v_mov_b32_e32 v48, v1
	s_waitcnt vmcnt(0)
	v_mul_f32_e32 v28, 0x43000000, v28
	ds_write2_b32 v46, v29, v28 offset0:188 offset1:254
	s_waitcnt lgkmcnt(0)
	ds_read2_b32 v[52:53], v33 offset1:16
	ds_read2_b32 v[54:55], v33 offset0:33 offset1:49
	ds_read2_b32 v[56:57], v33 offset0:66 offset1:82
	ds_read2_b32 v[58:59], v33 offset0:99 offset1:115
	ds_read2_b32 v[60:61], v33 offset0:132 offset1:148
	ds_read2_b32 v[62:63], v33 offset0:165 offset1:181
	ds_read2_b32 v[64:65], v33 offset0:198 offset1:214
	ds_read2_b32 v[66:67], v33 offset0:231 offset1:247
	ds_read2_b32 v[68:69], v47 offset0:8 offset1:24
	ds_read2_b32 v[70:71], v47 offset0:41 offset1:57
	ds_read2_b32 v[72:73], v47 offset0:74 offset1:90
	ds_read2_b32 v[74:75], v47 offset0:107 offset1:123
	ds_read2_b32 v[76:77], v47 offset0:140 offset1:156
	ds_read2_b32 v[78:79], v47 offset0:173 offset1:189
	ds_read2_b32 v[80:81], v47 offset0:206 offset1:222
	ds_read2_b32 v[82:83], v47 offset0:239 offset1:255
	s_waitcnt lgkmcnt(14)
	v_cvt_pk_fp8_f32 v48, v52, v54
	s_waitcnt lgkmcnt(10)
	v_cvt_pk_fp8_f32 v49, v60, v62
	s_waitcnt lgkmcnt(6)
	v_cvt_pk_fp8_f32 v50, v68, v70
	s_waitcnt lgkmcnt(2)
	v_cvt_pk_fp8_f32 v51, v76, v78
	v_cvt_pk_fp8_f32 v48, v56, v58 op_sel:[0,0,1]
	v_cvt_pk_fp8_f32 v49, v64, v66 op_sel:[0,0,1]
	v_cvt_pk_fp8_f32 v50, v72, v74 op_sel:[0,0,1]
	s_waitcnt lgkmcnt(0)
	v_cvt_pk_fp8_f32 v51, v80, v82 op_sel:[0,0,1]
	v_lshl_add_u64 v[28:29], s[4:5], 0, v[2:3]
	v_add_u32_e32 v52, s0, v32
	v_mad_i64_i32 v[84:85], s[4:5], v52, s13, v[28:29]
	global_store_dwordx4 v[84:85], v[48:51], off sc1 nt
	v_add_u32_e32 v52, s0, v34
	v_mad_i64_i32 v[28:29], s[4:5], v52, s13, v[28:29]
	v_mov_b32_e32 v48, v1
	v_mov_b32_e32 v49, v1
	v_mov_b32_e32 v50, v1
	v_mov_b32_e32 v51, v1
	v_cvt_pk_fp8_f32 v48, v53, v55
	v_cvt_pk_fp8_f32 v49, v61, v63
	v_cvt_pk_fp8_f32 v50, v69, v71
	v_cvt_pk_fp8_f32 v51, v77, v79
	v_cvt_pk_fp8_f32 v48, v57, v59 op_sel:[0,0,1]
	v_cvt_pk_fp8_f32 v49, v65, v67 op_sel:[0,0,1]
	v_cvt_pk_fp8_f32 v50, v73, v75 op_sel:[0,0,1]
	v_cvt_pk_fp8_f32 v51, v81, v83 op_sel:[0,0,1]
	s_mov_b64 s[4:5], 0
	global_store_dwordx4 v[28:29], v[48:51], off sc1 nt
	s_waitcnt lgkmcnt(0)
; #define LAS __attribute__((address_space(3)))
; __device__ __forceinline__ void tr_item8(const float* W, int ld, int K, int nblk, int item, unsigned char* WT, bool gu, float scale, LAS float* scr, int lane) {
;     const int kb = item / nblk, nb = item % nblk, k0 = 64 * kb, n0 = 32 * nb;
;     int drow0 = n0;
;     if (gu) { const int bj = n0 / FF, j = n0 - bj * FF; drow0 = 256 * (j / 128) + 128 * bj + (j % 128); }
;     { float t_[32];
; #pragma unroll
;       for (int i = 0; i < 32; ++i) t_[i] = W[(size_t)(k0 + 2 * i + (lane >> 5)) * ld + n0 + (lane & 31)];
; __device__ __forceinline__ void convert_items(Frame& F, const Args& a, int lo, int hi, int w, int nw) {
;     ...
;         if (r < NE * I_GU) { const int e = r / I_GU, rr = r % I_GU; tr_item8(a.in[18] + (size_t)e * D * 2 * FF, 2 * FF, D, 224, rr, F.ws + WS_WMGU + (size_t)e * 2 * FF * D, true, WSC_GU, scr, lane); continue; } r -= NE * I_GU;
.LBB0_1304:
	s_andn2_b64 vcc, exec, s[4:5]
	s_cbranch_vccnz .LBB0_1306
	s_add_i32 s0, s8, 0xde00
	s_bfe_u32 s4, s0, 0x70009
	s_mulk_i32 s4, 0x2493
	s_lshr_b32 s4, s4, 16
	s_mul_i32 s5, s4, 0xe00
	v_readlane_b32 s40, v254, 28
	s_sub_i32 s0, s0, s5
	s_mul_i32 s5, s4, 0x1c00000
	v_readlane_b32 s44, v254, 32
	v_readlane_b32 s45, v254, 33
	s_add_u32 s7, s44, s5
	s_addc_u32 s31, s45, 0
	s_mul_i32 s4, s4, 0x700000
	s_add_u32 s4, s36, s4
	s_addc_u32 s5, s37, 0
	s_bfe_u32 s6, s0, 0xb0005
	s_mulk_i32 s6, 0x2493
	s_lshr_b32 s6, s6, 16
	s_mul_i32 s40, s6, 0xe0
	v_readlane_b32 s41, v254, 29
	s_sub_i32 s40, s0, s40
	s_lshl_b32 s0, s40, 5
	s_and_b32 s41, s40, 0xffff
	s_cmpk_gt_u32 s41, 0x6f
	v_readlane_b32 s42, v254, 30
	s_cselect_b32 s41, 0xfffff200, 0
	s_cselect_b32 s42, 0x80, 0
	s_add_i32 s0, s41, s0
	s_sext_i32_i16 s41, s0
	s_bfe_u32 s41, s41, 0x70018
	v_readlane_b32 s43, v254, 31
	s_add_i32 s41, s0, s41
	s_sext_i32_i16 s43, s41
	s_and_b32 s41, s41, 0xff80
	s_sub_i32 s0, s0, s41
	s_lshl_b32 s43, s43, 1
	s_sext_i32_i16 s0, s0
	s_and_b32 s43, s43, 0xffffff00
	s_add_i32 s0, s42, s0
	s_lshl_b32 s40, s40, 7
	s_add_i32 s0, s0, s43
	s_lshl_b32 s6, s6, 6
	s_and_b32 s40, s40, 0x3ff80
	s_add_u32 s40, s7, s40
	s_addc_u32 s41, s31, 0
	v_add_u32_e32 v50, s6, v30
	v_lshl_add_u64 v[28:29], s[40:41], 0, v[0:1]
	v_mad_i64_i32 v[48:49], s[40:41], v50, s14, v[28:29]
	global_load_dword v51, v[48:49], off nt
	v_add_u32_e32 v48, 2, v50
	v_mad_i64_i32 v[48:49], s[40:41], v48, s14, v[28:29]
	global_load_dword v52, v[48:49], off nt
	v_add_u32_e32 v48, 4, v50
	v_mad_i64_i32 v[48:49], s[40:41], v48, s14, v[28:29]
	global_load_dword v53, v[48:49], off nt
	v_add_u32_e32 v48, 6, v50
	v_mad_i64_i32 v[48:49], s[40:41], v48, s14, v[28:29]
	global_load_dword v54, v[48:49], off nt
	v_add_u32_e32 v48, 8, v50
	v_mad_i64_i32 v[48:49], s[40:41], v48, s14, v[28:29]
	global_load_dword v55, v[48:49], off nt
	v_add_u32_e32 v48, 10, v50
	v_mad_i64_i32 v[48:49], s[40:41], v48, s14, v[28:29]
	global_load_dword v56, v[48:49], off nt
	v_add_u32_e32 v48, 12, v50
	v_mad_i64_i32 v[48:49], s[40:41], v48, s14, v[28:29]
	global_load_dword v57, v[48:49], off nt
	v_add_u32_e32 v48, 14, v50
	v_mad_i64_i32 v[48:49], s[40:41], v48, s14, v[28:29]
	global_load_dword v58, v[48:49], off nt
	v_add_u32_e32 v48, 16, v50
	v_mad_i64_i32 v[48:49], s[40:41], v48, s14, v[28:29]
	global_load_dword v59, v[48:49], off nt
	v_add_u32_e32 v48, 18, v50
	v_mad_i64_i32 v[48:49], s[40:41], v48, s14, v[28:29]
	global_load_dword v60, v[48:49], off nt
	v_add_u32_e32 v48, 20, v50
	v_mad_i64_i32 v[48:49], s[40:41], v48, s14, v[28:29]
	global_load_dword v61, v[48:49], off nt
	v_add_u32_e32 v48, 22, v50
	v_mad_i64_i32 v[48:49], s[40:41], v48, s14, v[28:29]
	global_load_dword v62, v[48:49], off nt
	v_add_u32_e32 v48, 24, v50
	v_mad_i64_i32 v[48:49], s[40:41], v48, s14, v[28:29]
	global_load_dword v63, v[48:49], off nt
	v_add_u32_e32 v48, 26, v50
	v_mad_i64_i32 v[48:49], s[40:41], v48, s14, v[28:29]
	global_load_dword v64, v[48:49], off nt
	v_add_u32_e32 v48, 28, v50
	v_mad_i64_i32 v[48:49], s[40:41], v48, s14, v[28:29]
	global_load_dword v65, v[48:49], off nt
	v_add_u32_e32 v48, 30, v50
	v_mad_i64_i32 v[48:49], s[40:41], v48, s14, v[28:29]
	global_load_dword v66, v[48:49], off nt
	v_add_u32_e32 v48, 32, v50
	v_mad_i64_i32 v[48:49], s[40:41], v48, s14, v[28:29]
	global_load_dword v67, v[48:49], off nt
	v_add_u32_e32 v48, 34, v50
	v_mad_i64_i32 v[48:49], s[40:41], v48, s14, v[28:29]
	global_load_dword v68, v[48:49], off nt
	v_add_u32_e32 v48, 36, v50
	v_mad_i64_i32 v[48:49], s[40:41], v48, s14, v[28:29]
	global_load_dword v69, v[48:49], off nt
	v_add_u32_e32 v48, 38, v50
	v_mad_i64_i32 v[48:49], s[40:41], v48, s14, v[28:29]
	global_load_dword v70, v[48:49], off nt
	v_add_u32_e32 v48, 40, v50
	v_mad_i64_i32 v[48:49], s[40:41], v48, s14, v[28:29]
	global_load_dword v71, v[48:49], off nt
	v_add_u32_e32 v48, 42, v50
	v_mad_i64_i32 v[48:49], s[40:41], v48, s14, v[28:29]
	global_load_dword v72, v[48:49], off nt
	v_add_u32_e32 v48, 44, v50
	v_mad_i64_i32 v[48:49], s[40:41], v48, s14, v[28:29]
	global_load_dword v73, v[48:49], off nt
	v_add_u32_e32 v48, 46, v50
	v_mad_i64_i32 v[48:49], s[40:41], v48, s14, v[28:29]
	global_load_dword v74, v[48:49], off nt
	v_add_u32_e32 v48, 48, v50
	v_mad_i64_i32 v[48:49], s[40:41], v48, s14, v[28:29]
	global_load_dword v75, v[48:49], off nt
	v_add_u32_e32 v48, 50, v50
	v_mad_i64_i32 v[48:49], s[40:41], v48, s14, v[28:29]
	global_load_dword v76, v[48:49], off nt
	v_add_u32_e32 v48, 52, v50
	v_mad_i64_i32 v[48:49], s[40:41], v48, s14, v[28:29]
	global_load_dword v77, v[48:49], off nt
	v_add_u32_e32 v48, 54, v50
	v_mad_i64_i32 v[48:49], s[40:41], v48, s14, v[28:29]
	global_load_dword v78, v[48:49], off nt
	v_add_u32_e32 v48, 56, v50
	v_mad_i64_i32 v[48:49], s[40:41], v48, s14, v[28:29]
	global_load_dword v79, v[48:49], off nt
	v_add_u32_e32 v48, 58, v50
	v_mad_i64_i32 v[48:49], s[40:41], v48, s14, v[28:29]
	global_load_dword v80, v[48:49], off nt
	v_add_u32_e32 v48, 60, v50
	v_mad_i64_i32 v[48:49], s[40:41], v48, s14, v[28:29]
	global_load_dword v48, v[48:49], off nt
	v_add_u32_e32 v49, 62, v50
	v_mad_i64_i32 v[28:29], s[40:41], v49, s14, v[28:29]
	global_load_dword v28, v[28:29], off nt
	s_waitcnt vmcnt(31)
; __device__ __forceinline__ unsigned cvt_pk4_fp8(float a, float b, float c, float d) { int w = 0; w = __builtin_amdgcn_cvt_pk_fp8_f32(a, b, w, false); w = __builtin_amdgcn_cvt_pk_fp8_f32(c, d, w, true); return (unsigned)w; }
; #define GAS __attribute__((address_space(1)))
; #define LAS __attribute__((address_space(3)))
; #define LDS_WAIT() asm volatile("s_waitcnt lgkmcnt(0)" ::: "memory")
; __device__ __forceinline__ void tr_item8(const float* W, int ld, int K, int nblk, int item, unsigned char* WT, bool gu, float scale, LAS float* scr, int lane) {
;     ...
; #pragma unroll
;       for (int i = 0; i < 32; ++i) scr[(2 * i + (lane >> 5)) * 33 + (lane & 31)] = t_[i] * scale; }
;     LDS_WAIT(); asm volatile("" ::: "memory");
;     const int c = lane & 3;
; #pragma unroll
;     for (int j = 0; j < 2; ++j) { const int n = (lane >> 2) + 16 * j; const LAS float* sp = scr + (16 * c) * 33 + n;
;         v4u o; o.x = pg8::cvt_pk4_fp8(sp[0 * 33], sp[1 * 33], sp[2 * 33], sp[3 * 33]); o.y = pg8::cvt_pk4_fp8(sp[4 * 33], sp[5 * 33], sp[6 * 33], sp[7 * 33]);
;         o.z = pg8::cvt_pk4_fp8(sp[8 * 33], sp[9 * 33], sp[10 * 33], sp[11 * 33]); o.w = pg8::cvt_pk4_fp8(sp[12 * 33], sp[13 * 33], sp[14 * 33], sp[15 * 33]);
;         *(GAS v4u*)(WT + (size_t)(drow0 + n) * K + k0 + 16 * c) = o; }
;     LDS_WAIT(); asm volatile("" ::: "memory");
	v_mul_f32_e32 v29, 0x42800000, v51
	s_waitcnt vmcnt(30)
	v_mul_f32_e32 v49, 0x42800000, v52
	ds_write2_b32 v31, v29, v49 offset1:66
	s_waitcnt vmcnt(29)
	v_mul_f32_e32 v29, 0x42800000, v53
	s_waitcnt vmcnt(28)
	v_mul_f32_e32 v49, 0x42800000, v54
	ds_write2_b32 v31, v29, v49 offset0:132 offset1:198
	s_waitcnt vmcnt(27)
	v_mul_f32_e32 v29, 0x42800000, v55
	s_waitcnt vmcnt(26)
	v_mul_f32_e32 v49, 0x42800000, v56
	ds_write2_b32 v40, v29, v49 offset0:8 offset1:74
	s_waitcnt vmcnt(25)
	v_mul_f32_e32 v29, 0x42800000, v57
	s_waitcnt vmcnt(24)
	v_mul_f32_e32 v49, 0x42800000, v58
	ds_write2_b32 v40, v29, v49 offset0:140 offset1:206
	s_waitcnt vmcnt(23)
	v_mul_f32_e32 v29, 0x42800000, v59
	s_waitcnt vmcnt(22)
	v_mul_f32_e32 v49, 0x42800000, v60
	ds_write2_b32 v41, v29, v49 offset0:16 offset1:82
	s_waitcnt vmcnt(21)
	v_mul_f32_e32 v29, 0x42800000, v61
	s_waitcnt vmcnt(20)
	v_mul_f32_e32 v49, 0x42800000, v62
	ds_write2_b32 v41, v29, v49 offset0:148 offset1:214
	s_waitcnt vmcnt(19)
	v_mul_f32_e32 v29, 0x42800000, v63
	s_waitcnt vmcnt(18)
	v_mul_f32_e32 v49, 0x42800000, v64
	ds_write2_b32 v42, v29, v49 offset0:24 offset1:90
	s_waitcnt vmcnt(17)
	v_mul_f32_e32 v29, 0x42800000, v65
	s_waitcnt vmcnt(16)
	v_mul_f32_e32 v49, 0x42800000, v66
	ds_write2_b32 v42, v29, v49 offset0:156 offset1:222
	s_waitcnt vmcnt(15)
	v_mul_f32_e32 v29, 0x42800000, v67
	s_waitcnt vmcnt(14)
	v_mul_f32_e32 v49, 0x42800000, v68
	ds_write2_b32 v43, v29, v49 offset0:32 offset1:98
	s_waitcnt vmcnt(13)
	v_mul_f32_e32 v29, 0x42800000, v69
	v_mov_b32_e32 v50, v1
	v_mov_b32_e32 v51, v1
	s_add_u32 s4, s4, s6
	s_waitcnt vmcnt(12)
	v_mul_f32_e32 v49, 0x42800000, v70
	ds_write2_b32 v43, v29, v49 offset0:164 offset1:230
	v_add_u32_e32 v84, s0, v32
	s_addc_u32 s5, s5, 0
	s_waitcnt vmcnt(11)
	v_mul_f32_e32 v29, 0x42800000, v71
	v_ashrrev_i32_e32 v85, 31, v84
	v_lshlrev_b64 v[84:85], 10, v[84:85]
	v_readlane_b32 s46, v254, 34
	s_waitcnt vmcnt(10)
	v_mul_f32_e32 v49, 0x42800000, v72
	ds_write2_b32 v44, v29, v49 offset0:40 offset1:106
	v_readlane_b32 s47, v254, 35
	s_waitcnt vmcnt(9)
	v_mul_f32_e32 v29, 0x42800000, v73
	s_waitcnt vmcnt(8)
	v_mul_f32_e32 v49, 0x42800000, v74
	ds_write2_b32 v44, v29, v49 offset0:172 offset1:238
	s_waitcnt vmcnt(7)
	v_mul_f32_e32 v29, 0x42800000, v75
	s_waitcnt vmcnt(6)
	v_mul_f32_e32 v49, 0x42800000, v76
	ds_write2_b32 v45, v29, v49 offset0:48 offset1:114
	s_waitcnt vmcnt(5)
	v_mul_f32_e32 v29, 0x42800000, v77
	s_waitcnt vmcnt(4)
	v_mul_f32_e32 v49, 0x42800000, v78
	ds_write2_b32 v45, v29, v49 offset0:180 offset1:246
	s_waitcnt vmcnt(3)
	v_mul_f32_e32 v29, 0x42800000, v79
	s_waitcnt vmcnt(2)
	v_mul_f32_e32 v49, 0x42800000, v80
	ds_write2_b32 v46, v29, v49 offset0:56 offset1:122
	v_mov_b32_e32 v49, v1
	s_waitcnt vmcnt(1)
	v_mul_f32_e32 v29, 0x42800000, v48
	v_mov_b32_e32 v48, v1
	s_waitcnt vmcnt(0)
	v_mul_f32_e32 v28, 0x42800000, v28
	ds_write2_b32 v46, v29, v28 offset0:188 offset1:254
	s_waitcnt lgkmcnt(0)
	ds_read2_b32 v[52:53], v33 offset1:16
	ds_read2_b32 v[54:55], v33 offset0:33 offset1:49
	ds_read2_b32 v[56:57], v33 offset0:66 offset1:82
	ds_read2_b32 v[58:59], v33 offset0:99 offset1:115
	ds_read2_b32 v[60:61], v33 offset0:132 offset1:148
	ds_read2_b32 v[62:63], v33 offset0:165 offset1:181
	ds_read2_b32 v[64:65], v33 offset0:198 offset1:214
	ds_read2_b32 v[66:67], v33 offset0:231 offset1:247
	ds_read2_b32 v[68:69], v47 offset0:8 offset1:24
	ds_read2_b32 v[70:71], v47 offset0:41 offset1:57
	ds_read2_b32 v[72:73], v47 offset0:74 offset1:90
	ds_read2_b32 v[74:75], v47 offset0:107 offset1:123
	ds_read2_b32 v[76:77], v47 offset0:140 offset1:156
	ds_read2_b32 v[78:79], v47 offset0:173 offset1:189
	ds_read2_b32 v[80:81], v47 offset0:206 offset1:222
	ds_read2_b32 v[82:83], v47 offset0:239 offset1:255
	s_waitcnt lgkmcnt(14)
	v_cvt_pk_fp8_f32 v48, v52, v54
	s_waitcnt lgkmcnt(10)
	v_cvt_pk_fp8_f32 v49, v60, v62
	s_waitcnt lgkmcnt(6)
	v_cvt_pk_fp8_f32 v50, v68, v70
	s_waitcnt lgkmcnt(2)
	v_cvt_pk_fp8_f32 v51, v76, v78
	v_cvt_pk_fp8_f32 v48, v56, v58 op_sel:[0,0,1]
	v_cvt_pk_fp8_f32 v49, v64, v66 op_sel:[0,0,1]
	v_cvt_pk_fp8_f32 v50, v72, v74 op_sel:[0,0,1]
	s_waitcnt lgkmcnt(0)
	v_cvt_pk_fp8_f32 v51, v80, v82 op_sel:[0,0,1]
	v_lshl_add_u64 v[28:29], s[4:5], 0, v[2:3]
	v_lshl_add_u64 v[84:85], v[28:29], 0, v[84:85]
	v_add_u32_e32 v52, s0, v34
	global_store_dwordx4 v[84:85], v[48:51], off sc1 nt
	s_nop 1
	v_mov_b32_e32 v48, v1
	v_mov_b32_e32 v49, v1
	v_mov_b32_e32 v50, v1
	v_mov_b32_e32 v51, v1
	v_cvt_pk_fp8_f32 v48, v53, v55
	v_cvt_pk_fp8_f32 v49, v61, v63
	v_cvt_pk_fp8_f32 v50, v69, v71
	v_cvt_pk_fp8_f32 v51, v77, v79
	v_cvt_pk_fp8_f32 v48, v57, v59 op_sel:[0,0,1]
	v_cvt_pk_fp8_f32 v49, v65, v67 op_sel:[0,0,1]
	v_cvt_pk_fp8_f32 v50, v73, v75 op_sel:[0,0,1]
	v_cvt_pk_fp8_f32 v51, v81, v83 op_sel:[0,0,1]
	v_ashrrev_i32_e32 v53, 31, v52
	v_lshlrev_b64 v[52:53], 10, v[52:53]
	v_lshl_add_u64 v[28:29], v[28:29], 0, v[52:53]
	global_store_dwordx4 v[28:29], v[48:51], off sc1 nt
	s_waitcnt lgkmcnt(0)

; #define LAS __attribute__((address_space(3)))
; __device__ __forceinline__ void tr_item8(const float* W, int ld, int K, int nblk, int item, unsigned char* WT, bool gu, float scale, LAS float* scr, int lane) {
;     const int kb = item / nblk, nb = item % nblk, k0 = 64 * kb, n0 = 32 * nb;
;     int drow0 = n0;
;     if (gu) { const int bj = n0 / FF, j = n0 - bj * FF; drow0 = 256 * (j / 128) + 128 * bj + (j % 128); }
;     { float t_[32];
; #pragma unroll
;       for (int i = 0; i < 32; ++i) t_[i] = W[(size_t)(k0 + 2 * i + (lane >> 5)) * ld + n0 + (lane & 31)];
; #pragma unroll
;       for (int i = 0; i < 32; ++i) scr[(2 * i + (lane >> 5)) * 33 + (lane & 31)] = t_[i] * scale; }
; __device__ __forceinline__ void convert_items(Frame& F, const Args& a, int lo, int hi, int w, int nw) {
;     ...
;         if (r < I_DN) { tr_item8(a.in[15], D, FF, 32, r, F.ws + WS_WDN, false, WSC_DN, scr, lane); continue; } r -= I_DN;
.LBB0_1307:
	s_andn2_b64 vcc, exec, s[4:5]
	s_cbranch_vccnz .LBB0_1309
	s_lshl_b32 s0, s8, 5
	s_and_b32 s4, s11, 0x1ffc0
	s_and_b32 s6, s0, 0x3e0
	v_add_u32_e32 v28, s4, v30
	s_lshl_b32 s0, s6, 2
	v_ashrrev_i32_e32 v29, 31, v28
	v_lshl_add_u64 v[48:49], v[4:5], 0, s[0:1]
	v_lshlrev_b64 v[28:29], 12, v[28:29]
	v_lshl_add_u64 v[28:29], v[48:49], 0, v[28:29]
	v_add_co_u32_e32 v48, vcc, 0x2000, v28
	global_load_dword v50, v[28:29], off nt
	s_nop 0
	v_addc_co_u32_e32 v49, vcc, 0, v29, vcc
	global_load_dword v51, v[48:49], off nt
	v_add_co_u32_e32 v48, vcc, 0x4000, v28
	s_mov_b32 s5, s1
	s_nop 0
	v_addc_co_u32_e32 v49, vcc, 0, v29, vcc
	global_load_dword v52, v[48:49], off nt
	v_add_co_u32_e32 v48, vcc, 0x6000, v28
	s_nop 1
	v_addc_co_u32_e32 v49, vcc, 0, v29, vcc
	global_load_dword v53, v[48:49], off nt
	v_add_co_u32_e32 v48, vcc, 0x8000, v28
	s_nop 1
	v_addc_co_u32_e32 v49, vcc, 0, v29, vcc
	global_load_dword v54, v[48:49], off nt
	v_add_co_u32_e32 v48, vcc, 0xa000, v28
	s_nop 1
	v_addc_co_u32_e32 v49, vcc, 0, v29, vcc
	global_load_dword v55, v[48:49], off nt
	v_add_co_u32_e32 v48, vcc, 0xc000, v28
	s_nop 1
	v_addc_co_u32_e32 v49, vcc, 0, v29, vcc
	global_load_dword v56, v[48:49], off nt
	v_add_co_u32_e32 v48, vcc, 0xe000, v28
	s_nop 1
	v_addc_co_u32_e32 v49, vcc, 0, v29, vcc
	global_load_dword v57, v[48:49], off nt
	v_add_co_u32_e32 v48, vcc, 0x10000, v28
	s_nop 1
	v_addc_co_u32_e32 v49, vcc, 0, v29, vcc
	global_load_dword v58, v[48:49], off nt
	v_add_co_u32_e32 v48, vcc, 0x12000, v28
	s_nop 1
	v_addc_co_u32_e32 v49, vcc, 0, v29, vcc
	global_load_dword v59, v[48:49], off nt
	v_add_co_u32_e32 v48, vcc, 0x14000, v28
	s_nop 1
	v_addc_co_u32_e32 v49, vcc, 0, v29, vcc
	global_load_dword v60, v[48:49], off nt
	v_add_co_u32_e32 v48, vcc, 0x16000, v28
	s_nop 1
	v_addc_co_u32_e32 v49, vcc, 0, v29, vcc
	global_load_dword v61, v[48:49], off nt
	v_add_co_u32_e32 v48, vcc, 0x18000, v28
	s_nop 1
	v_addc_co_u32_e32 v49, vcc, 0, v29, vcc
	global_load_dword v62, v[48:49], off nt
	v_add_co_u32_e32 v48, vcc, 0x1a000, v28
	s_nop 1
	v_addc_co_u32_e32 v49, vcc, 0, v29, vcc
	global_load_dword v63, v[48:49], off nt
	v_add_co_u32_e32 v48, vcc, 0x1c000, v28
	s_nop 1
	v_addc_co_u32_e32 v49, vcc, 0, v29, vcc
	global_load_dword v64, v[48:49], off nt
	v_add_co_u32_e32 v48, vcc, 0x1e000, v28
	s_nop 1
	v_addc_co_u32_e32 v49, vcc, 0, v29, vcc
	global_load_dword v65, v[48:49], off nt
	v_add_co_u32_e32 v48, vcc, 0x20000, v28
	s_nop 1
	v_addc_co_u32_e32 v49, vcc, 0, v29, vcc
	global_load_dword v66, v[48:49], off nt
	v_add_co_u32_e32 v48, vcc, 0x22000, v28
	s_nop 1
	v_addc_co_u32_e32 v49, vcc, 0, v29, vcc
	global_load_dword v67, v[48:49], off nt
	v_add_co_u32_e32 v48, vcc, 0x24000, v28
	s_nop 1
	v_addc_co_u32_e32 v49, vcc, 0, v29, vcc
	global_load_dword v68, v[48:49], off nt
	v_add_co_u32_e32 v48, vcc, 0x26000, v28
	s_nop 1
	v_addc_co_u32_e32 v49, vcc, 0, v29, vcc
	global_load_dword v69, v[48:49], off nt
	v_add_co_u32_e32 v48, vcc, 0x28000, v28
	s_nop 1
	v_addc_co_u32_e32 v49, vcc, 0, v29, vcc
	global_load_dword v70, v[48:49], off nt
	v_add_co_u32_e32 v48, vcc, 0x2a000, v28
	s_nop 1
	v_addc_co_u32_e32 v49, vcc, 0, v29, vcc
	global_load_dword v71, v[48:49], off nt
	v_add_co_u32_e32 v48, vcc, 0x2c000, v28
	s_nop 1
	v_addc_co_u32_e32 v49, vcc, 0, v29, vcc
	global_load_dword v72, v[48:49], off nt
	v_add_co_u32_e32 v48, vcc, 0x2e000, v28
	s_nop 1
	v_addc_co_u32_e32 v49, vcc, 0, v29, vcc
	global_load_dword v73, v[48:49], off nt
	v_add_co_u32_e32 v48, vcc, 0x30000, v28
	s_nop 1
	v_addc_co_u32_e32 v49, vcc, 0, v29, vcc
	global_load_dword v74, v[48:49], off nt
	v_add_co_u32_e32 v48, vcc, 0x32000, v28
	s_nop 1
	v_addc_co_u32_e32 v49, vcc, 0, v29, vcc
	global_load_dword v75, v[48:49], off nt
	v_add_co_u32_e32 v48, vcc, 0x34000, v28
	s_nop 1
	v_addc_co_u32_e32 v49, vcc, 0, v29, vcc
	global_load_dword v76, v[48:49], off nt
	v_add_co_u32_e32 v48, vcc, 0x36000, v28
	s_nop 1
	v_addc_co_u32_e32 v49, vcc, 0, v29, vcc
	global_load_dword v77, v[48:49], off nt
	v_add_co_u32_e32 v48, vcc, 0x38000, v28
	s_nop 1
	v_addc_co_u32_e32 v49, vcc, 0, v29, vcc
	global_load_dword v78, v[48:49], off nt
	v_add_co_u32_e32 v48, vcc, 0x3a000, v28
	s_nop 1
	v_addc_co_u32_e32 v49, vcc, 0, v29, vcc
	global_load_dword v79, v[48:49], off nt
	v_add_co_u32_e32 v48, vcc, 0x3c000, v28
	s_nop 1
	v_addc_co_u32_e32 v49, vcc, 0, v29, vcc
	v_add_co_u32_e32 v28, vcc, 0x3e000, v28
	global_load_dword v48, v[48:49], off nt
	s_nop 0
	v_addc_co_u32_e32 v29, vcc, 0, v29, vcc
	global_load_dword v28, v[28:29], off nt
	s_waitcnt vmcnt(31)
	v_mul_f32_e32 v29, 0x43000000, v50
	s_waitcnt vmcnt(30)
; __device__ __forceinline__ unsigned cvt_pk4_fp8(float a, float b, float c, float d) { int w = 0; w = __builtin_amdgcn_cvt_pk_fp8_f32(a, b, w, false); w = __builtin_amdgcn_cvt_pk_fp8_f32(c, d, w, true); return (unsigned)w; }
; #define GAS __attribute__((address_space(1)))
; #define LAS __attribute__((address_space(3)))
; #define LDS_WAIT() asm volatile("s_waitcnt lgkmcnt(0)" ::: "memory")
; __device__ __forceinline__ void tr_item8(const float* W, int ld, int K, int nblk, int item, unsigned char* WT, bool gu, float scale, LAS float* scr, int lane) {
;     ...
; #pragma unroll
;       for (int i = 0; i < 32; ++i) scr[(2 * i + (lane >> 5)) * 33 + (lane & 31)] = t_[i] * scale; }
;     LDS_WAIT(); asm volatile("" ::: "memory");
;     const int c = lane & 3;
; #pragma unroll
;     for (int j = 0; j < 2; ++j) { const int n = (lane >> 2) + 16 * j; const LAS float* sp = scr + (16 * c) * 33 + n;
;         v4u o; o.x = pg8::cvt_pk4_fp8(sp[0 * 33], sp[1 * 33], sp[2 * 33], sp[3 * 33]); o.y = pg8::cvt_pk4_fp8(sp[4 * 33], sp[5 * 33], sp[6 * 33], sp[7 * 33]);
;         o.z = pg8::cvt_pk4_fp8(sp[8 * 33], sp[9 * 33], sp[10 * 33], sp[11 * 33]); o.w = pg8::cvt_pk4_fp8(sp[12 * 33], sp[13 * 33], sp[14 * 33], sp[15 * 33]);
;         *(GAS v4u*)(WT + (size_t)(drow0 + n) * K + k0 + 16 * c) = o; }
;     LDS_WAIT(); asm volatile("" ::: "memory");
	v_mul_f32_e32 v49, 0x43000000, v51
	ds_write2_b32 v31, v29, v49 offset1:66
	s_waitcnt vmcnt(29)
	v_mul_f32_e32 v29, 0x43000000, v52
	s_waitcnt vmcnt(28)
	v_mul_f32_e32 v49, 0x43000000, v53
	ds_write2_b32 v31, v29, v49 offset0:132 offset1:198
	s_waitcnt vmcnt(27)
	v_mul_f32_e32 v29, 0x43000000, v54
	s_waitcnt vmcnt(26)
	v_mul_f32_e32 v49, 0x43000000, v55
	ds_write2_b32 v40, v29, v49 offset0:8 offset1:74
	s_waitcnt vmcnt(25)
	v_mul_f32_e32 v29, 0x43000000, v56
	s_waitcnt vmcnt(24)
	v_mul_f32_e32 v49, 0x43000000, v57
	ds_write2_b32 v40, v29, v49 offset0:140 offset1:206
	s_waitcnt vmcnt(23)
	v_mul_f32_e32 v29, 0x43000000, v58
	s_waitcnt vmcnt(22)
	v_mul_f32_e32 v49, 0x43000000, v59
	ds_write2_b32 v41, v29, v49 offset0:16 offset1:82
	s_waitcnt vmcnt(21)
	v_mul_f32_e32 v29, 0x43000000, v60
	s_waitcnt vmcnt(20)
	v_mul_f32_e32 v49, 0x43000000, v61
	ds_write2_b32 v41, v29, v49 offset0:148 offset1:214
	s_waitcnt vmcnt(19)
	v_mul_f32_e32 v29, 0x43000000, v62
	s_waitcnt vmcnt(18)
	v_mul_f32_e32 v49, 0x43000000, v63
	ds_write2_b32 v42, v29, v49 offset0:24 offset1:90
	s_waitcnt vmcnt(17)
	v_mul_f32_e32 v29, 0x43000000, v64
	s_waitcnt vmcnt(16)
	v_mul_f32_e32 v49, 0x43000000, v65
	ds_write2_b32 v42, v29, v49 offset0:156 offset1:222
	s_waitcnt vmcnt(15)
	v_mul_f32_e32 v29, 0x43000000, v66
	s_waitcnt vmcnt(14)
	v_mul_f32_e32 v49, 0x43000000, v67
	ds_write2_b32 v43, v29, v49 offset0:32 offset1:98
	s_waitcnt vmcnt(13)
	v_mul_f32_e32 v29, 0x43000000, v68
	s_waitcnt vmcnt(12)
	v_mul_f32_e32 v49, 0x43000000, v69
	ds_write2_b32 v43, v29, v49 offset0:164 offset1:230
	s_waitcnt vmcnt(11)
	v_mul_f32_e32 v29, 0x43000000, v70
	s_waitcnt vmcnt(10)
	v_mul_f32_e32 v49, 0x43000000, v71
	ds_write2_b32 v44, v29, v49 offset0:40 offset1:106
	s_waitcnt vmcnt(9)
	v_mul_f32_e32 v29, 0x43000000, v72
	s_waitcnt vmcnt(8)
	v_mul_f32_e32 v49, 0x43000000, v73
	ds_write2_b32 v44, v29, v49 offset0:172 offset1:238
	v_mov_b32_e32 v50, 0
	v_mov_b32_e32 v51, 0
	s_waitcnt vmcnt(7)
	v_mul_f32_e32 v29, 0x43000000, v74
	s_waitcnt vmcnt(6)
	v_mul_f32_e32 v49, 0x43000000, v75
	ds_write2_b32 v45, v29, v49 offset0:48 offset1:114
	s_waitcnt vmcnt(5)
	v_mul_f32_e32 v29, 0x43000000, v76
	s_waitcnt vmcnt(4)
	v_mul_f32_e32 v49, 0x43000000, v77
	ds_write2_b32 v45, v29, v49 offset0:180 offset1:246
	s_waitcnt vmcnt(3)
	v_mul_f32_e32 v29, 0x43000000, v78
	s_waitcnt vmcnt(2)
	v_mul_f32_e32 v49, 0x43000000, v79
	ds_write2_b32 v46, v29, v49 offset0:56 offset1:122
	v_mov_b32_e32 v49, 0
	s_waitcnt vmcnt(1)
	v_mul_f32_e32 v29, 0x43000000, v48
	v_mov_b32_e32 v48, 0
	s_waitcnt vmcnt(0)
	v_mul_f32_e32 v28, 0x43000000, v28
	ds_write2_b32 v46, v29, v28 offset0:188 offset1:254
	s_waitcnt lgkmcnt(0)
	ds_read2_b32 v[52:53], v33 offset1:16
	ds_read2_b32 v[54:55], v33 offset0:33 offset1:49
	ds_read2_b32 v[56:57], v33 offset0:66 offset1:82
	ds_read2_b32 v[58:59], v33 offset0:99 offset1:115
	ds_read2_b32 v[60:61], v33 offset0:132 offset1:148
	ds_read2_b32 v[62:63], v33 offset0:165 offset1:181
	ds_read2_b32 v[64:65], v33 offset0:198 offset1:214
	ds_read2_b32 v[66:67], v33 offset0:231 offset1:247
	ds_read2_b32 v[68:69], v47 offset0:8 offset1:24
	ds_read2_b32 v[70:71], v47 offset0:41 offset1:57
	ds_read2_b32 v[72:73], v47 offset0:74 offset1:90
	ds_read2_b32 v[74:75], v47 offset0:107 offset1:123
	ds_read2_b32 v[76:77], v47 offset0:140 offset1:156
	ds_read2_b32 v[78:79], v47 offset0:173 offset1:189
	ds_read2_b32 v[80:81], v47 offset0:206 offset1:222
	ds_read2_b32 v[82:83], v47 offset0:239 offset1:255
	s_waitcnt lgkmcnt(14)
	v_cvt_pk_fp8_f32 v48, v52, v54
	s_waitcnt lgkmcnt(10)
	v_cvt_pk_fp8_f32 v49, v60, v62
	s_waitcnt lgkmcnt(6)
	v_cvt_pk_fp8_f32 v50, v68, v70
	s_waitcnt lgkmcnt(2)
	v_cvt_pk_fp8_f32 v51, v76, v78
	v_cvt_pk_fp8_f32 v48, v56, v58 op_sel:[0,0,1]
	v_cvt_pk_fp8_f32 v49, v64, v66 op_sel:[0,0,1]
	v_cvt_pk_fp8_f32 v50, v72, v74 op_sel:[0,0,1]
	s_waitcnt lgkmcnt(0)
	v_cvt_pk_fp8_f32 v51, v80, v82 op_sel:[0,0,1]
	v_lshl_add_u64 v[28:29], v[16:17], 0, s[4:5]
	v_add_u32_e32 v52, s6, v32
	v_mad_i64_i32 v[84:85], s[4:5], v52, s13, v[28:29]
	global_store_dwordx4 v[84:85], v[48:51], off sc1 nt
	v_add_u32_e32 v52, s6, v34
	v_mad_i64_i32 v[28:29], s[4:5], v52, s13, v[28:29]
	v_mov_b32_e32 v48, 0
	v_mov_b32_e32 v49, 0
	v_mov_b32_e32 v50, 0
	v_mov_b32_e32 v51, 0
	v_cvt_pk_fp8_f32 v48, v53, v55
	v_cvt_pk_fp8_f32 v49, v61, v63
	v_cvt_pk_fp8_f32 v50, v69, v71
	v_cvt_pk_fp8_f32 v51, v77, v79
	v_cvt_pk_fp8_f32 v48, v57, v59 op_sel:[0,0,1]
	v_cvt_pk_fp8_f32 v49, v65, v67 op_sel:[0,0,1]
	v_cvt_pk_fp8_f32 v50, v73, v75 op_sel:[0,0,1]
	v_cvt_pk_fp8_f32 v51, v81, v83 op_sel:[0,0,1]
	global_store_dwordx4 v[28:29], v[48:51], off sc1 nt
	s_waitcnt lgkmcnt(0)

; #define LAS __attribute__((address_space(3)))
; __device__ __forceinline__ void tr_item8(const float* W, int ld, int K, int nblk, int item, unsigned char* WT, bool gu, float scale, LAS float* scr, int lane) {
;     const int kb = item / nblk, nb = item % nblk, k0 = 64 * kb, n0 = 32 * nb;
;     int drow0 = n0;
;     if (gu) { const int bj = n0 / FF, j = n0 - bj * FF; drow0 = 256 * (j / 128) + 128 * bj + (j % 128); }
;     { float t_[32];
; #pragma unroll
;       for (int i = 0; i < 32; ++i) t_[i] = W[(size_t)(k0 + 2 * i + (lane >> 5)) * ld + n0 + (lane & 31)];
; __device__ __forceinline__ void convert_items(Frame& F, const Args& a, int lo, int hi, int w, int nw) {
;     ...
;         if (r < I_GU) { tr_item8(a.in[14], 2 * FF, D, 224, r, F.ws + WS_WGU, true, WSC_GU, scr, lane); continue; } r -= I_GU;
.LBB0_1310:
	s_andn2_b64 vcc, exec, s[4:5]
	s_cbranch_vccnz .LBB0_1312
	s_add_i32 s0, s8, 0xf300
	s_bfe_u32 s4, s0, 0xb0005
	s_mulk_i32 s4, 0x2493
	s_lshr_b32 s4, s4, 16
	s_mul_i32 s5, s4, 0xe0
	s_sub_i32 s0, s0, s5
	s_lshl_b32 s5, s0, 5
	s_and_b32 s6, s0, 0xffff
	s_cmpk_gt_u32 s6, 0x6f
	s_cselect_b32 s31, 0xfffff200, 0
	s_cselect_b32 s40, 0x80, 0
	s_lshl_b32 s0, s0, 7
	s_lshl_b32 s4, s4, 6
	s_and_b32 s0, s0, 0x3ff80
	v_add_u32_e32 v64, s4, v30
	v_lshl_add_u64 v[28:29], v[6:7], 0, s[0:1]
	v_mad_i64_i32 v[48:49], s[6:7], v64, s14, v[28:29]
	v_add_u32_e32 v50, 2, v64
	v_add_u32_e32 v52, 4, v64
	v_add_u32_e32 v54, 6, v64
	v_add_u32_e32 v56, 8, v64
	v_add_u32_e32 v58, 10, v64
	v_add_u32_e32 v60, 12, v64
	v_add_u32_e32 v62, 14, v64
	v_mad_i64_i32 v[50:51], s[6:7], v50, s14, v[28:29]
	v_mad_i64_i32 v[52:53], s[6:7], v52, s14, v[28:29]
	v_mad_i64_i32 v[54:55], s[6:7], v54, s14, v[28:29]
	v_mad_i64_i32 v[56:57], s[6:7], v56, s14, v[28:29]
	v_mad_i64_i32 v[58:59], s[6:7], v58, s14, v[28:29]
	v_mad_i64_i32 v[60:61], s[6:7], v60, s14, v[28:29]
	v_mad_i64_i32 v[62:63], s[6:7], v62, s14, v[28:29]
	global_load_dword v65, v[48:49], off nt
	global_load_dword v66, v[50:51], off nt
	global_load_dword v67, v[52:53], off nt
	global_load_dword v68, v[54:55], off nt
	global_load_dword v69, v[56:57], off nt
	global_load_dword v70, v[58:59], off nt
	global_load_dword v71, v[60:61], off nt
	global_load_dword v72, v[62:63], off nt
	v_add_u32_e32 v48, 16, v64
	v_mad_i64_i32 v[48:49], s[6:7], v48, s14, v[28:29]
	v_add_u32_e32 v50, 18, v64
	v_add_u32_e32 v52, 20, v64
	v_add_u32_e32 v54, 22, v64
	v_add_u32_e32 v56, 24, v64
	v_add_u32_e32 v58, 26, v64
	v_add_u32_e32 v60, 28, v64
	v_add_u32_e32 v62, 30, v64
	v_mad_i64_i32 v[50:51], s[6:7], v50, s14, v[28:29]
	v_mad_i64_i32 v[52:53], s[6:7], v52, s14, v[28:29]
	v_mad_i64_i32 v[54:55], s[6:7], v54, s14, v[28:29]
	v_mad_i64_i32 v[56:57], s[6:7], v56, s14, v[28:29]
	v_mad_i64_i32 v[58:59], s[6:7], v58, s14, v[28:29]
	v_mad_i64_i32 v[60:61], s[6:7], v60, s14, v[28:29]
	v_mad_i64_i32 v[62:63], s[6:7], v62, s14, v[28:29]
	global_load_dword v73, v[48:49], off nt
	global_load_dword v74, v[50:51], off nt
	global_load_dword v75, v[52:53], off nt
	global_load_dword v76, v[54:55], off nt
	global_load_dword v77, v[56:57], off nt
	global_load_dword v78, v[58:59], off nt
	global_load_dword v79, v[60:61], off nt
	global_load_dword v80, v[62:63], off nt
	v_add_u32_e32 v48, 32, v64
	v_add_u32_e32 v50, 34, v64
	v_add_u32_e32 v52, 36, v64
	v_add_u32_e32 v54, 38, v64
	v_add_u32_e32 v60, 44, v64
	v_mad_i64_i32 v[48:49], s[6:7], v48, s14, v[28:29]
	v_mad_i64_i32 v[50:51], s[6:7], v50, s14, v[28:29]
	v_mad_i64_i32 v[52:53], s[6:7], v52, s14, v[28:29]
	v_mad_i64_i32 v[54:55], s[6:7], v54, s14, v[28:29]
	v_add_u32_e32 v56, 40, v64
	v_add_u32_e32 v58, 42, v64
	v_mad_i64_i32 v[60:61], s[6:7], v60, s14, v[28:29]
	v_add_u32_e32 v62, 46, v64
	v_mad_i64_i32 v[56:57], s[6:7], v56, s14, v[28:29]
	v_mad_i64_i32 v[58:59], s[6:7], v58, s14, v[28:29]
	v_mad_i64_i32 v[62:63], s[6:7], v62, s14, v[28:29]
	global_load_dword v81, v[48:49], off nt
	global_load_dword v82, v[50:51], off nt
	global_load_dword v83, v[52:53], off nt
	global_load_dword v84, v[54:55], off nt
	global_load_dword v85, v[56:57], off nt
	global_load_dword v86, v[58:59], off nt
	s_nop 0
	global_load_dword v60, v[60:61], off nt
	s_nop 0
	global_load_dword v61, v[62:63], off nt
	v_add_u32_e32 v48, 48, v64
	v_add_u32_e32 v50, 50, v64
	v_add_u32_e32 v52, 52, v64
	v_add_u32_e32 v54, 54, v64
	v_mad_i64_i32 v[48:49], s[6:7], v48, s14, v[28:29]
	v_mad_i64_i32 v[50:51], s[6:7], v50, s14, v[28:29]
	v_mad_i64_i32 v[52:53], s[6:7], v52, s14, v[28:29]
	v_mad_i64_i32 v[54:55], s[6:7], v54, s14, v[28:29]
	v_add_u32_e32 v56, 56, v64
	v_add_u32_e32 v58, 58, v64
	v_mad_i64_i32 v[56:57], s[6:7], v56, s14, v[28:29]
	v_mad_i64_i32 v[58:59], s[6:7], v58, s14, v[28:29]
	global_load_dword v62, v[48:49], off nt
	s_nop 0
	global_load_dword v50, v[50:51], off nt
	s_nop 0
	global_load_dword v51, v[52:53], off nt
	s_nop 0
	global_load_dword v52, v[54:55], off nt
	global_load_dword v53, v[56:57], off nt
	s_nop 0
	global_load_dword v54, v[58:59], off nt
	v_add_u32_e32 v48, 60, v64
	v_add_u32_e32 v55, 62, v64
	v_mad_i64_i32 v[48:49], s[6:7], v48, s14, v[28:29]
	v_mad_i64_i32 v[28:29], s[6:7], v55, s14, v[28:29]
	global_load_dword v48, v[48:49], off nt
	s_nop 0
	global_load_dword v28, v[28:29], off nt
	s_waitcnt vmcnt(31)
	v_mul_f32_e32 v29, 0x42800000, v65
	s_waitcnt vmcnt(30)
	v_mul_f32_e32 v49, 0x42800000, v66
	ds_write2_b32 v31, v29, v49 offset1:66
	s_waitcnt vmcnt(29)
	v_mul_f32_e32 v29, 0x42800000, v67
	s_waitcnt vmcnt(28)
	v_mul_f32_e32 v49, 0x42800000, v68
	ds_write2_b32 v31, v29, v49 offset0:132 offset1:198
	s_waitcnt vmcnt(27)
	v_mul_f32_e32 v29, 0x42800000, v69
	s_waitcnt vmcnt(26)
; __device__ __forceinline__ unsigned cvt_pk4_fp8(float a, float b, float c, float d) { int w = 0; w = __builtin_amdgcn_cvt_pk_fp8_f32(a, b, w, false); w = __builtin_amdgcn_cvt_pk_fp8_f32(c, d, w, true); return (unsigned)w; }
; #define GAS __attribute__((address_space(1)))
; #define LAS __attribute__((address_space(3)))
; #define LDS_WAIT() asm volatile("s_waitcnt lgkmcnt(0)" ::: "memory")
; __device__ __forceinline__ void tr_item8(const float* W, int ld, int K, int nblk, int item, unsigned char* WT, bool gu, float scale, LAS float* scr, int lane) {
;     ...
; #pragma unroll
;       for (int i = 0; i < 32; ++i) scr[(2 * i + (lane >> 5)) * 33 + (lane & 31)] = t_[i] * scale; }
;     LDS_WAIT(); asm volatile("" ::: "memory");
;     const int c = lane & 3;
; #pragma unroll
;     for (int j = 0; j < 2; ++j) { const int n = (lane >> 2) + 16 * j; const LAS float* sp = scr + (16 * c) * 33 + n;
;         v4u o; o.x = pg8::cvt_pk4_fp8(sp[0 * 33], sp[1 * 33], sp[2 * 33], sp[3 * 33]); o.y = pg8::cvt_pk4_fp8(sp[4 * 33], sp[5 * 33], sp[6 * 33], sp[7 * 33]);
;         o.z = pg8::cvt_pk4_fp8(sp[8 * 33], sp[9 * 33], sp[10 * 33], sp[11 * 33]); o.w = pg8::cvt_pk4_fp8(sp[12 * 33], sp[13 * 33], sp[14 * 33], sp[15 * 33]);
;         *(GAS v4u*)(WT + (size_t)(drow0 + n) * K + k0 + 16 * c) = o; }
;     LDS_WAIT(); asm volatile("" ::: "memory");
	v_mul_f32_e32 v49, 0x42800000, v70
	ds_write2_b32 v40, v29, v49 offset0:8 offset1:74
	s_waitcnt vmcnt(25)
	v_mul_f32_e32 v29, 0x42800000, v71
	s_waitcnt vmcnt(24)
	v_mul_f32_e32 v49, 0x42800000, v72
	ds_write2_b32 v40, v29, v49 offset0:140 offset1:206
	s_add_i32 s0, s31, s5
	s_sext_i32_i16 s5, s0
	s_bfe_u32 s5, s5, 0x70018
	s_add_i32 s5, s0, s5
	s_sext_i32_i16 s6, s5
	s_and_b32 s5, s5, 0xff80
	s_sub_i32 s0, s0, s5
	s_lshl_b32 s6, s6, 1
	s_sext_i32_i16 s0, s0
	s_waitcnt vmcnt(23)
	v_mul_f32_e32 v29, 0x42800000, v73
	s_waitcnt vmcnt(22)
	v_mul_f32_e32 v49, 0x42800000, v74
	ds_write2_b32 v41, v29, v49 offset0:16 offset1:82
	s_waitcnt vmcnt(21)
	v_mul_f32_e32 v29, 0x42800000, v75
	s_waitcnt vmcnt(20)
	v_mul_f32_e32 v49, 0x42800000, v76
	ds_write2_b32 v41, v29, v49 offset0:148 offset1:214
	s_waitcnt vmcnt(19)
	v_mul_f32_e32 v29, 0x42800000, v77
	s_waitcnt vmcnt(18)
	v_mul_f32_e32 v49, 0x42800000, v78
	ds_write2_b32 v42, v29, v49 offset0:24 offset1:90
	s_waitcnt vmcnt(17)
	v_mul_f32_e32 v29, 0x42800000, v79
	s_waitcnt vmcnt(16)
	v_mul_f32_e32 v49, 0x42800000, v80
	ds_write2_b32 v42, v29, v49 offset0:156 offset1:222
	s_and_b32 s6, s6, 0xffffff00
	s_add_i32 s0, s40, s0
	s_add_i32 s0, s0, s6
	s_mov_b32 s5, s1
	s_waitcnt vmcnt(15)
	v_mul_f32_e32 v29, 0x42800000, v81
	s_waitcnt vmcnt(14)
	v_mul_f32_e32 v49, 0x42800000, v82
	ds_write2_b32 v43, v29, v49 offset0:32 offset1:98
	s_waitcnt vmcnt(13)
	v_mul_f32_e32 v29, 0x42800000, v83
	s_waitcnt vmcnt(12)
	v_mul_f32_e32 v49, 0x42800000, v84
	ds_write2_b32 v43, v29, v49 offset0:164 offset1:230
	s_waitcnt vmcnt(11)
	v_mul_f32_e32 v29, 0x42800000, v85
	s_waitcnt vmcnt(10)
	v_mul_f32_e32 v49, 0x42800000, v86
	ds_write2_b32 v44, v29, v49 offset0:40 offset1:106
	s_waitcnt vmcnt(9)
	v_mul_f32_e32 v29, 0x42800000, v60
	s_waitcnt vmcnt(8)
	v_mul_f32_e32 v49, 0x42800000, v61
	ds_write2_b32 v44, v29, v49 offset0:172 offset1:238
	v_add_u32_e32 v84, s0, v32
	v_ashrrev_i32_e32 v85, 31, v84
	v_lshlrev_b64 v[84:85], 10, v[84:85]
	s_waitcnt vmcnt(7)
	v_mul_f32_e32 v29, 0x42800000, v62
	s_waitcnt vmcnt(6)
	v_mul_f32_e32 v49, 0x42800000, v50
	ds_write2_b32 v45, v29, v49 offset0:48 offset1:114
	s_waitcnt vmcnt(5)
	v_mul_f32_e32 v29, 0x42800000, v51
	s_waitcnt vmcnt(4)
	v_mul_f32_e32 v49, 0x42800000, v52
	ds_write2_b32 v45, v29, v49 offset0:180 offset1:246
	s_waitcnt vmcnt(3)
	v_mul_f32_e32 v29, 0x42800000, v53
	s_waitcnt vmcnt(2)
	v_mul_f32_e32 v49, 0x42800000, v54
	ds_write2_b32 v46, v29, v49 offset0:56 offset1:122
	v_mov_b32_e32 v49, 0
	v_mov_b32_e32 v50, 0
	s_waitcnt vmcnt(1)
	v_mul_f32_e32 v29, 0x42800000, v48
	s_waitcnt vmcnt(0)
	v_mul_f32_e32 v28, 0x42800000, v28
	ds_write2_b32 v46, v29, v28 offset0:188 offset1:254
	s_waitcnt lgkmcnt(0)
	ds_read2_b32 v[52:53], v33 offset1:16
	ds_read2_b32 v[54:55], v33 offset0:33 offset1:49
	ds_read2_b32 v[56:57], v33 offset0:66 offset1:82
	ds_read2_b32 v[58:59], v33 offset0:99 offset1:115
	ds_read2_b32 v[60:61], v33 offset0:132 offset1:148
	ds_read2_b32 v[62:63], v33 offset0:165 offset1:181
	ds_read2_b32 v[64:65], v33 offset0:198 offset1:214
	ds_read2_b32 v[66:67], v33 offset0:231 offset1:247
	ds_read2_b32 v[68:69], v47 offset0:8 offset1:24
	ds_read2_b32 v[70:71], v47 offset0:41 offset1:57
	ds_read2_b32 v[72:73], v47 offset0:74 offset1:90
	ds_read2_b32 v[74:75], v47 offset0:107 offset1:123
	ds_read2_b32 v[76:77], v47 offset0:140 offset1:156
	ds_read2_b32 v[78:79], v47 offset0:173 offset1:189
	v_mov_b32_e32 v48, 0
	ds_read2_b32 v[80:81], v47 offset0:206 offset1:222
	ds_read2_b32 v[82:83], v47 offset0:239 offset1:255
	v_mov_b32_e32 v51, 0
	s_waitcnt lgkmcnt(14)
	v_cvt_pk_fp8_f32 v48, v52, v54
	s_waitcnt lgkmcnt(10)
	v_cvt_pk_fp8_f32 v49, v60, v62
	s_waitcnt lgkmcnt(6)
	v_cvt_pk_fp8_f32 v50, v68, v70
	s_waitcnt lgkmcnt(2)
	v_cvt_pk_fp8_f32 v51, v76, v78
	v_cvt_pk_fp8_f32 v48, v56, v58 op_sel:[0,0,1]
	v_cvt_pk_fp8_f32 v49, v64, v66 op_sel:[0,0,1]
	v_cvt_pk_fp8_f32 v50, v72, v74 op_sel:[0,0,1]
	s_waitcnt lgkmcnt(0)
	v_cvt_pk_fp8_f32 v51, v80, v82 op_sel:[0,0,1]
	v_lshl_add_u64 v[28:29], v[18:19], 0, s[4:5]
	v_lshl_add_u64 v[84:85], v[28:29], 0, v[84:85]
	v_add_u32_e32 v52, s0, v34
	global_store_dwordx4 v[84:85], v[48:51], off sc1 nt
	s_nop 1
	v_mov_b32_e32 v48, 0
	v_mov_b32_e32 v49, 0
	v_mov_b32_e32 v50, 0
	v_mov_b32_e32 v51, 0
	v_cvt_pk_fp8_f32 v48, v53, v55
	v_cvt_pk_fp8_f32 v49, v61, v63
	v_cvt_pk_fp8_f32 v50, v69, v71
	v_cvt_pk_fp8_f32 v51, v77, v79
	v_cvt_pk_fp8_f32 v48, v57, v59 op_sel:[0,0,1]
	v_cvt_pk_fp8_f32 v49, v65, v67 op_sel:[0,0,1]
	v_cvt_pk_fp8_f32 v50, v73, v75 op_sel:[0,0,1]
	v_cvt_pk_fp8_f32 v51, v81, v83 op_sel:[0,0,1]
	v_ashrrev_i32_e32 v53, 31, v52
	v_lshlrev_b64 v[52:53], 10, v[52:53]
	v_lshl_add_u64 v[28:29], v[28:29], 0, v[52:53]
	global_store_dwordx4 v[28:29], v[48:51], off sc1 nt
	s_waitcnt lgkmcnt(0)

; #define LDS_WAIT() asm volatile("s_waitcnt lgkmcnt(0)" ::: "memory")
; __device__ __forceinline__ void tr_item(const float* W, int ld, int K, int nblk, int item, bf16* WT, bool gu, LAS float* scr, int lane) {
;     const int kb = item / nblk, nb = item % nblk, k0 = 64 * kb, n0 = 32 * nb;
;     int drow0 = n0;
;     if (gu) { const int bj = n0 / FF, j = n0 - bj * FF; drow0 = 256 * (j / 128) + 128 * bj + (j % 128); }
;     { float t_[32];
; #pragma unroll
;       for (int i = 0; i < 32; ++i) t_[i] = W[(size_t)(k0 + 2 * i + (lane >> 5)) * ld + n0 + (lane & 31)];
; #pragma unroll
;       for (int i = 0; i < 32; ++i) scr[(2 * i + (lane >> 5)) * 33 + (lane & 31)] = t_[i]; }
;     LDS_WAIT(); asm volatile("" ::: "memory");
; __device__ __forceinline__ void convert_items(Frame& F, const Args& a, int lo, int hi, int w, int nw) {
;     ...
;         if (r < I_SO) { tr_item(a.in[12], D, D, 32, r, (bf16*)(F.ws + WS_WSWAOUT), false, scr, lane); continue; } r -= I_SO;
.LBB0_1313:
	s_andn2_b64 vcc, exec, s[4:5]
	s_cbranch_vccnz .LBB0_1315
	s_add_i32 s0, s11, 0x2000
	s_and_b32 s5, s0, 0x1ffc0
	s_and_b32 s4, s9, 0x3e0
	v_add_u32_e32 v28, s5, v30
	s_lshl_b32 s0, s4, 2
	v_ashrrev_i32_e32 v29, 31, v28
	v_lshl_add_u64 v[48:49], v[8:9], 0, s[0:1]
	v_lshlrev_b64 v[28:29], 12, v[28:29]
	v_lshl_add_u64 v[28:29], v[48:49], 0, v[28:29]
	v_add_co_u32_e32 v48, vcc, 0x2000, v28
	global_load_dword v50, v[28:29], off nt
	s_nop 0
	v_addc_co_u32_e32 v49, vcc, 0, v29, vcc
	global_load_dword v51, v[48:49], off nt
	v_add_co_u32_e32 v48, vcc, 0x4000, v28
	s_lshl_b32 s0, s5, 1
	s_nop 0
	v_addc_co_u32_e32 v49, vcc, 0, v29, vcc
	global_load_dword v52, v[48:49], off nt
	v_add_co_u32_e32 v48, vcc, 0x6000, v28
	s_nop 1
	v_addc_co_u32_e32 v49, vcc, 0, v29, vcc
	global_load_dword v53, v[48:49], off nt
	v_add_co_u32_e32 v48, vcc, 0x8000, v28
	s_nop 1
	v_addc_co_u32_e32 v49, vcc, 0, v29, vcc
	global_load_dword v54, v[48:49], off nt
	v_add_co_u32_e32 v48, vcc, 0xa000, v28
	s_nop 1
	v_addc_co_u32_e32 v49, vcc, 0, v29, vcc
	global_load_dword v55, v[48:49], off nt
	v_add_co_u32_e32 v48, vcc, 0xc000, v28
	s_nop 1
	v_addc_co_u32_e32 v49, vcc, 0, v29, vcc
	global_load_dword v56, v[48:49], off nt
	v_add_co_u32_e32 v48, vcc, 0xe000, v28
	s_nop 1
	v_addc_co_u32_e32 v49, vcc, 0, v29, vcc
	global_load_dword v57, v[48:49], off nt
	v_add_co_u32_e32 v48, vcc, 0x10000, v28
	s_nop 1
	v_addc_co_u32_e32 v49, vcc, 0, v29, vcc
	global_load_dword v58, v[48:49], off nt
	v_add_co_u32_e32 v48, vcc, 0x12000, v28
	s_nop 1
	v_addc_co_u32_e32 v49, vcc, 0, v29, vcc
	global_load_dword v59, v[48:49], off nt
	v_add_co_u32_e32 v48, vcc, 0x14000, v28
	s_nop 1
	v_addc_co_u32_e32 v49, vcc, 0, v29, vcc
	global_load_dword v60, v[48:49], off nt
	v_add_co_u32_e32 v48, vcc, 0x16000, v28
	s_nop 1
	v_addc_co_u32_e32 v49, vcc, 0, v29, vcc
	global_load_dword v61, v[48:49], off nt
	v_add_co_u32_e32 v48, vcc, 0x18000, v28
	s_nop 1
	v_addc_co_u32_e32 v49, vcc, 0, v29, vcc
	global_load_dword v62, v[48:49], off nt
	v_add_co_u32_e32 v48, vcc, 0x1a000, v28
	s_nop 1
	v_addc_co_u32_e32 v49, vcc, 0, v29, vcc
	global_load_dword v63, v[48:49], off nt
	v_add_co_u32_e32 v48, vcc, 0x1c000, v28
	s_nop 1
	v_addc_co_u32_e32 v49, vcc, 0, v29, vcc
	global_load_dword v64, v[48:49], off nt
	v_add_co_u32_e32 v48, vcc, 0x1e000, v28
	s_nop 1
	v_addc_co_u32_e32 v49, vcc, 0, v29, vcc
	global_load_dword v65, v[48:49], off nt
	v_add_co_u32_e32 v48, vcc, 0x20000, v28
	s_nop 1
	v_addc_co_u32_e32 v49, vcc, 0, v29, vcc
	global_load_dword v66, v[48:49], off nt
	v_add_co_u32_e32 v48, vcc, 0x22000, v28
	s_nop 1
	v_addc_co_u32_e32 v49, vcc, 0, v29, vcc
	global_load_dword v67, v[48:49], off nt
	v_add_co_u32_e32 v48, vcc, 0x24000, v28
	s_nop 1
	v_addc_co_u32_e32 v49, vcc, 0, v29, vcc
	global_load_dword v68, v[48:49], off nt
	v_add_co_u32_e32 v48, vcc, 0x26000, v28
	s_nop 1
	v_addc_co_u32_e32 v49, vcc, 0, v29, vcc
	global_load_dword v69, v[48:49], off nt
	v_add_co_u32_e32 v48, vcc, 0x28000, v28
	s_nop 1
	v_addc_co_u32_e32 v49, vcc, 0, v29, vcc
	global_load_dword v70, v[48:49], off nt
	v_add_co_u32_e32 v48, vcc, 0x2a000, v28
	s_nop 1
	v_addc_co_u32_e32 v49, vcc, 0, v29, vcc
	global_load_dword v71, v[48:49], off nt
	v_add_co_u32_e32 v48, vcc, 0x2c000, v28
	s_nop 1
	v_addc_co_u32_e32 v49, vcc, 0, v29, vcc
	global_load_dword v72, v[48:49], off nt
	v_add_co_u32_e32 v48, vcc, 0x2e000, v28
	s_nop 1
	v_addc_co_u32_e32 v49, vcc, 0, v29, vcc
	global_load_dword v73, v[48:49], off nt
	v_add_co_u32_e32 v48, vcc, 0x30000, v28
	s_nop 1
	v_addc_co_u32_e32 v49, vcc, 0, v29, vcc
	global_load_dword v74, v[48:49], off nt
	v_add_co_u32_e32 v48, vcc, 0x32000, v28
	s_nop 1
	v_addc_co_u32_e32 v49, vcc, 0, v29, vcc
	global_load_dword v75, v[48:49], off nt
	v_add_co_u32_e32 v48, vcc, 0x34000, v28
	s_nop 1
	v_addc_co_u32_e32 v49, vcc, 0, v29, vcc
	global_load_dword v76, v[48:49], off nt
	v_add_co_u32_e32 v48, vcc, 0x36000, v28
	s_nop 1
	v_addc_co_u32_e32 v49, vcc, 0, v29, vcc
	global_load_dword v77, v[48:49], off nt
	v_add_co_u32_e32 v48, vcc, 0x38000, v28
	s_nop 1
	v_addc_co_u32_e32 v49, vcc, 0, v29, vcc
	global_load_dword v78, v[48:49], off nt
	v_add_co_u32_e32 v48, vcc, 0x3a000, v28
	s_nop 1
	v_addc_co_u32_e32 v49, vcc, 0, v29, vcc
	global_load_dword v79, v[48:49], off nt
	v_add_co_u32_e32 v48, vcc, 0x3c000, v28
	s_nop 1
	v_addc_co_u32_e32 v49, vcc, 0, v29, vcc
	v_add_co_u32_e32 v28, vcc, 0x3e000, v28
	global_load_dword v48, v[48:49], off nt
	s_nop 0
	v_addc_co_u32_e32 v29, vcc, 0, v29, vcc
	global_load_dword v28, v[28:29], off nt
	s_waitcnt vmcnt(30)
	ds_write2_b32 v31, v50, v51 offset1:66
	s_waitcnt vmcnt(28)
	ds_write2_b32 v31, v52, v53 offset0:132 offset1:198
	s_waitcnt vmcnt(26)
	ds_write2_b32 v40, v54, v55 offset0:8 offset1:74
	s_waitcnt vmcnt(24)
	ds_write2_b32 v40, v56, v57 offset0:140 offset1:206
	s_waitcnt vmcnt(22)
	ds_write2_b32 v41, v58, v59 offset0:16 offset1:82
	s_waitcnt vmcnt(20)
	ds_write2_b32 v41, v60, v61 offset0:148 offset1:214
	s_waitcnt vmcnt(18)
	ds_write2_b32 v42, v62, v63 offset0:24 offset1:90
	s_waitcnt vmcnt(16)
	ds_write2_b32 v42, v64, v65 offset0:156 offset1:222
	s_waitcnt vmcnt(14)
	ds_write2_b32 v43, v66, v67 offset0:32 offset1:98
	s_waitcnt vmcnt(12)
	ds_write2_b32 v43, v68, v69 offset0:164 offset1:230
	s_waitcnt vmcnt(10)
	ds_write2_b32 v44, v70, v71 offset0:40 offset1:106
	s_waitcnt vmcnt(8)
; #define GAS __attribute__((address_space(1)))
; #define LAS __attribute__((address_space(3)))
; #define LDS_WAIT() asm volatile("s_waitcnt lgkmcnt(0)" ::: "memory")
; __device__ __forceinline__ unsigned pk2(float lo, float hi) { return f2bf(lo) | (f2bf(hi) << 16); }
; __device__ __forceinline__ void tr_item(const float* W, int ld, int K, int nblk, int item, bf16* WT, bool gu, LAS float* scr, int lane) {
;     ...
;     const int c = lane & 7;
; #pragma unroll
;     for (int j = 0; j < 4; ++j) { const int n = (lane >> 3) + 8 * j; const LAS float* s = scr + (8 * c) * 33 + n;
;         v4u o; o.x = pk2(s[0 * 33], s[1 * 33]); o.y = pk2(s[2 * 33], s[3 * 33]); o.z = pk2(s[4 * 33], s[5 * 33]); o.w = pk2(s[6 * 33], s[7 * 33]);
;         *(GAS v4u*)(WT + (size_t)(drow0 + n) * K + k0 + 8 * c) = o; }
;     LDS_WAIT(); asm volatile("" ::: "memory");
	ds_write2_b32 v44, v72, v73 offset0:172 offset1:238
	s_waitcnt vmcnt(6)
	ds_write2_b32 v45, v74, v75 offset0:48 offset1:114
	s_waitcnt vmcnt(4)
	ds_write2_b32 v45, v76, v77 offset0:180 offset1:246
	s_waitcnt vmcnt(2)
	ds_write2_b32 v46, v78, v79 offset0:56 offset1:122
	s_waitcnt vmcnt(0)
	ds_write2_b32 v46, v48, v28 offset0:188 offset1:254
	s_waitcnt lgkmcnt(0)
	ds_read2_b32 v[52:53], v36 offset0:33 offset1:41
	ds_read2_b32 v[54:55], v36 offset1:8
	ds_read2_b32 v[56:57], v36 offset0:66 offset1:74
	ds_read2_b32 v[58:59], v36 offset0:99 offset1:107
	ds_read2_b32 v[60:61], v36 offset0:132 offset1:140
	ds_read2_b32 v[62:63], v36 offset0:165 offset1:173
	ds_read2_b32 v[64:65], v36 offset0:198 offset1:206
	ds_read2_b32 v[66:67], v36 offset0:231 offset1:239
	s_waitcnt lgkmcnt(7)
	v_bfe_u32 v49, v52, 16, 1
	s_waitcnt lgkmcnt(6)
	v_bfe_u32 v48, v54, 16, 1
	v_add3_u32 v48, v54, v48, s15
	v_lshrrev_b32_e32 v48, 16, v48
	v_add3_u32 v49, v52, v49, s15
	v_and_or_b32 v48, v49, s16, v48
	s_waitcnt lgkmcnt(5)
	v_bfe_u32 v49, v56, 16, 1
	v_add3_u32 v49, v56, v49, s15
	s_waitcnt lgkmcnt(4)
	v_bfe_u32 v50, v58, 16, 1
	v_lshrrev_b32_e32 v49, 16, v49
	v_add3_u32 v50, v58, v50, s15
	v_and_or_b32 v49, v50, s16, v49
	s_waitcnt lgkmcnt(3)
	v_bfe_u32 v50, v60, 16, 1
	v_add3_u32 v50, v60, v50, s15
	s_waitcnt lgkmcnt(2)
	v_bfe_u32 v51, v62, 16, 1
	v_lshrrev_b32_e32 v50, 16, v50
	v_add3_u32 v51, v62, v51, s15
	v_and_or_b32 v50, v51, s16, v50
	s_waitcnt lgkmcnt(1)
	v_bfe_u32 v51, v64, 16, 1
	v_add_u32_e32 v68, s4, v35
	v_add3_u32 v51, v64, v51, s15
	s_waitcnt lgkmcnt(0)
	v_bfe_u32 v52, v66, 16, 1
	v_ashrrev_i32_e32 v69, 31, v68
	v_lshl_add_u64 v[28:29], v[20:21], 0, s[0:1]
	v_lshrrev_b32_e32 v51, 16, v51
	v_add3_u32 v52, v66, v52, s15
	v_lshlrev_b64 v[68:69], 11, v[68:69]
	v_and_or_b32 v51, v52, s16, v51
	v_lshl_add_u64 v[68:69], v[28:29], 0, v[68:69]
	global_store_dwordx4 v[68:69], v[48:51], off sc1 nt
	v_bfe_u32 v52, v67, 16, 1
	v_add3_u32 v52, v67, v52, s15
	v_bfe_u32 v48, v55, 16, 1
	v_add3_u32 v48, v55, v48, s15
	v_bfe_u32 v49, v53, 16, 1
	v_lshrrev_b32_e32 v48, 16, v48
	v_add3_u32 v49, v53, v49, s15
	v_and_or_b32 v48, v49, s16, v48
	v_bfe_u32 v49, v57, 16, 1
	v_add3_u32 v49, v57, v49, s15
	v_bfe_u32 v50, v59, 16, 1
	v_lshrrev_b32_e32 v49, 16, v49
	v_add3_u32 v50, v59, v50, s15
	v_and_or_b32 v49, v50, s16, v49
	v_bfe_u32 v50, v61, 16, 1
	v_add3_u32 v50, v61, v50, s15
	v_bfe_u32 v51, v63, 16, 1
	v_lshrrev_b32_e32 v50, 16, v50
	v_add3_u32 v51, v63, v51, s15
	v_and_or_b32 v50, v51, s16, v50
	v_bfe_u32 v51, v65, 16, 1
	v_add3_u32 v51, v65, v51, s15
	v_lshrrev_b32_e32 v51, 16, v51
	v_and_or_b32 v51, v52, s16, v51
	v_add_u32_e32 v52, s4, v37
	v_ashrrev_i32_e32 v53, 31, v52
	v_lshlrev_b64 v[52:53], 11, v[52:53]
	v_lshl_add_u64 v[52:53], v[28:29], 0, v[52:53]
	global_store_dwordx4 v[52:53], v[48:51], off sc1 nt
	ds_read2_b32 v[52:53], v36 offset0:49 offset1:57
	ds_read2_b32 v[54:55], v36 offset0:16 offset1:24
	ds_read2_b32 v[56:57], v36 offset0:82 offset1:90
	ds_read2_b32 v[58:59], v36 offset0:115 offset1:123
	ds_read2_b32 v[60:61], v36 offset0:148 offset1:156
	ds_read2_b32 v[62:63], v36 offset0:181 offset1:189
	ds_read2_b32 v[64:65], v36 offset0:214 offset1:222
	ds_read2_b32 v[66:67], v36 offset0:247 offset1:255
	s_waitcnt lgkmcnt(7)
	v_bfe_u32 v49, v52, 16, 1
	s_waitcnt lgkmcnt(6)
	v_bfe_u32 v48, v54, 16, 1
	v_add3_u32 v48, v54, v48, s15
	v_lshrrev_b32_e32 v48, 16, v48
	v_add3_u32 v49, v52, v49, s15
	v_and_or_b32 v48, v49, s16, v48
	s_waitcnt lgkmcnt(5)
	v_bfe_u32 v49, v56, 16, 1
	v_add3_u32 v49, v56, v49, s15
	s_waitcnt lgkmcnt(4)
	v_bfe_u32 v50, v58, 16, 1
	v_lshrrev_b32_e32 v49, 16, v49
	v_add3_u32 v50, v58, v50, s15
	v_and_or_b32 v49, v50, s16, v49
	s_waitcnt lgkmcnt(3)
	v_bfe_u32 v50, v60, 16, 1
	v_add3_u32 v50, v60, v50, s15
	s_waitcnt lgkmcnt(2)
	v_bfe_u32 v51, v62, 16, 1
	v_lshrrev_b32_e32 v50, 16, v50
	v_add3_u32 v51, v62, v51, s15
	v_and_or_b32 v50, v51, s16, v50
	s_waitcnt lgkmcnt(1)
	v_bfe_u32 v51, v64, 16, 1
	v_add_u32_e32 v68, s4, v38
	v_add3_u32 v51, v64, v51, s15
	s_waitcnt lgkmcnt(0)
	v_bfe_u32 v52, v66, 16, 1
	v_ashrrev_i32_e32 v69, 31, v68
	v_lshrrev_b32_e32 v51, 16, v51
	v_add3_u32 v52, v66, v52, s15
	v_lshlrev_b64 v[68:69], 11, v[68:69]
	v_and_or_b32 v51, v52, s16, v51
	v_lshl_add_u64 v[68:69], v[28:29], 0, v[68:69]
	global_store_dwordx4 v[68:69], v[48:51], off sc1 nt
	v_bfe_u32 v52, v67, 16, 1
	v_add3_u32 v52, v67, v52, s15
	v_bfe_u32 v48, v55, 16, 1
	v_add3_u32 v48, v55, v48, s15
	v_bfe_u32 v49, v53, 16, 1
	v_lshrrev_b32_e32 v48, 16, v48
	v_add3_u32 v49, v53, v49, s15
	v_and_or_b32 v48, v49, s16, v48
	v_bfe_u32 v49, v57, 16, 1
	v_add3_u32 v49, v57, v49, s15
	v_bfe_u32 v50, v59, 16, 1
	v_lshrrev_b32_e32 v49, 16, v49
	v_add3_u32 v50, v59, v50, s15
	v_and_or_b32 v49, v50, s16, v49
	v_bfe_u32 v50, v61, 16, 1
	v_add3_u32 v50, v61, v50, s15
	v_bfe_u32 v51, v63, 16, 1
	v_lshrrev_b32_e32 v50, 16, v50
	v_add3_u32 v51, v63, v51, s15
	v_and_or_b32 v50, v51, s16, v50
	v_bfe_u32 v51, v65, 16, 1
	v_add3_u32 v51, v65, v51, s15
	v_lshrrev_b32_e32 v51, 16, v51
	v_and_or_b32 v51, v52, s16, v51
	v_add_u32_e32 v52, s4, v39
	v_ashrrev_i32_e32 v53, 31, v52
	v_lshlrev_b64 v[52:53], 11, v[52:53]
	v_lshl_add_u64 v[28:29], v[28:29], 0, v[52:53]
	global_store_dwordx4 v[28:29], v[48:51], off sc1 nt
	s_waitcnt lgkmcnt(0)

; __device__ __forceinline__ void tr_item(const float* W, int ld, int K, int nblk, int item, bf16* WT, bool gu, LAS float* scr, int lane) {
;     const int kb = item / nblk, nb = item % nblk, k0 = 64 * kb, n0 = 32 * nb;
;     int drow0 = n0;
;     if (gu) { const int bj = n0 / FF, j = n0 - bj * FF; drow0 = 256 * (j / 128) + 128 * bj + (j % 128); }
;     { float t_[32];
; #pragma unroll
;       for (int i = 0; i < 32; ++i) t_[i] = W[(size_t)(k0 + 2 * i + (lane >> 5)) * ld + n0 + (lane & 31)];
; #pragma unroll
; __device__ __forceinline__ void convert_items(Frame& F, const Args& a, int lo, int hi, int w, int nw) {
;     ...
;         if (r < I_SI) { tr_item(a.in[10], D + 512, D, 48, r, (bf16*)(F.ws + WS_WSWAIN), false, scr, lane); continue; } r -= I_SI;
.LBB0_1316:
	s_andn2_b64 vcc, exec, s[4:5]
	s_cbranch_vccnz .LBB0_1318
	s_add_i32 s0, s8, 0xf800
	s_and_b32 s4, s0, 0xffff
	s_mul_i32 s4, s4, 0xaaab
	s_lshr_b32 s5, s4, 21
	s_mul_i32 s4, s5, 48
	s_sub_i32 s0, s0, s4
	s_lshl_b32 s0, s0, 5
	s_and_b32 s4, s0, 0xffe0
	s_lshl_b32 s0, s4, 2
	v_lshl_add_u32 v50, s5, 6, v30
	v_lshl_add_u64 v[28:29], v[10:11], 0, s[0:1]
	v_mad_i64_i32 v[48:49], s[6:7], v50, s17, v[28:29]
	global_load_dword v51, v[48:49], off nt
	v_add_u32_e32 v48, 2, v50
	v_mad_i64_i32 v[48:49], s[6:7], v48, s17, v[28:29]
	global_load_dword v52, v[48:49], off nt
	v_add_u32_e32 v48, 4, v50
	v_mad_i64_i32 v[48:49], s[6:7], v48, s17, v[28:29]
	global_load_dword v53, v[48:49], off nt
	v_add_u32_e32 v48, 6, v50
	v_mad_i64_i32 v[48:49], s[6:7], v48, s17, v[28:29]
	global_load_dword v54, v[48:49], off nt
	v_add_u32_e32 v48, 8, v50
	v_mad_i64_i32 v[48:49], s[6:7], v48, s17, v[28:29]
	global_load_dword v55, v[48:49], off nt
	v_add_u32_e32 v48, 10, v50
	v_mad_i64_i32 v[48:49], s[6:7], v48, s17, v[28:29]
	global_load_dword v56, v[48:49], off nt
	v_add_u32_e32 v48, 12, v50
	v_mad_i64_i32 v[48:49], s[6:7], v48, s17, v[28:29]
	global_load_dword v57, v[48:49], off nt
	v_add_u32_e32 v48, 14, v50
	v_mad_i64_i32 v[48:49], s[6:7], v48, s17, v[28:29]
	global_load_dword v58, v[48:49], off nt
	v_add_u32_e32 v48, 16, v50
	v_mad_i64_i32 v[48:49], s[6:7], v48, s17, v[28:29]
	global_load_dword v59, v[48:49], off nt
	v_add_u32_e32 v48, 18, v50
	v_mad_i64_i32 v[48:49], s[6:7], v48, s17, v[28:29]
	global_load_dword v60, v[48:49], off nt
	v_add_u32_e32 v48, 20, v50
	v_mad_i64_i32 v[48:49], s[6:7], v48, s17, v[28:29]
	global_load_dword v61, v[48:49], off nt
	v_add_u32_e32 v48, 22, v50
	v_mad_i64_i32 v[48:49], s[6:7], v48, s17, v[28:29]
	global_load_dword v62, v[48:49], off nt
	v_add_u32_e32 v48, 24, v50
	v_mad_i64_i32 v[48:49], s[6:7], v48, s17, v[28:29]
	global_load_dword v63, v[48:49], off nt
	v_add_u32_e32 v48, 26, v50
	v_mad_i64_i32 v[48:49], s[6:7], v48, s17, v[28:29]
	global_load_dword v64, v[48:49], off nt
	v_add_u32_e32 v48, 28, v50
	v_mad_i64_i32 v[48:49], s[6:7], v48, s17, v[28:29]
	global_load_dword v65, v[48:49], off nt
	v_add_u32_e32 v48, 30, v50
	v_mad_i64_i32 v[48:49], s[6:7], v48, s17, v[28:29]
	global_load_dword v66, v[48:49], off nt
	v_add_u32_e32 v48, 32, v50
	v_mad_i64_i32 v[48:49], s[6:7], v48, s17, v[28:29]
	global_load_dword v67, v[48:49], off nt
	v_add_u32_e32 v48, 34, v50
	v_mad_i64_i32 v[48:49], s[6:7], v48, s17, v[28:29]
	global_load_dword v68, v[48:49], off nt
	v_add_u32_e32 v48, 36, v50
	v_mad_i64_i32 v[48:49], s[6:7], v48, s17, v[28:29]
	global_load_dword v69, v[48:49], off nt
	v_add_u32_e32 v48, 38, v50
	v_mad_i64_i32 v[48:49], s[6:7], v48, s17, v[28:29]
	global_load_dword v70, v[48:49], off nt
	v_add_u32_e32 v48, 40, v50
	v_mad_i64_i32 v[48:49], s[6:7], v48, s17, v[28:29]
	global_load_dword v71, v[48:49], off nt
	v_add_u32_e32 v48, 42, v50
	v_mad_i64_i32 v[48:49], s[6:7], v48, s17, v[28:29]
	global_load_dword v72, v[48:49], off nt
	v_add_u32_e32 v48, 44, v50
	v_mad_i64_i32 v[48:49], s[6:7], v48, s17, v[28:29]
	global_load_dword v73, v[48:49], off nt
	v_add_u32_e32 v48, 46, v50
	v_mad_i64_i32 v[48:49], s[6:7], v48, s17, v[28:29]
	global_load_dword v74, v[48:49], off nt
	v_add_u32_e32 v48, 48, v50
	v_mad_i64_i32 v[48:49], s[6:7], v48, s17, v[28:29]
	global_load_dword v75, v[48:49], off nt
	v_add_u32_e32 v48, 50, v50
	v_mad_i64_i32 v[48:49], s[6:7], v48, s17, v[28:29]
	global_load_dword v76, v[48:49], off nt
	v_add_u32_e32 v48, 52, v50
	v_mad_i64_i32 v[48:49], s[6:7], v48, s17, v[28:29]
	global_load_dword v77, v[48:49], off nt
	v_add_u32_e32 v48, 54, v50
	v_mad_i64_i32 v[48:49], s[6:7], v48, s17, v[28:29]
	global_load_dword v78, v[48:49], off nt
	v_add_u32_e32 v48, 56, v50
	v_mad_i64_i32 v[48:49], s[6:7], v48, s17, v[28:29]
	global_load_dword v79, v[48:49], off nt
	v_add_u32_e32 v48, 58, v50
	v_mad_i64_i32 v[48:49], s[6:7], v48, s17, v[28:29]
	global_load_dword v80, v[48:49], off nt
	v_add_u32_e32 v48, 60, v50
	v_mad_i64_i32 v[48:49], s[6:7], v48, s17, v[28:29]
	global_load_dword v48, v[48:49], off nt
	v_add_u32_e32 v49, 62, v50
	v_mad_i64_i32 v[28:29], s[6:7], v49, s17, v[28:29]
	global_load_dword v28, v[28:29], off nt
	s_waitcnt vmcnt(30)
	ds_write2_b32 v31, v51, v52 offset1:66
	s_waitcnt vmcnt(28)
	ds_write2_b32 v31, v53, v54 offset0:132 offset1:198
	s_waitcnt vmcnt(26)
	ds_write2_b32 v40, v55, v56 offset0:8 offset1:74
	s_waitcnt vmcnt(24)
	ds_write2_b32 v40, v57, v58 offset0:140 offset1:206
	s_waitcnt vmcnt(22)
	ds_write2_b32 v41, v59, v60 offset0:16 offset1:82
	s_waitcnt vmcnt(20)
	ds_write2_b32 v41, v61, v62 offset0:148 offset1:214
	s_waitcnt vmcnt(18)
	ds_write2_b32 v42, v63, v64 offset0:24 offset1:90
	s_waitcnt vmcnt(16)
	ds_write2_b32 v42, v65, v66 offset0:156 offset1:222
	s_waitcnt vmcnt(14)
	ds_write2_b32 v43, v67, v68 offset0:32 offset1:98
	s_waitcnt vmcnt(12)
	ds_write2_b32 v43, v69, v70 offset0:164 offset1:230
	s_waitcnt vmcnt(10)
	ds_write2_b32 v44, v71, v72 offset0:40 offset1:106
	s_waitcnt vmcnt(8)
	ds_write2_b32 v44, v73, v74 offset0:172 offset1:238
	s_waitcnt vmcnt(6)
	ds_write2_b32 v45, v75, v76 offset0:48 offset1:114
	s_waitcnt vmcnt(4)
; #define GAS __attribute__((address_space(1)))
; #define LAS __attribute__((address_space(3)))
; #define LDS_WAIT() asm volatile("s_waitcnt lgkmcnt(0)" ::: "memory")
; __device__ __forceinline__ unsigned pk2(float lo, float hi) { return f2bf(lo) | (f2bf(hi) << 16); }
; __device__ __forceinline__ void tr_item(const float* W, int ld, int K, int nblk, int item, bf16* WT, bool gu, LAS float* scr, int lane) {
;     ...
;     const int c = lane & 7;
; #pragma unroll
;     for (int j = 0; j < 4; ++j) { const int n = (lane >> 3) + 8 * j; const LAS float* s = scr + (8 * c) * 33 + n;
;         v4u o; o.x = pk2(s[0 * 33], s[1 * 33]); o.y = pk2(s[2 * 33], s[3 * 33]); o.z = pk2(s[4 * 33], s[5 * 33]); o.w = pk2(s[6 * 33], s[7 * 33]);
;         *(GAS v4u*)(WT + (size_t)(drow0 + n) * K + k0 + 8 * c) = o; }
;     LDS_WAIT(); asm volatile("" ::: "memory");
	ds_write2_b32 v45, v77, v78 offset0:180 offset1:246
	s_waitcnt vmcnt(2)
	ds_write2_b32 v46, v79, v80 offset0:56 offset1:122
	s_waitcnt vmcnt(0)
	ds_write2_b32 v46, v48, v28 offset0:188 offset1:254
	s_waitcnt lgkmcnt(0)
	ds_read2_b32 v[52:53], v36 offset0:33 offset1:41
	ds_read2_b32 v[54:55], v36 offset1:8
	ds_read2_b32 v[56:57], v36 offset0:66 offset1:74
	ds_read2_b32 v[58:59], v36 offset0:99 offset1:107
	ds_read2_b32 v[60:61], v36 offset0:132 offset1:140
	ds_read2_b32 v[62:63], v36 offset0:165 offset1:173
	ds_read2_b32 v[64:65], v36 offset0:198 offset1:206
	ds_read2_b32 v[66:67], v36 offset0:231 offset1:239
	s_waitcnt lgkmcnt(7)
	v_bfe_u32 v49, v52, 16, 1
	s_waitcnt lgkmcnt(6)
	v_bfe_u32 v48, v54, 16, 1
	v_add3_u32 v48, v54, v48, s15
	v_lshrrev_b32_e32 v48, 16, v48
	v_add3_u32 v49, v52, v49, s15
	v_and_or_b32 v48, v49, s16, v48
	s_waitcnt lgkmcnt(5)
	v_bfe_u32 v49, v56, 16, 1
	v_add3_u32 v49, v56, v49, s15
	s_waitcnt lgkmcnt(4)
	v_bfe_u32 v50, v58, 16, 1
	v_lshrrev_b32_e32 v49, 16, v49
	v_add3_u32 v50, v58, v50, s15
	v_and_or_b32 v49, v50, s16, v49
	s_waitcnt lgkmcnt(3)
	v_bfe_u32 v50, v60, 16, 1
	v_add3_u32 v50, v60, v50, s15
	s_waitcnt lgkmcnt(2)
	v_bfe_u32 v51, v62, 16, 1
	v_lshrrev_b32_e32 v50, 16, v50
	v_add3_u32 v51, v62, v51, s15
	v_and_or_b32 v50, v51, s16, v50
	s_waitcnt lgkmcnt(1)
	v_bfe_u32 v51, v64, 16, 1
	v_add_u32_e32 v68, s4, v35
	s_lshl_b32 s0, s5, 7
	v_add3_u32 v51, v64, v51, s15
	s_waitcnt lgkmcnt(0)
	v_bfe_u32 v52, v66, 16, 1
	v_ashrrev_i32_e32 v69, 31, v68
	v_lshl_add_u64 v[28:29], v[22:23], 0, s[0:1]
	v_lshrrev_b32_e32 v51, 16, v51
	v_add3_u32 v52, v66, v52, s15
	v_lshlrev_b64 v[68:69], 11, v[68:69]
	v_and_or_b32 v51, v52, s16, v51
	v_lshl_add_u64 v[68:69], v[28:29], 0, v[68:69]
	global_store_dwordx4 v[68:69], v[48:51], off sc1 nt
	v_bfe_u32 v52, v67, 16, 1
	v_add3_u32 v52, v67, v52, s15
	v_bfe_u32 v48, v55, 16, 1
	v_add3_u32 v48, v55, v48, s15
	v_bfe_u32 v49, v53, 16, 1
	v_lshrrev_b32_e32 v48, 16, v48
	v_add3_u32 v49, v53, v49, s15
	v_and_or_b32 v48, v49, s16, v48
	v_bfe_u32 v49, v57, 16, 1
	v_add3_u32 v49, v57, v49, s15
	v_bfe_u32 v50, v59, 16, 1
	v_lshrrev_b32_e32 v49, 16, v49
	v_add3_u32 v50, v59, v50, s15
	v_and_or_b32 v49, v50, s16, v49
	v_bfe_u32 v50, v61, 16, 1
	v_add3_u32 v50, v61, v50, s15
	v_bfe_u32 v51, v63, 16, 1
	v_lshrrev_b32_e32 v50, 16, v50
	v_add3_u32 v51, v63, v51, s15
	v_and_or_b32 v50, v51, s16, v50
	v_bfe_u32 v51, v65, 16, 1
	v_add3_u32 v51, v65, v51, s15
	v_lshrrev_b32_e32 v51, 16, v51
	v_and_or_b32 v51, v52, s16, v51
	v_add_u32_e32 v52, s4, v37
	v_ashrrev_i32_e32 v53, 31, v52
	v_lshlrev_b64 v[52:53], 11, v[52:53]
	v_lshl_add_u64 v[52:53], v[28:29], 0, v[52:53]
	global_store_dwordx4 v[52:53], v[48:51], off sc1 nt
	ds_read2_b32 v[52:53], v36 offset0:49 offset1:57
	ds_read2_b32 v[54:55], v36 offset0:16 offset1:24
	ds_read2_b32 v[56:57], v36 offset0:82 offset1:90
	ds_read2_b32 v[58:59], v36 offset0:115 offset1:123
	ds_read2_b32 v[60:61], v36 offset0:148 offset1:156
	ds_read2_b32 v[62:63], v36 offset0:181 offset1:189
	ds_read2_b32 v[64:65], v36 offset0:214 offset1:222
	ds_read2_b32 v[66:67], v36 offset0:247 offset1:255
	s_waitcnt lgkmcnt(7)
	v_bfe_u32 v49, v52, 16, 1
	s_waitcnt lgkmcnt(6)
	v_bfe_u32 v48, v54, 16, 1
	v_add3_u32 v48, v54, v48, s15
	v_lshrrev_b32_e32 v48, 16, v48
	v_add3_u32 v49, v52, v49, s15
	v_and_or_b32 v48, v49, s16, v48
	s_waitcnt lgkmcnt(5)
	v_bfe_u32 v49, v56, 16, 1
	v_add3_u32 v49, v56, v49, s15
	s_waitcnt lgkmcnt(4)
	v_bfe_u32 v50, v58, 16, 1
	v_lshrrev_b32_e32 v49, 16, v49
	v_add3_u32 v50, v58, v50, s15
	v_and_or_b32 v49, v50, s16, v49
	s_waitcnt lgkmcnt(3)
	v_bfe_u32 v50, v60, 16, 1
	v_add3_u32 v50, v60, v50, s15
	s_waitcnt lgkmcnt(2)
	v_bfe_u32 v51, v62, 16, 1
	v_lshrrev_b32_e32 v50, 16, v50
	v_add3_u32 v51, v62, v51, s15
	v_and_or_b32 v50, v51, s16, v50
	s_waitcnt lgkmcnt(1)
	v_bfe_u32 v51, v64, 16, 1
	v_add_u32_e32 v68, s4, v38
	v_add3_u32 v51, v64, v51, s15
	s_waitcnt lgkmcnt(0)
	v_bfe_u32 v52, v66, 16, 1
	v_ashrrev_i32_e32 v69, 31, v68
	v_lshrrev_b32_e32 v51, 16, v51
	v_add3_u32 v52, v66, v52, s15
	v_lshlrev_b64 v[68:69], 11, v[68:69]
	v_and_or_b32 v51, v52, s16, v51
	v_lshl_add_u64 v[68:69], v[28:29], 0, v[68:69]
	global_store_dwordx4 v[68:69], v[48:51], off sc1 nt
	v_bfe_u32 v52, v67, 16, 1
	v_add3_u32 v52, v67, v52, s15
	v_bfe_u32 v48, v55, 16, 1
	v_add3_u32 v48, v55, v48, s15
	v_bfe_u32 v49, v53, 16, 1
	v_lshrrev_b32_e32 v48, 16, v48
	v_add3_u32 v49, v53, v49, s15
	v_and_or_b32 v48, v49, s16, v48
	v_bfe_u32 v49, v57, 16, 1
	v_add3_u32 v49, v57, v49, s15
	v_bfe_u32 v50, v59, 16, 1
	v_lshrrev_b32_e32 v49, 16, v49
	v_add3_u32 v50, v59, v50, s15
	v_and_or_b32 v49, v50, s16, v49
	v_bfe_u32 v50, v61, 16, 1
	v_add3_u32 v50, v61, v50, s15
	v_bfe_u32 v51, v63, 16, 1
	v_lshrrev_b32_e32 v50, 16, v50
	v_add3_u32 v51, v63, v51, s15
	v_and_or_b32 v50, v51, s16, v50
	v_bfe_u32 v51, v65, 16, 1
	v_add3_u32 v51, v65, v51, s15
	v_lshrrev_b32_e32 v51, 16, v51
	v_and_or_b32 v51, v52, s16, v51
	v_add_u32_e32 v52, s4, v39
	v_ashrrev_i32_e32 v53, 31, v52
	v_lshlrev_b64 v[52:53], 11, v[52:53]
	v_lshl_add_u64 v[28:29], v[28:29], 0, v[52:53]
	global_store_dwordx4 v[28:29], v[48:51], off sc1 nt
	s_waitcnt lgkmcnt(0)

; #define LDS_WAIT() asm volatile("s_waitcnt lgkmcnt(0)" ::: "memory")
; __device__ __forceinline__ void tr_item(const float* W, int ld, int K, int nblk, int item, bf16* WT, bool gu, LAS float* scr, int lane) {
;     const int kb = item / nblk, nb = item % nblk, k0 = 64 * kb, n0 = 32 * nb;
;     int drow0 = n0;
;     if (gu) { const int bj = n0 / FF, j = n0 - bj * FF; drow0 = 256 * (j / 128) + 128 * bj + (j % 128); }
;     { float t_[32];
; #pragma unroll
;       for (int i = 0; i < 32; ++i) t_[i] = W[(size_t)(k0 + 2 * i + (lane >> 5)) * ld + n0 + (lane & 31)];
; #pragma unroll
;       for (int i = 0; i < 32; ++i) scr[(2 * i + (lane >> 5)) * 33 + (lane & 31)] = t_[i]; }
;     LDS_WAIT(); asm volatile("" ::: "memory");
; __device__ __forceinline__ void convert_items(Frame& F, const Args& a, int lo, int hi, int w, int nw) {
;     ...
;         if (r < I_FO) { tr_item(a.in[9], D, D, 32, r, (bf16*)(F.ws + WS_WFOXOUT), false, scr, lane); continue; } r -= I_FO;
.LBB0_1319:
	s_andn2_b64 vcc, exec, s[4:5]
	s_cbranch_vccnz .LBB0_1321
	s_add_i32 s0, s11, 0x2a00
	s_and_b32 s5, s0, 0x1ffc0
	s_and_b32 s4, s9, 0x3e0
	v_add_u32_e32 v28, s5, v30
	s_lshl_b32 s0, s4, 2
	v_ashrrev_i32_e32 v29, 31, v28
	v_lshl_add_u64 v[48:49], v[12:13], 0, s[0:1]
	v_lshlrev_b64 v[28:29], 12, v[28:29]
	v_lshl_add_u64 v[28:29], v[48:49], 0, v[28:29]
	v_add_co_u32_e32 v48, vcc, 0x2000, v28
	global_load_dword v50, v[28:29], off nt
	s_nop 0
	v_addc_co_u32_e32 v49, vcc, 0, v29, vcc
	global_load_dword v51, v[48:49], off nt
	v_add_co_u32_e32 v48, vcc, 0x4000, v28
	s_lshl_b32 s0, s5, 1
	s_nop 0
	v_addc_co_u32_e32 v49, vcc, 0, v29, vcc
	global_load_dword v52, v[48:49], off nt
	v_add_co_u32_e32 v48, vcc, 0x6000, v28
	s_nop 1
	v_addc_co_u32_e32 v49, vcc, 0, v29, vcc
	global_load_dword v53, v[48:49], off nt
	v_add_co_u32_e32 v48, vcc, 0x8000, v28
	s_nop 1
	v_addc_co_u32_e32 v49, vcc, 0, v29, vcc
	global_load_dword v54, v[48:49], off nt
	v_add_co_u32_e32 v48, vcc, 0xa000, v28
	s_nop 1
	v_addc_co_u32_e32 v49, vcc, 0, v29, vcc
	global_load_dword v55, v[48:49], off nt
	v_add_co_u32_e32 v48, vcc, 0xc000, v28
	s_nop 1
	v_addc_co_u32_e32 v49, vcc, 0, v29, vcc
	global_load_dword v56, v[48:49], off nt
	v_add_co_u32_e32 v48, vcc, 0xe000, v28
	s_nop 1
	v_addc_co_u32_e32 v49, vcc, 0, v29, vcc
	global_load_dword v57, v[48:49], off nt
	v_add_co_u32_e32 v48, vcc, 0x10000, v28
	s_nop 1
	v_addc_co_u32_e32 v49, vcc, 0, v29, vcc
	global_load_dword v58, v[48:49], off nt
	v_add_co_u32_e32 v48, vcc, 0x12000, v28
	s_nop 1
	v_addc_co_u32_e32 v49, vcc, 0, v29, vcc
	global_load_dword v59, v[48:49], off nt
	v_add_co_u32_e32 v48, vcc, 0x14000, v28
	s_nop 1
	v_addc_co_u32_e32 v49, vcc, 0, v29, vcc
	global_load_dword v60, v[48:49], off nt
	v_add_co_u32_e32 v48, vcc, 0x16000, v28
	s_nop 1
	v_addc_co_u32_e32 v49, vcc, 0, v29, vcc
	global_load_dword v61, v[48:49], off nt
	v_add_co_u32_e32 v48, vcc, 0x18000, v28
	s_nop 1
	v_addc_co_u32_e32 v49, vcc, 0, v29, vcc
	global_load_dword v62, v[48:49], off nt
	v_add_co_u32_e32 v48, vcc, 0x1a000, v28
	s_nop 1
	v_addc_co_u32_e32 v49, vcc, 0, v29, vcc
	global_load_dword v63, v[48:49], off nt
	v_add_co_u32_e32 v48, vcc, 0x1c000, v28
	s_nop 1
	v_addc_co_u32_e32 v49, vcc, 0, v29, vcc
	global_load_dword v64, v[48:49], off nt
	v_add_co_u32_e32 v48, vcc, 0x1e000, v28
	s_nop 1
	v_addc_co_u32_e32 v49, vcc, 0, v29, vcc
	global_load_dword v65, v[48:49], off nt
	v_add_co_u32_e32 v48, vcc, 0x20000, v28
	s_nop 1
	v_addc_co_u32_e32 v49, vcc, 0, v29, vcc
	global_load_dword v66, v[48:49], off nt
	v_add_co_u32_e32 v48, vcc, 0x22000, v28
	s_nop 1
	v_addc_co_u32_e32 v49, vcc, 0, v29, vcc
	global_load_dword v67, v[48:49], off nt
	v_add_co_u32_e32 v48, vcc, 0x24000, v28
	s_nop 1
	v_addc_co_u32_e32 v49, vcc, 0, v29, vcc
	global_load_dword v68, v[48:49], off nt
	v_add_co_u32_e32 v48, vcc, 0x26000, v28
	s_nop 1
	v_addc_co_u32_e32 v49, vcc, 0, v29, vcc
	global_load_dword v69, v[48:49], off nt
	v_add_co_u32_e32 v48, vcc, 0x28000, v28
	s_nop 1
	v_addc_co_u32_e32 v49, vcc, 0, v29, vcc
	global_load_dword v70, v[48:49], off nt
	v_add_co_u32_e32 v48, vcc, 0x2a000, v28
	s_nop 1
	v_addc_co_u32_e32 v49, vcc, 0, v29, vcc
	global_load_dword v71, v[48:49], off nt
	v_add_co_u32_e32 v48, vcc, 0x2c000, v28
	s_nop 1
	v_addc_co_u32_e32 v49, vcc, 0, v29, vcc
	global_load_dword v72, v[48:49], off nt
	v_add_co_u32_e32 v48, vcc, 0x2e000, v28
	s_nop 1
	v_addc_co_u32_e32 v49, vcc, 0, v29, vcc
	global_load_dword v73, v[48:49], off nt
	v_add_co_u32_e32 v48, vcc, 0x30000, v28
	s_nop 1
	v_addc_co_u32_e32 v49, vcc, 0, v29, vcc
	global_load_dword v74, v[48:49], off nt
	v_add_co_u32_e32 v48, vcc, 0x32000, v28
	s_nop 1
	v_addc_co_u32_e32 v49, vcc, 0, v29, vcc
	global_load_dword v75, v[48:49], off nt
	v_add_co_u32_e32 v48, vcc, 0x34000, v28
	s_nop 1
	v_addc_co_u32_e32 v49, vcc, 0, v29, vcc
	global_load_dword v76, v[48:49], off nt
	v_add_co_u32_e32 v48, vcc, 0x36000, v28
	s_nop 1
	v_addc_co_u32_e32 v49, vcc, 0, v29, vcc
	global_load_dword v77, v[48:49], off nt
	v_add_co_u32_e32 v48, vcc, 0x38000, v28
	s_nop 1
	v_addc_co_u32_e32 v49, vcc, 0, v29, vcc
	global_load_dword v78, v[48:49], off nt
	v_add_co_u32_e32 v48, vcc, 0x3a000, v28
	s_nop 1
	v_addc_co_u32_e32 v49, vcc, 0, v29, vcc
	global_load_dword v79, v[48:49], off nt
	v_add_co_u32_e32 v48, vcc, 0x3c000, v28
	s_nop 1
	v_addc_co_u32_e32 v49, vcc, 0, v29, vcc
	v_add_co_u32_e32 v28, vcc, 0x3e000, v28
	global_load_dword v48, v[48:49], off nt
	s_nop 0
	v_addc_co_u32_e32 v29, vcc, 0, v29, vcc
	global_load_dword v28, v[28:29], off nt
	s_waitcnt vmcnt(30)
	ds_write2_b32 v31, v50, v51 offset1:66
	s_waitcnt vmcnt(28)
	ds_write2_b32 v31, v52, v53 offset0:132 offset1:198
	s_waitcnt vmcnt(26)
	ds_write2_b32 v40, v54, v55 offset0:8 offset1:74
	s_waitcnt vmcnt(24)
	ds_write2_b32 v40, v56, v57 offset0:140 offset1:206
	s_waitcnt vmcnt(22)
	ds_write2_b32 v41, v58, v59 offset0:16 offset1:82
	s_waitcnt vmcnt(20)
	ds_write2_b32 v41, v60, v61 offset0:148 offset1:214
	s_waitcnt vmcnt(18)
	ds_write2_b32 v42, v62, v63 offset0:24 offset1:90
	s_waitcnt vmcnt(16)
	ds_write2_b32 v42, v64, v65 offset0:156 offset1:222
	s_waitcnt vmcnt(14)
	ds_write2_b32 v43, v66, v67 offset0:32 offset1:98
	s_waitcnt vmcnt(12)
	ds_write2_b32 v43, v68, v69 offset0:164 offset1:230
	s_waitcnt vmcnt(10)
	ds_write2_b32 v44, v70, v71 offset0:40 offset1:106
	s_waitcnt vmcnt(8)
; #define GAS __attribute__((address_space(1)))
; #define LAS __attribute__((address_space(3)))
; #define LDS_WAIT() asm volatile("s_waitcnt lgkmcnt(0)" ::: "memory")
; __device__ __forceinline__ unsigned pk2(float lo, float hi) { return f2bf(lo) | (f2bf(hi) << 16); }
; __device__ __forceinline__ void tr_item(const float* W, int ld, int K, int nblk, int item, bf16* WT, bool gu, LAS float* scr, int lane) {
;     ...
;     const int c = lane & 7;
; #pragma unroll
;     for (int j = 0; j < 4; ++j) { const int n = (lane >> 3) + 8 * j; const LAS float* s = scr + (8 * c) * 33 + n;
;         v4u o; o.x = pk2(s[0 * 33], s[1 * 33]); o.y = pk2(s[2 * 33], s[3 * 33]); o.z = pk2(s[4 * 33], s[5 * 33]); o.w = pk2(s[6 * 33], s[7 * 33]);
;         *(GAS v4u*)(WT + (size_t)(drow0 + n) * K + k0 + 8 * c) = o; }
;     LDS_WAIT(); asm volatile("" ::: "memory");
	ds_write2_b32 v44, v72, v73 offset0:172 offset1:238
	s_waitcnt vmcnt(6)
	ds_write2_b32 v45, v74, v75 offset0:48 offset1:114
	s_waitcnt vmcnt(4)
	ds_write2_b32 v45, v76, v77 offset0:180 offset1:246
	s_waitcnt vmcnt(2)
	ds_write2_b32 v46, v78, v79 offset0:56 offset1:122
	s_waitcnt vmcnt(0)
	ds_write2_b32 v46, v48, v28 offset0:188 offset1:254
	s_waitcnt lgkmcnt(0)
	ds_read2_b32 v[52:53], v36 offset0:33 offset1:41
	ds_read2_b32 v[54:55], v36 offset1:8
	ds_read2_b32 v[56:57], v36 offset0:66 offset1:74
	ds_read2_b32 v[58:59], v36 offset0:99 offset1:107
	ds_read2_b32 v[60:61], v36 offset0:132 offset1:140
	ds_read2_b32 v[62:63], v36 offset0:165 offset1:173
	ds_read2_b32 v[64:65], v36 offset0:198 offset1:206
	ds_read2_b32 v[66:67], v36 offset0:231 offset1:239
	s_waitcnt lgkmcnt(7)
	v_bfe_u32 v49, v52, 16, 1
	s_waitcnt lgkmcnt(6)
	v_bfe_u32 v48, v54, 16, 1
	v_add3_u32 v48, v54, v48, s15
	v_lshrrev_b32_e32 v48, 16, v48
	v_add3_u32 v49, v52, v49, s15
	v_and_or_b32 v48, v49, s16, v48
	s_waitcnt lgkmcnt(5)
	v_bfe_u32 v49, v56, 16, 1
	v_add3_u32 v49, v56, v49, s15
	s_waitcnt lgkmcnt(4)
	v_bfe_u32 v50, v58, 16, 1
	v_lshrrev_b32_e32 v49, 16, v49
	v_add3_u32 v50, v58, v50, s15
	v_and_or_b32 v49, v50, s16, v49
	s_waitcnt lgkmcnt(3)
	v_bfe_u32 v50, v60, 16, 1
	v_add3_u32 v50, v60, v50, s15
	s_waitcnt lgkmcnt(2)
	v_bfe_u32 v51, v62, 16, 1
	v_lshrrev_b32_e32 v50, 16, v50
	v_add3_u32 v51, v62, v51, s15
	v_and_or_b32 v50, v51, s16, v50
	s_waitcnt lgkmcnt(1)
	v_bfe_u32 v51, v64, 16, 1
	v_add_u32_e32 v68, s4, v35
	v_add3_u32 v51, v64, v51, s15
	s_waitcnt lgkmcnt(0)
	v_bfe_u32 v52, v66, 16, 1
	v_ashrrev_i32_e32 v69, 31, v68
	v_lshl_add_u64 v[28:29], v[24:25], 0, s[0:1]
	v_lshrrev_b32_e32 v51, 16, v51
	v_add3_u32 v52, v66, v52, s15
	v_lshlrev_b64 v[68:69], 11, v[68:69]
	v_and_or_b32 v51, v52, s16, v51
	v_lshl_add_u64 v[68:69], v[28:29], 0, v[68:69]
	global_store_dwordx4 v[68:69], v[48:51], off sc1 nt
	v_bfe_u32 v52, v67, 16, 1
	v_add3_u32 v52, v67, v52, s15
	v_bfe_u32 v48, v55, 16, 1
	v_add3_u32 v48, v55, v48, s15
	v_bfe_u32 v49, v53, 16, 1
	v_lshrrev_b32_e32 v48, 16, v48
	v_add3_u32 v49, v53, v49, s15
	v_and_or_b32 v48, v49, s16, v48
	v_bfe_u32 v49, v57, 16, 1
	v_add3_u32 v49, v57, v49, s15
	v_bfe_u32 v50, v59, 16, 1
	v_lshrrev_b32_e32 v49, 16, v49
	v_add3_u32 v50, v59, v50, s15
	v_and_or_b32 v49, v50, s16, v49
	v_bfe_u32 v50, v61, 16, 1
	v_add3_u32 v50, v61, v50, s15
	v_bfe_u32 v51, v63, 16, 1
	v_lshrrev_b32_e32 v50, 16, v50
	v_add3_u32 v51, v63, v51, s15
	v_and_or_b32 v50, v51, s16, v50
	v_bfe_u32 v51, v65, 16, 1
	v_add3_u32 v51, v65, v51, s15
	v_lshrrev_b32_e32 v51, 16, v51
	v_and_or_b32 v51, v52, s16, v51
	v_add_u32_e32 v52, s4, v37
	v_ashrrev_i32_e32 v53, 31, v52
	v_lshlrev_b64 v[52:53], 11, v[52:53]
	v_lshl_add_u64 v[52:53], v[28:29], 0, v[52:53]
	global_store_dwordx4 v[52:53], v[48:51], off sc1 nt
	ds_read2_b32 v[52:53], v36 offset0:49 offset1:57
	ds_read2_b32 v[54:55], v36 offset0:16 offset1:24
	ds_read2_b32 v[56:57], v36 offset0:82 offset1:90
	ds_read2_b32 v[58:59], v36 offset0:115 offset1:123
	ds_read2_b32 v[60:61], v36 offset0:148 offset1:156
	ds_read2_b32 v[62:63], v36 offset0:181 offset1:189
	ds_read2_b32 v[64:65], v36 offset0:214 offset1:222
	ds_read2_b32 v[66:67], v36 offset0:247 offset1:255
	s_waitcnt lgkmcnt(7)
	v_bfe_u32 v49, v52, 16, 1
	s_waitcnt lgkmcnt(6)
	v_bfe_u32 v48, v54, 16, 1
	v_add3_u32 v48, v54, v48, s15
	v_lshrrev_b32_e32 v48, 16, v48
	v_add3_u32 v49, v52, v49, s15
	v_and_or_b32 v48, v49, s16, v48
	s_waitcnt lgkmcnt(5)
	v_bfe_u32 v49, v56, 16, 1
	v_add3_u32 v49, v56, v49, s15
	s_waitcnt lgkmcnt(4)
	v_bfe_u32 v50, v58, 16, 1
	v_lshrrev_b32_e32 v49, 16, v49
	v_add3_u32 v50, v58, v50, s15
	v_and_or_b32 v49, v50, s16, v49
	s_waitcnt lgkmcnt(3)
	v_bfe_u32 v50, v60, 16, 1
	v_add3_u32 v50, v60, v50, s15
	s_waitcnt lgkmcnt(2)
	v_bfe_u32 v51, v62, 16, 1
	v_lshrrev_b32_e32 v50, 16, v50
	v_add3_u32 v51, v62, v51, s15
	v_and_or_b32 v50, v51, s16, v50
	s_waitcnt lgkmcnt(1)
	v_bfe_u32 v51, v64, 16, 1
	v_add_u32_e32 v68, s4, v38
	v_add3_u32 v51, v64, v51, s15
	s_waitcnt lgkmcnt(0)
	v_bfe_u32 v52, v66, 16, 1
	v_ashrrev_i32_e32 v69, 31, v68
	v_lshrrev_b32_e32 v51, 16, v51
	v_add3_u32 v52, v66, v52, s15
	v_lshlrev_b64 v[68:69], 11, v[68:69]
	v_and_or_b32 v51, v52, s16, v51
	v_lshl_add_u64 v[68:69], v[28:29], 0, v[68:69]
	global_store_dwordx4 v[68:69], v[48:51], off sc1 nt
	v_bfe_u32 v52, v67, 16, 1
	v_add3_u32 v52, v67, v52, s15
	v_bfe_u32 v48, v55, 16, 1
	v_add3_u32 v48, v55, v48, s15
	v_bfe_u32 v49, v53, 16, 1
	v_lshrrev_b32_e32 v48, 16, v48
	v_add3_u32 v49, v53, v49, s15
	v_and_or_b32 v48, v49, s16, v48
	v_bfe_u32 v49, v57, 16, 1
	v_add3_u32 v49, v57, v49, s15
	v_bfe_u32 v50, v59, 16, 1
	v_lshrrev_b32_e32 v49, 16, v49
	v_add3_u32 v50, v59, v50, s15
	v_and_or_b32 v49, v50, s16, v49
	v_bfe_u32 v50, v61, 16, 1
	v_add3_u32 v50, v61, v50, s15
	v_bfe_u32 v51, v63, 16, 1
	v_lshrrev_b32_e32 v50, 16, v50
	v_add3_u32 v51, v63, v51, s15
	v_and_or_b32 v50, v51, s16, v50
	v_bfe_u32 v51, v65, 16, 1
	v_add3_u32 v51, v65, v51, s15
	v_lshrrev_b32_e32 v51, 16, v51
	v_and_or_b32 v51, v52, s16, v51
	v_add_u32_e32 v52, s4, v39
	v_ashrrev_i32_e32 v53, 31, v52
	v_lshlrev_b64 v[52:53], 11, v[52:53]
	v_lshl_add_u64 v[28:29], v[28:29], 0, v[52:53]
	global_store_dwordx4 v[28:29], v[48:51], off sc1 nt
	s_waitcnt lgkmcnt(0)

; #define LDS_WAIT() asm volatile("s_waitcnt lgkmcnt(0)" ::: "memory")
; __device__ __forceinline__ void tr_item(const float* W, int ld, int K, int nblk, int item, bf16* WT, bool gu, LAS float* scr, int lane) {
;     const int kb = item / nblk, nb = item % nblk, k0 = 64 * kb, n0 = 32 * nb;
;     int drow0 = n0;
;     if (gu) { const int bj = n0 / FF, j = n0 - bj * FF; drow0 = 256 * (j / 128) + 128 * bj + (j % 128); }
;     { float t_[32];
; #pragma unroll
;       for (int i = 0; i < 32; ++i) t_[i] = W[(size_t)(k0 + 2 * i + (lane >> 5)) * ld + n0 + (lane & 31)];
; #pragma unroll
;       for (int i = 0; i < 32; ++i) scr[(2 * i + (lane >> 5)) * 33 + (lane & 31)] = t_[i]; }
;     LDS_WAIT(); asm volatile("" ::: "memory");
; __device__ __forceinline__ void convert_items(Frame& F, const Args& a, int lo, int hi, int w, int nw) {
;     ...
;         if (r < I_FI) { tr_item(a.in[7], 3 * D + 16, D, 96, r, (bf16*)(F.ws + WS_WFOXIN), false, scr, lane); continue; } r -= I_FI;
.LBB0_1322:
	s_andn2_b64 vcc, exec, s[4:5]
	s_cbranch_vccnz .LBB0_1295
	s_mul_hi_i32 s0, s8, 0x2aaaaaab
	s_lshr_b32 s4, s0, 31
	s_ashr_i32 s0, s0, 4
	s_add_i32 s0, s0, s4
	s_lshl_b32 s6, s0, 6
	s_mulk_i32 s0, 0xf400
	s_add_i32 s4, s9, s0
	s_ashr_i32 s5, s4, 31
	v_add_u32_e32 v50, s6, v30
	v_lshl_add_u64 v[28:29], s[4:5], 2, v[14:15]
	v_mad_i64_i32 v[48:49], s[40:41], v50, s30, v[28:29]
	global_load_dword v51, v[48:49], off nt
	v_add_u32_e32 v48, 2, v50
	v_mad_i64_i32 v[48:49], s[40:41], v48, s30, v[28:29]
	global_load_dword v52, v[48:49], off nt
	v_add_u32_e32 v48, 4, v50
	v_mad_i64_i32 v[48:49], s[40:41], v48, s30, v[28:29]
	global_load_dword v53, v[48:49], off nt
	v_add_u32_e32 v48, 6, v50
	v_mad_i64_i32 v[48:49], s[40:41], v48, s30, v[28:29]
	global_load_dword v54, v[48:49], off nt
	v_add_u32_e32 v48, 8, v50
	v_mad_i64_i32 v[48:49], s[40:41], v48, s30, v[28:29]
	global_load_dword v55, v[48:49], off nt
	v_add_u32_e32 v48, 10, v50
	v_mad_i64_i32 v[48:49], s[40:41], v48, s30, v[28:29]
	global_load_dword v56, v[48:49], off nt
	v_add_u32_e32 v48, 12, v50
	v_mad_i64_i32 v[48:49], s[40:41], v48, s30, v[28:29]
	global_load_dword v57, v[48:49], off nt
	v_add_u32_e32 v48, 14, v50
	v_mad_i64_i32 v[48:49], s[40:41], v48, s30, v[28:29]
	global_load_dword v58, v[48:49], off nt
	v_add_u32_e32 v48, 16, v50
	v_mad_i64_i32 v[48:49], s[40:41], v48, s30, v[28:29]
	global_load_dword v59, v[48:49], off nt
	v_add_u32_e32 v48, 18, v50
	v_mad_i64_i32 v[48:49], s[40:41], v48, s30, v[28:29]
	global_load_dword v60, v[48:49], off nt
	v_add_u32_e32 v48, 20, v50
	v_mad_i64_i32 v[48:49], s[40:41], v48, s30, v[28:29]
	global_load_dword v61, v[48:49], off nt
	v_add_u32_e32 v48, 22, v50
	v_mad_i64_i32 v[48:49], s[40:41], v48, s30, v[28:29]
	global_load_dword v62, v[48:49], off nt
	v_add_u32_e32 v48, 24, v50
	v_mad_i64_i32 v[48:49], s[40:41], v48, s30, v[28:29]
	global_load_dword v63, v[48:49], off nt
	v_add_u32_e32 v48, 26, v50
	v_mad_i64_i32 v[48:49], s[40:41], v48, s30, v[28:29]
	global_load_dword v64, v[48:49], off nt
	v_add_u32_e32 v48, 28, v50
	v_mad_i64_i32 v[48:49], s[40:41], v48, s30, v[28:29]
	global_load_dword v65, v[48:49], off nt
	v_add_u32_e32 v48, 30, v50
	v_mad_i64_i32 v[48:49], s[40:41], v48, s30, v[28:29]
	global_load_dword v66, v[48:49], off nt
	v_add_u32_e32 v48, 32, v50
	v_mad_i64_i32 v[48:49], s[40:41], v48, s30, v[28:29]
	global_load_dword v67, v[48:49], off nt
	v_add_u32_e32 v48, 34, v50
	v_mad_i64_i32 v[48:49], s[40:41], v48, s30, v[28:29]
	global_load_dword v68, v[48:49], off nt
	v_add_u32_e32 v48, 36, v50
	v_mad_i64_i32 v[48:49], s[40:41], v48, s30, v[28:29]
	global_load_dword v69, v[48:49], off nt
	v_add_u32_e32 v48, 38, v50
	v_mad_i64_i32 v[48:49], s[40:41], v48, s30, v[28:29]
	global_load_dword v70, v[48:49], off nt
	v_add_u32_e32 v48, 40, v50
	v_mad_i64_i32 v[48:49], s[40:41], v48, s30, v[28:29]
	global_load_dword v71, v[48:49], off nt
	v_add_u32_e32 v48, 42, v50
	v_mad_i64_i32 v[48:49], s[40:41], v48, s30, v[28:29]
	global_load_dword v72, v[48:49], off nt
	v_add_u32_e32 v48, 44, v50
	v_mad_i64_i32 v[48:49], s[40:41], v48, s30, v[28:29]
	global_load_dword v73, v[48:49], off nt
	v_add_u32_e32 v48, 46, v50
	v_mad_i64_i32 v[48:49], s[40:41], v48, s30, v[28:29]
	global_load_dword v74, v[48:49], off nt
	v_add_u32_e32 v48, 48, v50
	v_mad_i64_i32 v[48:49], s[40:41], v48, s30, v[28:29]
	global_load_dword v75, v[48:49], off nt
	v_add_u32_e32 v48, 50, v50
	v_mad_i64_i32 v[48:49], s[40:41], v48, s30, v[28:29]
	global_load_dword v76, v[48:49], off nt
	v_add_u32_e32 v48, 52, v50
	v_mad_i64_i32 v[48:49], s[40:41], v48, s30, v[28:29]
	global_load_dword v77, v[48:49], off nt
	v_add_u32_e32 v48, 54, v50
	v_mad_i64_i32 v[48:49], s[40:41], v48, s30, v[28:29]
	global_load_dword v78, v[48:49], off nt
	v_add_u32_e32 v48, 56, v50
	v_mad_i64_i32 v[48:49], s[40:41], v48, s30, v[28:29]
	global_load_dword v79, v[48:49], off nt
	v_add_u32_e32 v48, 58, v50
	v_mad_i64_i32 v[48:49], s[40:41], v48, s30, v[28:29]
	global_load_dword v80, v[48:49], off nt
	v_add_u32_e32 v48, 60, v50
	v_mad_i64_i32 v[48:49], s[40:41], v48, s30, v[28:29]
	global_load_dword v48, v[48:49], off nt
	v_add_u32_e32 v49, 62, v50
	v_mad_i64_i32 v[28:29], s[40:41], v49, s30, v[28:29]
	global_load_dword v28, v[28:29], off nt
	s_waitcnt vmcnt(30)
	ds_write2_b32 v31, v51, v52 offset1:66
	s_waitcnt vmcnt(28)
	ds_write2_b32 v31, v53, v54 offset0:132 offset1:198
	s_waitcnt vmcnt(26)
	ds_write2_b32 v40, v55, v56 offset0:8 offset1:74
	s_waitcnt vmcnt(24)
	ds_write2_b32 v40, v57, v58 offset0:140 offset1:206
	s_waitcnt vmcnt(22)
	ds_write2_b32 v41, v59, v60 offset0:16 offset1:82
	s_waitcnt vmcnt(20)
	ds_write2_b32 v41, v61, v62 offset0:148 offset1:214
	s_waitcnt vmcnt(18)
	ds_write2_b32 v42, v63, v64 offset0:24 offset1:90
	s_waitcnt vmcnt(16)
	ds_write2_b32 v42, v65, v66 offset0:156 offset1:222
	s_waitcnt vmcnt(14)
	ds_write2_b32 v43, v67, v68 offset0:32 offset1:98
	s_waitcnt vmcnt(12)
	ds_write2_b32 v43, v69, v70 offset0:164 offset1:230
	s_waitcnt vmcnt(10)
	ds_write2_b32 v44, v71, v72 offset0:40 offset1:106
	s_waitcnt vmcnt(8)
	ds_write2_b32 v44, v73, v74 offset0:172 offset1:238
	s_waitcnt vmcnt(6)
	ds_write2_b32 v45, v75, v76 offset0:48 offset1:114
	s_waitcnt vmcnt(4)
; #define GAS __attribute__((address_space(1)))
; #define LAS __attribute__((address_space(3)))
; #define LDS_WAIT() asm volatile("s_waitcnt lgkmcnt(0)" ::: "memory")
; __device__ __forceinline__ unsigned pk2(float lo, float hi) { return f2bf(lo) | (f2bf(hi) << 16); }
; __device__ __forceinline__ void tr_item(const float* W, int ld, int K, int nblk, int item, bf16* WT, bool gu, LAS float* scr, int lane) {
;     ...
;     const int c = lane & 7;
; #pragma unroll
;     for (int j = 0; j < 4; ++j) { const int n = (lane >> 3) + 8 * j; const LAS float* s = scr + (8 * c) * 33 + n;
;         v4u o; o.x = pk2(s[0 * 33], s[1 * 33]); o.y = pk2(s[2 * 33], s[3 * 33]); o.z = pk2(s[4 * 33], s[5 * 33]); o.w = pk2(s[6 * 33], s[7 * 33]);
;         *(GAS v4u*)(WT + (size_t)(drow0 + n) * K + k0 + 8 * c) = o; }
;     LDS_WAIT(); asm volatile("" ::: "memory");
	ds_write2_b32 v45, v77, v78 offset0:180 offset1:246
	s_waitcnt vmcnt(2)
	ds_write2_b32 v46, v79, v80 offset0:56 offset1:122
	s_waitcnt vmcnt(0)
	ds_write2_b32 v46, v48, v28 offset0:188 offset1:254
	s_waitcnt lgkmcnt(0)
	ds_read2_b32 v[52:53], v36 offset0:33 offset1:41
	ds_read2_b32 v[54:55], v36 offset1:8
	ds_read2_b32 v[56:57], v36 offset0:66 offset1:74
	ds_read2_b32 v[58:59], v36 offset0:99 offset1:107
	ds_read2_b32 v[60:61], v36 offset0:132 offset1:140
	ds_read2_b32 v[62:63], v36 offset0:165 offset1:173
	ds_read2_b32 v[64:65], v36 offset0:198 offset1:206
	ds_read2_b32 v[66:67], v36 offset0:231 offset1:239
	s_waitcnt lgkmcnt(7)
	v_bfe_u32 v49, v52, 16, 1
	s_waitcnt lgkmcnt(6)
	v_bfe_u32 v48, v54, 16, 1
	v_add3_u32 v48, v54, v48, s15
	v_lshrrev_b32_e32 v48, 16, v48
	v_add3_u32 v49, v52, v49, s15
	v_and_or_b32 v48, v49, s16, v48
	s_waitcnt lgkmcnt(5)
	v_bfe_u32 v49, v56, 16, 1
	v_add3_u32 v49, v56, v49, s15
	s_waitcnt lgkmcnt(4)
	v_bfe_u32 v50, v58, 16, 1
	v_lshrrev_b32_e32 v49, 16, v49
	v_add3_u32 v50, v58, v50, s15
	v_and_or_b32 v49, v50, s16, v49
	s_waitcnt lgkmcnt(3)
	v_bfe_u32 v50, v60, 16, 1
	v_add3_u32 v50, v60, v50, s15
	s_waitcnt lgkmcnt(2)
	v_bfe_u32 v51, v62, 16, 1
	v_lshrrev_b32_e32 v50, 16, v50
	v_add3_u32 v51, v62, v51, s15
	v_and_or_b32 v50, v51, s16, v50
	s_waitcnt lgkmcnt(1)
	v_bfe_u32 v51, v64, 16, 1
	v_add_u32_e32 v68, s4, v35
	s_ashr_i32 s7, s6, 31
	v_add3_u32 v51, v64, v51, s15
	s_waitcnt lgkmcnt(0)
	v_bfe_u32 v52, v66, 16, 1
	v_ashrrev_i32_e32 v69, 31, v68
	v_lshl_add_u64 v[28:29], s[6:7], 1, v[26:27]
	v_lshrrev_b32_e32 v51, 16, v51
	v_add3_u32 v52, v66, v52, s15
	v_lshlrev_b64 v[70:71], 11, v[68:69]
	v_and_or_b32 v51, v52, s16, v51
	v_lshl_add_u64 v[70:71], v[28:29], 0, v[70:71]
	global_store_dwordx4 v[70:71], v[48:51], off sc1 nt
	v_bfe_u32 v52, v67, 16, 1
	v_add3_u32 v52, v67, v52, s15
	v_bfe_u32 v48, v55, 16, 1
	v_add3_u32 v48, v55, v48, s15
	v_bfe_u32 v49, v53, 16, 1
	v_lshrrev_b32_e32 v48, 16, v48
	v_add3_u32 v49, v53, v49, s15
	v_and_or_b32 v48, v49, s16, v48
	v_bfe_u32 v49, v57, 16, 1
	v_add3_u32 v49, v57, v49, s15
	v_bfe_u32 v50, v59, 16, 1
	v_lshrrev_b32_e32 v49, 16, v49
	v_add3_u32 v50, v59, v50, s15
	v_and_or_b32 v49, v50, s16, v49
	v_bfe_u32 v50, v61, 16, 1
	v_add3_u32 v50, v61, v50, s15
	v_bfe_u32 v51, v63, 16, 1
	v_lshrrev_b32_e32 v50, 16, v50
	v_add3_u32 v51, v63, v51, s15
	v_and_or_b32 v50, v51, s16, v50
	v_bfe_u32 v51, v65, 16, 1
	v_add3_u32 v51, v65, v51, s15
	v_lshrrev_b32_e32 v51, 16, v51
	v_and_or_b32 v51, v52, s16, v51
	v_add_u32_e32 v52, 8, v68
	v_ashrrev_i32_e32 v53, 31, v52
	v_lshlrev_b64 v[52:53], 11, v[52:53]
	v_lshl_add_u64 v[52:53], v[28:29], 0, v[52:53]
	global_store_dwordx4 v[52:53], v[48:51], off sc1 nt
	ds_read2_b32 v[52:53], v36 offset0:49 offset1:57
	ds_read2_b32 v[54:55], v36 offset0:16 offset1:24
	ds_read2_b32 v[56:57], v36 offset0:82 offset1:90
	ds_read2_b32 v[58:59], v36 offset0:115 offset1:123
	ds_read2_b32 v[60:61], v36 offset0:148 offset1:156
	ds_read2_b32 v[62:63], v36 offset0:181 offset1:189
	ds_read2_b32 v[64:65], v36 offset0:214 offset1:222
	ds_read2_b32 v[66:67], v36 offset0:247 offset1:255
	s_waitcnt lgkmcnt(7)
	v_bfe_u32 v49, v52, 16, 1
	s_waitcnt lgkmcnt(6)
	v_bfe_u32 v48, v54, 16, 1
	v_add3_u32 v48, v54, v48, s15
	v_lshrrev_b32_e32 v48, 16, v48
	v_add3_u32 v49, v52, v49, s15
	v_and_or_b32 v48, v49, s16, v48
	s_waitcnt lgkmcnt(5)
	v_bfe_u32 v49, v56, 16, 1
	v_add3_u32 v49, v56, v49, s15
	s_waitcnt lgkmcnt(4)
	v_bfe_u32 v50, v58, 16, 1
	v_lshrrev_b32_e32 v49, 16, v49
	v_add3_u32 v50, v58, v50, s15
	v_and_or_b32 v49, v50, s16, v49
	s_waitcnt lgkmcnt(3)
	v_bfe_u32 v50, v60, 16, 1
	v_add3_u32 v50, v60, v50, s15
	s_waitcnt lgkmcnt(2)
	v_bfe_u32 v51, v62, 16, 1
	v_lshrrev_b32_e32 v50, 16, v50
	v_add3_u32 v51, v62, v51, s15
	v_and_or_b32 v50, v51, s16, v50
	s_waitcnt lgkmcnt(1)
	v_bfe_u32 v51, v64, 16, 1
	v_add_u32_e32 v70, 16, v68
	v_add3_u32 v51, v64, v51, s15
	s_waitcnt lgkmcnt(0)
	v_bfe_u32 v52, v66, 16, 1
	v_ashrrev_i32_e32 v71, 31, v70
	v_lshrrev_b32_e32 v51, 16, v51
	v_add3_u32 v52, v66, v52, s15
	v_lshlrev_b64 v[70:71], 11, v[70:71]
	v_and_or_b32 v51, v52, s16, v51
	v_lshl_add_u64 v[70:71], v[28:29], 0, v[70:71]
	global_store_dwordx4 v[70:71], v[48:51], off sc1 nt
	v_bfe_u32 v52, v67, 16, 1
	v_add3_u32 v52, v67, v52, s15
	v_bfe_u32 v48, v55, 16, 1
	v_add3_u32 v48, v55, v48, s15
	v_bfe_u32 v49, v53, 16, 1
	v_lshrrev_b32_e32 v48, 16, v48
	v_add3_u32 v49, v53, v49, s15
	v_and_or_b32 v48, v49, s16, v48
	v_bfe_u32 v49, v57, 16, 1
	v_add3_u32 v49, v57, v49, s15
	v_bfe_u32 v50, v59, 16, 1
	v_lshrrev_b32_e32 v49, 16, v49
	v_add3_u32 v50, v59, v50, s15
	v_and_or_b32 v49, v50, s16, v49
	v_bfe_u32 v50, v61, 16, 1
	v_add3_u32 v50, v61, v50, s15
	v_bfe_u32 v51, v63, 16, 1
	v_lshrrev_b32_e32 v50, 16, v50
	v_add3_u32 v51, v63, v51, s15
	v_and_or_b32 v50, v51, s16, v50
	v_bfe_u32 v51, v65, 16, 1
	v_add3_u32 v51, v65, v51, s15
	v_lshrrev_b32_e32 v51, 16, v51
	v_and_or_b32 v51, v52, s16, v51
	v_add_u32_e32 v52, 24, v68
	v_ashrrev_i32_e32 v53, 31, v52
	v_lshlrev_b64 v[52:53], 11, v[52:53]
	v_lshl_add_u64 v[28:29], v[28:29], 0, v[52:53]
	global_store_dwordx4 v[28:29], v[48:51], off sc1 nt
	s_waitcnt lgkmcnt(0)
	s_branch .LBB0_1295

; #define LAS __attribute__((address_space(3)))
; __device__ __forceinline__ void tr_item8(const float* W, int ld, int K, int nblk, int item, unsigned char* WT, bool gu, float scale, LAS float* scr, int lane) {
;     const int kb = item / nblk, nb = item % nblk, k0 = 64 * kb, n0 = 32 * nb;
;     int drow0 = n0;
;     if (gu) { const int bj = n0 / FF, j = n0 - bj * FF; drow0 = 256 * (j / 128) + 128 * bj + (j % 128); }
;     { float t_[32];
; #pragma unroll
;       for (int i = 0; i < 32; ++i) t_[i] = W[(size_t)(k0 + 2 * i + (lane >> 5)) * ld + n0 + (lane & 31)];
; __device__ __forceinline__ void convert_items(Frame& F, const Args& a, int lo, int hi, int w, int nw) {
;     ...
;         { const int e = r / I_DN, rr = r % I_DN; tr_item8(a.in[19] + (size_t)e * FF * D, D, FF, 32, rr, F.ws + WS_WMDN + (size_t)e * D * FF, false, WSC_DN, scr, lane); }
.LBB0_1330:
	s_cmpk_gt_i32 s8, 0x5ff
	s_mov_b64 s[4:5], -1
	s_cbranch_scc0 .LBB0_1356
	s_cmpk_gt_u32 s8, 0x7ff
	s_cbranch_scc0 .LBB0_1353
	s_cmpk_gt_u32 s8, 0xaff
	s_cbranch_scc0 .LBB0_1350
	s_cmpk_gt_u32 s8, 0xcff
	s_cbranch_scc0 .LBB0_1347
	s_cmpk_gt_u32 s8, 0x1aff
	s_cbranch_scc0 .LBB0_1344
	s_cmpk_gt_u32 s8, 0x21ff
	s_cbranch_scc0 .LBB0_1341
	s_cmpk_gt_u32 s8, 0x91ff
	s_cbranch_scc0 .LBB0_1338
	s_add_i32 s0, s8, 0x6e00
	s_bfe_u32 s4, s0, 0x80008
	s_mulk_i32 s4, 0x2493
	s_lshr_b32 s4, s4, 16
	s_mul_i32 s5, s4, 0x700
	v_readlane_b32 s40, v254, 28
	s_sub_i32 s6, s0, s5
	s_mul_i32 s0, s4, 0xe00000
	v_readlane_b32 s46, v254, 34
	v_readlane_b32 s47, v254, 35
	s_add_u32 s7, s46, s0
	s_addc_u32 s31, s47, 0
	s_mul_i32 s4, s4, 0x380000
	s_add_u32 s4, s66, s4
	s_addc_u32 s5, s58, 0
	s_lshl_b32 s0, s6, 5
	s_and_b32 s0, s0, 0x3e0
	s_lshl_b32 s6, s6, 1
	s_and_b32 s6, s6, 0xfc0
	s_lshl_b32 s40, s0, 2
	v_readlane_b32 s41, v254, 29
	v_add_u32_e32 v28, s6, v30
	s_add_u32 s40, s7, s40
	s_addc_u32 s41, s31, 0
	v_ashrrev_i32_e32 v29, 31, v28
	v_lshl_add_u64 v[48:49], s[40:41], 0, v[0:1]
	v_lshlrev_b64 v[28:29], 12, v[28:29]
	v_lshl_add_u64 v[28:29], v[48:49], 0, v[28:29]
	s_movk_i32 s7, 0x2000
	v_add_co_u32_e32 v48, vcc, s7, v28
	s_movk_i32 s7, 0x4000
	s_nop 0
	v_addc_co_u32_e32 v49, vcc, 0, v29, vcc
	global_load_dword v50, v[28:29], off nt
	global_load_dword v51, v[48:49], off nt
	v_add_co_u32_e32 v48, vcc, s7, v28
	s_movk_i32 s7, 0x6000
	s_nop 0
	v_addc_co_u32_e32 v49, vcc, 0, v29, vcc
	global_load_dword v52, v[48:49], off nt
	v_add_co_u32_e32 v48, vcc, s7, v28
	s_mov_b32 s7, 0x8000
	s_nop 0
	v_addc_co_u32_e32 v49, vcc, 0, v29, vcc
	global_load_dword v53, v[48:49], off nt
	v_add_co_u32_e32 v48, vcc, s7, v28
	s_mov_b32 s7, 0xa000
	s_nop 0
	v_addc_co_u32_e32 v49, vcc, 0, v29, vcc
	global_load_dword v54, v[48:49], off nt
	v_add_co_u32_e32 v48, vcc, s7, v28
	s_mov_b32 s7, 0xc000
	s_nop 0
	v_addc_co_u32_e32 v49, vcc, 0, v29, vcc
	global_load_dword v55, v[48:49], off nt
	v_add_co_u32_e32 v48, vcc, s7, v28
	s_mov_b32 s7, 0xe000
	s_nop 0
	v_addc_co_u32_e32 v49, vcc, 0, v29, vcc
	global_load_dword v56, v[48:49], off nt
	v_add_co_u32_e32 v48, vcc, s7, v28
	s_mov_b32 s7, 0x10000
	s_nop 0
	v_addc_co_u32_e32 v49, vcc, 0, v29, vcc
	global_load_dword v57, v[48:49], off nt
	v_add_co_u32_e32 v48, vcc, s7, v28
	s_mov_b32 s7, 0x12000
	s_nop 0
	v_addc_co_u32_e32 v49, vcc, 0, v29, vcc
	global_load_dword v58, v[48:49], off nt
	v_add_co_u32_e32 v48, vcc, s7, v28
	s_mov_b32 s7, 0x14000
	s_nop 0
	v_addc_co_u32_e32 v49, vcc, 0, v29, vcc
	global_load_dword v59, v[48:49], off nt
	v_add_co_u32_e32 v48, vcc, s7, v28
	s_mov_b32 s7, 0x16000
	s_nop 0
	v_addc_co_u32_e32 v49, vcc, 0, v29, vcc
	global_load_dword v60, v[48:49], off nt
	v_add_co_u32_e32 v48, vcc, s7, v28
	s_mov_b32 s7, 0x18000
	s_nop 0
	v_addc_co_u32_e32 v49, vcc, 0, v29, vcc
	global_load_dword v61, v[48:49], off nt
	v_add_co_u32_e32 v48, vcc, s7, v28
	s_mov_b32 s7, 0x1a000
	s_nop 0
	v_addc_co_u32_e32 v49, vcc, 0, v29, vcc
	global_load_dword v62, v[48:49], off nt
	v_add_co_u32_e32 v48, vcc, s7, v28
	s_mov_b32 s7, 0x1c000
	s_nop 0
	v_addc_co_u32_e32 v49, vcc, 0, v29, vcc
	global_load_dword v63, v[48:49], off nt
	v_add_co_u32_e32 v48, vcc, s7, v28
	s_mov_b32 s7, 0x1e000
	s_nop 0
	v_addc_co_u32_e32 v49, vcc, 0, v29, vcc
	global_load_dword v64, v[48:49], off nt
	v_add_co_u32_e32 v48, vcc, s7, v28
	s_mov_b32 s7, 0x20000
	s_nop 0
	v_addc_co_u32_e32 v49, vcc, 0, v29, vcc
	global_load_dword v65, v[48:49], off nt
	v_add_co_u32_e32 v48, vcc, s7, v28
	s_mov_b32 s7, 0x22000
	s_nop 0
	v_addc_co_u32_e32 v49, vcc, 0, v29, vcc
	global_load_dword v66, v[48:49], off nt
	v_add_co_u32_e32 v48, vcc, s7, v28
	s_mov_b32 s7, 0x24000
	s_nop 0
	v_addc_co_u32_e32 v49, vcc, 0, v29, vcc
	global_load_dword v67, v[48:49], off nt
	v_add_co_u32_e32 v48, vcc, s7, v28
	s_mov_b32 s7, 0x26000
	s_nop 0
	v_addc_co_u32_e32 v49, vcc, 0, v29, vcc
	global_load_dword v68, v[48:49], off nt
	v_add_co_u32_e32 v48, vcc, s7, v28
	s_mov_b32 s7, 0x28000
	s_nop 0
	v_addc_co_u32_e32 v49, vcc, 0, v29, vcc
	global_load_dword v69, v[48:49], off nt
	v_add_co_u32_e32 v48, vcc, s7, v28
	s_mov_b32 s7, 0x2a000
	s_nop 0
	v_addc_co_u32_e32 v49, vcc, 0, v29, vcc
	global_load_dword v70, v[48:49], off nt
	v_add_co_u32_e32 v48, vcc, s7, v28
	s_mov_b32 s7, 0x2c000
	s_nop 0
	v_addc_co_u32_e32 v49, vcc, 0, v29, vcc
	global_load_dword v71, v[48:49], off nt
	v_add_co_u32_e32 v48, vcc, s7, v28
	s_mov_b32 s7, 0x2e000
	s_nop 0
	v_addc_co_u32_e32 v49, vcc, 0, v29, vcc
	global_load_dword v72, v[48:49], off nt
	v_add_co_u32_e32 v48, vcc, s7, v28
	s_mov_b32 s7, 0x30000
	s_nop 0
	v_addc_co_u32_e32 v49, vcc, 0, v29, vcc
	global_load_dword v73, v[48:49], off nt
	v_add_co_u32_e32 v48, vcc, s7, v28
	s_mov_b32 s7, 0x32000
	s_nop 0
	v_addc_co_u32_e32 v49, vcc, 0, v29, vcc
	global_load_dword v74, v[48:49], off nt
	v_add_co_u32_e32 v48, vcc, s7, v28
	s_mov_b32 s7, 0x34000
	s_nop 0
	v_addc_co_u32_e32 v49, vcc, 0, v29, vcc
	global_load_dword v75, v[48:49], off nt
	v_add_co_u32_e32 v48, vcc, s7, v28
	s_mov_b32 s7, 0x36000
	s_nop 0
	v_addc_co_u32_e32 v49, vcc, 0, v29, vcc
	global_load_dword v76, v[48:49], off nt
	v_add_co_u32_e32 v48, vcc, s7, v28
	s_mov_b32 s7, 0x38000
	s_nop 0
	v_addc_co_u32_e32 v49, vcc, 0, v29, vcc
	global_load_dword v77, v[48:49], off nt
	v_add_co_u32_e32 v48, vcc, s7, v28
	s_mov_b32 s7, 0x3a000
	s_nop 0
	v_addc_co_u32_e32 v49, vcc, 0, v29, vcc
	global_load_dword v78, v[48:49], off nt
	v_add_co_u32_e32 v48, vcc, s7, v28
	s_mov_b32 s7, 0x3c000
	s_nop 0
	v_addc_co_u32_e32 v49, vcc, 0, v29, vcc
	global_load_dword v79, v[48:49], off nt
	v_add_co_u32_e32 v48, vcc, s7, v28
	s_mov_b32 s7, 0x3e000
	s_nop 0
	v_addc_co_u32_e32 v49, vcc, 0, v29, vcc
	v_add_co_u32_e32 v28, vcc, s7, v28
	global_load_dword v48, v[48:49], off nt
	s_nop 0
	v_addc_co_u32_e32 v29, vcc, 0, v29, vcc
	global_load_dword v28, v[28:29], off nt
	s_waitcnt vmcnt(0)
; __device__ __forceinline__ unsigned cvt_pk4_fp8(float a, float b, float c, float d) { int w = 0; w = __builtin_amdgcn_cvt_pk_fp8_f32(a, b, w, false); w = __builtin_amdgcn_cvt_pk_fp8_f32(c, d, w, true); return (unsigned)w; }
; #define GAS __attribute__((address_space(1)))
; #define LAS __attribute__((address_space(3)))
; #define LDS_WAIT() asm volatile("s_waitcnt lgkmcnt(0)" ::: "memory")
; __device__ __forceinline__ void tr_item8(const float* W, int ld, int K, int nblk, int item, unsigned char* WT, bool gu, float scale, LAS float* scr, int lane) {
;     ...
; #pragma unroll
;       for (int i = 0; i < 32; ++i) scr[(2 * i + (lane >> 5)) * 33 + (lane & 31)] = t_[i] * scale; }
;     LDS_WAIT(); asm volatile("" ::: "memory");
;     const int c = lane & 3;
; #pragma unroll
;     for (int j = 0; j < 2; ++j) { const int n = (lane >> 2) + 16 * j; const LAS float* sp = scr + (16 * c) * 33 + n;
;         v4u o; o.x = pg8::cvt_pk4_fp8(sp[0 * 33], sp[1 * 33], sp[2 * 33], sp[3 * 33]); o.y = pg8::cvt_pk4_fp8(sp[4 * 33], sp[5 * 33], sp[6 * 33], sp[7 * 33]);
;         o.z = pg8::cvt_pk4_fp8(sp[8 * 33], sp[9 * 33], sp[10 * 33], sp[11 * 33]); o.w = pg8::cvt_pk4_fp8(sp[12 * 33], sp[13 * 33], sp[14 * 33], sp[15 * 33]);
;         *(GAS v4u*)(WT + (size_t)(drow0 + n) * K + k0 + 16 * c) = o; }
;     LDS_WAIT(); asm volatile("" ::: "memory");
	v_mul_f32_e32 v29, 0x43000000, v50
	v_mul_f32_e32 v49, 0x43000000, v51
	ds_write2_b32 v31, v29, v49 offset1:66
	v_mul_f32_e32 v29, 0x43000000, v52
	v_mul_f32_e32 v49, 0x43000000, v53
	ds_write2_b32 v31, v29, v49 offset0:132 offset1:198
	v_mul_f32_e32 v29, 0x43000000, v54
	v_mul_f32_e32 v49, 0x43000000, v55
	ds_write2_b32 v40, v29, v49 offset0:8 offset1:74
	v_mul_f32_e32 v29, 0x43000000, v56
	v_mul_f32_e32 v49, 0x43000000, v57
	ds_write2_b32 v40, v29, v49 offset0:140 offset1:206
	v_mul_f32_e32 v29, 0x43000000, v58
	v_mul_f32_e32 v49, 0x43000000, v59
	ds_write2_b32 v41, v29, v49 offset0:16 offset1:82
	v_mul_f32_e32 v29, 0x43000000, v60
	v_mul_f32_e32 v49, 0x43000000, v61
	ds_write2_b32 v41, v29, v49 offset0:148 offset1:214
	v_mul_f32_e32 v29, 0x43000000, v62
	v_mul_f32_e32 v49, 0x43000000, v63
	ds_write2_b32 v42, v29, v49 offset0:24 offset1:90
	v_mul_f32_e32 v29, 0x43000000, v64
	v_mul_f32_e32 v49, 0x43000000, v65
	ds_write2_b32 v42, v29, v49 offset0:156 offset1:222
	v_mul_f32_e32 v29, 0x43000000, v66
	v_mul_f32_e32 v49, 0x43000000, v67
	ds_write2_b32 v43, v29, v49 offset0:32 offset1:98
	v_mul_f32_e32 v29, 0x43000000, v68
	v_mul_f32_e32 v49, 0x43000000, v69
	ds_write2_b32 v43, v29, v49 offset0:164 offset1:230
	v_mul_f32_e32 v29, 0x43000000, v70
	v_mul_f32_e32 v49, 0x43000000, v71
	ds_write2_b32 v44, v29, v49 offset0:40 offset1:106
	v_mul_f32_e32 v29, 0x43000000, v72
	v_mul_f32_e32 v49, 0x43000000, v73
	ds_write2_b32 v44, v29, v49 offset0:172 offset1:238
	v_mov_b32_e32 v50, v1
	v_mov_b32_e32 v51, v1
	v_mul_f32_e32 v29, 0x43000000, v74
	s_add_u32 s4, s4, s6
	s_addc_u32 s5, s5, 0
	v_readlane_b32 s42, v254, 30
	v_readlane_b32 s43, v254, 31
	v_readlane_b32 s44, v254, 32
	v_mul_f32_e32 v49, 0x43000000, v75
	ds_write2_b32 v45, v29, v49 offset0:48 offset1:114
	v_readlane_b32 s45, v254, 33
	v_mul_f32_e32 v29, 0x43000000, v76
	v_mul_f32_e32 v49, 0x43000000, v77
	ds_write2_b32 v45, v29, v49 offset0:180 offset1:246
	v_mul_f32_e32 v29, 0x43000000, v78
	v_mul_f32_e32 v49, 0x43000000, v79
	ds_write2_b32 v46, v29, v49 offset0:56 offset1:122
	v_mov_b32_e32 v49, v1
	v_mul_f32_e32 v29, 0x43000000, v48
	v_mov_b32_e32 v48, v1
	v_mul_f32_e32 v28, 0x43000000, v28
	ds_write2_b32 v46, v29, v28 offset0:188 offset1:254
	s_waitcnt lgkmcnt(0)
	ds_read2_b32 v[52:53], v33 offset1:16
	ds_read2_b32 v[54:55], v33 offset0:33 offset1:49
	ds_read2_b32 v[56:57], v33 offset0:66 offset1:82
	ds_read2_b32 v[58:59], v33 offset0:99 offset1:115
	ds_read2_b32 v[60:61], v33 offset0:132 offset1:148
	ds_read2_b32 v[62:63], v33 offset0:165 offset1:181
	ds_read2_b32 v[64:65], v33 offset0:198 offset1:214
	ds_read2_b32 v[66:67], v33 offset0:231 offset1:247
	ds_read2_b32 v[68:69], v47 offset0:8 offset1:24
	ds_read2_b32 v[70:71], v47 offset0:41 offset1:57
	ds_read2_b32 v[72:73], v47 offset0:74 offset1:90
	ds_read2_b32 v[74:75], v47 offset0:107 offset1:123
	ds_read2_b32 v[76:77], v47 offset0:140 offset1:156
	ds_read2_b32 v[78:79], v47 offset0:173 offset1:189
	ds_read2_b32 v[80:81], v47 offset0:206 offset1:222
	ds_read2_b32 v[82:83], v47 offset0:239 offset1:255
	s_waitcnt lgkmcnt(14)
	v_cvt_pk_fp8_f32 v48, v52, v54
	s_waitcnt lgkmcnt(10)
	v_cvt_pk_fp8_f32 v49, v60, v62
	s_waitcnt lgkmcnt(6)
	v_cvt_pk_fp8_f32 v50, v68, v70
	s_waitcnt lgkmcnt(2)
	v_cvt_pk_fp8_f32 v51, v76, v78
	v_cvt_pk_fp8_f32 v48, v56, v58 op_sel:[0,0,1]
	v_cvt_pk_fp8_f32 v49, v64, v66 op_sel:[0,0,1]
	v_cvt_pk_fp8_f32 v50, v72, v74 op_sel:[0,0,1]
	s_waitcnt lgkmcnt(0)
	v_cvt_pk_fp8_f32 v51, v80, v82 op_sel:[0,0,1]
	v_lshl_add_u64 v[28:29], s[4:5], 0, v[2:3]
	v_add_u32_e32 v52, s0, v32
	v_mad_i64_i32 v[84:85], s[4:5], v52, s13, v[28:29]
	global_store_dwordx4 v[84:85], v[48:51], off sc1 nt
	v_add_u32_e32 v52, s0, v34
	v_mad_i64_i32 v[28:29], s[4:5], v52, s13, v[28:29]
	v_mov_b32_e32 v48, v1
	v_mov_b32_e32 v49, v1
	v_mov_b32_e32 v50, v1
	v_mov_b32_e32 v51, v1
	v_cvt_pk_fp8_f32 v48, v53, v55
	v_cvt_pk_fp8_f32 v49, v61, v63
	v_cvt_pk_fp8_f32 v50, v69, v71
	v_cvt_pk_fp8_f32 v51, v77, v79
	v_cvt_pk_fp8_f32 v48, v57, v59 op_sel:[0,0,1]
	v_cvt_pk_fp8_f32 v49, v65, v67 op_sel:[0,0,1]
	v_cvt_pk_fp8_f32 v50, v73, v75 op_sel:[0,0,1]
	v_cvt_pk_fp8_f32 v51, v81, v83 op_sel:[0,0,1]
	s_mov_b64 s[4:5], 0
	global_store_dwordx4 v[28:29], v[48:51], off sc1 nt
	s_waitcnt lgkmcnt(0)
; __device__ __forceinline__ void tr_item8(const float* W, int ld, int K, int nblk, int item, unsigned char* WT, bool gu, float scale, LAS float* scr, int lane) {
;     const int kb = item / nblk, nb = item % nblk, k0 = 64 * kb, n0 = 32 * nb;
;     int drow0 = n0;
;     if (gu) { const int bj = n0 / FF, j = n0 - bj * FF; drow0 = 256 * (j / 128) + 128 * bj + (j % 128); }
;     { float t_[32];
; #pragma unroll
;       for (int i = 0; i < 32; ++i) t_[i] = W[(size_t)(k0 + 2 * i + (lane >> 5)) * ld + n0 + (lane & 31)];
; __device__ __forceinline__ void convert_items(Frame& F, const Args& a, int lo, int hi, int w, int nw) {
;     ...
;         if (r < NE * I_GU) { const int e = r / I_GU, rr = r % I_GU; tr_item8(a.in[18] + (size_t)e * D * 2 * FF, 2 * FF, D, 224, rr, F.ws + WS_WMGU + (size_t)e * 2 * FF * D, true, WSC_GU, scr, lane); continue; } r -= NE * I_GU;
.LBB0_1338:
	s_andn2_b64 vcc, exec, s[4:5]
	s_cbranch_vccnz .LBB0_1340
	s_add_i32 s0, s8, 0xde00
	s_bfe_u32 s4, s0, 0x70009
	s_mulk_i32 s4, 0x2493
	s_lshr_b32 s4, s4, 16
	s_mul_i32 s5, s4, 0xe00
	v_readlane_b32 s40, v254, 28
	s_sub_i32 s0, s0, s5
	s_mul_i32 s5, s4, 0x1c00000
	v_readlane_b32 s44, v254, 32
	v_readlane_b32 s45, v254, 33
	s_add_u32 s7, s44, s5
	s_addc_u32 s31, s45, 0
	s_mul_i32 s4, s4, 0x700000
	s_add_u32 s4, s36, s4
	s_addc_u32 s5, s37, 0
	s_bfe_u32 s6, s0, 0xb0005
	s_mulk_i32 s6, 0x2493
	s_lshr_b32 s6, s6, 16
	s_mul_i32 s40, s6, 0xe0
	v_readlane_b32 s41, v254, 29
	s_sub_i32 s40, s0, s40
	s_lshl_b32 s0, s40, 5
	s_and_b32 s41, s40, 0xffff
	s_cmpk_gt_u32 s41, 0x6f
	v_readlane_b32 s42, v254, 30
	s_cselect_b32 s41, 0xfffff200, 0
	s_cselect_b32 s42, 0x80, 0
	s_add_i32 s0, s41, s0
	s_sext_i32_i16 s41, s0
	s_bfe_u32 s41, s41, 0x70018
	v_readlane_b32 s43, v254, 31
	s_add_i32 s41, s0, s41
	s_sext_i32_i16 s43, s41
	s_and_b32 s41, s41, 0xff80
	s_sub_i32 s0, s0, s41
	s_lshl_b32 s43, s43, 1
	s_sext_i32_i16 s0, s0
	s_and_b32 s43, s43, 0xffffff00
	s_add_i32 s0, s42, s0
	s_lshl_b32 s40, s40, 7
	s_add_i32 s0, s0, s43
	s_lshl_b32 s6, s6, 6
	s_and_b32 s40, s40, 0x3ff80
	s_add_u32 s40, s7, s40
	s_addc_u32 s41, s31, 0
	v_add_u32_e32 v50, s6, v30
	v_lshl_add_u64 v[28:29], s[40:41], 0, v[0:1]
	v_mad_i64_i32 v[48:49], s[40:41], v50, s14, v[28:29]
	global_load_dword v51, v[48:49], off nt
	v_add_u32_e32 v48, 2, v50
	v_mad_i64_i32 v[48:49], s[40:41], v48, s14, v[28:29]
	global_load_dword v52, v[48:49], off nt
	v_add_u32_e32 v48, 4, v50
	v_mad_i64_i32 v[48:49], s[40:41], v48, s14, v[28:29]
	global_load_dword v53, v[48:49], off nt
	v_add_u32_e32 v48, 6, v50
	v_mad_i64_i32 v[48:49], s[40:41], v48, s14, v[28:29]
	global_load_dword v54, v[48:49], off nt
	v_add_u32_e32 v48, 8, v50
	v_mad_i64_i32 v[48:49], s[40:41], v48, s14, v[28:29]
	global_load_dword v55, v[48:49], off nt
	v_add_u32_e32 v48, 10, v50
	v_mad_i64_i32 v[48:49], s[40:41], v48, s14, v[28:29]
	global_load_dword v56, v[48:49], off nt
	v_add_u32_e32 v48, 12, v50
	v_mad_i64_i32 v[48:49], s[40:41], v48, s14, v[28:29]
	global_load_dword v57, v[48:49], off nt
	v_add_u32_e32 v48, 14, v50
	v_mad_i64_i32 v[48:49], s[40:41], v48, s14, v[28:29]
	global_load_dword v58, v[48:49], off nt
	v_add_u32_e32 v48, 16, v50
	v_mad_i64_i32 v[48:49], s[40:41], v48, s14, v[28:29]
	global_load_dword v59, v[48:49], off nt
	v_add_u32_e32 v48, 18, v50
	v_mad_i64_i32 v[48:49], s[40:41], v48, s14, v[28:29]
	global_load_dword v60, v[48:49], off nt
	v_add_u32_e32 v48, 20, v50
	v_mad_i64_i32 v[48:49], s[40:41], v48, s14, v[28:29]
	global_load_dword v61, v[48:49], off nt
	v_add_u32_e32 v48, 22, v50
	v_mad_i64_i32 v[48:49], s[40:41], v48, s14, v[28:29]
	global_load_dword v62, v[48:49], off nt
	v_add_u32_e32 v48, 24, v50
	v_mad_i64_i32 v[48:49], s[40:41], v48, s14, v[28:29]
	global_load_dword v63, v[48:49], off nt
	v_add_u32_e32 v48, 26, v50
	v_mad_i64_i32 v[48:49], s[40:41], v48, s14, v[28:29]
	global_load_dword v64, v[48:49], off nt
	v_add_u32_e32 v48, 28, v50
	v_mad_i64_i32 v[48:49], s[40:41], v48, s14, v[28:29]
	global_load_dword v65, v[48:49], off nt
	v_add_u32_e32 v48, 30, v50
	v_mad_i64_i32 v[48:49], s[40:41], v48, s14, v[28:29]
	global_load_dword v66, v[48:49], off nt
	v_add_u32_e32 v48, 32, v50
	v_mad_i64_i32 v[48:49], s[40:41], v48, s14, v[28:29]
	global_load_dword v67, v[48:49], off nt
	v_add_u32_e32 v48, 34, v50
	v_mad_i64_i32 v[48:49], s[40:41], v48, s14, v[28:29]
	global_load_dword v68, v[48:49], off nt
	v_add_u32_e32 v48, 36, v50
	v_mad_i64_i32 v[48:49], s[40:41], v48, s14, v[28:29]
	global_load_dword v69, v[48:49], off nt
	v_add_u32_e32 v48, 38, v50
	v_mad_i64_i32 v[48:49], s[40:41], v48, s14, v[28:29]
	global_load_dword v70, v[48:49], off nt
	v_add_u32_e32 v48, 40, v50
	v_mad_i64_i32 v[48:49], s[40:41], v48, s14, v[28:29]
	global_load_dword v71, v[48:49], off nt
	v_add_u32_e32 v48, 42, v50
	v_mad_i64_i32 v[48:49], s[40:41], v48, s14, v[28:29]
	global_load_dword v72, v[48:49], off nt
	v_add_u32_e32 v48, 44, v50
	v_mad_i64_i32 v[48:49], s[40:41], v48, s14, v[28:29]
	global_load_dword v73, v[48:49], off nt
	v_add_u32_e32 v48, 46, v50
	v_mad_i64_i32 v[48:49], s[40:41], v48, s14, v[28:29]
	global_load_dword v74, v[48:49], off nt
	v_add_u32_e32 v48, 48, v50
	v_mad_i64_i32 v[48:49], s[40:41], v48, s14, v[28:29]
	global_load_dword v75, v[48:49], off nt
	v_add_u32_e32 v48, 50, v50
	v_mad_i64_i32 v[48:49], s[40:41], v48, s14, v[28:29]
	global_load_dword v76, v[48:49], off nt
	v_add_u32_e32 v48, 52, v50
	v_mad_i64_i32 v[48:49], s[40:41], v48, s14, v[28:29]
	global_load_dword v77, v[48:49], off nt
	v_add_u32_e32 v48, 54, v50
	v_mad_i64_i32 v[48:49], s[40:41], v48, s14, v[28:29]
	global_load_dword v78, v[48:49], off nt
	v_add_u32_e32 v48, 56, v50
	v_mad_i64_i32 v[48:49], s[40:41], v48, s14, v[28:29]
	global_load_dword v79, v[48:49], off nt
	v_add_u32_e32 v48, 58, v50
	v_mad_i64_i32 v[48:49], s[40:41], v48, s14, v[28:29]
	global_load_dword v80, v[48:49], off nt
	v_add_u32_e32 v48, 60, v50
	v_mad_i64_i32 v[48:49], s[40:41], v48, s14, v[28:29]
	global_load_dword v48, v[48:49], off nt
	v_add_u32_e32 v49, 62, v50
	v_mad_i64_i32 v[28:29], s[40:41], v49, s14, v[28:29]
	global_load_dword v28, v[28:29], off nt
	s_waitcnt vmcnt(0)
; __device__ __forceinline__ unsigned cvt_pk4_fp8(float a, float b, float c, float d) { int w = 0; w = __builtin_amdgcn_cvt_pk_fp8_f32(a, b, w, false); w = __builtin_amdgcn_cvt_pk_fp8_f32(c, d, w, true); return (unsigned)w; }
; #define GAS __attribute__((address_space(1)))
; #define LAS __attribute__((address_space(3)))
; #define LDS_WAIT() asm volatile("s_waitcnt lgkmcnt(0)" ::: "memory")
; __device__ __forceinline__ void tr_item8(const float* W, int ld, int K, int nblk, int item, unsigned char* WT, bool gu, float scale, LAS float* scr, int lane) {
;     ...
;       for (int i = 0; i < 32; ++i) scr[(2 * i + (lane >> 5)) * 33 + (lane & 31)] = t_[i] * scale; }
;     LDS_WAIT(); asm volatile("" ::: "memory");
;     const int c = lane & 3;
; #pragma unroll
;     for (int j = 0; j < 2; ++j) { const int n = (lane >> 2) + 16 * j; const LAS float* sp = scr + (16 * c) * 33 + n;
;         v4u o; o.x = pg8::cvt_pk4_fp8(sp[0 * 33], sp[1 * 33], sp[2 * 33], sp[3 * 33]); o.y = pg8::cvt_pk4_fp8(sp[4 * 33], sp[5 * 33], sp[6 * 33], sp[7 * 33]);
;         o.z = pg8::cvt_pk4_fp8(sp[8 * 33], sp[9 * 33], sp[10 * 33], sp[11 * 33]); o.w = pg8::cvt_pk4_fp8(sp[12 * 33], sp[13 * 33], sp[14 * 33], sp[15 * 33]);
;         *(GAS v4u*)(WT + (size_t)(drow0 + n) * K + k0 + 16 * c) = o; }
;     LDS_WAIT(); asm volatile("" ::: "memory");
	v_mul_f32_e32 v29, 0x42800000, v51
	v_mul_f32_e32 v49, 0x42800000, v52
	ds_write2_b32 v31, v29, v49 offset1:66
	v_mul_f32_e32 v29, 0x42800000, v53
	v_mul_f32_e32 v49, 0x42800000, v54
	ds_write2_b32 v31, v29, v49 offset0:132 offset1:198
	v_mul_f32_e32 v29, 0x42800000, v55
	v_mul_f32_e32 v49, 0x42800000, v56
	ds_write2_b32 v40, v29, v49 offset0:8 offset1:74
	v_mul_f32_e32 v29, 0x42800000, v57
	v_mul_f32_e32 v49, 0x42800000, v58
	ds_write2_b32 v40, v29, v49 offset0:140 offset1:206
	v_mul_f32_e32 v29, 0x42800000, v59
	v_mul_f32_e32 v49, 0x42800000, v60
	ds_write2_b32 v41, v29, v49 offset0:16 offset1:82
	v_mul_f32_e32 v29, 0x42800000, v61
	v_mul_f32_e32 v49, 0x42800000, v62
	ds_write2_b32 v41, v29, v49 offset0:148 offset1:214
	v_mul_f32_e32 v29, 0x42800000, v63
	v_mul_f32_e32 v49, 0x42800000, v64
	ds_write2_b32 v42, v29, v49 offset0:24 offset1:90
	v_mul_f32_e32 v29, 0x42800000, v65
	v_mul_f32_e32 v49, 0x42800000, v66
	ds_write2_b32 v42, v29, v49 offset0:156 offset1:222
	v_mul_f32_e32 v29, 0x42800000, v67
	v_mul_f32_e32 v49, 0x42800000, v68
	ds_write2_b32 v43, v29, v49 offset0:32 offset1:98
	v_mul_f32_e32 v29, 0x42800000, v69
	v_mov_b32_e32 v50, v1
	v_mov_b32_e32 v51, v1
	s_add_u32 s4, s4, s6
	v_mul_f32_e32 v49, 0x42800000, v70
	ds_write2_b32 v43, v29, v49 offset0:164 offset1:230
	v_add_u32_e32 v84, s0, v32
	s_addc_u32 s5, s5, 0
	v_mul_f32_e32 v29, 0x42800000, v71
	v_ashrrev_i32_e32 v85, 31, v84
	v_lshlrev_b64 v[84:85], 10, v[84:85]
	v_readlane_b32 s46, v254, 34
	v_mul_f32_e32 v49, 0x42800000, v72
	ds_write2_b32 v44, v29, v49 offset0:40 offset1:106
	v_readlane_b32 s47, v254, 35
	v_mul_f32_e32 v29, 0x42800000, v73
	v_mul_f32_e32 v49, 0x42800000, v74
	ds_write2_b32 v44, v29, v49 offset0:172 offset1:238
	v_mul_f32_e32 v29, 0x42800000, v75
	v_mul_f32_e32 v49, 0x42800000, v76
	ds_write2_b32 v45, v29, v49 offset0:48 offset1:114
	v_mul_f32_e32 v29, 0x42800000, v77
	v_mul_f32_e32 v49, 0x42800000, v78
	ds_write2_b32 v45, v29, v49 offset0:180 offset1:246
	v_mul_f32_e32 v29, 0x42800000, v79
	v_mul_f32_e32 v49, 0x42800000, v80
	ds_write2_b32 v46, v29, v49 offset0:56 offset1:122
	v_mov_b32_e32 v49, v1
	v_mul_f32_e32 v29, 0x42800000, v48
	v_mov_b32_e32 v48, v1
	v_mul_f32_e32 v28, 0x42800000, v28
	ds_write2_b32 v46, v29, v28 offset0:188 offset1:254
	s_waitcnt lgkmcnt(0)
	ds_read2_b32 v[52:53], v33 offset1:16
	ds_read2_b32 v[54:55], v33 offset0:33 offset1:49
	ds_read2_b32 v[56:57], v33 offset0:66 offset1:82
	ds_read2_b32 v[58:59], v33 offset0:99 offset1:115
	ds_read2_b32 v[60:61], v33 offset0:132 offset1:148
	ds_read2_b32 v[62:63], v33 offset0:165 offset1:181
	ds_read2_b32 v[64:65], v33 offset0:198 offset1:214
	ds_read2_b32 v[66:67], v33 offset0:231 offset1:247
	ds_read2_b32 v[68:69], v47 offset0:8 offset1:24
	ds_read2_b32 v[70:71], v47 offset0:41 offset1:57
	ds_read2_b32 v[72:73], v47 offset0:74 offset1:90
	ds_read2_b32 v[74:75], v47 offset0:107 offset1:123
	ds_read2_b32 v[76:77], v47 offset0:140 offset1:156
	ds_read2_b32 v[78:79], v47 offset0:173 offset1:189
	ds_read2_b32 v[80:81], v47 offset0:206 offset1:222
	ds_read2_b32 v[82:83], v47 offset0:239 offset1:255
	s_waitcnt lgkmcnt(14)
	v_cvt_pk_fp8_f32 v48, v52, v54
	s_waitcnt lgkmcnt(10)
	v_cvt_pk_fp8_f32 v49, v60, v62
	s_waitcnt lgkmcnt(6)
	v_cvt_pk_fp8_f32 v50, v68, v70
	s_waitcnt lgkmcnt(2)
	v_cvt_pk_fp8_f32 v51, v76, v78
	v_cvt_pk_fp8_f32 v48, v56, v58 op_sel:[0,0,1]
	v_cvt_pk_fp8_f32 v49, v64, v66 op_sel:[0,0,1]
	v_cvt_pk_fp8_f32 v50, v72, v74 op_sel:[0,0,1]
	s_waitcnt lgkmcnt(0)
	v_cvt_pk_fp8_f32 v51, v80, v82 op_sel:[0,0,1]
	v_lshl_add_u64 v[28:29], s[4:5], 0, v[2:3]
	v_lshl_add_u64 v[84:85], v[28:29], 0, v[84:85]
	v_add_u32_e32 v52, s0, v34
	global_store_dwordx4 v[84:85], v[48:51], off sc1 nt
	s_nop 1
	v_mov_b32_e32 v48, v1
	v_mov_b32_e32 v49, v1
	v_mov_b32_e32 v50, v1
	v_mov_b32_e32 v51, v1
	v_cvt_pk_fp8_f32 v48, v53, v55
	v_cvt_pk_fp8_f32 v49, v61, v63
	v_cvt_pk_fp8_f32 v50, v69, v71
	v_cvt_pk_fp8_f32 v51, v77, v79
	v_cvt_pk_fp8_f32 v48, v57, v59 op_sel:[0,0,1]
	v_cvt_pk_fp8_f32 v49, v65, v67 op_sel:[0,0,1]
	v_cvt_pk_fp8_f32 v50, v73, v75 op_sel:[0,0,1]
	v_cvt_pk_fp8_f32 v51, v81, v83 op_sel:[0,0,1]
	v_ashrrev_i32_e32 v53, 31, v52
	v_lshlrev_b64 v[52:53], 10, v[52:53]
	v_lshl_add_u64 v[28:29], v[28:29], 0, v[52:53]
	global_store_dwordx4 v[28:29], v[48:51], off sc1 nt
	s_waitcnt lgkmcnt(0)

; __device__ __forceinline__ void tr_item8(const float* W, int ld, int K, int nblk, int item, unsigned char* WT, bool gu, float scale, LAS float* scr, int lane) {
;     const int kb = item / nblk, nb = item % nblk, k0 = 64 * kb, n0 = 32 * nb;
;     int drow0 = n0;
;     if (gu) { const int bj = n0 / FF, j = n0 - bj * FF; drow0 = 256 * (j / 128) + 128 * bj + (j % 128); }
;     { float t_[32];
; #pragma unroll
;       for (int i = 0; i < 32; ++i) t_[i] = W[(size_t)(k0 + 2 * i + (lane >> 5)) * ld + n0 + (lane & 31)];
; __device__ __forceinline__ void convert_items(Frame& F, const Args& a, int lo, int hi, int w, int nw) {
;     ...
;         if (r < I_DN) { tr_item8(a.in[15], D, FF, 32, r, F.ws + WS_WDN, false, WSC_DN, scr, lane); continue; } r -= I_DN;
.LBB0_1341:
	s_andn2_b64 vcc, exec, s[4:5]
	s_cbranch_vccnz .LBB0_1343
	s_lshl_b32 s0, s8, 5
	s_and_b32 s4, s12, 0x1ffc0
	s_and_b32 s6, s0, 0x3e0
	v_add_u32_e32 v28, s4, v30
	s_lshl_b32 s0, s6, 2
	v_ashrrev_i32_e32 v29, 31, v28
	v_lshl_add_u64 v[48:49], v[4:5], 0, s[0:1]
	v_lshlrev_b64 v[28:29], 12, v[28:29]
	v_lshl_add_u64 v[28:29], v[48:49], 0, v[28:29]
	v_add_co_u32_e32 v48, vcc, 0x2000, v28
	global_load_dword v50, v[28:29], off nt
	s_nop 0
	v_addc_co_u32_e32 v49, vcc, 0, v29, vcc
	global_load_dword v51, v[48:49], off nt
	v_add_co_u32_e32 v48, vcc, 0x4000, v28
	s_mov_b32 s5, s1
	s_nop 0
	v_addc_co_u32_e32 v49, vcc, 0, v29, vcc
	global_load_dword v52, v[48:49], off nt
	v_add_co_u32_e32 v48, vcc, 0x6000, v28
	s_nop 1
	v_addc_co_u32_e32 v49, vcc, 0, v29, vcc
	global_load_dword v53, v[48:49], off nt
	v_add_co_u32_e32 v48, vcc, 0x8000, v28
	s_nop 1
	v_addc_co_u32_e32 v49, vcc, 0, v29, vcc
	global_load_dword v54, v[48:49], off nt
	v_add_co_u32_e32 v48, vcc, 0xa000, v28
	s_nop 1
	v_addc_co_u32_e32 v49, vcc, 0, v29, vcc
	global_load_dword v55, v[48:49], off nt
	v_add_co_u32_e32 v48, vcc, 0xc000, v28
	s_nop 1
	v_addc_co_u32_e32 v49, vcc, 0, v29, vcc
	global_load_dword v56, v[48:49], off nt
	v_add_co_u32_e32 v48, vcc, 0xe000, v28
	s_nop 1
	v_addc_co_u32_e32 v49, vcc, 0, v29, vcc
	global_load_dword v57, v[48:49], off nt
	v_add_co_u32_e32 v48, vcc, 0x10000, v28
	s_nop 1
	v_addc_co_u32_e32 v49, vcc, 0, v29, vcc
	global_load_dword v58, v[48:49], off nt
	v_add_co_u32_e32 v48, vcc, 0x12000, v28
	s_nop 1
	v_addc_co_u32_e32 v49, vcc, 0, v29, vcc
	global_load_dword v59, v[48:49], off nt
	v_add_co_u32_e32 v48, vcc, 0x14000, v28
	s_nop 1
	v_addc_co_u32_e32 v49, vcc, 0, v29, vcc
	global_load_dword v60, v[48:49], off nt
	v_add_co_u32_e32 v48, vcc, 0x16000, v28
	s_nop 1
	v_addc_co_u32_e32 v49, vcc, 0, v29, vcc
	global_load_dword v61, v[48:49], off nt
	v_add_co_u32_e32 v48, vcc, 0x18000, v28
	s_nop 1
	v_addc_co_u32_e32 v49, vcc, 0, v29, vcc
	global_load_dword v62, v[48:49], off nt
	v_add_co_u32_e32 v48, vcc, 0x1a000, v28
	s_nop 1
	v_addc_co_u32_e32 v49, vcc, 0, v29, vcc
	global_load_dword v63, v[48:49], off nt
	v_add_co_u32_e32 v48, vcc, 0x1c000, v28
	s_nop 1
	v_addc_co_u32_e32 v49, vcc, 0, v29, vcc
	global_load_dword v64, v[48:49], off nt
	v_add_co_u32_e32 v48, vcc, 0x1e000, v28
	s_nop 1
	v_addc_co_u32_e32 v49, vcc, 0, v29, vcc
	global_load_dword v65, v[48:49], off nt
	v_add_co_u32_e32 v48, vcc, 0x20000, v28
	s_nop 1
	v_addc_co_u32_e32 v49, vcc, 0, v29, vcc
	global_load_dword v66, v[48:49], off nt
	v_add_co_u32_e32 v48, vcc, 0x22000, v28
	s_nop 1
	v_addc_co_u32_e32 v49, vcc, 0, v29, vcc
	global_load_dword v67, v[48:49], off nt
	v_add_co_u32_e32 v48, vcc, 0x24000, v28
	s_nop 1
	v_addc_co_u32_e32 v49, vcc, 0, v29, vcc
	global_load_dword v68, v[48:49], off nt
	v_add_co_u32_e32 v48, vcc, 0x26000, v28
	s_nop 1
	v_addc_co_u32_e32 v49, vcc, 0, v29, vcc
	global_load_dword v69, v[48:49], off nt
	v_add_co_u32_e32 v48, vcc, 0x28000, v28
	s_nop 1
	v_addc_co_u32_e32 v49, vcc, 0, v29, vcc
	global_load_dword v70, v[48:49], off nt
	v_add_co_u32_e32 v48, vcc, 0x2a000, v28
	s_nop 1
	v_addc_co_u32_e32 v49, vcc, 0, v29, vcc
	global_load_dword v71, v[48:49], off nt
	v_add_co_u32_e32 v48, vcc, 0x2c000, v28
	s_nop 1
	v_addc_co_u32_e32 v49, vcc, 0, v29, vcc
	global_load_dword v72, v[48:49], off nt
	v_add_co_u32_e32 v48, vcc, 0x2e000, v28
	s_nop 1
	v_addc_co_u32_e32 v49, vcc, 0, v29, vcc
	global_load_dword v73, v[48:49], off nt
	v_add_co_u32_e32 v48, vcc, 0x30000, v28
	s_nop 1
	v_addc_co_u32_e32 v49, vcc, 0, v29, vcc
	global_load_dword v74, v[48:49], off nt
	v_add_co_u32_e32 v48, vcc, 0x32000, v28
	s_nop 1
	v_addc_co_u32_e32 v49, vcc, 0, v29, vcc
	global_load_dword v75, v[48:49], off nt
	v_add_co_u32_e32 v48, vcc, 0x34000, v28
	s_nop 1
	v_addc_co_u32_e32 v49, vcc, 0, v29, vcc
	global_load_dword v76, v[48:49], off nt
	v_add_co_u32_e32 v48, vcc, 0x36000, v28
	s_nop 1
	v_addc_co_u32_e32 v49, vcc, 0, v29, vcc
	global_load_dword v77, v[48:49], off nt
	v_add_co_u32_e32 v48, vcc, 0x38000, v28
	s_nop 1
	v_addc_co_u32_e32 v49, vcc, 0, v29, vcc
	global_load_dword v78, v[48:49], off nt
	v_add_co_u32_e32 v48, vcc, 0x3a000, v28
	s_nop 1
	v_addc_co_u32_e32 v49, vcc, 0, v29, vcc
	global_load_dword v79, v[48:49], off nt
	v_add_co_u32_e32 v48, vcc, 0x3c000, v28
	s_nop 1
	v_addc_co_u32_e32 v49, vcc, 0, v29, vcc
	v_add_co_u32_e32 v28, vcc, 0x3e000, v28
	global_load_dword v48, v[48:49], off nt
	s_nop 0
	v_addc_co_u32_e32 v29, vcc, 0, v29, vcc
	global_load_dword v28, v[28:29], off nt
	s_waitcnt vmcnt(0)
; __device__ __forceinline__ unsigned cvt_pk4_fp8(float a, float b, float c, float d) { int w = 0; w = __builtin_amdgcn_cvt_pk_fp8_f32(a, b, w, false); w = __builtin_amdgcn_cvt_pk_fp8_f32(c, d, w, true); return (unsigned)w; }
; #define GAS __attribute__((address_space(1)))
; #define LAS __attribute__((address_space(3)))
; #define LDS_WAIT() asm volatile("s_waitcnt lgkmcnt(0)" ::: "memory")
; __device__ __forceinline__ void tr_item8(const float* W, int ld, int K, int nblk, int item, unsigned char* WT, bool gu, float scale, LAS float* scr, int lane) {
;     ...
;       for (int i = 0; i < 32; ++i) scr[(2 * i + (lane >> 5)) * 33 + (lane & 31)] = t_[i] * scale; }
;     LDS_WAIT(); asm volatile("" ::: "memory");
;     const int c = lane & 3;
; #pragma unroll
;     for (int j = 0; j < 2; ++j) { const int n = (lane >> 2) + 16 * j; const LAS float* sp = scr + (16 * c) * 33 + n;
;         v4u o; o.x = pg8::cvt_pk4_fp8(sp[0 * 33], sp[1 * 33], sp[2 * 33], sp[3 * 33]); o.y = pg8::cvt_pk4_fp8(sp[4 * 33], sp[5 * 33], sp[6 * 33], sp[7 * 33]);
;         o.z = pg8::cvt_pk4_fp8(sp[8 * 33], sp[9 * 33], sp[10 * 33], sp[11 * 33]); o.w = pg8::cvt_pk4_fp8(sp[12 * 33], sp[13 * 33], sp[14 * 33], sp[15 * 33]);
;         *(GAS v4u*)(WT + (size_t)(drow0 + n) * K + k0 + 16 * c) = o; }
;     LDS_WAIT(); asm volatile("" ::: "memory");
	v_mul_f32_e32 v29, 0x43000000, v50
	v_mul_f32_e32 v49, 0x43000000, v51
	ds_write2_b32 v31, v29, v49 offset1:66
	v_mul_f32_e32 v29, 0x43000000, v52
	v_mul_f32_e32 v49, 0x43000000, v53
	ds_write2_b32 v31, v29, v49 offset0:132 offset1:198
	v_mul_f32_e32 v29, 0x43000000, v54
	v_mul_f32_e32 v49, 0x43000000, v55
	ds_write2_b32 v40, v29, v49 offset0:8 offset1:74
	v_mul_f32_e32 v29, 0x43000000, v56
	v_mul_f32_e32 v49, 0x43000000, v57
	ds_write2_b32 v40, v29, v49 offset0:140 offset1:206
	v_mul_f32_e32 v29, 0x43000000, v58
	v_mul_f32_e32 v49, 0x43000000, v59
	ds_write2_b32 v41, v29, v49 offset0:16 offset1:82
	v_mul_f32_e32 v29, 0x43000000, v60
	v_mul_f32_e32 v49, 0x43000000, v61
	ds_write2_b32 v41, v29, v49 offset0:148 offset1:214
	v_mul_f32_e32 v29, 0x43000000, v62
	v_mul_f32_e32 v49, 0x43000000, v63
	ds_write2_b32 v42, v29, v49 offset0:24 offset1:90
	v_mul_f32_e32 v29, 0x43000000, v64
	v_mul_f32_e32 v49, 0x43000000, v65
	ds_write2_b32 v42, v29, v49 offset0:156 offset1:222
	v_mul_f32_e32 v29, 0x43000000, v66
	v_mul_f32_e32 v49, 0x43000000, v67
	ds_write2_b32 v43, v29, v49 offset0:32 offset1:98
	v_mul_f32_e32 v29, 0x43000000, v68
	v_mul_f32_e32 v49, 0x43000000, v69
	ds_write2_b32 v43, v29, v49 offset0:164 offset1:230
	v_mul_f32_e32 v29, 0x43000000, v70
	v_mul_f32_e32 v49, 0x43000000, v71
	ds_write2_b32 v44, v29, v49 offset0:40 offset1:106
	v_mul_f32_e32 v29, 0x43000000, v72
	v_mul_f32_e32 v49, 0x43000000, v73
	ds_write2_b32 v44, v29, v49 offset0:172 offset1:238
	v_mov_b32_e32 v50, 0
	v_mov_b32_e32 v51, 0
	v_mul_f32_e32 v29, 0x43000000, v74
	v_mul_f32_e32 v49, 0x43000000, v75
	ds_write2_b32 v45, v29, v49 offset0:48 offset1:114
	v_mul_f32_e32 v29, 0x43000000, v76
	v_mul_f32_e32 v49, 0x43000000, v77
	ds_write2_b32 v45, v29, v49 offset0:180 offset1:246
	v_mul_f32_e32 v29, 0x43000000, v78
	v_mul_f32_e32 v49, 0x43000000, v79
	ds_write2_b32 v46, v29, v49 offset0:56 offset1:122
	v_mov_b32_e32 v49, 0
	v_mul_f32_e32 v29, 0x43000000, v48
	v_mov_b32_e32 v48, 0
	v_mul_f32_e32 v28, 0x43000000, v28
	ds_write2_b32 v46, v29, v28 offset0:188 offset1:254
	s_waitcnt lgkmcnt(0)
	ds_read2_b32 v[52:53], v33 offset1:16
	ds_read2_b32 v[54:55], v33 offset0:33 offset1:49
	ds_read2_b32 v[56:57], v33 offset0:66 offset1:82
	ds_read2_b32 v[58:59], v33 offset0:99 offset1:115
	ds_read2_b32 v[60:61], v33 offset0:132 offset1:148
	ds_read2_b32 v[62:63], v33 offset0:165 offset1:181
	ds_read2_b32 v[64:65], v33 offset0:198 offset1:214
	ds_read2_b32 v[66:67], v33 offset0:231 offset1:247
	ds_read2_b32 v[68:69], v47 offset0:8 offset1:24
	ds_read2_b32 v[70:71], v47 offset0:41 offset1:57
	ds_read2_b32 v[72:73], v47 offset0:74 offset1:90
	ds_read2_b32 v[74:75], v47 offset0:107 offset1:123
	ds_read2_b32 v[76:77], v47 offset0:140 offset1:156
	ds_read2_b32 v[78:79], v47 offset0:173 offset1:189
	ds_read2_b32 v[80:81], v47 offset0:206 offset1:222
	ds_read2_b32 v[82:83], v47 offset0:239 offset1:255
	s_waitcnt lgkmcnt(14)
	v_cvt_pk_fp8_f32 v48, v52, v54
	s_waitcnt lgkmcnt(10)
	v_cvt_pk_fp8_f32 v49, v60, v62
	s_waitcnt lgkmcnt(6)
	v_cvt_pk_fp8_f32 v50, v68, v70
	s_waitcnt lgkmcnt(2)
	v_cvt_pk_fp8_f32 v51, v76, v78
	v_cvt_pk_fp8_f32 v48, v56, v58 op_sel:[0,0,1]
	v_cvt_pk_fp8_f32 v49, v64, v66 op_sel:[0,0,1]
	v_cvt_pk_fp8_f32 v50, v72, v74 op_sel:[0,0,1]
	s_waitcnt lgkmcnt(0)
	v_cvt_pk_fp8_f32 v51, v80, v82 op_sel:[0,0,1]
	v_lshl_add_u64 v[28:29], v[16:17], 0, s[4:5]
	v_add_u32_e32 v52, s6, v32
	v_mad_i64_i32 v[84:85], s[4:5], v52, s13, v[28:29]
	global_store_dwordx4 v[84:85], v[48:51], off sc1 nt
	v_add_u32_e32 v52, s6, v34
	v_mad_i64_i32 v[28:29], s[4:5], v52, s13, v[28:29]
	v_mov_b32_e32 v48, 0
	v_mov_b32_e32 v49, 0
	v_mov_b32_e32 v50, 0
	v_mov_b32_e32 v51, 0
	v_cvt_pk_fp8_f32 v48, v53, v55
	v_cvt_pk_fp8_f32 v49, v61, v63
	v_cvt_pk_fp8_f32 v50, v69, v71
	v_cvt_pk_fp8_f32 v51, v77, v79
	v_cvt_pk_fp8_f32 v48, v57, v59 op_sel:[0,0,1]
	v_cvt_pk_fp8_f32 v49, v65, v67 op_sel:[0,0,1]
	v_cvt_pk_fp8_f32 v50, v73, v75 op_sel:[0,0,1]
	v_cvt_pk_fp8_f32 v51, v81, v83 op_sel:[0,0,1]
	global_store_dwordx4 v[28:29], v[48:51], off sc1 nt
	s_waitcnt lgkmcnt(0)

; __device__ __forceinline__ void tr_item8(const float* W, int ld, int K, int nblk, int item, unsigned char* WT, bool gu, float scale, LAS float* scr, int lane) {
;     const int kb = item / nblk, nb = item % nblk, k0 = 64 * kb, n0 = 32 * nb;
;     int drow0 = n0;
;     if (gu) { const int bj = n0 / FF, j = n0 - bj * FF; drow0 = 256 * (j / 128) + 128 * bj + (j % 128); }
;     { float t_[32];
; #pragma unroll
;       for (int i = 0; i < 32; ++i) t_[i] = W[(size_t)(k0 + 2 * i + (lane >> 5)) * ld + n0 + (lane & 31)];
; __device__ __forceinline__ void convert_items(Frame& F, const Args& a, int lo, int hi, int w, int nw) {
;     ...
;         if (r < I_GU) { tr_item8(a.in[14], 2 * FF, D, 224, r, F.ws + WS_WGU, true, WSC_GU, scr, lane); continue; } r -= I_GU;
.LBB0_1344:
	s_andn2_b64 vcc, exec, s[4:5]
	s_cbranch_vccnz .LBB0_1346
	s_add_i32 s0, s8, 0xf300
	s_bfe_u32 s4, s0, 0xb0005
	s_mulk_i32 s4, 0x2493
	s_lshr_b32 s4, s4, 16
	s_mul_i32 s5, s4, 0xe0
	s_sub_i32 s0, s0, s5
	s_lshl_b32 s5, s0, 5
	s_and_b32 s6, s0, 0xffff
	s_cmpk_gt_u32 s6, 0x6f
	s_cselect_b32 s31, 0xfffff200, 0
	s_cselect_b32 s40, 0x80, 0
	s_lshl_b32 s0, s0, 7
	s_lshl_b32 s4, s4, 6
	s_and_b32 s0, s0, 0x3ff80
	v_add_u32_e32 v64, s4, v30
	v_lshl_add_u64 v[28:29], v[6:7], 0, s[0:1]
	v_mad_i64_i32 v[48:49], s[6:7], v64, s14, v[28:29]
	v_add_u32_e32 v50, 2, v64
	v_add_u32_e32 v52, 4, v64
	v_add_u32_e32 v54, 6, v64
	v_add_u32_e32 v56, 8, v64
	v_add_u32_e32 v58, 10, v64
	v_add_u32_e32 v60, 12, v64
	v_add_u32_e32 v62, 14, v64
	v_mad_i64_i32 v[50:51], s[6:7], v50, s14, v[28:29]
	v_mad_i64_i32 v[52:53], s[6:7], v52, s14, v[28:29]
	v_mad_i64_i32 v[54:55], s[6:7], v54, s14, v[28:29]
	v_mad_i64_i32 v[56:57], s[6:7], v56, s14, v[28:29]
	v_mad_i64_i32 v[58:59], s[6:7], v58, s14, v[28:29]
	v_mad_i64_i32 v[60:61], s[6:7], v60, s14, v[28:29]
	v_mad_i64_i32 v[62:63], s[6:7], v62, s14, v[28:29]
	global_load_dword v65, v[48:49], off nt
	global_load_dword v66, v[50:51], off nt
	global_load_dword v67, v[52:53], off nt
	global_load_dword v68, v[54:55], off nt
	global_load_dword v69, v[56:57], off nt
	global_load_dword v70, v[58:59], off nt
	global_load_dword v71, v[60:61], off nt
	global_load_dword v72, v[62:63], off nt
	v_add_u32_e32 v48, 16, v64
	v_mad_i64_i32 v[48:49], s[6:7], v48, s14, v[28:29]
	v_add_u32_e32 v50, 18, v64
	v_add_u32_e32 v52, 20, v64
	v_add_u32_e32 v54, 22, v64
	v_add_u32_e32 v56, 24, v64
	v_add_u32_e32 v58, 26, v64
	v_add_u32_e32 v60, 28, v64
	v_add_u32_e32 v62, 30, v64
	v_mad_i64_i32 v[50:51], s[6:7], v50, s14, v[28:29]
	v_mad_i64_i32 v[52:53], s[6:7], v52, s14, v[28:29]
	v_mad_i64_i32 v[54:55], s[6:7], v54, s14, v[28:29]
	v_mad_i64_i32 v[56:57], s[6:7], v56, s14, v[28:29]
	v_mad_i64_i32 v[58:59], s[6:7], v58, s14, v[28:29]
	v_mad_i64_i32 v[60:61], s[6:7], v60, s14, v[28:29]
	v_mad_i64_i32 v[62:63], s[6:7], v62, s14, v[28:29]
	global_load_dword v73, v[48:49], off nt
	global_load_dword v74, v[50:51], off nt
	global_load_dword v75, v[52:53], off nt
	global_load_dword v76, v[54:55], off nt
	global_load_dword v77, v[56:57], off nt
	global_load_dword v78, v[58:59], off nt
	global_load_dword v79, v[60:61], off nt
	global_load_dword v80, v[62:63], off nt
	v_add_u32_e32 v48, 32, v64
	v_add_u32_e32 v50, 34, v64
	v_add_u32_e32 v52, 36, v64
	v_add_u32_e32 v54, 38, v64
	v_add_u32_e32 v60, 44, v64
	v_mad_i64_i32 v[48:49], s[6:7], v48, s14, v[28:29]
	v_mad_i64_i32 v[50:51], s[6:7], v50, s14, v[28:29]
	v_mad_i64_i32 v[52:53], s[6:7], v52, s14, v[28:29]
	v_mad_i64_i32 v[54:55], s[6:7], v54, s14, v[28:29]
	v_add_u32_e32 v56, 40, v64
	v_add_u32_e32 v58, 42, v64
	v_mad_i64_i32 v[60:61], s[6:7], v60, s14, v[28:29]
	v_add_u32_e32 v62, 46, v64
	v_mad_i64_i32 v[56:57], s[6:7], v56, s14, v[28:29]
	v_mad_i64_i32 v[58:59], s[6:7], v58, s14, v[28:29]
	v_mad_i64_i32 v[62:63], s[6:7], v62, s14, v[28:29]
	global_load_dword v81, v[48:49], off nt
	global_load_dword v82, v[50:51], off nt
	global_load_dword v83, v[52:53], off nt
	global_load_dword v84, v[54:55], off nt
	global_load_dword v85, v[56:57], off nt
	global_load_dword v86, v[58:59], off nt
	s_nop 0
	global_load_dword v60, v[60:61], off nt
	s_nop 0
	global_load_dword v61, v[62:63], off nt
	v_add_u32_e32 v48, 48, v64
	v_add_u32_e32 v50, 50, v64
	v_add_u32_e32 v52, 52, v64
	v_add_u32_e32 v54, 54, v64
	v_mad_i64_i32 v[48:49], s[6:7], v48, s14, v[28:29]
	v_mad_i64_i32 v[50:51], s[6:7], v50, s14, v[28:29]
	v_mad_i64_i32 v[52:53], s[6:7], v52, s14, v[28:29]
	v_mad_i64_i32 v[54:55], s[6:7], v54, s14, v[28:29]
	v_add_u32_e32 v56, 56, v64
	v_add_u32_e32 v58, 58, v64
	v_mad_i64_i32 v[56:57], s[6:7], v56, s14, v[28:29]
	v_mad_i64_i32 v[58:59], s[6:7], v58, s14, v[28:29]
	global_load_dword v62, v[48:49], off nt
	s_nop 0
	global_load_dword v50, v[50:51], off nt
	s_nop 0
	global_load_dword v51, v[52:53], off nt
	s_nop 0
	global_load_dword v52, v[54:55], off nt
	global_load_dword v53, v[56:57], off nt
	s_nop 0
	global_load_dword v54, v[58:59], off nt
	v_add_u32_e32 v48, 60, v64
	v_add_u32_e32 v55, 62, v64
	v_mad_i64_i32 v[48:49], s[6:7], v48, s14, v[28:29]
	v_mad_i64_i32 v[28:29], s[6:7], v55, s14, v[28:29]
	global_load_dword v48, v[48:49], off nt
	s_nop 0
	global_load_dword v28, v[28:29], off nt
	s_waitcnt vmcnt(0)
; __device__ __forceinline__ unsigned cvt_pk4_fp8(float a, float b, float c, float d) { int w = 0; w = __builtin_amdgcn_cvt_pk_fp8_f32(a, b, w, false); w = __builtin_amdgcn_cvt_pk_fp8_f32(c, d, w, true); return (unsigned)w; }
; #define GAS __attribute__((address_space(1)))
; #define LAS __attribute__((address_space(3)))
; #define LDS_WAIT() asm volatile("s_waitcnt lgkmcnt(0)" ::: "memory")
; __device__ __forceinline__ void tr_item8(const float* W, int ld, int K, int nblk, int item, unsigned char* WT, bool gu, float scale, LAS float* scr, int lane) {
;     ...
;     if (gu) { const int bj = n0 / FF, j = n0 - bj * FF; drow0 = 256 * (j / 128) + 128 * bj + (j % 128); }
;     ...
;       for (int i = 0; i < 32; ++i) scr[(2 * i + (lane >> 5)) * 33 + (lane & 31)] = t_[i] * scale; }
;     LDS_WAIT(); asm volatile("" ::: "memory");
;     const int c = lane & 3;
; #pragma unroll
;     for (int j = 0; j < 2; ++j) { const int n = (lane >> 2) + 16 * j; const LAS float* sp = scr + (16 * c) * 33 + n;
;         v4u o; o.x = pg8::cvt_pk4_fp8(sp[0 * 33], sp[1 * 33], sp[2 * 33], sp[3 * 33]); o.y = pg8::cvt_pk4_fp8(sp[4 * 33], sp[5 * 33], sp[6 * 33], sp[7 * 33]);
;         o.z = pg8::cvt_pk4_fp8(sp[8 * 33], sp[9 * 33], sp[10 * 33], sp[11 * 33]); o.w = pg8::cvt_pk4_fp8(sp[12 * 33], sp[13 * 33], sp[14 * 33], sp[15 * 33]);
;         *(GAS v4u*)(WT + (size_t)(drow0 + n) * K + k0 + 16 * c) = o; }
;     LDS_WAIT(); asm volatile("" ::: "memory");
	v_mul_f32_e32 v29, 0x42800000, v65
	v_mul_f32_e32 v49, 0x42800000, v66
	ds_write2_b32 v31, v29, v49 offset1:66
	v_mul_f32_e32 v29, 0x42800000, v67
	v_mul_f32_e32 v49, 0x42800000, v68
	ds_write2_b32 v31, v29, v49 offset0:132 offset1:198
	v_mul_f32_e32 v29, 0x42800000, v69
	v_mul_f32_e32 v49, 0x42800000, v70
	ds_write2_b32 v40, v29, v49 offset0:8 offset1:74
	v_mul_f32_e32 v29, 0x42800000, v71
	v_mul_f32_e32 v49, 0x42800000, v72
	ds_write2_b32 v40, v29, v49 offset0:140 offset1:206
	s_add_i32 s0, s31, s5
	s_sext_i32_i16 s5, s0
	s_bfe_u32 s5, s5, 0x70018
	s_add_i32 s5, s0, s5
	s_sext_i32_i16 s6, s5
	s_and_b32 s5, s5, 0xff80
	s_sub_i32 s0, s0, s5
	s_lshl_b32 s6, s6, 1
	s_sext_i32_i16 s0, s0
	v_mul_f32_e32 v29, 0x42800000, v73
	v_mul_f32_e32 v49, 0x42800000, v74
	ds_write2_b32 v41, v29, v49 offset0:16 offset1:82
	v_mul_f32_e32 v29, 0x42800000, v75
	v_mul_f32_e32 v49, 0x42800000, v76
	ds_write2_b32 v41, v29, v49 offset0:148 offset1:214
	v_mul_f32_e32 v29, 0x42800000, v77
	v_mul_f32_e32 v49, 0x42800000, v78
	ds_write2_b32 v42, v29, v49 offset0:24 offset1:90
	v_mul_f32_e32 v29, 0x42800000, v79
	v_mul_f32_e32 v49, 0x42800000, v80
	ds_write2_b32 v42, v29, v49 offset0:156 offset1:222
	s_and_b32 s6, s6, 0xffffff00
	s_add_i32 s0, s40, s0
	s_add_i32 s0, s0, s6
	s_mov_b32 s5, s1
	v_mul_f32_e32 v29, 0x42800000, v81
	v_mul_f32_e32 v49, 0x42800000, v82
	ds_write2_b32 v43, v29, v49 offset0:32 offset1:98
	v_mul_f32_e32 v29, 0x42800000, v83
	v_mul_f32_e32 v49, 0x42800000, v84
	ds_write2_b32 v43, v29, v49 offset0:164 offset1:230
	v_mul_f32_e32 v29, 0x42800000, v85
	v_mul_f32_e32 v49, 0x42800000, v86
	ds_write2_b32 v44, v29, v49 offset0:40 offset1:106
	v_mul_f32_e32 v29, 0x42800000, v60
	v_mul_f32_e32 v49, 0x42800000, v61
	ds_write2_b32 v44, v29, v49 offset0:172 offset1:238
	v_add_u32_e32 v84, s0, v32
	v_ashrrev_i32_e32 v85, 31, v84
	v_lshlrev_b64 v[84:85], 10, v[84:85]
	v_mul_f32_e32 v29, 0x42800000, v62
	v_mul_f32_e32 v49, 0x42800000, v50
	ds_write2_b32 v45, v29, v49 offset0:48 offset1:114
	v_mul_f32_e32 v29, 0x42800000, v51
	v_mul_f32_e32 v49, 0x42800000, v52
	ds_write2_b32 v45, v29, v49 offset0:180 offset1:246
	v_mul_f32_e32 v29, 0x42800000, v53
	v_mul_f32_e32 v49, 0x42800000, v54
	ds_write2_b32 v46, v29, v49 offset0:56 offset1:122
	v_mov_b32_e32 v49, 0
	v_mov_b32_e32 v50, 0
	v_mul_f32_e32 v29, 0x42800000, v48
	v_mul_f32_e32 v28, 0x42800000, v28
	ds_write2_b32 v46, v29, v28 offset0:188 offset1:254
	s_waitcnt lgkmcnt(0)
	ds_read2_b32 v[52:53], v33 offset1:16
	ds_read2_b32 v[54:55], v33 offset0:33 offset1:49
	ds_read2_b32 v[56:57], v33 offset0:66 offset1:82
	ds_read2_b32 v[58:59], v33 offset0:99 offset1:115
	ds_read2_b32 v[60:61], v33 offset0:132 offset1:148
	ds_read2_b32 v[62:63], v33 offset0:165 offset1:181
	ds_read2_b32 v[64:65], v33 offset0:198 offset1:214
	ds_read2_b32 v[66:67], v33 offset0:231 offset1:247
	ds_read2_b32 v[68:69], v47 offset0:8 offset1:24
	ds_read2_b32 v[70:71], v47 offset0:41 offset1:57
	ds_read2_b32 v[72:73], v47 offset0:74 offset1:90
	ds_read2_b32 v[74:75], v47 offset0:107 offset1:123
	ds_read2_b32 v[76:77], v47 offset0:140 offset1:156
	ds_read2_b32 v[78:79], v47 offset0:173 offset1:189
	v_mov_b32_e32 v48, 0
	ds_read2_b32 v[80:81], v47 offset0:206 offset1:222
	ds_read2_b32 v[82:83], v47 offset0:239 offset1:255
	v_mov_b32_e32 v51, 0
	s_waitcnt lgkmcnt(14)
	v_cvt_pk_fp8_f32 v48, v52, v54
	s_waitcnt lgkmcnt(10)
	v_cvt_pk_fp8_f32 v49, v60, v62
	s_waitcnt lgkmcnt(6)
	v_cvt_pk_fp8_f32 v50, v68, v70
	s_waitcnt lgkmcnt(2)
	v_cvt_pk_fp8_f32 v51, v76, v78
	v_cvt_pk_fp8_f32 v48, v56, v58 op_sel:[0,0,1]
	v_cvt_pk_fp8_f32 v49, v64, v66 op_sel:[0,0,1]
	v_cvt_pk_fp8_f32 v50, v72, v74 op_sel:[0,0,1]
	s_waitcnt lgkmcnt(0)
	v_cvt_pk_fp8_f32 v51, v80, v82 op_sel:[0,0,1]
	v_lshl_add_u64 v[28:29], v[18:19], 0, s[4:5]
	v_lshl_add_u64 v[84:85], v[28:29], 0, v[84:85]
	v_add_u32_e32 v52, s0, v34
	global_store_dwordx4 v[84:85], v[48:51], off sc1 nt
	s_nop 1
	v_mov_b32_e32 v48, 0
	v_mov_b32_e32 v49, 0
	v_mov_b32_e32 v50, 0
	v_mov_b32_e32 v51, 0
	v_cvt_pk_fp8_f32 v48, v53, v55
	v_cvt_pk_fp8_f32 v49, v61, v63
	v_cvt_pk_fp8_f32 v50, v69, v71
	v_cvt_pk_fp8_f32 v51, v77, v79
	v_cvt_pk_fp8_f32 v48, v57, v59 op_sel:[0,0,1]
	v_cvt_pk_fp8_f32 v49, v65, v67 op_sel:[0,0,1]
	v_cvt_pk_fp8_f32 v50, v73, v75 op_sel:[0,0,1]
	v_cvt_pk_fp8_f32 v51, v81, v83 op_sel:[0,0,1]
	v_ashrrev_i32_e32 v53, 31, v52
	v_lshlrev_b64 v[52:53], 10, v[52:53]
	v_lshl_add_u64 v[28:29], v[28:29], 0, v[52:53]
	global_store_dwordx4 v[28:29], v[48:51], off sc1 nt
	s_waitcnt lgkmcnt(0)

; __device__ __forceinline__ void tr_item(const float* W, int ld, int K, int nblk, int item, bf16* WT, bool gu, LAS float* scr, int lane) {
;     const int kb = item / nblk, nb = item % nblk, k0 = 64 * kb, n0 = 32 * nb;
;     int drow0 = n0;
;     if (gu) { const int bj = n0 / FF, j = n0 - bj * FF; drow0 = 256 * (j / 128) + 128 * bj + (j % 128); }
;     { float t_[32];
; #pragma unroll
;       for (int i = 0; i < 32; ++i) t_[i] = W[(size_t)(k0 + 2 * i + (lane >> 5)) * ld + n0 + (lane & 31)];
; #pragma unroll
;       for (int i = 0; i < 32; ++i) scr[(2 * i + (lane >> 5)) * 33 + (lane & 31)] = t_[i]; }
; __device__ __forceinline__ void convert_items(Frame& F, const Args& a, int lo, int hi, int w, int nw) {
;     ...
;         if (r < I_SO) { tr_item(a.in[12], D, D, 32, r, (bf16*)(F.ws + WS_WSWAOUT), false, scr, lane); continue; } r -= I_SO;
.LBB0_1347:
	s_andn2_b64 vcc, exec, s[4:5]
	s_cbranch_vccnz .LBB0_1349
	s_add_i32 s0, s12, 0x2000
	s_and_b32 s5, s0, 0x1ffc0
	s_and_b32 s4, s9, 0x3e0
	v_add_u32_e32 v28, s5, v30
	s_lshl_b32 s0, s4, 2
	v_ashrrev_i32_e32 v29, 31, v28
	v_lshl_add_u64 v[48:49], v[8:9], 0, s[0:1]
	v_lshlrev_b64 v[28:29], 12, v[28:29]
	v_lshl_add_u64 v[28:29], v[48:49], 0, v[28:29]
	v_add_co_u32_e32 v48, vcc, 0x2000, v28
	global_load_dword v50, v[28:29], off nt
	s_nop 0
	v_addc_co_u32_e32 v49, vcc, 0, v29, vcc
	global_load_dword v51, v[48:49], off nt
	v_add_co_u32_e32 v48, vcc, 0x4000, v28
	s_lshl_b32 s0, s5, 1
	s_nop 0
	v_addc_co_u32_e32 v49, vcc, 0, v29, vcc
	global_load_dword v52, v[48:49], off nt
	v_add_co_u32_e32 v48, vcc, 0x6000, v28
	s_nop 1
	v_addc_co_u32_e32 v49, vcc, 0, v29, vcc
	global_load_dword v53, v[48:49], off nt
	v_add_co_u32_e32 v48, vcc, 0x8000, v28
	s_nop 1
	v_addc_co_u32_e32 v49, vcc, 0, v29, vcc
	global_load_dword v54, v[48:49], off nt
	v_add_co_u32_e32 v48, vcc, 0xa000, v28
	s_nop 1
	v_addc_co_u32_e32 v49, vcc, 0, v29, vcc
	global_load_dword v55, v[48:49], off nt
	v_add_co_u32_e32 v48, vcc, 0xc000, v28
	s_nop 1
	v_addc_co_u32_e32 v49, vcc, 0, v29, vcc
	global_load_dword v56, v[48:49], off nt
	v_add_co_u32_e32 v48, vcc, 0xe000, v28
	s_nop 1
	v_addc_co_u32_e32 v49, vcc, 0, v29, vcc
	global_load_dword v57, v[48:49], off nt
	v_add_co_u32_e32 v48, vcc, 0x10000, v28
	s_nop 1
	v_addc_co_u32_e32 v49, vcc, 0, v29, vcc
	global_load_dword v58, v[48:49], off nt
	v_add_co_u32_e32 v48, vcc, 0x12000, v28
	s_nop 1
	v_addc_co_u32_e32 v49, vcc, 0, v29, vcc
	global_load_dword v59, v[48:49], off nt
	v_add_co_u32_e32 v48, vcc, 0x14000, v28
	s_nop 1
	v_addc_co_u32_e32 v49, vcc, 0, v29, vcc
	global_load_dword v60, v[48:49], off nt
	v_add_co_u32_e32 v48, vcc, 0x16000, v28
	s_nop 1
	v_addc_co_u32_e32 v49, vcc, 0, v29, vcc
	global_load_dword v61, v[48:49], off nt
	v_add_co_u32_e32 v48, vcc, 0x18000, v28
	s_nop 1
	v_addc_co_u32_e32 v49, vcc, 0, v29, vcc
	global_load_dword v62, v[48:49], off nt
	v_add_co_u32_e32 v48, vcc, 0x1a000, v28
	s_nop 1
	v_addc_co_u32_e32 v49, vcc, 0, v29, vcc
	global_load_dword v63, v[48:49], off nt
	v_add_co_u32_e32 v48, vcc, 0x1c000, v28
	s_nop 1
	v_addc_co_u32_e32 v49, vcc, 0, v29, vcc
	global_load_dword v64, v[48:49], off nt
	v_add_co_u32_e32 v48, vcc, 0x1e000, v28
	s_nop 1
	v_addc_co_u32_e32 v49, vcc, 0, v29, vcc
	global_load_dword v65, v[48:49], off nt
	v_add_co_u32_e32 v48, vcc, 0x20000, v28
	s_nop 1
	v_addc_co_u32_e32 v49, vcc, 0, v29, vcc
	global_load_dword v66, v[48:49], off nt
	v_add_co_u32_e32 v48, vcc, 0x22000, v28
	s_nop 1
	v_addc_co_u32_e32 v49, vcc, 0, v29, vcc
	global_load_dword v67, v[48:49], off nt
	v_add_co_u32_e32 v48, vcc, 0x24000, v28
	s_nop 1
	v_addc_co_u32_e32 v49, vcc, 0, v29, vcc
	global_load_dword v68, v[48:49], off nt
	v_add_co_u32_e32 v48, vcc, 0x26000, v28
	s_nop 1
	v_addc_co_u32_e32 v49, vcc, 0, v29, vcc
	global_load_dword v69, v[48:49], off nt
	v_add_co_u32_e32 v48, vcc, 0x28000, v28
	s_nop 1
	v_addc_co_u32_e32 v49, vcc, 0, v29, vcc
	global_load_dword v70, v[48:49], off nt
	v_add_co_u32_e32 v48, vcc, 0x2a000, v28
	s_nop 1
	v_addc_co_u32_e32 v49, vcc, 0, v29, vcc
	global_load_dword v71, v[48:49], off nt
	v_add_co_u32_e32 v48, vcc, 0x2c000, v28
	s_nop 1
	v_addc_co_u32_e32 v49, vcc, 0, v29, vcc
	global_load_dword v72, v[48:49], off nt
	v_add_co_u32_e32 v48, vcc, 0x2e000, v28
	s_nop 1
	v_addc_co_u32_e32 v49, vcc, 0, v29, vcc
	global_load_dword v73, v[48:49], off nt
	v_add_co_u32_e32 v48, vcc, 0x30000, v28
	s_nop 1
	v_addc_co_u32_e32 v49, vcc, 0, v29, vcc
	global_load_dword v74, v[48:49], off nt
	v_add_co_u32_e32 v48, vcc, 0x32000, v28
	s_nop 1
	v_addc_co_u32_e32 v49, vcc, 0, v29, vcc
	global_load_dword v75, v[48:49], off nt
	v_add_co_u32_e32 v48, vcc, 0x34000, v28
	s_nop 1
	v_addc_co_u32_e32 v49, vcc, 0, v29, vcc
	global_load_dword v76, v[48:49], off nt
	v_add_co_u32_e32 v48, vcc, 0x36000, v28
	s_nop 1
	v_addc_co_u32_e32 v49, vcc, 0, v29, vcc
	global_load_dword v77, v[48:49], off nt
	v_add_co_u32_e32 v48, vcc, 0x38000, v28
	s_nop 1
	v_addc_co_u32_e32 v49, vcc, 0, v29, vcc
	global_load_dword v78, v[48:49], off nt
	v_add_co_u32_e32 v48, vcc, 0x3a000, v28
	s_nop 1
	v_addc_co_u32_e32 v49, vcc, 0, v29, vcc
	global_load_dword v79, v[48:49], off nt
	v_add_co_u32_e32 v48, vcc, 0x3c000, v28
	s_nop 1
	v_addc_co_u32_e32 v49, vcc, 0, v29, vcc
	v_add_co_u32_e32 v28, vcc, 0x3e000, v28
	global_load_dword v48, v[48:49], off nt
	s_nop 0
	v_addc_co_u32_e32 v29, vcc, 0, v29, vcc
	global_load_dword v28, v[28:29], off nt
	s_waitcnt vmcnt(0)
	ds_write2_b32 v31, v50, v51 offset1:66
	ds_write2_b32 v31, v52, v53 offset0:132 offset1:198
	ds_write2_b32 v40, v54, v55 offset0:8 offset1:74
	ds_write2_b32 v40, v56, v57 offset0:140 offset1:206
	ds_write2_b32 v41, v58, v59 offset0:16 offset1:82
	ds_write2_b32 v41, v60, v61 offset0:148 offset1:214
	ds_write2_b32 v42, v62, v63 offset0:24 offset1:90
	ds_write2_b32 v42, v64, v65 offset0:156 offset1:222
	ds_write2_b32 v43, v66, v67 offset0:32 offset1:98
	ds_write2_b32 v43, v68, v69 offset0:164 offset1:230
	ds_write2_b32 v44, v70, v71 offset0:40 offset1:106
	ds_write2_b32 v44, v72, v73 offset0:172 offset1:238
	ds_write2_b32 v45, v74, v75 offset0:48 offset1:114
	ds_write2_b32 v45, v76, v77 offset0:180 offset1:246
	ds_write2_b32 v46, v78, v79 offset0:56 offset1:122
	ds_write2_b32 v46, v48, v28 offset0:188 offset1:254
	s_waitcnt lgkmcnt(0)
; #define GAS __attribute__((address_space(1)))
; #define LAS __attribute__((address_space(3)))
; #define LDS_WAIT() asm volatile("s_waitcnt lgkmcnt(0)" ::: "memory")
; __device__ __forceinline__ unsigned pk2(float lo, float hi) { return f2bf(lo) | (f2bf(hi) << 16); }
; __device__ __forceinline__ void tr_item(const float* W, int ld, int K, int nblk, int item, bf16* WT, bool gu, LAS float* scr, int lane) {
;     ...
;     LDS_WAIT(); asm volatile("" ::: "memory");
;     const int c = lane & 7;
; #pragma unroll
;     for (int j = 0; j < 4; ++j) { const int n = (lane >> 3) + 8 * j; const LAS float* s = scr + (8 * c) * 33 + n;
;         v4u o; o.x = pk2(s[0 * 33], s[1 * 33]); o.y = pk2(s[2 * 33], s[3 * 33]); o.z = pk2(s[4 * 33], s[5 * 33]); o.w = pk2(s[6 * 33], s[7 * 33]);
;         *(GAS v4u*)(WT + (size_t)(drow0 + n) * K + k0 + 8 * c) = o; }
;     LDS_WAIT(); asm volatile("" ::: "memory");
	ds_read2_b32 v[52:53], v36 offset0:33 offset1:41
	ds_read2_b32 v[54:55], v36 offset1:8
	ds_read2_b32 v[56:57], v36 offset0:66 offset1:74
	ds_read2_b32 v[58:59], v36 offset0:99 offset1:107
	ds_read2_b32 v[60:61], v36 offset0:132 offset1:140
	ds_read2_b32 v[62:63], v36 offset0:165 offset1:173
	ds_read2_b32 v[64:65], v36 offset0:198 offset1:206
	ds_read2_b32 v[66:67], v36 offset0:231 offset1:239
	s_waitcnt lgkmcnt(7)
	v_bfe_u32 v49, v52, 16, 1
	s_waitcnt lgkmcnt(6)
	v_bfe_u32 v48, v54, 16, 1
	v_add3_u32 v48, v54, v48, s15
	v_lshrrev_b32_e32 v48, 16, v48
	v_add3_u32 v49, v52, v49, s15
	v_and_or_b32 v48, v49, s16, v48
	s_waitcnt lgkmcnt(5)
	v_bfe_u32 v49, v56, 16, 1
	v_add3_u32 v49, v56, v49, s15
	s_waitcnt lgkmcnt(4)
	v_bfe_u32 v50, v58, 16, 1
	v_lshrrev_b32_e32 v49, 16, v49
	v_add3_u32 v50, v58, v50, s15
	v_and_or_b32 v49, v50, s16, v49
	s_waitcnt lgkmcnt(3)
	v_bfe_u32 v50, v60, 16, 1
	v_add3_u32 v50, v60, v50, s15
	s_waitcnt lgkmcnt(2)
	v_bfe_u32 v51, v62, 16, 1
	v_lshrrev_b32_e32 v50, 16, v50
	v_add3_u32 v51, v62, v51, s15
	v_and_or_b32 v50, v51, s16, v50
	s_waitcnt lgkmcnt(1)
	v_bfe_u32 v51, v64, 16, 1
	v_add_u32_e32 v68, s4, v35
	v_add3_u32 v51, v64, v51, s15
	s_waitcnt lgkmcnt(0)
	v_bfe_u32 v52, v66, 16, 1
	v_ashrrev_i32_e32 v69, 31, v68
	v_lshl_add_u64 v[28:29], v[20:21], 0, s[0:1]
	v_lshrrev_b32_e32 v51, 16, v51
	v_add3_u32 v52, v66, v52, s15
	v_lshlrev_b64 v[68:69], 11, v[68:69]
	v_and_or_b32 v51, v52, s16, v51
	v_lshl_add_u64 v[68:69], v[28:29], 0, v[68:69]
	global_store_dwordx4 v[68:69], v[48:51], off sc1 nt
	v_bfe_u32 v52, v67, 16, 1
	v_add3_u32 v52, v67, v52, s15
	v_bfe_u32 v48, v55, 16, 1
	v_add3_u32 v48, v55, v48, s15
	v_bfe_u32 v49, v53, 16, 1
	v_lshrrev_b32_e32 v48, 16, v48
	v_add3_u32 v49, v53, v49, s15
	v_and_or_b32 v48, v49, s16, v48
	v_bfe_u32 v49, v57, 16, 1
	v_add3_u32 v49, v57, v49, s15
	v_bfe_u32 v50, v59, 16, 1
	v_lshrrev_b32_e32 v49, 16, v49
	v_add3_u32 v50, v59, v50, s15
	v_and_or_b32 v49, v50, s16, v49
	v_bfe_u32 v50, v61, 16, 1
	v_add3_u32 v50, v61, v50, s15
	v_bfe_u32 v51, v63, 16, 1
	v_lshrrev_b32_e32 v50, 16, v50
	v_add3_u32 v51, v63, v51, s15
	v_and_or_b32 v50, v51, s16, v50
	v_bfe_u32 v51, v65, 16, 1
	v_add3_u32 v51, v65, v51, s15
	v_lshrrev_b32_e32 v51, 16, v51
	v_and_or_b32 v51, v52, s16, v51
	v_add_u32_e32 v52, s4, v37
	v_ashrrev_i32_e32 v53, 31, v52
	v_lshlrev_b64 v[52:53], 11, v[52:53]
	v_lshl_add_u64 v[52:53], v[28:29], 0, v[52:53]
	global_store_dwordx4 v[52:53], v[48:51], off sc1 nt
	ds_read2_b32 v[52:53], v36 offset0:49 offset1:57
	ds_read2_b32 v[54:55], v36 offset0:16 offset1:24
	ds_read2_b32 v[56:57], v36 offset0:82 offset1:90
	ds_read2_b32 v[58:59], v36 offset0:115 offset1:123
	ds_read2_b32 v[60:61], v36 offset0:148 offset1:156
	ds_read2_b32 v[62:63], v36 offset0:181 offset1:189
	ds_read2_b32 v[64:65], v36 offset0:214 offset1:222
	ds_read2_b32 v[66:67], v36 offset0:247 offset1:255
	s_waitcnt lgkmcnt(7)
	v_bfe_u32 v49, v52, 16, 1
	s_waitcnt lgkmcnt(6)
	v_bfe_u32 v48, v54, 16, 1
	v_add3_u32 v48, v54, v48, s15
	v_lshrrev_b32_e32 v48, 16, v48
	v_add3_u32 v49, v52, v49, s15
	v_and_or_b32 v48, v49, s16, v48
	s_waitcnt lgkmcnt(5)
	v_bfe_u32 v49, v56, 16, 1
	v_add3_u32 v49, v56, v49, s15
	s_waitcnt lgkmcnt(4)
	v_bfe_u32 v50, v58, 16, 1
	v_lshrrev_b32_e32 v49, 16, v49
	v_add3_u32 v50, v58, v50, s15
	v_and_or_b32 v49, v50, s16, v49
	s_waitcnt lgkmcnt(3)
	v_bfe_u32 v50, v60, 16, 1
	v_add3_u32 v50, v60, v50, s15
	s_waitcnt lgkmcnt(2)
	v_bfe_u32 v51, v62, 16, 1
	v_lshrrev_b32_e32 v50, 16, v50
	v_add3_u32 v51, v62, v51, s15
	v_and_or_b32 v50, v51, s16, v50
	s_waitcnt lgkmcnt(1)
	v_bfe_u32 v51, v64, 16, 1
	v_add_u32_e32 v68, s4, v38
	v_add3_u32 v51, v64, v51, s15
	s_waitcnt lgkmcnt(0)
	v_bfe_u32 v52, v66, 16, 1
	v_ashrrev_i32_e32 v69, 31, v68
	v_lshrrev_b32_e32 v51, 16, v51
	v_add3_u32 v52, v66, v52, s15
	v_lshlrev_b64 v[68:69], 11, v[68:69]
	v_and_or_b32 v51, v52, s16, v51
	v_lshl_add_u64 v[68:69], v[28:29], 0, v[68:69]
	global_store_dwordx4 v[68:69], v[48:51], off sc1 nt
	v_bfe_u32 v52, v67, 16, 1
	v_add3_u32 v52, v67, v52, s15
	v_bfe_u32 v48, v55, 16, 1
	v_add3_u32 v48, v55, v48, s15
	v_bfe_u32 v49, v53, 16, 1
	v_lshrrev_b32_e32 v48, 16, v48
	v_add3_u32 v49, v53, v49, s15
	v_and_or_b32 v48, v49, s16, v48
	v_bfe_u32 v49, v57, 16, 1
	v_add3_u32 v49, v57, v49, s15
	v_bfe_u32 v50, v59, 16, 1
	v_lshrrev_b32_e32 v49, 16, v49
	v_add3_u32 v50, v59, v50, s15
	v_and_or_b32 v49, v50, s16, v49
	v_bfe_u32 v50, v61, 16, 1
	v_add3_u32 v50, v61, v50, s15
	v_bfe_u32 v51, v63, 16, 1
	v_lshrrev_b32_e32 v50, 16, v50
	v_add3_u32 v51, v63, v51, s15
	v_and_or_b32 v50, v51, s16, v50
	v_bfe_u32 v51, v65, 16, 1
	v_add3_u32 v51, v65, v51, s15
	v_lshrrev_b32_e32 v51, 16, v51
	v_and_or_b32 v51, v52, s16, v51
	v_add_u32_e32 v52, s4, v39
	v_ashrrev_i32_e32 v53, 31, v52
	v_lshlrev_b64 v[52:53], 11, v[52:53]
	v_lshl_add_u64 v[28:29], v[28:29], 0, v[52:53]
	global_store_dwordx4 v[28:29], v[48:51], off sc1 nt
	s_waitcnt lgkmcnt(0)

; __device__ __forceinline__ void tr_item(const float* W, int ld, int K, int nblk, int item, bf16* WT, bool gu, LAS float* scr, int lane) {
;     const int kb = item / nblk, nb = item % nblk, k0 = 64 * kb, n0 = 32 * nb;
;     int drow0 = n0;
;     if (gu) { const int bj = n0 / FF, j = n0 - bj * FF; drow0 = 256 * (j / 128) + 128 * bj + (j % 128); }
;     { float t_[32];
; #pragma unroll
;       for (int i = 0; i < 32; ++i) t_[i] = W[(size_t)(k0 + 2 * i + (lane >> 5)) * ld + n0 + (lane & 31)];
; #pragma unroll
;       for (int i = 0; i < 32; ++i) scr[(2 * i + (lane >> 5)) * 33 + (lane & 31)] = t_[i]; }
; __device__ __forceinline__ void convert_items(Frame& F, const Args& a, int lo, int hi, int w, int nw) {
;     ...
;         if (r < I_SI) { tr_item(a.in[10], D + 512, D, 48, r, (bf16*)(F.ws + WS_WSWAIN), false, scr, lane); continue; } r -= I_SI;
.LBB0_1350:
	s_andn2_b64 vcc, exec, s[4:5]
	s_cbranch_vccnz .LBB0_1352
	s_add_i32 s0, s8, 0xf800
	s_and_b32 s4, s0, 0xffff
	s_mul_i32 s4, s4, 0xaaab
	s_lshr_b32 s5, s4, 21
	s_mul_i32 s4, s5, 48
	s_sub_i32 s0, s0, s4
	s_lshl_b32 s0, s0, 5
	s_and_b32 s4, s0, 0xffe0
	s_lshl_b32 s0, s4, 2
	v_lshl_add_u32 v50, s5, 6, v30
	v_lshl_add_u64 v[28:29], v[10:11], 0, s[0:1]
	v_mad_i64_i32 v[48:49], s[6:7], v50, s17, v[28:29]
	global_load_dword v51, v[48:49], off nt
	v_add_u32_e32 v48, 2, v50
	v_mad_i64_i32 v[48:49], s[6:7], v48, s17, v[28:29]
	global_load_dword v52, v[48:49], off nt
	v_add_u32_e32 v48, 4, v50
	v_mad_i64_i32 v[48:49], s[6:7], v48, s17, v[28:29]
	global_load_dword v53, v[48:49], off nt
	v_add_u32_e32 v48, 6, v50
	v_mad_i64_i32 v[48:49], s[6:7], v48, s17, v[28:29]
	global_load_dword v54, v[48:49], off nt
	v_add_u32_e32 v48, 8, v50
	v_mad_i64_i32 v[48:49], s[6:7], v48, s17, v[28:29]
	global_load_dword v55, v[48:49], off nt
	v_add_u32_e32 v48, 10, v50
	v_mad_i64_i32 v[48:49], s[6:7], v48, s17, v[28:29]
	global_load_dword v56, v[48:49], off nt
	v_add_u32_e32 v48, 12, v50
	v_mad_i64_i32 v[48:49], s[6:7], v48, s17, v[28:29]
	global_load_dword v57, v[48:49], off nt
	v_add_u32_e32 v48, 14, v50
	v_mad_i64_i32 v[48:49], s[6:7], v48, s17, v[28:29]
	global_load_dword v58, v[48:49], off nt
	v_add_u32_e32 v48, 16, v50
	v_mad_i64_i32 v[48:49], s[6:7], v48, s17, v[28:29]
	global_load_dword v59, v[48:49], off nt
	v_add_u32_e32 v48, 18, v50
	v_mad_i64_i32 v[48:49], s[6:7], v48, s17, v[28:29]
	global_load_dword v60, v[48:49], off nt
	v_add_u32_e32 v48, 20, v50
	v_mad_i64_i32 v[48:49], s[6:7], v48, s17, v[28:29]
	global_load_dword v61, v[48:49], off nt
	v_add_u32_e32 v48, 22, v50
	v_mad_i64_i32 v[48:49], s[6:7], v48, s17, v[28:29]
	global_load_dword v62, v[48:49], off nt
	v_add_u32_e32 v48, 24, v50
	v_mad_i64_i32 v[48:49], s[6:7], v48, s17, v[28:29]
	global_load_dword v63, v[48:49], off nt
	v_add_u32_e32 v48, 26, v50
	v_mad_i64_i32 v[48:49], s[6:7], v48, s17, v[28:29]
	global_load_dword v64, v[48:49], off nt
	v_add_u32_e32 v48, 28, v50
	v_mad_i64_i32 v[48:49], s[6:7], v48, s17, v[28:29]
	global_load_dword v65, v[48:49], off nt
	v_add_u32_e32 v48, 30, v50
	v_mad_i64_i32 v[48:49], s[6:7], v48, s17, v[28:29]
	global_load_dword v66, v[48:49], off nt
	v_add_u32_e32 v48, 32, v50
	v_mad_i64_i32 v[48:49], s[6:7], v48, s17, v[28:29]
	global_load_dword v67, v[48:49], off nt
	v_add_u32_e32 v48, 34, v50
	v_mad_i64_i32 v[48:49], s[6:7], v48, s17, v[28:29]
	global_load_dword v68, v[48:49], off nt
	v_add_u32_e32 v48, 36, v50
	v_mad_i64_i32 v[48:49], s[6:7], v48, s17, v[28:29]
	global_load_dword v69, v[48:49], off nt
	v_add_u32_e32 v48, 38, v50
	v_mad_i64_i32 v[48:49], s[6:7], v48, s17, v[28:29]
	global_load_dword v70, v[48:49], off nt
	v_add_u32_e32 v48, 40, v50
	v_mad_i64_i32 v[48:49], s[6:7], v48, s17, v[28:29]
	global_load_dword v71, v[48:49], off nt
	v_add_u32_e32 v48, 42, v50
	v_mad_i64_i32 v[48:49], s[6:7], v48, s17, v[28:29]
	global_load_dword v72, v[48:49], off nt
	v_add_u32_e32 v48, 44, v50
	v_mad_i64_i32 v[48:49], s[6:7], v48, s17, v[28:29]
	global_load_dword v73, v[48:49], off nt
	v_add_u32_e32 v48, 46, v50
	v_mad_i64_i32 v[48:49], s[6:7], v48, s17, v[28:29]
	global_load_dword v74, v[48:49], off nt
	v_add_u32_e32 v48, 48, v50
	v_mad_i64_i32 v[48:49], s[6:7], v48, s17, v[28:29]
	global_load_dword v75, v[48:49], off nt
	v_add_u32_e32 v48, 50, v50
	v_mad_i64_i32 v[48:49], s[6:7], v48, s17, v[28:29]
	global_load_dword v76, v[48:49], off nt
	v_add_u32_e32 v48, 52, v50
	v_mad_i64_i32 v[48:49], s[6:7], v48, s17, v[28:29]
	global_load_dword v77, v[48:49], off nt
	v_add_u32_e32 v48, 54, v50
	v_mad_i64_i32 v[48:49], s[6:7], v48, s17, v[28:29]
	global_load_dword v78, v[48:49], off nt
	v_add_u32_e32 v48, 56, v50
	v_mad_i64_i32 v[48:49], s[6:7], v48, s17, v[28:29]
	global_load_dword v79, v[48:49], off nt
	v_add_u32_e32 v48, 58, v50
	v_mad_i64_i32 v[48:49], s[6:7], v48, s17, v[28:29]
	global_load_dword v80, v[48:49], off nt
	v_add_u32_e32 v48, 60, v50
	v_mad_i64_i32 v[48:49], s[6:7], v48, s17, v[28:29]
	global_load_dword v48, v[48:49], off nt
	v_add_u32_e32 v49, 62, v50
	v_mad_i64_i32 v[28:29], s[6:7], v49, s17, v[28:29]
	global_load_dword v28, v[28:29], off nt
	s_waitcnt vmcnt(0)
	ds_write2_b32 v31, v51, v52 offset1:66
	ds_write2_b32 v31, v53, v54 offset0:132 offset1:198
	ds_write2_b32 v40, v55, v56 offset0:8 offset1:74
	ds_write2_b32 v40, v57, v58 offset0:140 offset1:206
	ds_write2_b32 v41, v59, v60 offset0:16 offset1:82
	ds_write2_b32 v41, v61, v62 offset0:148 offset1:214
	ds_write2_b32 v42, v63, v64 offset0:24 offset1:90
	ds_write2_b32 v42, v65, v66 offset0:156 offset1:222
	ds_write2_b32 v43, v67, v68 offset0:32 offset1:98
	ds_write2_b32 v43, v69, v70 offset0:164 offset1:230
	ds_write2_b32 v44, v71, v72 offset0:40 offset1:106
	ds_write2_b32 v44, v73, v74 offset0:172 offset1:238
	ds_write2_b32 v45, v75, v76 offset0:48 offset1:114
	ds_write2_b32 v45, v77, v78 offset0:180 offset1:246
	ds_write2_b32 v46, v79, v80 offset0:56 offset1:122
	ds_write2_b32 v46, v48, v28 offset0:188 offset1:254
	s_waitcnt lgkmcnt(0)
; #define GAS __attribute__((address_space(1)))
; #define LAS __attribute__((address_space(3)))
; #define LDS_WAIT() asm volatile("s_waitcnt lgkmcnt(0)" ::: "memory")
; __device__ __forceinline__ unsigned pk2(float lo, float hi) { return f2bf(lo) | (f2bf(hi) << 16); }
; __device__ __forceinline__ void tr_item(const float* W, int ld, int K, int nblk, int item, bf16* WT, bool gu, LAS float* scr, int lane) {
;     ...
;     LDS_WAIT(); asm volatile("" ::: "memory");
;     const int c = lane & 7;
; #pragma unroll
;     for (int j = 0; j < 4; ++j) { const int n = (lane >> 3) + 8 * j; const LAS float* s = scr + (8 * c) * 33 + n;
;         v4u o; o.x = pk2(s[0 * 33], s[1 * 33]); o.y = pk2(s[2 * 33], s[3 * 33]); o.z = pk2(s[4 * 33], s[5 * 33]); o.w = pk2(s[6 * 33], s[7 * 33]);
;         *(GAS v4u*)(WT + (size_t)(drow0 + n) * K + k0 + 8 * c) = o; }
;     LDS_WAIT(); asm volatile("" ::: "memory");
	ds_read2_b32 v[52:53], v36 offset0:33 offset1:41
	ds_read2_b32 v[54:55], v36 offset1:8
	ds_read2_b32 v[56:57], v36 offset0:66 offset1:74
	ds_read2_b32 v[58:59], v36 offset0:99 offset1:107
	ds_read2_b32 v[60:61], v36 offset0:132 offset1:140
	ds_read2_b32 v[62:63], v36 offset0:165 offset1:173
	ds_read2_b32 v[64:65], v36 offset0:198 offset1:206
	ds_read2_b32 v[66:67], v36 offset0:231 offset1:239
	s_waitcnt lgkmcnt(7)
	v_bfe_u32 v49, v52, 16, 1
	s_waitcnt lgkmcnt(6)
	v_bfe_u32 v48, v54, 16, 1
	v_add3_u32 v48, v54, v48, s15
	v_lshrrev_b32_e32 v48, 16, v48
	v_add3_u32 v49, v52, v49, s15
	v_and_or_b32 v48, v49, s16, v48
	s_waitcnt lgkmcnt(5)
	v_bfe_u32 v49, v56, 16, 1
	v_add3_u32 v49, v56, v49, s15
	s_waitcnt lgkmcnt(4)
	v_bfe_u32 v50, v58, 16, 1
	v_lshrrev_b32_e32 v49, 16, v49
	v_add3_u32 v50, v58, v50, s15
	v_and_or_b32 v49, v50, s16, v49
	s_waitcnt lgkmcnt(3)
	v_bfe_u32 v50, v60, 16, 1
	v_add3_u32 v50, v60, v50, s15
	s_waitcnt lgkmcnt(2)
	v_bfe_u32 v51, v62, 16, 1
	v_lshrrev_b32_e32 v50, 16, v50
	v_add3_u32 v51, v62, v51, s15
	v_and_or_b32 v50, v51, s16, v50
	s_waitcnt lgkmcnt(1)
	v_bfe_u32 v51, v64, 16, 1
	v_add_u32_e32 v68, s4, v35
	s_lshl_b32 s0, s5, 7
	v_add3_u32 v51, v64, v51, s15
	s_waitcnt lgkmcnt(0)
	v_bfe_u32 v52, v66, 16, 1
	v_ashrrev_i32_e32 v69, 31, v68
	v_lshl_add_u64 v[28:29], v[22:23], 0, s[0:1]
	v_lshrrev_b32_e32 v51, 16, v51
	v_add3_u32 v52, v66, v52, s15
	v_lshlrev_b64 v[68:69], 11, v[68:69]
	v_and_or_b32 v51, v52, s16, v51
	v_lshl_add_u64 v[68:69], v[28:29], 0, v[68:69]
	global_store_dwordx4 v[68:69], v[48:51], off sc1 nt
	v_bfe_u32 v52, v67, 16, 1
	v_add3_u32 v52, v67, v52, s15
	v_bfe_u32 v48, v55, 16, 1
	v_add3_u32 v48, v55, v48, s15
	v_bfe_u32 v49, v53, 16, 1
	v_lshrrev_b32_e32 v48, 16, v48
	v_add3_u32 v49, v53, v49, s15
	v_and_or_b32 v48, v49, s16, v48
	v_bfe_u32 v49, v57, 16, 1
	v_add3_u32 v49, v57, v49, s15
	v_bfe_u32 v50, v59, 16, 1
	v_lshrrev_b32_e32 v49, 16, v49
	v_add3_u32 v50, v59, v50, s15
	v_and_or_b32 v49, v50, s16, v49
	v_bfe_u32 v50, v61, 16, 1
	v_add3_u32 v50, v61, v50, s15
	v_bfe_u32 v51, v63, 16, 1
	v_lshrrev_b32_e32 v50, 16, v50
	v_add3_u32 v51, v63, v51, s15
	v_and_or_b32 v50, v51, s16, v50
	v_bfe_u32 v51, v65, 16, 1
	v_add3_u32 v51, v65, v51, s15
	v_lshrrev_b32_e32 v51, 16, v51
	v_and_or_b32 v51, v52, s16, v51
	v_add_u32_e32 v52, s4, v37
	v_ashrrev_i32_e32 v53, 31, v52
	v_lshlrev_b64 v[52:53], 11, v[52:53]
	v_lshl_add_u64 v[52:53], v[28:29], 0, v[52:53]
	global_store_dwordx4 v[52:53], v[48:51], off sc1 nt
	ds_read2_b32 v[52:53], v36 offset0:49 offset1:57
	ds_read2_b32 v[54:55], v36 offset0:16 offset1:24
	ds_read2_b32 v[56:57], v36 offset0:82 offset1:90
	ds_read2_b32 v[58:59], v36 offset0:115 offset1:123
	ds_read2_b32 v[60:61], v36 offset0:148 offset1:156
	ds_read2_b32 v[62:63], v36 offset0:181 offset1:189
	ds_read2_b32 v[64:65], v36 offset0:214 offset1:222
	ds_read2_b32 v[66:67], v36 offset0:247 offset1:255
	s_waitcnt lgkmcnt(7)
	v_bfe_u32 v49, v52, 16, 1
	s_waitcnt lgkmcnt(6)
	v_bfe_u32 v48, v54, 16, 1
	v_add3_u32 v48, v54, v48, s15
	v_lshrrev_b32_e32 v48, 16, v48
	v_add3_u32 v49, v52, v49, s15
	v_and_or_b32 v48, v49, s16, v48
	s_waitcnt lgkmcnt(5)
	v_bfe_u32 v49, v56, 16, 1
	v_add3_u32 v49, v56, v49, s15
	s_waitcnt lgkmcnt(4)
	v_bfe_u32 v50, v58, 16, 1
	v_lshrrev_b32_e32 v49, 16, v49
	v_add3_u32 v50, v58, v50, s15
	v_and_or_b32 v49, v50, s16, v49
	s_waitcnt lgkmcnt(3)
	v_bfe_u32 v50, v60, 16, 1
	v_add3_u32 v50, v60, v50, s15
	s_waitcnt lgkmcnt(2)
	v_bfe_u32 v51, v62, 16, 1
	v_lshrrev_b32_e32 v50, 16, v50
	v_add3_u32 v51, v62, v51, s15
	v_and_or_b32 v50, v51, s16, v50
	s_waitcnt lgkmcnt(1)
	v_bfe_u32 v51, v64, 16, 1
	v_add_u32_e32 v68, s4, v38
	v_add3_u32 v51, v64, v51, s15
	s_waitcnt lgkmcnt(0)
	v_bfe_u32 v52, v66, 16, 1
	v_ashrrev_i32_e32 v69, 31, v68
	v_lshrrev_b32_e32 v51, 16, v51
	v_add3_u32 v52, v66, v52, s15
	v_lshlrev_b64 v[68:69], 11, v[68:69]
	v_and_or_b32 v51, v52, s16, v51
	v_lshl_add_u64 v[68:69], v[28:29], 0, v[68:69]
	global_store_dwordx4 v[68:69], v[48:51], off sc1 nt
	v_bfe_u32 v52, v67, 16, 1
	v_add3_u32 v52, v67, v52, s15
	v_bfe_u32 v48, v55, 16, 1
	v_add3_u32 v48, v55, v48, s15
	v_bfe_u32 v49, v53, 16, 1
	v_lshrrev_b32_e32 v48, 16, v48
	v_add3_u32 v49, v53, v49, s15
	v_and_or_b32 v48, v49, s16, v48
	v_bfe_u32 v49, v57, 16, 1
	v_add3_u32 v49, v57, v49, s15
	v_bfe_u32 v50, v59, 16, 1
	v_lshrrev_b32_e32 v49, 16, v49
	v_add3_u32 v50, v59, v50, s15
	v_and_or_b32 v49, v50, s16, v49
	v_bfe_u32 v50, v61, 16, 1
	v_add3_u32 v50, v61, v50, s15
	v_bfe_u32 v51, v63, 16, 1
	v_lshrrev_b32_e32 v50, 16, v50
	v_add3_u32 v51, v63, v51, s15
	v_and_or_b32 v50, v51, s16, v50
	v_bfe_u32 v51, v65, 16, 1
	v_add3_u32 v51, v65, v51, s15
	v_lshrrev_b32_e32 v51, 16, v51
	v_and_or_b32 v51, v52, s16, v51
	v_add_u32_e32 v52, s4, v39
	v_ashrrev_i32_e32 v53, 31, v52
	v_lshlrev_b64 v[52:53], 11, v[52:53]
	v_lshl_add_u64 v[28:29], v[28:29], 0, v[52:53]
	global_store_dwordx4 v[28:29], v[48:51], off sc1 nt
	s_waitcnt lgkmcnt(0)

; __device__ __forceinline__ void tr_item(const float* W, int ld, int K, int nblk, int item, bf16* WT, bool gu, LAS float* scr, int lane) {
;     const int kb = item / nblk, nb = item % nblk, k0 = 64 * kb, n0 = 32 * nb;
;     int drow0 = n0;
;     if (gu) { const int bj = n0 / FF, j = n0 - bj * FF; drow0 = 256 * (j / 128) + 128 * bj + (j % 128); }
;     { float t_[32];
; #pragma unroll
;       for (int i = 0; i < 32; ++i) t_[i] = W[(size_t)(k0 + 2 * i + (lane >> 5)) * ld + n0 + (lane & 31)];
; #pragma unroll
;       for (int i = 0; i < 32; ++i) scr[(2 * i + (lane >> 5)) * 33 + (lane & 31)] = t_[i]; }
; __device__ __forceinline__ void convert_items(Frame& F, const Args& a, int lo, int hi, int w, int nw) {
;     ...
;         if (r < I_FO) { tr_item(a.in[9], D, D, 32, r, (bf16*)(F.ws + WS_WFOXOUT), false, scr, lane); continue; } r -= I_FO;
.LBB0_1353:
	s_andn2_b64 vcc, exec, s[4:5]
	s_cbranch_vccnz .LBB0_1355
	s_add_i32 s0, s12, 0x2a00
	s_and_b32 s5, s0, 0x1ffc0
	s_and_b32 s4, s9, 0x3e0
	v_add_u32_e32 v28, s5, v30
	s_lshl_b32 s0, s4, 2
	v_ashrrev_i32_e32 v29, 31, v28
	v_lshl_add_u64 v[48:49], v[12:13], 0, s[0:1]
	v_lshlrev_b64 v[28:29], 12, v[28:29]
	v_lshl_add_u64 v[28:29], v[48:49], 0, v[28:29]
	v_add_co_u32_e32 v48, vcc, 0x2000, v28
	global_load_dword v50, v[28:29], off nt
	s_nop 0
	v_addc_co_u32_e32 v49, vcc, 0, v29, vcc
	global_load_dword v51, v[48:49], off nt
	v_add_co_u32_e32 v48, vcc, 0x4000, v28
	s_lshl_b32 s0, s5, 1
	s_nop 0
	v_addc_co_u32_e32 v49, vcc, 0, v29, vcc
	global_load_dword v52, v[48:49], off nt
	v_add_co_u32_e32 v48, vcc, 0x6000, v28
	s_nop 1
	v_addc_co_u32_e32 v49, vcc, 0, v29, vcc
	global_load_dword v53, v[48:49], off nt
	v_add_co_u32_e32 v48, vcc, 0x8000, v28
	s_nop 1
	v_addc_co_u32_e32 v49, vcc, 0, v29, vcc
	global_load_dword v54, v[48:49], off nt
	v_add_co_u32_e32 v48, vcc, 0xa000, v28
	s_nop 1
	v_addc_co_u32_e32 v49, vcc, 0, v29, vcc
	global_load_dword v55, v[48:49], off nt
	v_add_co_u32_e32 v48, vcc, 0xc000, v28
	s_nop 1
	v_addc_co_u32_e32 v49, vcc, 0, v29, vcc
	global_load_dword v56, v[48:49], off nt
	v_add_co_u32_e32 v48, vcc, 0xe000, v28
	s_nop 1
	v_addc_co_u32_e32 v49, vcc, 0, v29, vcc
	global_load_dword v57, v[48:49], off nt
	v_add_co_u32_e32 v48, vcc, 0x10000, v28
	s_nop 1
	v_addc_co_u32_e32 v49, vcc, 0, v29, vcc
	global_load_dword v58, v[48:49], off nt
	v_add_co_u32_e32 v48, vcc, 0x12000, v28
	s_nop 1
	v_addc_co_u32_e32 v49, vcc, 0, v29, vcc
	global_load_dword v59, v[48:49], off nt
	v_add_co_u32_e32 v48, vcc, 0x14000, v28
	s_nop 1
	v_addc_co_u32_e32 v49, vcc, 0, v29, vcc
	global_load_dword v60, v[48:49], off nt
	v_add_co_u32_e32 v48, vcc, 0x16000, v28
	s_nop 1
	v_addc_co_u32_e32 v49, vcc, 0, v29, vcc
	global_load_dword v61, v[48:49], off nt
	v_add_co_u32_e32 v48, vcc, 0x18000, v28
	s_nop 1
	v_addc_co_u32_e32 v49, vcc, 0, v29, vcc
	global_load_dword v62, v[48:49], off nt
	v_add_co_u32_e32 v48, vcc, 0x1a000, v28
	s_nop 1
	v_addc_co_u32_e32 v49, vcc, 0, v29, vcc
	global_load_dword v63, v[48:49], off nt
	v_add_co_u32_e32 v48, vcc, 0x1c000, v28
	s_nop 1
	v_addc_co_u32_e32 v49, vcc, 0, v29, vcc
	global_load_dword v64, v[48:49], off nt
	v_add_co_u32_e32 v48, vcc, 0x1e000, v28
	s_nop 1
	v_addc_co_u32_e32 v49, vcc, 0, v29, vcc
	global_load_dword v65, v[48:49], off nt
	v_add_co_u32_e32 v48, vcc, 0x20000, v28
	s_nop 1
	v_addc_co_u32_e32 v49, vcc, 0, v29, vcc
	global_load_dword v66, v[48:49], off nt
	v_add_co_u32_e32 v48, vcc, 0x22000, v28
	s_nop 1
	v_addc_co_u32_e32 v49, vcc, 0, v29, vcc
	global_load_dword v67, v[48:49], off nt
	v_add_co_u32_e32 v48, vcc, 0x24000, v28
	s_nop 1
	v_addc_co_u32_e32 v49, vcc, 0, v29, vcc
	global_load_dword v68, v[48:49], off nt
	v_add_co_u32_e32 v48, vcc, 0x26000, v28
	s_nop 1
	v_addc_co_u32_e32 v49, vcc, 0, v29, vcc
	global_load_dword v69, v[48:49], off nt
	v_add_co_u32_e32 v48, vcc, 0x28000, v28
	s_nop 1
	v_addc_co_u32_e32 v49, vcc, 0, v29, vcc
	global_load_dword v70, v[48:49], off nt
	v_add_co_u32_e32 v48, vcc, 0x2a000, v28
	s_nop 1
	v_addc_co_u32_e32 v49, vcc, 0, v29, vcc
	global_load_dword v71, v[48:49], off nt
	v_add_co_u32_e32 v48, vcc, 0x2c000, v28
	s_nop 1
	v_addc_co_u32_e32 v49, vcc, 0, v29, vcc
	global_load_dword v72, v[48:49], off nt
	v_add_co_u32_e32 v48, vcc, 0x2e000, v28
	s_nop 1
	v_addc_co_u32_e32 v49, vcc, 0, v29, vcc
	global_load_dword v73, v[48:49], off nt
	v_add_co_u32_e32 v48, vcc, 0x30000, v28
	s_nop 1
	v_addc_co_u32_e32 v49, vcc, 0, v29, vcc
	global_load_dword v74, v[48:49], off nt
	v_add_co_u32_e32 v48, vcc, 0x32000, v28
	s_nop 1
	v_addc_co_u32_e32 v49, vcc, 0, v29, vcc
	global_load_dword v75, v[48:49], off nt
	v_add_co_u32_e32 v48, vcc, 0x34000, v28
	s_nop 1
	v_addc_co_u32_e32 v49, vcc, 0, v29, vcc
	global_load_dword v76, v[48:49], off nt
	v_add_co_u32_e32 v48, vcc, 0x36000, v28
	s_nop 1
	v_addc_co_u32_e32 v49, vcc, 0, v29, vcc
	global_load_dword v77, v[48:49], off nt
	v_add_co_u32_e32 v48, vcc, 0x38000, v28
	s_nop 1
	v_addc_co_u32_e32 v49, vcc, 0, v29, vcc
	global_load_dword v78, v[48:49], off nt
	v_add_co_u32_e32 v48, vcc, 0x3a000, v28
	s_nop 1
	v_addc_co_u32_e32 v49, vcc, 0, v29, vcc
	global_load_dword v79, v[48:49], off nt
	v_add_co_u32_e32 v48, vcc, 0x3c000, v28
	s_nop 1
	v_addc_co_u32_e32 v49, vcc, 0, v29, vcc
	v_add_co_u32_e32 v28, vcc, 0x3e000, v28
	global_load_dword v48, v[48:49], off nt
	s_nop 0
	v_addc_co_u32_e32 v29, vcc, 0, v29, vcc
	global_load_dword v28, v[28:29], off nt
	s_waitcnt vmcnt(0)
	ds_write2_b32 v31, v50, v51 offset1:66
	ds_write2_b32 v31, v52, v53 offset0:132 offset1:198
	ds_write2_b32 v40, v54, v55 offset0:8 offset1:74
	ds_write2_b32 v40, v56, v57 offset0:140 offset1:206
	ds_write2_b32 v41, v58, v59 offset0:16 offset1:82
	ds_write2_b32 v41, v60, v61 offset0:148 offset1:214
	ds_write2_b32 v42, v62, v63 offset0:24 offset1:90
	ds_write2_b32 v42, v64, v65 offset0:156 offset1:222
	ds_write2_b32 v43, v66, v67 offset0:32 offset1:98
	ds_write2_b32 v43, v68, v69 offset0:164 offset1:230
	ds_write2_b32 v44, v70, v71 offset0:40 offset1:106
	ds_write2_b32 v44, v72, v73 offset0:172 offset1:238
	ds_write2_b32 v45, v74, v75 offset0:48 offset1:114
	ds_write2_b32 v45, v76, v77 offset0:180 offset1:246
	ds_write2_b32 v46, v78, v79 offset0:56 offset1:122
	ds_write2_b32 v46, v48, v28 offset0:188 offset1:254
	s_waitcnt lgkmcnt(0)
; #define GAS __attribute__((address_space(1)))
; #define LAS __attribute__((address_space(3)))
; #define LDS_WAIT() asm volatile("s_waitcnt lgkmcnt(0)" ::: "memory")
; __device__ __forceinline__ unsigned pk2(float lo, float hi) { return f2bf(lo) | (f2bf(hi) << 16); }
; __device__ __forceinline__ void tr_item(const float* W, int ld, int K, int nblk, int item, bf16* WT, bool gu, LAS float* scr, int lane) {
;     ...
;     LDS_WAIT(); asm volatile("" ::: "memory");
;     const int c = lane & 7;
; #pragma unroll
;     for (int j = 0; j < 4; ++j) { const int n = (lane >> 3) + 8 * j; const LAS float* s = scr + (8 * c) * 33 + n;
;         v4u o; o.x = pk2(s[0 * 33], s[1 * 33]); o.y = pk2(s[2 * 33], s[3 * 33]); o.z = pk2(s[4 * 33], s[5 * 33]); o.w = pk2(s[6 * 33], s[7 * 33]);
;         *(GAS v4u*)(WT + (size_t)(drow0 + n) * K + k0 + 8 * c) = o; }
;     LDS_WAIT(); asm volatile("" ::: "memory");
	ds_read2_b32 v[52:53], v36 offset0:33 offset1:41
	ds_read2_b32 v[54:55], v36 offset1:8
	ds_read2_b32 v[56:57], v36 offset0:66 offset1:74
	ds_read2_b32 v[58:59], v36 offset0:99 offset1:107
	ds_read2_b32 v[60:61], v36 offset0:132 offset1:140
	ds_read2_b32 v[62:63], v36 offset0:165 offset1:173
	ds_read2_b32 v[64:65], v36 offset0:198 offset1:206
	ds_read2_b32 v[66:67], v36 offset0:231 offset1:239
	s_waitcnt lgkmcnt(7)
	v_bfe_u32 v49, v52, 16, 1
	s_waitcnt lgkmcnt(6)
	v_bfe_u32 v48, v54, 16, 1
	v_add3_u32 v48, v54, v48, s15
	v_lshrrev_b32_e32 v48, 16, v48
	v_add3_u32 v49, v52, v49, s15
	v_and_or_b32 v48, v49, s16, v48
	s_waitcnt lgkmcnt(5)
	v_bfe_u32 v49, v56, 16, 1
	v_add3_u32 v49, v56, v49, s15
	s_waitcnt lgkmcnt(4)
	v_bfe_u32 v50, v58, 16, 1
	v_lshrrev_b32_e32 v49, 16, v49
	v_add3_u32 v50, v58, v50, s15
	v_and_or_b32 v49, v50, s16, v49
	s_waitcnt lgkmcnt(3)
	v_bfe_u32 v50, v60, 16, 1
	v_add3_u32 v50, v60, v50, s15
	s_waitcnt lgkmcnt(2)
	v_bfe_u32 v51, v62, 16, 1
	v_lshrrev_b32_e32 v50, 16, v50
	v_add3_u32 v51, v62, v51, s15
	v_and_or_b32 v50, v51, s16, v50
	s_waitcnt lgkmcnt(1)
	v_bfe_u32 v51, v64, 16, 1
	v_add_u32_e32 v68, s4, v35
	v_add3_u32 v51, v64, v51, s15
	s_waitcnt lgkmcnt(0)
	v_bfe_u32 v52, v66, 16, 1
	v_ashrrev_i32_e32 v69, 31, v68
	v_lshl_add_u64 v[28:29], v[24:25], 0, s[0:1]
	v_lshrrev_b32_e32 v51, 16, v51
	v_add3_u32 v52, v66, v52, s15
	v_lshlrev_b64 v[68:69], 11, v[68:69]
	v_and_or_b32 v51, v52, s16, v51
	v_lshl_add_u64 v[68:69], v[28:29], 0, v[68:69]
	global_store_dwordx4 v[68:69], v[48:51], off sc1 nt
	v_bfe_u32 v52, v67, 16, 1
	v_add3_u32 v52, v67, v52, s15
	v_bfe_u32 v48, v55, 16, 1
	v_add3_u32 v48, v55, v48, s15
	v_bfe_u32 v49, v53, 16, 1
	v_lshrrev_b32_e32 v48, 16, v48
	v_add3_u32 v49, v53, v49, s15
	v_and_or_b32 v48, v49, s16, v48
	v_bfe_u32 v49, v57, 16, 1
	v_add3_u32 v49, v57, v49, s15
	v_bfe_u32 v50, v59, 16, 1
	v_lshrrev_b32_e32 v49, 16, v49
	v_add3_u32 v50, v59, v50, s15
	v_and_or_b32 v49, v50, s16, v49
	v_bfe_u32 v50, v61, 16, 1
	v_add3_u32 v50, v61, v50, s15
	v_bfe_u32 v51, v63, 16, 1
	v_lshrrev_b32_e32 v50, 16, v50
	v_add3_u32 v51, v63, v51, s15
	v_and_or_b32 v50, v51, s16, v50
	v_bfe_u32 v51, v65, 16, 1
	v_add3_u32 v51, v65, v51, s15
	v_lshrrev_b32_e32 v51, 16, v51
	v_and_or_b32 v51, v52, s16, v51
	v_add_u32_e32 v52, s4, v37
	v_ashrrev_i32_e32 v53, 31, v52
	v_lshlrev_b64 v[52:53], 11, v[52:53]
	v_lshl_add_u64 v[52:53], v[28:29], 0, v[52:53]
	global_store_dwordx4 v[52:53], v[48:51], off sc1 nt
	ds_read2_b32 v[52:53], v36 offset0:49 offset1:57
	ds_read2_b32 v[54:55], v36 offset0:16 offset1:24
	ds_read2_b32 v[56:57], v36 offset0:82 offset1:90
	ds_read2_b32 v[58:59], v36 offset0:115 offset1:123
	ds_read2_b32 v[60:61], v36 offset0:148 offset1:156
	ds_read2_b32 v[62:63], v36 offset0:181 offset1:189
	ds_read2_b32 v[64:65], v36 offset0:214 offset1:222
	ds_read2_b32 v[66:67], v36 offset0:247 offset1:255
	s_waitcnt lgkmcnt(7)
	v_bfe_u32 v49, v52, 16, 1
	s_waitcnt lgkmcnt(6)
	v_bfe_u32 v48, v54, 16, 1
	v_add3_u32 v48, v54, v48, s15
	v_lshrrev_b32_e32 v48, 16, v48
	v_add3_u32 v49, v52, v49, s15
	v_and_or_b32 v48, v49, s16, v48
	s_waitcnt lgkmcnt(5)
	v_bfe_u32 v49, v56, 16, 1
	v_add3_u32 v49, v56, v49, s15
	s_waitcnt lgkmcnt(4)
	v_bfe_u32 v50, v58, 16, 1
	v_lshrrev_b32_e32 v49, 16, v49
	v_add3_u32 v50, v58, v50, s15
	v_and_or_b32 v49, v50, s16, v49
	s_waitcnt lgkmcnt(3)
	v_bfe_u32 v50, v60, 16, 1
	v_add3_u32 v50, v60, v50, s15
	s_waitcnt lgkmcnt(2)
	v_bfe_u32 v51, v62, 16, 1
	v_lshrrev_b32_e32 v50, 16, v50
	v_add3_u32 v51, v62, v51, s15
	v_and_or_b32 v50, v51, s16, v50
	s_waitcnt lgkmcnt(1)
	v_bfe_u32 v51, v64, 16, 1
	v_add_u32_e32 v68, s4, v38
	v_add3_u32 v51, v64, v51, s15
	s_waitcnt lgkmcnt(0)
	v_bfe_u32 v52, v66, 16, 1
	v_ashrrev_i32_e32 v69, 31, v68
	v_lshrrev_b32_e32 v51, 16, v51
	v_add3_u32 v52, v66, v52, s15
	v_lshlrev_b64 v[68:69], 11, v[68:69]
	v_and_or_b32 v51, v52, s16, v51
	v_lshl_add_u64 v[68:69], v[28:29], 0, v[68:69]
	global_store_dwordx4 v[68:69], v[48:51], off sc1 nt
	v_bfe_u32 v52, v67, 16, 1
	v_add3_u32 v52, v67, v52, s15
	v_bfe_u32 v48, v55, 16, 1
	v_add3_u32 v48, v55, v48, s15
	v_bfe_u32 v49, v53, 16, 1
	v_lshrrev_b32_e32 v48, 16, v48
	v_add3_u32 v49, v53, v49, s15
	v_and_or_b32 v48, v49, s16, v48
	v_bfe_u32 v49, v57, 16, 1
	v_add3_u32 v49, v57, v49, s15
	v_bfe_u32 v50, v59, 16, 1
	v_lshrrev_b32_e32 v49, 16, v49
	v_add3_u32 v50, v59, v50, s15
	v_and_or_b32 v49, v50, s16, v49
	v_bfe_u32 v50, v61, 16, 1
	v_add3_u32 v50, v61, v50, s15
	v_bfe_u32 v51, v63, 16, 1
	v_lshrrev_b32_e32 v50, 16, v50
	v_add3_u32 v51, v63, v51, s15
	v_and_or_b32 v50, v51, s16, v50
	v_bfe_u32 v51, v65, 16, 1
	v_add3_u32 v51, v65, v51, s15
	v_lshrrev_b32_e32 v51, 16, v51
	v_and_or_b32 v51, v52, s16, v51
	v_add_u32_e32 v52, s4, v39
	v_ashrrev_i32_e32 v53, 31, v52
	v_lshlrev_b64 v[52:53], 11, v[52:53]
	v_lshl_add_u64 v[28:29], v[28:29], 0, v[52:53]
	global_store_dwordx4 v[28:29], v[48:51], off sc1 nt
	s_waitcnt lgkmcnt(0)

; __device__ __forceinline__ void tr_item(const float* W, int ld, int K, int nblk, int item, bf16* WT, bool gu, LAS float* scr, int lane) {
;     const int kb = item / nblk, nb = item % nblk, k0 = 64 * kb, n0 = 32 * nb;
;     int drow0 = n0;
;     if (gu) { const int bj = n0 / FF, j = n0 - bj * FF; drow0 = 256 * (j / 128) + 128 * bj + (j % 128); }
;     { float t_[32];
; #pragma unroll
;       for (int i = 0; i < 32; ++i) t_[i] = W[(size_t)(k0 + 2 * i + (lane >> 5)) * ld + n0 + (lane & 31)];
; #pragma unroll
;       for (int i = 0; i < 32; ++i) scr[(2 * i + (lane >> 5)) * 33 + (lane & 31)] = t_[i]; }
; __device__ __forceinline__ void convert_items(Frame& F, const Args& a, int lo, int hi, int w, int nw) {
;     ...
;         if (r < I_FI) { tr_item(a.in[7], 3 * D + 16, D, 96, r, (bf16*)(F.ws + WS_WFOXIN), false, scr, lane); continue; } r -= I_FI;
.LBB0_1356:
	s_andn2_b64 vcc, exec, s[4:5]
	s_cbranch_vccnz .LBB0_1329
	s_mul_hi_i32 s0, s8, 0x2aaaaaab
	s_lshr_b32 s4, s0, 31
	s_ashr_i32 s0, s0, 4
	s_add_i32 s0, s0, s4
	s_lshl_b32 s6, s0, 6
	s_mulk_i32 s0, 0xf400
	s_add_i32 s4, s9, s0
	s_ashr_i32 s5, s4, 31
	v_add_u32_e32 v50, s6, v30
	v_lshl_add_u64 v[28:29], s[4:5], 2, v[14:15]
	v_mad_i64_i32 v[48:49], s[40:41], v50, s30, v[28:29]
	global_load_dword v51, v[48:49], off nt
	v_add_u32_e32 v48, 2, v50
	v_mad_i64_i32 v[48:49], s[40:41], v48, s30, v[28:29]
	global_load_dword v52, v[48:49], off nt
	v_add_u32_e32 v48, 4, v50
	v_mad_i64_i32 v[48:49], s[40:41], v48, s30, v[28:29]
	global_load_dword v53, v[48:49], off nt
	v_add_u32_e32 v48, 6, v50
	v_mad_i64_i32 v[48:49], s[40:41], v48, s30, v[28:29]
	global_load_dword v54, v[48:49], off nt
	v_add_u32_e32 v48, 8, v50
	v_mad_i64_i32 v[48:49], s[40:41], v48, s30, v[28:29]
	global_load_dword v55, v[48:49], off nt
	v_add_u32_e32 v48, 10, v50
	v_mad_i64_i32 v[48:49], s[40:41], v48, s30, v[28:29]
	global_load_dword v56, v[48:49], off nt
	v_add_u32_e32 v48, 12, v50
	v_mad_i64_i32 v[48:49], s[40:41], v48, s30, v[28:29]
	global_load_dword v57, v[48:49], off nt
	v_add_u32_e32 v48, 14, v50
	v_mad_i64_i32 v[48:49], s[40:41], v48, s30, v[28:29]
	global_load_dword v58, v[48:49], off nt
	v_add_u32_e32 v48, 16, v50
	v_mad_i64_i32 v[48:49], s[40:41], v48, s30, v[28:29]
	global_load_dword v59, v[48:49], off nt
	v_add_u32_e32 v48, 18, v50
	v_mad_i64_i32 v[48:49], s[40:41], v48, s30, v[28:29]
	global_load_dword v60, v[48:49], off nt
	v_add_u32_e32 v48, 20, v50
	v_mad_i64_i32 v[48:49], s[40:41], v48, s30, v[28:29]
	global_load_dword v61, v[48:49], off nt
	v_add_u32_e32 v48, 22, v50
	v_mad_i64_i32 v[48:49], s[40:41], v48, s30, v[28:29]
	global_load_dword v62, v[48:49], off nt
	v_add_u32_e32 v48, 24, v50
	v_mad_i64_i32 v[48:49], s[40:41], v48, s30, v[28:29]
	global_load_dword v63, v[48:49], off nt
	v_add_u32_e32 v48, 26, v50
	v_mad_i64_i32 v[48:49], s[40:41], v48, s30, v[28:29]
	global_load_dword v64, v[48:49], off nt
	v_add_u32_e32 v48, 28, v50
	v_mad_i64_i32 v[48:49], s[40:41], v48, s30, v[28:29]
	global_load_dword v65, v[48:49], off nt
	v_add_u32_e32 v48, 30, v50
	v_mad_i64_i32 v[48:49], s[40:41], v48, s30, v[28:29]
	global_load_dword v66, v[48:49], off nt
	v_add_u32_e32 v48, 32, v50
	v_mad_i64_i32 v[48:49], s[40:41], v48, s30, v[28:29]
	global_load_dword v67, v[48:49], off nt
	v_add_u32_e32 v48, 34, v50
	v_mad_i64_i32 v[48:49], s[40:41], v48, s30, v[28:29]
	global_load_dword v68, v[48:49], off nt
	v_add_u32_e32 v48, 36, v50
	v_mad_i64_i32 v[48:49], s[40:41], v48, s30, v[28:29]
	global_load_dword v69, v[48:49], off nt
	v_add_u32_e32 v48, 38, v50
	v_mad_i64_i32 v[48:49], s[40:41], v48, s30, v[28:29]
	global_load_dword v70, v[48:49], off nt
	v_add_u32_e32 v48, 40, v50
	v_mad_i64_i32 v[48:49], s[40:41], v48, s30, v[28:29]
	global_load_dword v71, v[48:49], off nt
	v_add_u32_e32 v48, 42, v50
	v_mad_i64_i32 v[48:49], s[40:41], v48, s30, v[28:29]
	global_load_dword v72, v[48:49], off nt
	v_add_u32_e32 v48, 44, v50
	v_mad_i64_i32 v[48:49], s[40:41], v48, s30, v[28:29]
	global_load_dword v73, v[48:49], off nt
	v_add_u32_e32 v48, 46, v50
	v_mad_i64_i32 v[48:49], s[40:41], v48, s30, v[28:29]
	global_load_dword v74, v[48:49], off nt
	v_add_u32_e32 v48, 48, v50
	v_mad_i64_i32 v[48:49], s[40:41], v48, s30, v[28:29]
	global_load_dword v75, v[48:49], off nt
	v_add_u32_e32 v48, 50, v50
	v_mad_i64_i32 v[48:49], s[40:41], v48, s30, v[28:29]
	global_load_dword v76, v[48:49], off nt
	v_add_u32_e32 v48, 52, v50
	v_mad_i64_i32 v[48:49], s[40:41], v48, s30, v[28:29]
	global_load_dword v77, v[48:49], off nt
	v_add_u32_e32 v48, 54, v50
	v_mad_i64_i32 v[48:49], s[40:41], v48, s30, v[28:29]
	global_load_dword v78, v[48:49], off nt
	v_add_u32_e32 v48, 56, v50
	v_mad_i64_i32 v[48:49], s[40:41], v48, s30, v[28:29]
	global_load_dword v79, v[48:49], off nt
	v_add_u32_e32 v48, 58, v50
	v_mad_i64_i32 v[48:49], s[40:41], v48, s30, v[28:29]
	global_load_dword v80, v[48:49], off nt
	v_add_u32_e32 v48, 60, v50
	v_mad_i64_i32 v[48:49], s[40:41], v48, s30, v[28:29]
	global_load_dword v48, v[48:49], off nt
	v_add_u32_e32 v49, 62, v50
	v_mad_i64_i32 v[28:29], s[40:41], v49, s30, v[28:29]
	global_load_dword v28, v[28:29], off nt
	s_waitcnt vmcnt(0)
	ds_write2_b32 v31, v51, v52 offset1:66
	ds_write2_b32 v31, v53, v54 offset0:132 offset1:198
	ds_write2_b32 v40, v55, v56 offset0:8 offset1:74
	ds_write2_b32 v40, v57, v58 offset0:140 offset1:206
	ds_write2_b32 v41, v59, v60 offset0:16 offset1:82
	ds_write2_b32 v41, v61, v62 offset0:148 offset1:214
	ds_write2_b32 v42, v63, v64 offset0:24 offset1:90
	ds_write2_b32 v42, v65, v66 offset0:156 offset1:222
	ds_write2_b32 v43, v67, v68 offset0:32 offset1:98
	ds_write2_b32 v43, v69, v70 offset0:164 offset1:230
	ds_write2_b32 v44, v71, v72 offset0:40 offset1:106
	ds_write2_b32 v44, v73, v74 offset0:172 offset1:238
	ds_write2_b32 v45, v75, v76 offset0:48 offset1:114
	ds_write2_b32 v45, v77, v78 offset0:180 offset1:246
	ds_write2_b32 v46, v79, v80 offset0:56 offset1:122
	ds_write2_b32 v46, v48, v28 offset0:188 offset1:254
	s_waitcnt lgkmcnt(0)
; #define GAS __attribute__((address_space(1)))
; #define LAS __attribute__((address_space(3)))
; #define LDS_WAIT() asm volatile("s_waitcnt lgkmcnt(0)" ::: "memory")
; __device__ __forceinline__ unsigned pk2(float lo, float hi) { return f2bf(lo) | (f2bf(hi) << 16); }
; __device__ __forceinline__ void tr_item(const float* W, int ld, int K, int nblk, int item, bf16* WT, bool gu, LAS float* scr, int lane) {
;     ...
;     LDS_WAIT(); asm volatile("" ::: "memory");
;     const int c = lane & 7;
; #pragma unroll
;     for (int j = 0; j < 4; ++j) { const int n = (lane >> 3) + 8 * j; const LAS float* s = scr + (8 * c) * 33 + n;
;         v4u o; o.x = pk2(s[0 * 33], s[1 * 33]); o.y = pk2(s[2 * 33], s[3 * 33]); o.z = pk2(s[4 * 33], s[5 * 33]); o.w = pk2(s[6 * 33], s[7 * 33]);
;         *(GAS v4u*)(WT + (size_t)(drow0 + n) * K + k0 + 8 * c) = o; }
;     LDS_WAIT(); asm volatile("" ::: "memory");
; __device__ __forceinline__ void convert_items(Frame& F, const Args& a, int lo, int hi, int w, int nw) {
;     ...
;     for (int it = lo + w; it < hi; it += nw) {
	ds_read2_b32 v[52:53], v36 offset0:33 offset1:41
	ds_read2_b32 v[54:55], v36 offset1:8
	ds_read2_b32 v[56:57], v36 offset0:66 offset1:74
	ds_read2_b32 v[58:59], v36 offset0:99 offset1:107
	ds_read2_b32 v[60:61], v36 offset0:132 offset1:140
	ds_read2_b32 v[62:63], v36 offset0:165 offset1:173
	ds_read2_b32 v[64:65], v36 offset0:198 offset1:206
	ds_read2_b32 v[66:67], v36 offset0:231 offset1:239
	s_waitcnt lgkmcnt(7)
	v_bfe_u32 v49, v52, 16, 1
	s_waitcnt lgkmcnt(6)
	v_bfe_u32 v48, v54, 16, 1
	v_add3_u32 v48, v54, v48, s15
	v_lshrrev_b32_e32 v48, 16, v48
	v_add3_u32 v49, v52, v49, s15
	v_and_or_b32 v48, v49, s16, v48
	s_waitcnt lgkmcnt(5)
	v_bfe_u32 v49, v56, 16, 1
	v_add3_u32 v49, v56, v49, s15
	s_waitcnt lgkmcnt(4)
	v_bfe_u32 v50, v58, 16, 1
	v_lshrrev_b32_e32 v49, 16, v49
	v_add3_u32 v50, v58, v50, s15
	v_and_or_b32 v49, v50, s16, v49
	s_waitcnt lgkmcnt(3)
	v_bfe_u32 v50, v60, 16, 1
	v_add3_u32 v50, v60, v50, s15
	s_waitcnt lgkmcnt(2)
	v_bfe_u32 v51, v62, 16, 1
	v_lshrrev_b32_e32 v50, 16, v50
	v_add3_u32 v51, v62, v51, s15
	v_and_or_b32 v50, v51, s16, v50
	s_waitcnt lgkmcnt(1)
	v_bfe_u32 v51, v64, 16, 1
	v_add_u32_e32 v68, s4, v35
	s_ashr_i32 s7, s6, 31
	v_add3_u32 v51, v64, v51, s15
	s_waitcnt lgkmcnt(0)
	v_bfe_u32 v52, v66, 16, 1
	v_ashrrev_i32_e32 v69, 31, v68
	v_lshl_add_u64 v[28:29], s[6:7], 1, v[26:27]
	v_lshrrev_b32_e32 v51, 16, v51
	v_add3_u32 v52, v66, v52, s15
	v_lshlrev_b64 v[70:71], 11, v[68:69]
	v_and_or_b32 v51, v52, s16, v51
	v_lshl_add_u64 v[70:71], v[28:29], 0, v[70:71]
	global_store_dwordx4 v[70:71], v[48:51], off sc1 nt
	v_bfe_u32 v52, v67, 16, 1
	v_add3_u32 v52, v67, v52, s15
	v_bfe_u32 v48, v55, 16, 1
	v_add3_u32 v48, v55, v48, s15
	v_bfe_u32 v49, v53, 16, 1
	v_lshrrev_b32_e32 v48, 16, v48
	v_add3_u32 v49, v53, v49, s15
	v_and_or_b32 v48, v49, s16, v48
	v_bfe_u32 v49, v57, 16, 1
	v_add3_u32 v49, v57, v49, s15
	v_bfe_u32 v50, v59, 16, 1
	v_lshrrev_b32_e32 v49, 16, v49
	v_add3_u32 v50, v59, v50, s15
	v_and_or_b32 v49, v50, s16, v49
	v_bfe_u32 v50, v61, 16, 1
	v_add3_u32 v50, v61, v50, s15
	v_bfe_u32 v51, v63, 16, 1
	v_lshrrev_b32_e32 v50, 16, v50
	v_add3_u32 v51, v63, v51, s15
	v_and_or_b32 v50, v51, s16, v50
	v_bfe_u32 v51, v65, 16, 1
	v_add3_u32 v51, v65, v51, s15
	v_lshrrev_b32_e32 v51, 16, v51
	v_and_or_b32 v51, v52, s16, v51
	v_add_u32_e32 v52, 8, v68
	v_ashrrev_i32_e32 v53, 31, v52
	v_lshlrev_b64 v[52:53], 11, v[52:53]
	v_lshl_add_u64 v[52:53], v[28:29], 0, v[52:53]
	global_store_dwordx4 v[52:53], v[48:51], off sc1 nt
	ds_read2_b32 v[52:53], v36 offset0:49 offset1:57
	ds_read2_b32 v[54:55], v36 offset0:16 offset1:24
	ds_read2_b32 v[56:57], v36 offset0:82 offset1:90
	ds_read2_b32 v[58:59], v36 offset0:115 offset1:123
	ds_read2_b32 v[60:61], v36 offset0:148 offset1:156
	ds_read2_b32 v[62:63], v36 offset0:181 offset1:189
	ds_read2_b32 v[64:65], v36 offset0:214 offset1:222
	ds_read2_b32 v[66:67], v36 offset0:247 offset1:255
	s_waitcnt lgkmcnt(7)
	v_bfe_u32 v49, v52, 16, 1
	s_waitcnt lgkmcnt(6)
	v_bfe_u32 v48, v54, 16, 1
	v_add3_u32 v48, v54, v48, s15
	v_lshrrev_b32_e32 v48, 16, v48
	v_add3_u32 v49, v52, v49, s15
	v_and_or_b32 v48, v49, s16, v48
	s_waitcnt lgkmcnt(5)
	v_bfe_u32 v49, v56, 16, 1
	v_add3_u32 v49, v56, v49, s15
	s_waitcnt lgkmcnt(4)
	v_bfe_u32 v50, v58, 16, 1
	v_lshrrev_b32_e32 v49, 16, v49
	v_add3_u32 v50, v58, v50, s15
	v_and_or_b32 v49, v50, s16, v49
	s_waitcnt lgkmcnt(3)
	v_bfe_u32 v50, v60, 16, 1
	v_add3_u32 v50, v60, v50, s15
	s_waitcnt lgkmcnt(2)
	v_bfe_u32 v51, v62, 16, 1
	v_lshrrev_b32_e32 v50, 16, v50
	v_add3_u32 v51, v62, v51, s15
	v_and_or_b32 v50, v51, s16, v50
	s_waitcnt lgkmcnt(1)
	v_bfe_u32 v51, v64, 16, 1
	v_add_u32_e32 v70, 16, v68
	v_add3_u32 v51, v64, v51, s15
	s_waitcnt lgkmcnt(0)
	v_bfe_u32 v52, v66, 16, 1
	v_ashrrev_i32_e32 v71, 31, v70
	v_lshrrev_b32_e32 v51, 16, v51
	v_add3_u32 v52, v66, v52, s15
	v_lshlrev_b64 v[70:71], 11, v[70:71]
	v_and_or_b32 v51, v52, s16, v51
	v_lshl_add_u64 v[70:71], v[28:29], 0, v[70:71]
	global_store_dwordx4 v[70:71], v[48:51], off sc1 nt
	v_bfe_u32 v52, v67, 16, 1
	v_add3_u32 v52, v67, v52, s15
	v_bfe_u32 v48, v55, 16, 1
	v_add3_u32 v48, v55, v48, s15
	v_bfe_u32 v49, v53, 16, 1
	v_lshrrev_b32_e32 v48, 16, v48
	v_add3_u32 v49, v53, v49, s15
	v_and_or_b32 v48, v49, s16, v48
	v_bfe_u32 v49, v57, 16, 1
	v_add3_u32 v49, v57, v49, s15
	v_bfe_u32 v50, v59, 16, 1
	v_lshrrev_b32_e32 v49, 16, v49
	v_add3_u32 v50, v59, v50, s15
	v_and_or_b32 v49, v50, s16, v49
	v_bfe_u32 v50, v61, 16, 1
	v_add3_u32 v50, v61, v50, s15
	v_bfe_u32 v51, v63, 16, 1
	v_lshrrev_b32_e32 v50, 16, v50
	v_add3_u32 v51, v63, v51, s15
	v_and_or_b32 v50, v51, s16, v50
	v_bfe_u32 v51, v65, 16, 1
	v_add3_u32 v51, v65, v51, s15
	v_lshrrev_b32_e32 v51, 16, v51
	v_and_or_b32 v51, v52, s16, v51
	v_add_u32_e32 v52, 24, v68
	v_ashrrev_i32_e32 v53, 31, v52
	v_lshlrev_b64 v[52:53], 11, v[52:53]
	v_lshl_add_u64 v[28:29], v[28:29], 0, v[52:53]
	global_store_dwordx4 v[28:29], v[48:51], off sc1 nt
	s_waitcnt lgkmcnt(0)
	s_branch .LBB0_1329

; __device__ __forceinline__ void tr_item8(const float* W, int ld, int K, int nblk, int item, unsigned char* WT, bool gu, float scale, LAS float* scr, int lane) {
;     const int kb = item / nblk, nb = item % nblk, k0 = 64 * kb, n0 = 32 * nb;
;     int drow0 = n0;
;     if (gu) { const int bj = n0 / FF, j = n0 - bj * FF; drow0 = 256 * (j / 128) + 128 * bj + (j % 128); }
;     { float t_[32];
; #pragma unroll
;       for (int i = 0; i < 32; ++i) t_[i] = W[(size_t)(k0 + 2 * i + (lane >> 5)) * ld + n0 + (lane & 31)];
; #pragma unroll
;       for (int i = 0; i < 32; ++i) scr[(2 * i + (lane >> 5)) * 33 + (lane & 31)] = t_[i] * scale; }
; __device__ __forceinline__ void convert_items(Frame& F, const Args& a, int lo, int hi, int w, int nw) {
;     ...
;         int r = it;
;         if (r < I_FI) { tr_item(a.in[7], 3 * D + 16, D, 96, r, (bf16*)(F.ws + WS_WFOXIN), false, scr, lane); continue; } r -= I_FI;
;         if (r < I_FO) { tr_item(a.in[9], D, D, 32, r, (bf16*)(F.ws + WS_WFOXOUT), false, scr, lane); continue; } r -= I_FO;
;         if (r < I_SI) { tr_item(a.in[10], D + 512, D, 48, r, (bf16*)(F.ws + WS_WSWAIN), false, scr, lane); continue; } r -= I_SI;
;         if (r < I_SO) { tr_item(a.in[12], D, D, 32, r, (bf16*)(F.ws + WS_WSWAOUT), false, scr, lane); continue; } r -= I_SO;
;         if (r < I_GU) { tr_item8(a.in[14], 2 * FF, D, 224, r, F.ws + WS_WGU, true, WSC_GU, scr, lane); continue; } r -= I_GU;
;         if (r < I_DN) { tr_item8(a.in[15], D, FF, 32, r, F.ws + WS_WDN, false, WSC_DN, scr, lane); continue; } r -= I_DN;
;         if (r < NE * I_GU) { const int e = r / I_GU, rr = r % I_GU; tr_item8(a.in[18] + (size_t)e * D * 2 * FF, 2 * FF, D, 224, rr, F.ws + WS_WMGU + (size_t)e * 2 * FF * D, true, WSC_GU, scr, lane); continue; } r -= NE * I_GU;
;         { const int e = r / I_DN, rr = r % I_DN; tr_item8(a.in[19] + (size_t)e * FF * D, D, FF, 32, rr, F.ws + WS_WMDN + (size_t)e * D * FF, false, WSC_DN, scr, lane); }
.LBB0_1406:
	s_cmpk_gt_i32 s3, 0x5ff
	s_mov_b64 s[4:5], -1
	s_cbranch_scc0 .LBB0_1432
	s_cmpk_gt_u32 s3, 0x7ff
	s_cbranch_scc0 .LBB0_1429
	s_cmpk_gt_u32 s3, 0xaff
	s_cbranch_scc0 .LBB0_1426
	s_cmpk_gt_u32 s3, 0xcff
	s_cbranch_scc0 .LBB0_1423
	s_cmpk_gt_u32 s3, 0x1aff
	s_cbranch_scc0 .LBB0_1420
	s_cmpk_gt_u32 s3, 0x21ff
	s_cbranch_scc0 .LBB0_1417
	s_cmpk_gt_u32 s3, 0x91ff
	s_cbranch_scc0 .LBB0_1414
	s_add_i32 s0, s3, 0x6e00
	s_bfe_u32 s4, s0, 0x80008
	s_mulk_i32 s4, 0x2493
	s_lshr_b32 s4, s4, 16
	s_mul_i32 s5, s4, 0x700
	s_sub_i32 s6, s0, s5
	s_mul_i32 s0, s4, 0xe00000
	s_add_u32 s7, s74, s0
	s_addc_u32 s61, s75, 0
	s_mul_i32 s4, s4, 0x380000
	s_add_u32 s4, s66, s4
	s_addc_u32 s5, s88, 0
	s_lshl_b32 s0, s6, 5
	s_and_b32 s0, s0, 0x3e0
	s_lshl_b32 s6, s6, 1
	s_and_b32 s6, s6, 0xfc0
	s_lshl_b32 s62, s0, 2
	v_add_u32_e32 v46, s6, v28
	s_add_u32 s62, s7, s62
	s_addc_u32 s63, s61, 0
	v_ashrrev_i32_e32 v47, 31, v46
	v_lshl_add_u64 v[48:49], s[62:63], 0, v[0:1]
	v_lshlrev_b64 v[46:47], 12, v[46:47]
	v_lshl_add_u64 v[46:47], v[48:49], 0, v[46:47]
	v_add_co_u32_e32 v48, vcc, s10, v46
	s_add_u32 s4, s4, s6
	s_nop 0
	v_addc_co_u32_e32 v49, vcc, 0, v47, vcc
	v_add_co_u32_e32 v50, vcc, s11, v46
	s_addc_u32 s5, s5, 0
	s_nop 0
	v_addc_co_u32_e32 v51, vcc, 0, v47, vcc
	v_add_co_u32_e32 v52, vcc, s12, v46
	s_nop 1
	v_addc_co_u32_e32 v53, vcc, 0, v47, vcc
	v_add_co_u32_e32 v54, vcc, s13, v46
	s_nop 1
	v_addc_co_u32_e32 v55, vcc, 0, v47, vcc
	v_add_co_u32_e32 v56, vcc, s14, v46
	s_nop 1
	v_addc_co_u32_e32 v57, vcc, 0, v47, vcc
	v_add_co_u32_e32 v58, vcc, s15, v46
	s_nop 1
	v_addc_co_u32_e32 v59, vcc, 0, v47, vcc
	v_add_co_u32_e32 v60, vcc, s16, v46
	s_nop 1
	v_addc_co_u32_e32 v61, vcc, 0, v47, vcc
	global_load_dword v64, v[46:47], off nt
	global_load_dword v65, v[48:49], off nt
	global_load_dword v66, v[50:51], off nt
	global_load_dword v67, v[52:53], off nt
	global_load_dword v68, v[54:55], off nt
	global_load_dword v69, v[56:57], off nt
	global_load_dword v70, v[58:59], off nt
	global_load_dword v71, v[60:61], off nt
	v_add_co_u32_e32 v48, vcc, s17, v46
	s_nop 1
	v_addc_co_u32_e32 v49, vcc, 0, v47, vcc
	v_add_co_u32_e32 v50, vcc, s26, v46
	s_nop 1
	v_addc_co_u32_e32 v51, vcc, 0, v47, vcc
	v_add_co_u32_e32 v52, vcc, s27, v46
	s_nop 1
	v_addc_co_u32_e32 v53, vcc, 0, v47, vcc
	v_add_co_u32_e32 v54, vcc, s30, v46
	s_nop 1
	v_addc_co_u32_e32 v55, vcc, 0, v47, vcc
	v_add_co_u32_e32 v56, vcc, s31, v46
	s_nop 1
	v_addc_co_u32_e32 v57, vcc, 0, v47, vcc
	v_add_co_u32_e32 v58, vcc, s36, v46
	s_nop 1
	v_addc_co_u32_e32 v59, vcc, 0, v47, vcc
	v_add_co_u32_e32 v60, vcc, s37, v46
	s_nop 1
	v_addc_co_u32_e32 v61, vcc, 0, v47, vcc
	v_add_co_u32_e32 v62, vcc, s38, v46
	s_nop 1
	v_addc_co_u32_e32 v63, vcc, 0, v47, vcc
	global_load_dword v72, v[48:49], off nt
	global_load_dword v73, v[50:51], off nt
	global_load_dword v74, v[52:53], off nt
	global_load_dword v75, v[54:55], off nt
	global_load_dword v76, v[56:57], off nt
	global_load_dword v77, v[58:59], off nt
	global_load_dword v78, v[60:61], off nt
	global_load_dword v79, v[62:63], off nt
	v_add_co_u32_e32 v48, vcc, s39, v46
	s_nop 1
	v_addc_co_u32_e32 v49, vcc, 0, v47, vcc
	v_add_co_u32_e32 v50, vcc, s40, v46
	s_nop 1
	v_addc_co_u32_e32 v51, vcc, 0, v47, vcc
	v_add_co_u32_e32 v52, vcc, s41, v46
	s_nop 1
	v_addc_co_u32_e32 v53, vcc, 0, v47, vcc
	v_add_co_u32_e32 v54, vcc, s42, v46
	s_nop 1
	v_addc_co_u32_e32 v55, vcc, 0, v47, vcc
	v_add_co_u32_e32 v56, vcc, s43, v46
	s_nop 1
	v_addc_co_u32_e32 v57, vcc, 0, v47, vcc
	v_add_co_u32_e32 v58, vcc, s44, v46
	s_nop 1
	v_addc_co_u32_e32 v59, vcc, 0, v47, vcc
	v_add_co_u32_e32 v60, vcc, s45, v46
	s_nop 1
	v_addc_co_u32_e32 v61, vcc, 0, v47, vcc
	v_add_co_u32_e32 v62, vcc, s46, v46
	s_nop 1
	v_addc_co_u32_e32 v63, vcc, 0, v47, vcc
	global_load_dword v80, v[48:49], off nt
	global_load_dword v81, v[50:51], off nt
	global_load_dword v82, v[52:53], off nt
	global_load_dword v83, v[54:55], off nt
	global_load_dword v84, v[56:57], off nt
	global_load_dword v85, v[58:59], off nt
	s_nop 0
	global_load_dword v60, v[60:61], off nt
	s_nop 0
	global_load_dword v61, v[62:63], off nt
	v_add_co_u32_e32 v48, vcc, s47, v46
	s_nop 1
	v_addc_co_u32_e32 v49, vcc, 0, v47, vcc
	v_add_co_u32_e32 v50, vcc, s48, v46
	s_nop 1
	v_addc_co_u32_e32 v51, vcc, 0, v47, vcc
	v_add_co_u32_e32 v52, vcc, s49, v46
	s_nop 1
	v_addc_co_u32_e32 v53, vcc, 0, v47, vcc
	v_add_co_u32_e32 v54, vcc, s50, v46
	s_nop 1
	v_addc_co_u32_e32 v55, vcc, 0, v47, vcc
	v_add_co_u32_e32 v56, vcc, s51, v46
	s_nop 1
	v_addc_co_u32_e32 v57, vcc, 0, v47, vcc
	v_add_co_u32_e32 v58, vcc, s52, v46
	s_nop 1
	v_addc_co_u32_e32 v59, vcc, 0, v47, vcc
	global_load_dword v62, v[48:49], off nt
	s_nop 0
	global_load_dword v50, v[50:51], off nt
	s_nop 0
	global_load_dword v51, v[52:53], off nt
	s_nop 0
	global_load_dword v52, v[54:55], off nt
	global_load_dword v53, v[56:57], off nt
	s_nop 0
	global_load_dword v54, v[58:59], off nt
	v_add_co_u32_e32 v48, vcc, s53, v46
	s_nop 1
	v_addc_co_u32_e32 v49, vcc, 0, v47, vcc
	v_add_co_u32_e32 v46, vcc, s54, v46
	s_nop 1
	v_addc_co_u32_e32 v47, vcc, 0, v47, vcc
	global_load_dword v48, v[48:49], off nt
	s_nop 0
	global_load_dword v46, v[46:47], off nt
	s_waitcnt vmcnt(31)
	v_mul_f32_e32 v47, 0x43000000, v64
	s_waitcnt vmcnt(30)
	v_mul_f32_e32 v49, 0x43000000, v65
	ds_write2_b32 v29, v47, v49 offset1:66
	s_waitcnt vmcnt(29)
	v_mul_f32_e32 v47, 0x43000000, v66
	s_waitcnt vmcnt(28)
	v_mul_f32_e32 v49, 0x43000000, v67
	ds_write2_b32 v29, v47, v49 offset0:132 offset1:198
	s_waitcnt vmcnt(27)
	v_mul_f32_e32 v47, 0x43000000, v68
	s_waitcnt vmcnt(26)
	v_mul_f32_e32 v49, 0x43000000, v69
	ds_write2_b32 v38, v47, v49 offset0:8 offset1:74
	s_waitcnt vmcnt(25)
; __device__ __forceinline__ unsigned cvt_pk4_fp8(float a, float b, float c, float d) { int w = 0; w = __builtin_amdgcn_cvt_pk_fp8_f32(a, b, w, false); w = __builtin_amdgcn_cvt_pk_fp8_f32(c, d, w, true); return (unsigned)w; }
; #define GAS __attribute__((address_space(1)))
; #define LAS __attribute__((address_space(3)))
; #define LDS_WAIT() asm volatile("s_waitcnt lgkmcnt(0)" ::: "memory")
; __device__ __forceinline__ void tr_item8(const float* W, int ld, int K, int nblk, int item, unsigned char* WT, bool gu, float scale, LAS float* scr, int lane) {
;     ...
;       for (int i = 0; i < 32; ++i) scr[(2 * i + (lane >> 5)) * 33 + (lane & 31)] = t_[i] * scale; }
;     LDS_WAIT(); asm volatile("" ::: "memory");
;     const int c = lane & 3;
; #pragma unroll
;     for (int j = 0; j < 2; ++j) { const int n = (lane >> 2) + 16 * j; const LAS float* sp = scr + (16 * c) * 33 + n;
;         v4u o; o.x = pg8::cvt_pk4_fp8(sp[0 * 33], sp[1 * 33], sp[2 * 33], sp[3 * 33]); o.y = pg8::cvt_pk4_fp8(sp[4 * 33], sp[5 * 33], sp[6 * 33], sp[7 * 33]);
;         o.z = pg8::cvt_pk4_fp8(sp[8 * 33], sp[9 * 33], sp[10 * 33], sp[11 * 33]); o.w = pg8::cvt_pk4_fp8(sp[12 * 33], sp[13 * 33], sp[14 * 33], sp[15 * 33]);
;         *(GAS v4u*)(WT + (size_t)(drow0 + n) * K + k0 + 16 * c) = o; }
;     LDS_WAIT(); asm volatile("" ::: "memory");
	v_mul_f32_e32 v47, 0x43000000, v70
	s_waitcnt vmcnt(24)
	v_mul_f32_e32 v49, 0x43000000, v71
	ds_write2_b32 v38, v47, v49 offset0:140 offset1:206
	s_waitcnt vmcnt(23)
	v_mul_f32_e32 v47, 0x43000000, v72
	s_waitcnt vmcnt(22)
	v_mul_f32_e32 v49, 0x43000000, v73
	ds_write2_b32 v39, v47, v49 offset0:16 offset1:82
	s_waitcnt vmcnt(21)
	v_mul_f32_e32 v47, 0x43000000, v74
	s_waitcnt vmcnt(20)
	v_mul_f32_e32 v49, 0x43000000, v75
	ds_write2_b32 v39, v47, v49 offset0:148 offset1:214
	s_waitcnt vmcnt(19)
	v_mul_f32_e32 v47, 0x43000000, v76
	s_waitcnt vmcnt(18)
	v_mul_f32_e32 v49, 0x43000000, v77
	ds_write2_b32 v40, v47, v49 offset0:24 offset1:90
	s_waitcnt vmcnt(17)
	v_mul_f32_e32 v47, 0x43000000, v78
	s_waitcnt vmcnt(16)
	v_mul_f32_e32 v49, 0x43000000, v79
	ds_write2_b32 v40, v47, v49 offset0:156 offset1:222
	s_waitcnt vmcnt(15)
	v_mul_f32_e32 v47, 0x43000000, v80
	s_waitcnt vmcnt(14)
	v_mul_f32_e32 v49, 0x43000000, v81
	ds_write2_b32 v41, v47, v49 offset0:32 offset1:98
	s_waitcnt vmcnt(13)
	v_mul_f32_e32 v47, 0x43000000, v82
	s_waitcnt vmcnt(12)
	v_mul_f32_e32 v49, 0x43000000, v83
	ds_write2_b32 v41, v47, v49 offset0:164 offset1:230
	s_waitcnt vmcnt(11)
	v_mul_f32_e32 v47, 0x43000000, v84
	s_waitcnt vmcnt(10)
	v_mul_f32_e32 v49, 0x43000000, v85
	ds_write2_b32 v42, v47, v49 offset0:40 offset1:106
	s_waitcnt vmcnt(9)
	v_mul_f32_e32 v47, 0x43000000, v60
	s_waitcnt vmcnt(8)
	v_mul_f32_e32 v49, 0x43000000, v61
	ds_write2_b32 v42, v47, v49 offset0:172 offset1:238
	s_waitcnt vmcnt(7)
	v_mul_f32_e32 v47, 0x43000000, v62
	s_waitcnt vmcnt(6)
	v_mul_f32_e32 v49, 0x43000000, v50
	ds_write2_b32 v43, v47, v49 offset0:48 offset1:114
	s_waitcnt vmcnt(5)
	v_mul_f32_e32 v47, 0x43000000, v51
	s_waitcnt vmcnt(4)
	v_mul_f32_e32 v49, 0x43000000, v52
	ds_write2_b32 v43, v47, v49 offset0:180 offset1:246
	s_waitcnt vmcnt(3)
	v_mul_f32_e32 v47, 0x43000000, v53
	s_waitcnt vmcnt(2)
	v_mul_f32_e32 v49, 0x43000000, v54
	ds_write2_b32 v44, v47, v49 offset0:56 offset1:122
	v_mov_b32_e32 v49, v1
	v_lshl_add_u64 v[50:51], s[4:5], 0, v[2:3]
	s_waitcnt vmcnt(1)
	v_mul_f32_e32 v47, 0x43000000, v48
	s_waitcnt vmcnt(0)
	v_mul_f32_e32 v46, 0x43000000, v46
	ds_write2_b32 v44, v47, v46 offset0:188 offset1:254
	s_waitcnt lgkmcnt(0)
	ds_read2_b32 v[52:53], v31 offset1:16
	ds_read2_b32 v[54:55], v31 offset0:33 offset1:49
	ds_read2_b32 v[56:57], v31 offset0:66 offset1:82
	ds_read2_b32 v[58:59], v31 offset0:99 offset1:115
	ds_read2_b32 v[60:61], v31 offset0:132 offset1:148
	ds_read2_b32 v[62:63], v31 offset0:165 offset1:181
	ds_read2_b32 v[64:65], v31 offset0:198 offset1:214
	ds_read2_b32 v[66:67], v31 offset0:231 offset1:247
	ds_read2_b32 v[68:69], v45 offset0:8 offset1:24
	ds_read2_b32 v[70:71], v45 offset0:41 offset1:57
	ds_read2_b32 v[72:73], v45 offset0:74 offset1:90
	ds_read2_b32 v[74:75], v45 offset0:107 offset1:123
	ds_read2_b32 v[76:77], v45 offset0:140 offset1:156
	ds_read2_b32 v[78:79], v45 offset0:173 offset1:189
	v_mov_b32_e32 v46, v1
	v_mov_b32_e32 v47, v1
	v_mov_b32_e32 v48, v1
	ds_read2_b32 v[80:81], v45 offset0:206 offset1:222
	ds_read2_b32 v[82:83], v45 offset0:239 offset1:255
	s_waitcnt lgkmcnt(14)
	v_cvt_pk_fp8_f32 v46, v52, v54
	s_waitcnt lgkmcnt(10)
	v_cvt_pk_fp8_f32 v47, v60, v62
	s_waitcnt lgkmcnt(6)
	v_cvt_pk_fp8_f32 v48, v68, v70
	s_waitcnt lgkmcnt(2)
	v_cvt_pk_fp8_f32 v49, v76, v78
	v_cvt_pk_fp8_f32 v46, v56, v58 op_sel:[0,0,1]
	v_cvt_pk_fp8_f32 v47, v64, v66 op_sel:[0,0,1]
	v_cvt_pk_fp8_f32 v48, v72, v74 op_sel:[0,0,1]
	s_waitcnt lgkmcnt(0)
	v_cvt_pk_fp8_f32 v49, v80, v82 op_sel:[0,0,1]
	v_add_u32_e32 v52, s0, v30
	v_mad_i64_i32 v[84:85], s[4:5], v52, s55, v[50:51]
	global_store_dwordx4 v[84:85], v[46:49], off sc1 nt
	v_add_u32_e32 v52, s0, v32
	v_mad_i64_i32 v[50:51], s[4:5], v52, s55, v[50:51]
	v_mov_b32_e32 v46, v1
	v_mov_b32_e32 v47, v1
	v_mov_b32_e32 v48, v1
	v_mov_b32_e32 v49, v1
	v_cvt_pk_fp8_f32 v46, v53, v55
	v_cvt_pk_fp8_f32 v47, v61, v63
	v_cvt_pk_fp8_f32 v48, v69, v71
	v_cvt_pk_fp8_f32 v49, v77, v79
	v_cvt_pk_fp8_f32 v46, v57, v59 op_sel:[0,0,1]
	v_cvt_pk_fp8_f32 v47, v65, v67 op_sel:[0,0,1]
	v_cvt_pk_fp8_f32 v48, v73, v75 op_sel:[0,0,1]
	v_cvt_pk_fp8_f32 v49, v81, v83 op_sel:[0,0,1]
	s_mov_b64 s[4:5], 0
	global_store_dwordx4 v[50:51], v[46:49], off sc1 nt
	s_waitcnt lgkmcnt(0)
; __device__ __forceinline__ void tr_item8(const float* W, int ld, int K, int nblk, int item, unsigned char* WT, bool gu, float scale, LAS float* scr, int lane) {
;     const int kb = item / nblk, nb = item % nblk, k0 = 64 * kb, n0 = 32 * nb;
;     int drow0 = n0;
;     if (gu) { const int bj = n0 / FF, j = n0 - bj * FF; drow0 = 256 * (j / 128) + 128 * bj + (j % 128); }
;     { float t_[32];
; #pragma unroll
;       for (int i = 0; i < 32; ++i) t_[i] = W[(size_t)(k0 + 2 * i + (lane >> 5)) * ld + n0 + (lane & 31)];
; __device__ __forceinline__ void convert_items(Frame& F, const Args& a, int lo, int hi, int w, int nw) {
;     ...
;         if (r < NE * I_GU) { const int e = r / I_GU, rr = r % I_GU; tr_item8(a.in[18] + (size_t)e * D * 2 * FF, 2 * FF, D, 224, rr, F.ws + WS_WMGU + (size_t)e * 2 * FF * D, true, WSC_GU, scr, lane); continue; } r -= NE * I_GU;
.LBB0_1414:
	s_andn2_b64 vcc, exec, s[4:5]
	s_cbranch_vccnz .LBB0_1416
	s_add_i32 s0, s3, 0xde00
	s_bfe_u32 s4, s0, 0x70009
	s_mulk_i32 s4, 0x2493
	s_lshr_b32 s4, s4, 16
	s_mul_i32 s5, s4, 0xe00
	s_sub_i32 s0, s0, s5
	s_mul_i32 s5, s4, 0x1c00000
	s_add_u32 s6, s72, s5
	s_addc_u32 s7, s73, 0
	s_mul_i32 s4, s4, 0x700000
	s_add_u32 s4, s89, s4
	s_addc_u32 s5, s90, 0
	s_bfe_u32 s61, s0, 0xb0005
	s_mulk_i32 s61, 0x2493
	s_lshr_b32 s61, s61, 16
	s_mul_i32 s62, s61, 0xe0
	s_sub_i32 s62, s0, s62
	s_lshl_b32 s0, s62, 5
	s_and_b32 s63, s62, 0xffff
	s_cmpk_gt_u32 s63, 0x6f
	s_cselect_b32 s63, 0xfffff200, 0
	s_cselect_b32 s64, 0x80, 0
	s_add_i32 s0, s63, s0
	s_sext_i32_i16 s63, s0
	s_bfe_u32 s63, s63, 0x70018
	s_add_i32 s63, s0, s63
	s_sext_i32_i16 s65, s63
	s_and_b32 s63, s63, 0xff80
	s_sub_i32 s0, s0, s63
	s_lshl_b32 s65, s65, 1
	s_sext_i32_i16 s0, s0
	s_and_b32 s65, s65, 0xffffff00
	s_add_i32 s0, s64, s0
	s_lshl_b32 s62, s62, 7
	s_add_i32 s0, s0, s65
	s_lshl_b32 s61, s61, 6
	s_and_b32 s62, s62, 0x3ff80
	s_add_u32 s6, s6, s62
	s_addc_u32 s7, s7, 0
	v_add_u32_e32 v64, s61, v28
	v_lshl_add_u64 v[46:47], s[6:7], 0, v[0:1]
	v_mad_i64_i32 v[48:49], s[6:7], v64, s56, v[46:47]
	v_add_u32_e32 v50, 2, v64
	v_add_u32_e32 v52, 4, v64
	v_add_u32_e32 v54, 6, v64
	v_add_u32_e32 v56, 8, v64
	v_add_u32_e32 v58, 10, v64
	v_add_u32_e32 v60, 12, v64
	v_add_u32_e32 v62, 14, v64
	v_mad_i64_i32 v[50:51], s[6:7], v50, s56, v[46:47]
	v_mad_i64_i32 v[52:53], s[6:7], v52, s56, v[46:47]
	v_mad_i64_i32 v[54:55], s[6:7], v54, s56, v[46:47]
	v_mad_i64_i32 v[56:57], s[6:7], v56, s56, v[46:47]
	v_mad_i64_i32 v[58:59], s[6:7], v58, s56, v[46:47]
	v_mad_i64_i32 v[60:61], s[6:7], v60, s56, v[46:47]
	v_mad_i64_i32 v[62:63], s[6:7], v62, s56, v[46:47]
	global_load_dword v65, v[48:49], off nt
	global_load_dword v66, v[50:51], off nt
	global_load_dword v67, v[52:53], off nt
	global_load_dword v68, v[54:55], off nt
	global_load_dword v69, v[56:57], off nt
	global_load_dword v70, v[58:59], off nt
	global_load_dword v71, v[60:61], off nt
	global_load_dword v72, v[62:63], off nt
	v_add_u32_e32 v48, 16, v64
	v_mad_i64_i32 v[48:49], s[6:7], v48, s56, v[46:47]
	v_add_u32_e32 v50, 18, v64
	v_add_u32_e32 v52, 20, v64
	v_add_u32_e32 v54, 22, v64
	v_add_u32_e32 v56, 24, v64
	v_add_u32_e32 v58, 26, v64
	v_add_u32_e32 v60, 28, v64
	v_add_u32_e32 v62, 30, v64
	v_mad_i64_i32 v[50:51], s[6:7], v50, s56, v[46:47]
	v_mad_i64_i32 v[52:53], s[6:7], v52, s56, v[46:47]
	v_mad_i64_i32 v[54:55], s[6:7], v54, s56, v[46:47]
	v_mad_i64_i32 v[56:57], s[6:7], v56, s56, v[46:47]
	v_mad_i64_i32 v[58:59], s[6:7], v58, s56, v[46:47]
	v_mad_i64_i32 v[60:61], s[6:7], v60, s56, v[46:47]
	v_mad_i64_i32 v[62:63], s[6:7], v62, s56, v[46:47]
	global_load_dword v73, v[48:49], off nt
	global_load_dword v74, v[50:51], off nt
	global_load_dword v75, v[52:53], off nt
	global_load_dword v76, v[54:55], off nt
	global_load_dword v77, v[56:57], off nt
	global_load_dword v78, v[58:59], off nt
	global_load_dword v79, v[60:61], off nt
	global_load_dword v80, v[62:63], off nt
	v_add_u32_e32 v48, 32, v64
	v_add_u32_e32 v50, 34, v64
	v_add_u32_e32 v52, 36, v64
	v_add_u32_e32 v54, 38, v64
	v_add_u32_e32 v60, 44, v64
	v_mad_i64_i32 v[48:49], s[6:7], v48, s56, v[46:47]
	v_mad_i64_i32 v[50:51], s[6:7], v50, s56, v[46:47]
	v_mad_i64_i32 v[52:53], s[6:7], v52, s56, v[46:47]
	v_mad_i64_i32 v[54:55], s[6:7], v54, s56, v[46:47]
	v_add_u32_e32 v56, 40, v64
	v_add_u32_e32 v58, 42, v64
	v_mad_i64_i32 v[60:61], s[6:7], v60, s56, v[46:47]
	v_add_u32_e32 v62, 46, v64
	v_mad_i64_i32 v[56:57], s[6:7], v56, s56, v[46:47]
	v_mad_i64_i32 v[58:59], s[6:7], v58, s56, v[46:47]
	v_mad_i64_i32 v[62:63], s[6:7], v62, s56, v[46:47]
	global_load_dword v81, v[48:49], off nt
	global_load_dword v82, v[50:51], off nt
	global_load_dword v83, v[52:53], off nt
	global_load_dword v84, v[54:55], off nt
	global_load_dword v85, v[56:57], off nt
	global_load_dword v86, v[58:59], off nt
	s_nop 0
	global_load_dword v60, v[60:61], off nt
	s_nop 0
	global_load_dword v61, v[62:63], off nt
	v_add_u32_e32 v48, 48, v64
	v_add_u32_e32 v50, 50, v64
	v_add_u32_e32 v52, 52, v64
	v_add_u32_e32 v54, 54, v64
	v_mad_i64_i32 v[48:49], s[6:7], v48, s56, v[46:47]
	v_mad_i64_i32 v[50:51], s[6:7], v50, s56, v[46:47]
	v_mad_i64_i32 v[52:53], s[6:7], v52, s56, v[46:47]
	v_mad_i64_i32 v[54:55], s[6:7], v54, s56, v[46:47]
	v_add_u32_e32 v56, 56, v64
	v_add_u32_e32 v58, 58, v64
	v_mad_i64_i32 v[56:57], s[6:7], v56, s56, v[46:47]
	v_mad_i64_i32 v[58:59], s[6:7], v58, s56, v[46:47]
	global_load_dword v62, v[48:49], off nt
	s_nop 0
	global_load_dword v50, v[50:51], off nt
	s_nop 0
	global_load_dword v51, v[52:53], off nt
	s_nop 0
	global_load_dword v52, v[54:55], off nt
	global_load_dword v53, v[56:57], off nt
	s_nop 0
	global_load_dword v54, v[58:59], off nt
	v_add_u32_e32 v48, 60, v64
	v_add_u32_e32 v55, 62, v64
	v_mad_i64_i32 v[48:49], s[6:7], v48, s56, v[46:47]
	v_mad_i64_i32 v[46:47], s[6:7], v55, s56, v[46:47]
	global_load_dword v48, v[48:49], off nt
	s_nop 0
	global_load_dword v46, v[46:47], off nt
	s_waitcnt vmcnt(31)
; __device__ __forceinline__ unsigned cvt_pk4_fp8(float a, float b, float c, float d) { int w = 0; w = __builtin_amdgcn_cvt_pk_fp8_f32(a, b, w, false); w = __builtin_amdgcn_cvt_pk_fp8_f32(c, d, w, true); return (unsigned)w; }
; #define GAS __attribute__((address_space(1)))
; #define LAS __attribute__((address_space(3)))
; #define LDS_WAIT() asm volatile("s_waitcnt lgkmcnt(0)" ::: "memory")
; __device__ __forceinline__ void tr_item8(const float* W, int ld, int K, int nblk, int item, unsigned char* WT, bool gu, float scale, LAS float* scr, int lane) {
;     ...
;       for (int i = 0; i < 32; ++i) scr[(2 * i + (lane >> 5)) * 33 + (lane & 31)] = t_[i] * scale; }
;     LDS_WAIT(); asm volatile("" ::: "memory");
;     const int c = lane & 3;
; #pragma unroll
;     for (int j = 0; j < 2; ++j) { const int n = (lane >> 2) + 16 * j; const LAS float* sp = scr + (16 * c) * 33 + n;
;         v4u o; o.x = pg8::cvt_pk4_fp8(sp[0 * 33], sp[1 * 33], sp[2 * 33], sp[3 * 33]); o.y = pg8::cvt_pk4_fp8(sp[4 * 33], sp[5 * 33], sp[6 * 33], sp[7 * 33]);
;         o.z = pg8::cvt_pk4_fp8(sp[8 * 33], sp[9 * 33], sp[10 * 33], sp[11 * 33]); o.w = pg8::cvt_pk4_fp8(sp[12 * 33], sp[13 * 33], sp[14 * 33], sp[15 * 33]);
;         *(GAS v4u*)(WT + (size_t)(drow0 + n) * K + k0 + 16 * c) = o; }
;     LDS_WAIT(); asm volatile("" ::: "memory");
	v_mul_f32_e32 v47, 0x42800000, v65
	s_waitcnt vmcnt(30)
	v_mul_f32_e32 v49, 0x42800000, v66
	ds_write2_b32 v29, v47, v49 offset1:66
	s_waitcnt vmcnt(29)
	v_mul_f32_e32 v47, 0x42800000, v67
	s_waitcnt vmcnt(28)
	v_mul_f32_e32 v49, 0x42800000, v68
	ds_write2_b32 v29, v47, v49 offset0:132 offset1:198
	s_waitcnt vmcnt(27)
	v_mul_f32_e32 v47, 0x42800000, v69
	s_waitcnt vmcnt(26)
	v_mul_f32_e32 v49, 0x42800000, v70
	ds_write2_b32 v38, v47, v49 offset0:8 offset1:74
	s_waitcnt vmcnt(25)
	v_mul_f32_e32 v47, 0x42800000, v71
	s_waitcnt vmcnt(24)
	v_mul_f32_e32 v49, 0x42800000, v72
	ds_write2_b32 v38, v47, v49 offset0:140 offset1:206
	s_add_u32 s4, s4, s61
	s_addc_u32 s5, s5, 0
	s_waitcnt vmcnt(23)
	v_mul_f32_e32 v47, 0x42800000, v73
	s_waitcnt vmcnt(22)
	v_mul_f32_e32 v49, 0x42800000, v74
	ds_write2_b32 v39, v47, v49 offset0:16 offset1:82
	s_waitcnt vmcnt(21)
	v_mul_f32_e32 v47, 0x42800000, v75
	s_waitcnt vmcnt(20)
	v_mul_f32_e32 v49, 0x42800000, v76
	ds_write2_b32 v39, v47, v49 offset0:148 offset1:214
	s_waitcnt vmcnt(19)
	v_mul_f32_e32 v47, 0x42800000, v77
	s_waitcnt vmcnt(18)
	v_mul_f32_e32 v49, 0x42800000, v78
	ds_write2_b32 v40, v47, v49 offset0:24 offset1:90
	s_waitcnt vmcnt(17)
	v_mul_f32_e32 v47, 0x42800000, v79
	s_waitcnt vmcnt(16)
	v_mul_f32_e32 v49, 0x42800000, v80
	ds_write2_b32 v40, v47, v49 offset0:156 offset1:222
	s_waitcnt vmcnt(15)
	v_mul_f32_e32 v47, 0x42800000, v81
	s_waitcnt vmcnt(14)
	v_mul_f32_e32 v49, 0x42800000, v82
	ds_write2_b32 v41, v47, v49 offset0:32 offset1:98
	s_waitcnt vmcnt(13)
	v_mul_f32_e32 v47, 0x42800000, v83
	s_waitcnt vmcnt(12)
	v_mul_f32_e32 v49, 0x42800000, v84
	ds_write2_b32 v41, v47, v49 offset0:164 offset1:230
	s_waitcnt vmcnt(11)
	v_mul_f32_e32 v47, 0x42800000, v85
	s_waitcnt vmcnt(10)
	v_mul_f32_e32 v49, 0x42800000, v86
	ds_write2_b32 v42, v47, v49 offset0:40 offset1:106
	s_waitcnt vmcnt(9)
	v_mul_f32_e32 v47, 0x42800000, v60
	s_waitcnt vmcnt(8)
	v_mul_f32_e32 v49, 0x42800000, v61
	ds_write2_b32 v42, v47, v49 offset0:172 offset1:238
	v_add_u32_e32 v84, s0, v30
	v_ashrrev_i32_e32 v85, 31, v84
	v_lshlrev_b64 v[84:85], 10, v[84:85]
	s_waitcnt vmcnt(7)
	v_mul_f32_e32 v47, 0x42800000, v62
	s_waitcnt vmcnt(6)
	v_mul_f32_e32 v49, 0x42800000, v50
	ds_write2_b32 v43, v47, v49 offset0:48 offset1:114
	s_waitcnt vmcnt(5)
	v_mul_f32_e32 v47, 0x42800000, v51
	s_waitcnt vmcnt(4)
	v_mul_f32_e32 v49, 0x42800000, v52
	ds_write2_b32 v43, v47, v49 offset0:180 offset1:246
	s_waitcnt vmcnt(3)
	v_mul_f32_e32 v47, 0x42800000, v53
	s_waitcnt vmcnt(2)
	v_mul_f32_e32 v49, 0x42800000, v54
	ds_write2_b32 v44, v47, v49 offset0:56 offset1:122
	v_mov_b32_e32 v49, v1
	v_lshl_add_u64 v[50:51], s[4:5], 0, v[2:3]
	s_waitcnt vmcnt(1)
	v_mul_f32_e32 v47, 0x42800000, v48
	s_waitcnt vmcnt(0)
	v_mul_f32_e32 v46, 0x42800000, v46
	ds_write2_b32 v44, v47, v46 offset0:188 offset1:254
	s_waitcnt lgkmcnt(0)
	ds_read2_b32 v[52:53], v31 offset1:16
	ds_read2_b32 v[54:55], v31 offset0:33 offset1:49
	ds_read2_b32 v[56:57], v31 offset0:66 offset1:82
	ds_read2_b32 v[58:59], v31 offset0:99 offset1:115
	ds_read2_b32 v[60:61], v31 offset0:132 offset1:148
	ds_read2_b32 v[62:63], v31 offset0:165 offset1:181
	ds_read2_b32 v[64:65], v31 offset0:198 offset1:214
	ds_read2_b32 v[66:67], v31 offset0:231 offset1:247
	ds_read2_b32 v[68:69], v45 offset0:8 offset1:24
	ds_read2_b32 v[70:71], v45 offset0:41 offset1:57
	ds_read2_b32 v[72:73], v45 offset0:74 offset1:90
	ds_read2_b32 v[74:75], v45 offset0:107 offset1:123
	ds_read2_b32 v[76:77], v45 offset0:140 offset1:156
	ds_read2_b32 v[78:79], v45 offset0:173 offset1:189
	v_mov_b32_e32 v46, v1
	v_mov_b32_e32 v47, v1
	v_mov_b32_e32 v48, v1
	ds_read2_b32 v[80:81], v45 offset0:206 offset1:222
	ds_read2_b32 v[82:83], v45 offset0:239 offset1:255
	s_waitcnt lgkmcnt(14)
	v_cvt_pk_fp8_f32 v46, v52, v54
	s_waitcnt lgkmcnt(10)
	v_cvt_pk_fp8_f32 v47, v60, v62
	s_waitcnt lgkmcnt(6)
	v_cvt_pk_fp8_f32 v48, v68, v70
	s_waitcnt lgkmcnt(2)
	v_cvt_pk_fp8_f32 v49, v76, v78
	v_cvt_pk_fp8_f32 v46, v56, v58 op_sel:[0,0,1]
	v_cvt_pk_fp8_f32 v47, v64, v66 op_sel:[0,0,1]
	v_cvt_pk_fp8_f32 v48, v72, v74 op_sel:[0,0,1]
	s_waitcnt lgkmcnt(0)
	v_cvt_pk_fp8_f32 v49, v80, v82 op_sel:[0,0,1]
	v_lshl_add_u64 v[84:85], v[50:51], 0, v[84:85]
	v_add_u32_e32 v52, s0, v32
	global_store_dwordx4 v[84:85], v[46:49], off sc1 nt
	s_nop 1
	v_mov_b32_e32 v46, v1
	v_mov_b32_e32 v47, v1
	v_mov_b32_e32 v48, v1
	v_mov_b32_e32 v49, v1
	v_cvt_pk_fp8_f32 v46, v53, v55
	v_cvt_pk_fp8_f32 v47, v61, v63
	v_cvt_pk_fp8_f32 v48, v69, v71
	v_cvt_pk_fp8_f32 v49, v77, v79
	v_cvt_pk_fp8_f32 v46, v57, v59 op_sel:[0,0,1]
	v_cvt_pk_fp8_f32 v47, v65, v67 op_sel:[0,0,1]
	v_cvt_pk_fp8_f32 v48, v73, v75 op_sel:[0,0,1]
	v_cvt_pk_fp8_f32 v49, v81, v83 op_sel:[0,0,1]
	v_ashrrev_i32_e32 v53, 31, v52
	v_lshlrev_b64 v[52:53], 10, v[52:53]
	v_lshl_add_u64 v[50:51], v[50:51], 0, v[52:53]
	global_store_dwordx4 v[50:51], v[46:49], off sc1 nt
	s_waitcnt lgkmcnt(0)

; __device__ __forceinline__ void tr_item8(const float* W, int ld, int K, int nblk, int item, unsigned char* WT, bool gu, float scale, LAS float* scr, int lane) {
;     const int kb = item / nblk, nb = item % nblk, k0 = 64 * kb, n0 = 32 * nb;
;     int drow0 = n0;
;     if (gu) { const int bj = n0 / FF, j = n0 - bj * FF; drow0 = 256 * (j / 128) + 128 * bj + (j % 128); }
;     { float t_[32];
; #pragma unroll
;       for (int i = 0; i < 32; ++i) t_[i] = W[(size_t)(k0 + 2 * i + (lane >> 5)) * ld + n0 + (lane & 31)];
; #pragma unroll
;       for (int i = 0; i < 32; ++i) scr[(2 * i + (lane >> 5)) * 33 + (lane & 31)] = t_[i] * scale; }
; __device__ __forceinline__ void convert_items(Frame& F, const Args& a, int lo, int hi, int w, int nw) {
;     ...
;         if (r < I_DN) { tr_item8(a.in[15], D, FF, 32, r, F.ws + WS_WDN, false, WSC_DN, scr, lane); continue; } r -= I_DN;
.LBB0_1417:
	s_andn2_b64 vcc, exec, s[4:5]
	s_cbranch_vccnz .LBB0_1419
	s_lshl_b32 s0, s3, 5
	s_and_b32 s4, s9, 0x1ffc0
	s_and_b32 s6, s0, 0x3e0
	v_add_u32_e32 v46, s4, v28
	s_lshl_b32 s0, s6, 2
	v_ashrrev_i32_e32 v47, 31, v46
	v_lshl_add_u64 v[48:49], v[4:5], 0, s[0:1]
	v_lshlrev_b64 v[46:47], 12, v[46:47]
	v_lshl_add_u64 v[46:47], v[48:49], 0, v[46:47]
	v_add_co_u32_e32 v48, vcc, 0x2000, v46
	s_mov_b32 s5, s1
	s_nop 0
	v_addc_co_u32_e32 v49, vcc, 0, v47, vcc
	v_add_co_u32_e32 v50, vcc, 0x4000, v46
	s_nop 1
	v_addc_co_u32_e32 v51, vcc, 0, v47, vcc
	v_add_co_u32_e32 v52, vcc, 0x6000, v46
	s_nop 1
	v_addc_co_u32_e32 v53, vcc, 0, v47, vcc
	v_add_co_u32_e32 v54, vcc, 0x8000, v46
	s_nop 1
	v_addc_co_u32_e32 v55, vcc, 0, v47, vcc
	v_add_co_u32_e32 v56, vcc, 0xa000, v46
	s_nop 1
	v_addc_co_u32_e32 v57, vcc, 0, v47, vcc
	v_add_co_u32_e32 v58, vcc, 0xc000, v46
	s_nop 1
	v_addc_co_u32_e32 v59, vcc, 0, v47, vcc
	v_add_co_u32_e32 v60, vcc, 0xe000, v46
	s_nop 1
	v_addc_co_u32_e32 v61, vcc, 0, v47, vcc
	global_load_dword v64, v[46:47], off nt
	global_load_dword v65, v[48:49], off nt
	global_load_dword v66, v[50:51], off nt
	global_load_dword v67, v[52:53], off nt
	global_load_dword v68, v[54:55], off nt
	global_load_dword v69, v[56:57], off nt
	global_load_dword v70, v[58:59], off nt
	global_load_dword v71, v[60:61], off nt
	v_add_co_u32_e32 v48, vcc, 0x10000, v46
	s_nop 1
	v_addc_co_u32_e32 v49, vcc, 0, v47, vcc
	v_add_co_u32_e32 v50, vcc, 0x12000, v46
	s_nop 1
	v_addc_co_u32_e32 v51, vcc, 0, v47, vcc
	v_add_co_u32_e32 v52, vcc, 0x14000, v46
	s_nop 1
	v_addc_co_u32_e32 v53, vcc, 0, v47, vcc
	v_add_co_u32_e32 v54, vcc, 0x16000, v46
	s_nop 1
	v_addc_co_u32_e32 v55, vcc, 0, v47, vcc
	v_add_co_u32_e32 v56, vcc, 0x18000, v46
	s_nop 1
	v_addc_co_u32_e32 v57, vcc, 0, v47, vcc
	v_add_co_u32_e32 v58, vcc, 0x1a000, v46
	s_nop 1
	v_addc_co_u32_e32 v59, vcc, 0, v47, vcc
	v_add_co_u32_e32 v60, vcc, 0x1c000, v46
	s_nop 1
	v_addc_co_u32_e32 v61, vcc, 0, v47, vcc
	v_add_co_u32_e32 v62, vcc, 0x1e000, v46
	s_nop 1
	v_addc_co_u32_e32 v63, vcc, 0, v47, vcc
	global_load_dword v72, v[48:49], off nt
	global_load_dword v73, v[50:51], off nt
	global_load_dword v74, v[52:53], off nt
	global_load_dword v75, v[54:55], off nt
	global_load_dword v76, v[56:57], off nt
	global_load_dword v77, v[58:59], off nt
	global_load_dword v78, v[60:61], off nt
	global_load_dword v79, v[62:63], off nt
	v_add_co_u32_e32 v48, vcc, 0x20000, v46
	s_nop 1
	v_addc_co_u32_e32 v49, vcc, 0, v47, vcc
	v_add_co_u32_e32 v50, vcc, 0x22000, v46
	s_nop 1
	v_addc_co_u32_e32 v51, vcc, 0, v47, vcc
	v_add_co_u32_e32 v52, vcc, 0x24000, v46
	s_nop 1
	v_addc_co_u32_e32 v53, vcc, 0, v47, vcc
	v_add_co_u32_e32 v54, vcc, 0x26000, v46
	s_nop 1
	v_addc_co_u32_e32 v55, vcc, 0, v47, vcc
	v_add_co_u32_e32 v56, vcc, 0x28000, v46
	s_nop 1
	v_addc_co_u32_e32 v57, vcc, 0, v47, vcc
	v_add_co_u32_e32 v58, vcc, 0x2a000, v46
	s_nop 1
	v_addc_co_u32_e32 v59, vcc, 0, v47, vcc
	v_add_co_u32_e32 v60, vcc, 0x2c000, v46
	s_nop 1
	v_addc_co_u32_e32 v61, vcc, 0, v47, vcc
	v_add_co_u32_e32 v62, vcc, 0x2e000, v46
	s_nop 1
	v_addc_co_u32_e32 v63, vcc, 0, v47, vcc
	global_load_dword v80, v[48:49], off nt
	global_load_dword v81, v[50:51], off nt
	global_load_dword v82, v[52:53], off nt
	global_load_dword v83, v[54:55], off nt
	global_load_dword v84, v[56:57], off nt
	global_load_dword v85, v[58:59], off nt
	s_nop 0
	global_load_dword v60, v[60:61], off nt
	s_nop 0
	global_load_dword v61, v[62:63], off nt
	v_add_co_u32_e32 v48, vcc, 0x30000, v46
	s_nop 1
	v_addc_co_u32_e32 v49, vcc, 0, v47, vcc
	v_add_co_u32_e32 v50, vcc, 0x32000, v46
	s_nop 1
	v_addc_co_u32_e32 v51, vcc, 0, v47, vcc
	v_add_co_u32_e32 v52, vcc, 0x34000, v46
	s_nop 1
	v_addc_co_u32_e32 v53, vcc, 0, v47, vcc
	v_add_co_u32_e32 v54, vcc, 0x36000, v46
	s_nop 1
	v_addc_co_u32_e32 v55, vcc, 0, v47, vcc
	v_add_co_u32_e32 v56, vcc, 0x38000, v46
	s_nop 1
	v_addc_co_u32_e32 v57, vcc, 0, v47, vcc
	v_add_co_u32_e32 v58, vcc, 0x3a000, v46
	s_nop 1
	v_addc_co_u32_e32 v59, vcc, 0, v47, vcc
	global_load_dword v62, v[48:49], off nt
	s_nop 0
	global_load_dword v50, v[50:51], off nt
	s_nop 0
	global_load_dword v51, v[52:53], off nt
	s_nop 0
	global_load_dword v52, v[54:55], off nt
	global_load_dword v53, v[56:57], off nt
	s_nop 0
	global_load_dword v54, v[58:59], off nt
	v_add_co_u32_e32 v48, vcc, 0x3c000, v46
	s_nop 1
	v_addc_co_u32_e32 v49, vcc, 0, v47, vcc
	v_add_co_u32_e32 v46, vcc, 0x3e000, v46
	s_nop 1
	v_addc_co_u32_e32 v47, vcc, 0, v47, vcc
	global_load_dword v48, v[48:49], off nt
	s_nop 0
	global_load_dword v46, v[46:47], off nt
	s_waitcnt vmcnt(31)
	v_mul_f32_e32 v47, 0x43000000, v64
	s_waitcnt vmcnt(30)
; __device__ __forceinline__ unsigned cvt_pk4_fp8(float a, float b, float c, float d) { int w = 0; w = __builtin_amdgcn_cvt_pk_fp8_f32(a, b, w, false); w = __builtin_amdgcn_cvt_pk_fp8_f32(c, d, w, true); return (unsigned)w; }
; #define GAS __attribute__((address_space(1)))
; #define LAS __attribute__((address_space(3)))
; #define LDS_WAIT() asm volatile("s_waitcnt lgkmcnt(0)" ::: "memory")
; __device__ __forceinline__ void tr_item8(const float* W, int ld, int K, int nblk, int item, unsigned char* WT, bool gu, float scale, LAS float* scr, int lane) {
;     ...
;       for (int i = 0; i < 32; ++i) scr[(2 * i + (lane >> 5)) * 33 + (lane & 31)] = t_[i] * scale; }
;     LDS_WAIT(); asm volatile("" ::: "memory");
;     const int c = lane & 3;
; #pragma unroll
;     for (int j = 0; j < 2; ++j) { const int n = (lane >> 2) + 16 * j; const LAS float* sp = scr + (16 * c) * 33 + n;
;         v4u o; o.x = pg8::cvt_pk4_fp8(sp[0 * 33], sp[1 * 33], sp[2 * 33], sp[3 * 33]); o.y = pg8::cvt_pk4_fp8(sp[4 * 33], sp[5 * 33], sp[6 * 33], sp[7 * 33]);
;         o.z = pg8::cvt_pk4_fp8(sp[8 * 33], sp[9 * 33], sp[10 * 33], sp[11 * 33]); o.w = pg8::cvt_pk4_fp8(sp[12 * 33], sp[13 * 33], sp[14 * 33], sp[15 * 33]);
;         *(GAS v4u*)(WT + (size_t)(drow0 + n) * K + k0 + 16 * c) = o; }
;     LDS_WAIT(); asm volatile("" ::: "memory");
	v_mul_f32_e32 v49, 0x43000000, v65
	ds_write2_b32 v29, v47, v49 offset1:66
	s_waitcnt vmcnt(29)
	v_mul_f32_e32 v47, 0x43000000, v66
	s_waitcnt vmcnt(28)
	v_mul_f32_e32 v49, 0x43000000, v67
	ds_write2_b32 v29, v47, v49 offset0:132 offset1:198
	s_waitcnt vmcnt(27)
	v_mul_f32_e32 v47, 0x43000000, v68
	s_waitcnt vmcnt(26)
	v_mul_f32_e32 v49, 0x43000000, v69
	ds_write2_b32 v38, v47, v49 offset0:8 offset1:74
	s_waitcnt vmcnt(25)
	v_mul_f32_e32 v47, 0x43000000, v70
	s_waitcnt vmcnt(24)
	v_mul_f32_e32 v49, 0x43000000, v71
	ds_write2_b32 v38, v47, v49 offset0:140 offset1:206
	s_waitcnt vmcnt(23)
	v_mul_f32_e32 v47, 0x43000000, v72
	s_waitcnt vmcnt(22)
	v_mul_f32_e32 v49, 0x43000000, v73
	ds_write2_b32 v39, v47, v49 offset0:16 offset1:82
	s_waitcnt vmcnt(21)
	v_mul_f32_e32 v47, 0x43000000, v74
	s_waitcnt vmcnt(20)
	v_mul_f32_e32 v49, 0x43000000, v75
	ds_write2_b32 v39, v47, v49 offset0:148 offset1:214
	s_waitcnt vmcnt(19)
	v_mul_f32_e32 v47, 0x43000000, v76
	s_waitcnt vmcnt(18)
	v_mul_f32_e32 v49, 0x43000000, v77
	ds_write2_b32 v40, v47, v49 offset0:24 offset1:90
	s_waitcnt vmcnt(17)
	v_mul_f32_e32 v47, 0x43000000, v78
	s_waitcnt vmcnt(16)
	v_mul_f32_e32 v49, 0x43000000, v79
	ds_write2_b32 v40, v47, v49 offset0:156 offset1:222
	s_waitcnt vmcnt(15)
	v_mul_f32_e32 v47, 0x43000000, v80
	s_waitcnt vmcnt(14)
	v_mul_f32_e32 v49, 0x43000000, v81
	ds_write2_b32 v41, v47, v49 offset0:32 offset1:98
	s_waitcnt vmcnt(13)
	v_mul_f32_e32 v47, 0x43000000, v82
	s_waitcnt vmcnt(12)
	v_mul_f32_e32 v49, 0x43000000, v83
	ds_write2_b32 v41, v47, v49 offset0:164 offset1:230
	s_waitcnt vmcnt(11)
	v_mul_f32_e32 v47, 0x43000000, v84
	s_waitcnt vmcnt(10)
	v_mul_f32_e32 v49, 0x43000000, v85
	ds_write2_b32 v42, v47, v49 offset0:40 offset1:106
	s_waitcnt vmcnt(9)
	v_mul_f32_e32 v47, 0x43000000, v60
	s_waitcnt vmcnt(8)
	v_mul_f32_e32 v49, 0x43000000, v61
	ds_write2_b32 v42, v47, v49 offset0:172 offset1:238
	s_waitcnt vmcnt(7)
	v_mul_f32_e32 v47, 0x43000000, v62
	s_waitcnt vmcnt(6)
	v_mul_f32_e32 v49, 0x43000000, v50
	ds_write2_b32 v43, v47, v49 offset0:48 offset1:114
	s_waitcnt vmcnt(5)
	v_mul_f32_e32 v47, 0x43000000, v51
	s_waitcnt vmcnt(4)
	v_mul_f32_e32 v49, 0x43000000, v52
	ds_write2_b32 v43, v47, v49 offset0:180 offset1:246
	s_waitcnt vmcnt(3)
	v_mul_f32_e32 v47, 0x43000000, v53
	s_waitcnt vmcnt(2)
	v_mul_f32_e32 v49, 0x43000000, v54
	ds_write2_b32 v44, v47, v49 offset0:56 offset1:122
	v_mov_b32_e32 v49, 0
	v_lshl_add_u64 v[50:51], v[16:17], 0, s[4:5]
	s_waitcnt vmcnt(1)
	v_mul_f32_e32 v47, 0x43000000, v48
	s_waitcnt vmcnt(0)
	v_mul_f32_e32 v46, 0x43000000, v46
	ds_write2_b32 v44, v47, v46 offset0:188 offset1:254
	s_waitcnt lgkmcnt(0)
	ds_read2_b32 v[52:53], v31 offset1:16
	ds_read2_b32 v[54:55], v31 offset0:33 offset1:49
	ds_read2_b32 v[56:57], v31 offset0:66 offset1:82
	ds_read2_b32 v[58:59], v31 offset0:99 offset1:115
	ds_read2_b32 v[60:61], v31 offset0:132 offset1:148
	ds_read2_b32 v[62:63], v31 offset0:165 offset1:181
	ds_read2_b32 v[64:65], v31 offset0:198 offset1:214
	ds_read2_b32 v[66:67], v31 offset0:231 offset1:247
	ds_read2_b32 v[68:69], v45 offset0:8 offset1:24
	ds_read2_b32 v[70:71], v45 offset0:41 offset1:57
	ds_read2_b32 v[72:73], v45 offset0:74 offset1:90
	ds_read2_b32 v[74:75], v45 offset0:107 offset1:123
	ds_read2_b32 v[76:77], v45 offset0:140 offset1:156
	ds_read2_b32 v[78:79], v45 offset0:173 offset1:189
	v_mov_b32_e32 v46, 0
	v_mov_b32_e32 v47, 0
	v_mov_b32_e32 v48, 0
	ds_read2_b32 v[80:81], v45 offset0:206 offset1:222
	ds_read2_b32 v[82:83], v45 offset0:239 offset1:255
	s_waitcnt lgkmcnt(14)
	v_cvt_pk_fp8_f32 v46, v52, v54
	s_waitcnt lgkmcnt(10)
	v_cvt_pk_fp8_f32 v47, v60, v62
	s_waitcnt lgkmcnt(6)
	v_cvt_pk_fp8_f32 v48, v68, v70
	s_waitcnt lgkmcnt(2)
	v_cvt_pk_fp8_f32 v49, v76, v78
	v_cvt_pk_fp8_f32 v46, v56, v58 op_sel:[0,0,1]
	v_cvt_pk_fp8_f32 v47, v64, v66 op_sel:[0,0,1]
	v_cvt_pk_fp8_f32 v48, v72, v74 op_sel:[0,0,1]
	s_waitcnt lgkmcnt(0)
	v_cvt_pk_fp8_f32 v49, v80, v82 op_sel:[0,0,1]
	v_add_u32_e32 v52, s6, v30
	v_mad_i64_i32 v[84:85], s[4:5], v52, s55, v[50:51]
	global_store_dwordx4 v[84:85], v[46:49], off sc1 nt
	v_add_u32_e32 v52, s6, v32
	v_mad_i64_i32 v[50:51], s[4:5], v52, s55, v[50:51]
	v_mov_b32_e32 v46, 0
	v_mov_b32_e32 v47, 0
	v_mov_b32_e32 v48, 0
	v_mov_b32_e32 v49, 0
	v_cvt_pk_fp8_f32 v46, v53, v55
	v_cvt_pk_fp8_f32 v47, v61, v63
	v_cvt_pk_fp8_f32 v48, v69, v71
	v_cvt_pk_fp8_f32 v49, v77, v79
	v_cvt_pk_fp8_f32 v46, v57, v59 op_sel:[0,0,1]
	v_cvt_pk_fp8_f32 v47, v65, v67 op_sel:[0,0,1]
	v_cvt_pk_fp8_f32 v48, v73, v75 op_sel:[0,0,1]
	v_cvt_pk_fp8_f32 v49, v81, v83 op_sel:[0,0,1]
	global_store_dwordx4 v[50:51], v[46:49], off sc1 nt
	s_waitcnt lgkmcnt(0)

; __device__ __forceinline__ void tr_item8(const float* W, int ld, int K, int nblk, int item, unsigned char* WT, bool gu, float scale, LAS float* scr, int lane) {
;     const int kb = item / nblk, nb = item % nblk, k0 = 64 * kb, n0 = 32 * nb;
;     int drow0 = n0;
;     if (gu) { const int bj = n0 / FF, j = n0 - bj * FF; drow0 = 256 * (j / 128) + 128 * bj + (j % 128); }
;     { float t_[32];
; #pragma unroll
;       for (int i = 0; i < 32; ++i) t_[i] = W[(size_t)(k0 + 2 * i + (lane >> 5)) * ld + n0 + (lane & 31)];
; #pragma unroll
;       for (int i = 0; i < 32; ++i) scr[(2 * i + (lane >> 5)) * 33 + (lane & 31)] = t_[i] * scale; }
; __device__ __forceinline__ void convert_items(Frame& F, const Args& a, int lo, int hi, int w, int nw) {
;     ...
;         if (r < I_GU) { tr_item8(a.in[14], 2 * FF, D, 224, r, F.ws + WS_WGU, true, WSC_GU, scr, lane); continue; } r -= I_GU;
.LBB0_1420:
	s_andn2_b64 vcc, exec, s[4:5]
	s_cbranch_vccnz .LBB0_1422
	s_add_i32 s0, s3, 0xf300
	s_bfe_u32 s4, s0, 0xb0005
	s_mulk_i32 s4, 0x2493
	s_lshr_b32 s4, s4, 16
	s_mul_i32 s5, s4, 0xe0
	s_sub_i32 s0, s0, s5
	s_lshl_b32 s5, s0, 5
	s_and_b32 s6, s0, 0xffff
	s_cmpk_gt_u32 s6, 0x6f
	s_cselect_b32 s61, 0xfffff200, 0
	s_cselect_b32 s62, 0x80, 0
	s_lshl_b32 s0, s0, 7
	s_lshl_b32 s4, s4, 6
	s_and_b32 s0, s0, 0x3ff80
	v_add_u32_e32 v64, s4, v28
	v_lshl_add_u64 v[46:47], v[6:7], 0, s[0:1]
	v_mad_i64_i32 v[48:49], s[6:7], v64, s56, v[46:47]
	v_add_u32_e32 v50, 2, v64
	v_add_u32_e32 v52, 4, v64
	v_add_u32_e32 v54, 6, v64
	v_add_u32_e32 v56, 8, v64
	v_add_u32_e32 v58, 10, v64
	v_add_u32_e32 v60, 12, v64
	v_add_u32_e32 v62, 14, v64
	v_mad_i64_i32 v[50:51], s[6:7], v50, s56, v[46:47]
	v_mad_i64_i32 v[52:53], s[6:7], v52, s56, v[46:47]
	v_mad_i64_i32 v[54:55], s[6:7], v54, s56, v[46:47]
	v_mad_i64_i32 v[56:57], s[6:7], v56, s56, v[46:47]
	v_mad_i64_i32 v[58:59], s[6:7], v58, s56, v[46:47]
	v_mad_i64_i32 v[60:61], s[6:7], v60, s56, v[46:47]
	v_mad_i64_i32 v[62:63], s[6:7], v62, s56, v[46:47]
	global_load_dword v65, v[48:49], off nt
	global_load_dword v66, v[50:51], off nt
	global_load_dword v67, v[52:53], off nt
	global_load_dword v68, v[54:55], off nt
	global_load_dword v69, v[56:57], off nt
	global_load_dword v70, v[58:59], off nt
	global_load_dword v71, v[60:61], off nt
	global_load_dword v72, v[62:63], off nt
	v_add_u32_e32 v48, 16, v64
	v_mad_i64_i32 v[48:49], s[6:7], v48, s56, v[46:47]
	v_add_u32_e32 v50, 18, v64
	v_add_u32_e32 v52, 20, v64
	v_add_u32_e32 v54, 22, v64
	v_add_u32_e32 v56, 24, v64
	v_add_u32_e32 v58, 26, v64
	v_add_u32_e32 v60, 28, v64
	v_add_u32_e32 v62, 30, v64
	v_mad_i64_i32 v[50:51], s[6:7], v50, s56, v[46:47]
	v_mad_i64_i32 v[52:53], s[6:7], v52, s56, v[46:47]
	v_mad_i64_i32 v[54:55], s[6:7], v54, s56, v[46:47]
	v_mad_i64_i32 v[56:57], s[6:7], v56, s56, v[46:47]
	v_mad_i64_i32 v[58:59], s[6:7], v58, s56, v[46:47]
	v_mad_i64_i32 v[60:61], s[6:7], v60, s56, v[46:47]
	v_mad_i64_i32 v[62:63], s[6:7], v62, s56, v[46:47]
	global_load_dword v73, v[48:49], off nt
	global_load_dword v74, v[50:51], off nt
	global_load_dword v75, v[52:53], off nt
	global_load_dword v76, v[54:55], off nt
	global_load_dword v77, v[56:57], off nt
	global_load_dword v78, v[58:59], off nt
	global_load_dword v79, v[60:61], off nt
	global_load_dword v80, v[62:63], off nt
	v_add_u32_e32 v48, 32, v64
	v_add_u32_e32 v50, 34, v64
	v_add_u32_e32 v52, 36, v64
	v_add_u32_e32 v54, 38, v64
	v_add_u32_e32 v60, 44, v64
	v_mad_i64_i32 v[48:49], s[6:7], v48, s56, v[46:47]
	v_mad_i64_i32 v[50:51], s[6:7], v50, s56, v[46:47]
	v_mad_i64_i32 v[52:53], s[6:7], v52, s56, v[46:47]
	v_mad_i64_i32 v[54:55], s[6:7], v54, s56, v[46:47]
	v_add_u32_e32 v56, 40, v64
	v_add_u32_e32 v58, 42, v64
	v_mad_i64_i32 v[60:61], s[6:7], v60, s56, v[46:47]
	v_add_u32_e32 v62, 46, v64
	v_mad_i64_i32 v[56:57], s[6:7], v56, s56, v[46:47]
	v_mad_i64_i32 v[58:59], s[6:7], v58, s56, v[46:47]
	v_mad_i64_i32 v[62:63], s[6:7], v62, s56, v[46:47]
	global_load_dword v81, v[48:49], off nt
	global_load_dword v82, v[50:51], off nt
	global_load_dword v83, v[52:53], off nt
	global_load_dword v84, v[54:55], off nt
	global_load_dword v85, v[56:57], off nt
	global_load_dword v86, v[58:59], off nt
	s_nop 0
	global_load_dword v60, v[60:61], off nt
	s_nop 0
	global_load_dword v61, v[62:63], off nt
	v_add_u32_e32 v48, 48, v64
	v_add_u32_e32 v50, 50, v64
	v_add_u32_e32 v52, 52, v64
	v_add_u32_e32 v54, 54, v64
	v_mad_i64_i32 v[48:49], s[6:7], v48, s56, v[46:47]
	v_mad_i64_i32 v[50:51], s[6:7], v50, s56, v[46:47]
	v_mad_i64_i32 v[52:53], s[6:7], v52, s56, v[46:47]
	v_mad_i64_i32 v[54:55], s[6:7], v54, s56, v[46:47]
	v_add_u32_e32 v56, 56, v64
	v_add_u32_e32 v58, 58, v64
	v_mad_i64_i32 v[56:57], s[6:7], v56, s56, v[46:47]
	v_mad_i64_i32 v[58:59], s[6:7], v58, s56, v[46:47]
	global_load_dword v62, v[48:49], off nt
	s_nop 0
	global_load_dword v50, v[50:51], off nt
	s_nop 0
	global_load_dword v51, v[52:53], off nt
	s_nop 0
	global_load_dword v52, v[54:55], off nt
	global_load_dword v53, v[56:57], off nt
	s_nop 0
	global_load_dword v54, v[58:59], off nt
	v_add_u32_e32 v48, 60, v64
	v_add_u32_e32 v55, 62, v64
	v_mad_i64_i32 v[48:49], s[6:7], v48, s56, v[46:47]
	v_mad_i64_i32 v[46:47], s[6:7], v55, s56, v[46:47]
	global_load_dword v48, v[48:49], off nt
	s_nop 0
	global_load_dword v46, v[46:47], off nt
	s_waitcnt vmcnt(31)
	v_mul_f32_e32 v47, 0x42800000, v65
	s_waitcnt vmcnt(30)
	v_mul_f32_e32 v49, 0x42800000, v66
	ds_write2_b32 v29, v47, v49 offset1:66
	s_waitcnt vmcnt(29)
	v_mul_f32_e32 v47, 0x42800000, v67
	s_waitcnt vmcnt(28)
	v_mul_f32_e32 v49, 0x42800000, v68
	ds_write2_b32 v29, v47, v49 offset0:132 offset1:198
	s_waitcnt vmcnt(27)
	v_mul_f32_e32 v47, 0x42800000, v69
	s_waitcnt vmcnt(26)
; __device__ __forceinline__ unsigned cvt_pk4_fp8(float a, float b, float c, float d) { int w = 0; w = __builtin_amdgcn_cvt_pk_fp8_f32(a, b, w, false); w = __builtin_amdgcn_cvt_pk_fp8_f32(c, d, w, true); return (unsigned)w; }
; #define GAS __attribute__((address_space(1)))
; #define LAS __attribute__((address_space(3)))
; #define LDS_WAIT() asm volatile("s_waitcnt lgkmcnt(0)" ::: "memory")
; __device__ __forceinline__ void tr_item8(const float* W, int ld, int K, int nblk, int item, unsigned char* WT, bool gu, float scale, LAS float* scr, int lane) {
;     ...
;     if (gu) { const int bj = n0 / FF, j = n0 - bj * FF; drow0 = 256 * (j / 128) + 128 * bj + (j % 128); }
;     ...
;       for (int i = 0; i < 32; ++i) scr[(2 * i + (lane >> 5)) * 33 + (lane & 31)] = t_[i] * scale; }
;     LDS_WAIT(); asm volatile("" ::: "memory");
;     const int c = lane & 3;
; #pragma unroll
;     for (int j = 0; j < 2; ++j) { const int n = (lane >> 2) + 16 * j; const LAS float* sp = scr + (16 * c) * 33 + n;
;         v4u o; o.x = pg8::cvt_pk4_fp8(sp[0 * 33], sp[1 * 33], sp[2 * 33], sp[3 * 33]); o.y = pg8::cvt_pk4_fp8(sp[4 * 33], sp[5 * 33], sp[6 * 33], sp[7 * 33]);
;         o.z = pg8::cvt_pk4_fp8(sp[8 * 33], sp[9 * 33], sp[10 * 33], sp[11 * 33]); o.w = pg8::cvt_pk4_fp8(sp[12 * 33], sp[13 * 33], sp[14 * 33], sp[15 * 33]);
;         *(GAS v4u*)(WT + (size_t)(drow0 + n) * K + k0 + 16 * c) = o; }
;     LDS_WAIT(); asm volatile("" ::: "memory");
	v_mul_f32_e32 v49, 0x42800000, v70
	ds_write2_b32 v38, v47, v49 offset0:8 offset1:74
	s_waitcnt vmcnt(25)
	v_mul_f32_e32 v47, 0x42800000, v71
	s_waitcnt vmcnt(24)
	v_mul_f32_e32 v49, 0x42800000, v72
	ds_write2_b32 v38, v47, v49 offset0:140 offset1:206
	s_add_i32 s0, s61, s5
	s_sext_i32_i16 s5, s0
	s_bfe_u32 s5, s5, 0x70018
	s_add_i32 s5, s0, s5
	s_sext_i32_i16 s6, s5
	s_and_b32 s5, s5, 0xff80
	s_sub_i32 s0, s0, s5
	s_lshl_b32 s6, s6, 1
	s_sext_i32_i16 s0, s0
	s_waitcnt vmcnt(23)
	v_mul_f32_e32 v47, 0x42800000, v73
	s_waitcnt vmcnt(22)
	v_mul_f32_e32 v49, 0x42800000, v74
	ds_write2_b32 v39, v47, v49 offset0:16 offset1:82
	s_waitcnt vmcnt(21)
	v_mul_f32_e32 v47, 0x42800000, v75
	s_waitcnt vmcnt(20)
	v_mul_f32_e32 v49, 0x42800000, v76
	ds_write2_b32 v39, v47, v49 offset0:148 offset1:214
	s_waitcnt vmcnt(19)
	v_mul_f32_e32 v47, 0x42800000, v77
	s_waitcnt vmcnt(18)
	v_mul_f32_e32 v49, 0x42800000, v78
	ds_write2_b32 v40, v47, v49 offset0:24 offset1:90
	s_waitcnt vmcnt(17)
	v_mul_f32_e32 v47, 0x42800000, v79
	s_waitcnt vmcnt(16)
	v_mul_f32_e32 v49, 0x42800000, v80
	ds_write2_b32 v40, v47, v49 offset0:156 offset1:222
	s_and_b32 s6, s6, 0xffffff00
	s_add_i32 s0, s62, s0
	s_add_i32 s0, s0, s6
	s_mov_b32 s5, s1
	s_waitcnt vmcnt(15)
	v_mul_f32_e32 v47, 0x42800000, v81
	s_waitcnt vmcnt(14)
	v_mul_f32_e32 v49, 0x42800000, v82
	ds_write2_b32 v41, v47, v49 offset0:32 offset1:98
	s_waitcnt vmcnt(13)
	v_mul_f32_e32 v47, 0x42800000, v83
	s_waitcnt vmcnt(12)
	v_mul_f32_e32 v49, 0x42800000, v84
	ds_write2_b32 v41, v47, v49 offset0:164 offset1:230
	s_waitcnt vmcnt(11)
	v_mul_f32_e32 v47, 0x42800000, v85
	s_waitcnt vmcnt(10)
	v_mul_f32_e32 v49, 0x42800000, v86
	ds_write2_b32 v42, v47, v49 offset0:40 offset1:106
	s_waitcnt vmcnt(9)
	v_mul_f32_e32 v47, 0x42800000, v60
	s_waitcnt vmcnt(8)
	v_mul_f32_e32 v49, 0x42800000, v61
	ds_write2_b32 v42, v47, v49 offset0:172 offset1:238
	v_add_u32_e32 v84, s0, v30
	v_ashrrev_i32_e32 v85, 31, v84
	v_lshlrev_b64 v[84:85], 10, v[84:85]
	s_waitcnt vmcnt(7)
	v_mul_f32_e32 v47, 0x42800000, v62
	s_waitcnt vmcnt(6)
	v_mul_f32_e32 v49, 0x42800000, v50
	ds_write2_b32 v43, v47, v49 offset0:48 offset1:114
	s_waitcnt vmcnt(5)
	v_mul_f32_e32 v47, 0x42800000, v51
	s_waitcnt vmcnt(4)
	v_mul_f32_e32 v49, 0x42800000, v52
	ds_write2_b32 v43, v47, v49 offset0:180 offset1:246
	s_waitcnt vmcnt(3)
	v_mul_f32_e32 v47, 0x42800000, v53
	s_waitcnt vmcnt(2)
	v_mul_f32_e32 v49, 0x42800000, v54
	ds_write2_b32 v44, v47, v49 offset0:56 offset1:122
	v_mov_b32_e32 v49, 0
	v_lshl_add_u64 v[50:51], v[18:19], 0, s[4:5]
	s_waitcnt vmcnt(1)
	v_mul_f32_e32 v47, 0x42800000, v48
	s_waitcnt vmcnt(0)
	v_mul_f32_e32 v46, 0x42800000, v46
	ds_write2_b32 v44, v47, v46 offset0:188 offset1:254
	s_waitcnt lgkmcnt(0)
	ds_read2_b32 v[52:53], v31 offset1:16
	ds_read2_b32 v[54:55], v31 offset0:33 offset1:49
	ds_read2_b32 v[56:57], v31 offset0:66 offset1:82
	ds_read2_b32 v[58:59], v31 offset0:99 offset1:115
	ds_read2_b32 v[60:61], v31 offset0:132 offset1:148
	ds_read2_b32 v[62:63], v31 offset0:165 offset1:181
	ds_read2_b32 v[64:65], v31 offset0:198 offset1:214
	ds_read2_b32 v[66:67], v31 offset0:231 offset1:247
	ds_read2_b32 v[68:69], v45 offset0:8 offset1:24
	ds_read2_b32 v[70:71], v45 offset0:41 offset1:57
	ds_read2_b32 v[72:73], v45 offset0:74 offset1:90
	ds_read2_b32 v[74:75], v45 offset0:107 offset1:123
	ds_read2_b32 v[76:77], v45 offset0:140 offset1:156
	ds_read2_b32 v[78:79], v45 offset0:173 offset1:189
	v_mov_b32_e32 v46, 0
	v_mov_b32_e32 v47, 0
	v_mov_b32_e32 v48, 0
	ds_read2_b32 v[80:81], v45 offset0:206 offset1:222
	ds_read2_b32 v[82:83], v45 offset0:239 offset1:255
	s_waitcnt lgkmcnt(14)
	v_cvt_pk_fp8_f32 v46, v52, v54
	s_waitcnt lgkmcnt(10)
	v_cvt_pk_fp8_f32 v47, v60, v62
	s_waitcnt lgkmcnt(6)
	v_cvt_pk_fp8_f32 v48, v68, v70
	s_waitcnt lgkmcnt(2)
	v_cvt_pk_fp8_f32 v49, v76, v78
	v_cvt_pk_fp8_f32 v46, v56, v58 op_sel:[0,0,1]
	v_cvt_pk_fp8_f32 v47, v64, v66 op_sel:[0,0,1]
	v_cvt_pk_fp8_f32 v48, v72, v74 op_sel:[0,0,1]
	s_waitcnt lgkmcnt(0)
	v_cvt_pk_fp8_f32 v49, v80, v82 op_sel:[0,0,1]
	v_lshl_add_u64 v[84:85], v[50:51], 0, v[84:85]
	v_add_u32_e32 v52, s0, v32
	global_store_dwordx4 v[84:85], v[46:49], off sc1 nt
	s_nop 1
	v_mov_b32_e32 v46, 0
	v_mov_b32_e32 v47, 0
	v_mov_b32_e32 v48, 0
	v_mov_b32_e32 v49, 0
	v_cvt_pk_fp8_f32 v46, v53, v55
	v_cvt_pk_fp8_f32 v47, v61, v63
	v_cvt_pk_fp8_f32 v48, v69, v71
	v_cvt_pk_fp8_f32 v49, v77, v79
	v_cvt_pk_fp8_f32 v46, v57, v59 op_sel:[0,0,1]
	v_cvt_pk_fp8_f32 v47, v65, v67 op_sel:[0,0,1]
	v_cvt_pk_fp8_f32 v48, v73, v75 op_sel:[0,0,1]
	v_cvt_pk_fp8_f32 v49, v81, v83 op_sel:[0,0,1]
	v_ashrrev_i32_e32 v53, 31, v52
	v_lshlrev_b64 v[52:53], 10, v[52:53]
	v_lshl_add_u64 v[50:51], v[50:51], 0, v[52:53]
	global_store_dwordx4 v[50:51], v[46:49], off sc1 nt
	s_waitcnt lgkmcnt(0)

; #define LDS_WAIT() asm volatile("s_waitcnt lgkmcnt(0)" ::: "memory")
; __device__ __forceinline__ void tr_item(const float* W, int ld, int K, int nblk, int item, bf16* WT, bool gu, LAS float* scr, int lane) {
;     const int kb = item / nblk, nb = item % nblk, k0 = 64 * kb, n0 = 32 * nb;
;     int drow0 = n0;
;     if (gu) { const int bj = n0 / FF, j = n0 - bj * FF; drow0 = 256 * (j / 128) + 128 * bj + (j % 128); }
;     { float t_[32];
; #pragma unroll
;       for (int i = 0; i < 32; ++i) t_[i] = W[(size_t)(k0 + 2 * i + (lane >> 5)) * ld + n0 + (lane & 31)];
; #pragma unroll
;       for (int i = 0; i < 32; ++i) scr[(2 * i + (lane >> 5)) * 33 + (lane & 31)] = t_[i]; }
;     LDS_WAIT(); asm volatile("" ::: "memory");
; __device__ __forceinline__ void convert_items(Frame& F, const Args& a, int lo, int hi, int w, int nw) {
;     ...
;         if (r < I_SO) { tr_item(a.in[12], D, D, 32, r, (bf16*)(F.ws + WS_WSWAOUT), false, scr, lane); continue; } r -= I_SO;
.LBB0_1423:
	s_andn2_b64 vcc, exec, s[4:5]
	s_cbranch_vccnz .LBB0_1425
	s_add_i32 s0, s9, 0x2000
	s_and_b32 s5, s0, 0x1ffc0
	s_and_b32 s4, s8, 0x3e0
	v_add_u32_e32 v46, s5, v28
	s_lshl_b32 s0, s4, 2
	v_ashrrev_i32_e32 v47, 31, v46
	v_lshl_add_u64 v[48:49], v[8:9], 0, s[0:1]
	v_lshlrev_b64 v[46:47], 12, v[46:47]
	v_lshl_add_u64 v[46:47], v[48:49], 0, v[46:47]
	v_add_co_u32_e32 v48, vcc, 0x2000, v46
	s_lshl_b32 s0, s5, 1
	s_nop 0
	v_addc_co_u32_e32 v49, vcc, 0, v47, vcc
	v_add_co_u32_e32 v50, vcc, 0x4000, v46
	s_nop 1
	v_addc_co_u32_e32 v51, vcc, 0, v47, vcc
	v_add_co_u32_e32 v52, vcc, 0x6000, v46
	s_nop 1
	v_addc_co_u32_e32 v53, vcc, 0, v47, vcc
	v_add_co_u32_e32 v54, vcc, 0x8000, v46
	s_nop 1
	v_addc_co_u32_e32 v55, vcc, 0, v47, vcc
	v_add_co_u32_e32 v56, vcc, 0xa000, v46
	s_nop 1
	v_addc_co_u32_e32 v57, vcc, 0, v47, vcc
	v_add_co_u32_e32 v58, vcc, 0xc000, v46
	s_nop 1
	v_addc_co_u32_e32 v59, vcc, 0, v47, vcc
	v_add_co_u32_e32 v60, vcc, 0xe000, v46
	s_nop 1
	v_addc_co_u32_e32 v61, vcc, 0, v47, vcc
	global_load_dword v64, v[46:47], off nt
	global_load_dword v65, v[48:49], off nt
	global_load_dword v66, v[50:51], off nt
	global_load_dword v67, v[52:53], off nt
	global_load_dword v68, v[54:55], off nt
	global_load_dword v69, v[56:57], off nt
	global_load_dword v70, v[58:59], off nt
	global_load_dword v71, v[60:61], off nt
	v_add_co_u32_e32 v48, vcc, 0x10000, v46
	s_nop 1
	v_addc_co_u32_e32 v49, vcc, 0, v47, vcc
	v_add_co_u32_e32 v50, vcc, 0x12000, v46
	s_nop 1
	v_addc_co_u32_e32 v51, vcc, 0, v47, vcc
	v_add_co_u32_e32 v52, vcc, 0x14000, v46
	s_nop 1
	v_addc_co_u32_e32 v53, vcc, 0, v47, vcc
	v_add_co_u32_e32 v54, vcc, 0x16000, v46
	s_nop 1
	v_addc_co_u32_e32 v55, vcc, 0, v47, vcc
	v_add_co_u32_e32 v56, vcc, 0x18000, v46
	s_nop 1
	v_addc_co_u32_e32 v57, vcc, 0, v47, vcc
	v_add_co_u32_e32 v58, vcc, 0x1a000, v46
	s_nop 1
	v_addc_co_u32_e32 v59, vcc, 0, v47, vcc
	v_add_co_u32_e32 v60, vcc, 0x1c000, v46
	s_nop 1
	v_addc_co_u32_e32 v61, vcc, 0, v47, vcc
	v_add_co_u32_e32 v62, vcc, 0x1e000, v46
	s_nop 1
	v_addc_co_u32_e32 v63, vcc, 0, v47, vcc
	global_load_dword v72, v[48:49], off nt
	global_load_dword v73, v[50:51], off nt
	global_load_dword v74, v[52:53], off nt
	global_load_dword v75, v[54:55], off nt
	global_load_dword v76, v[56:57], off nt
	global_load_dword v77, v[58:59], off nt
	global_load_dword v78, v[60:61], off nt
	global_load_dword v79, v[62:63], off nt
	v_add_co_u32_e32 v48, vcc, 0x20000, v46
	s_nop 1
	v_addc_co_u32_e32 v49, vcc, 0, v47, vcc
	v_add_co_u32_e32 v50, vcc, 0x22000, v46
	s_nop 1
	v_addc_co_u32_e32 v51, vcc, 0, v47, vcc
	v_add_co_u32_e32 v52, vcc, 0x24000, v46
	s_nop 1
	v_addc_co_u32_e32 v53, vcc, 0, v47, vcc
	v_add_co_u32_e32 v54, vcc, 0x26000, v46
	s_nop 1
	v_addc_co_u32_e32 v55, vcc, 0, v47, vcc
	v_add_co_u32_e32 v56, vcc, 0x28000, v46
	s_nop 1
	v_addc_co_u32_e32 v57, vcc, 0, v47, vcc
	v_add_co_u32_e32 v58, vcc, 0x2a000, v46
	s_nop 1
	v_addc_co_u32_e32 v59, vcc, 0, v47, vcc
	v_add_co_u32_e32 v60, vcc, 0x2c000, v46
	s_nop 1
	v_addc_co_u32_e32 v61, vcc, 0, v47, vcc
	v_add_co_u32_e32 v62, vcc, 0x2e000, v46
	s_nop 1
	v_addc_co_u32_e32 v63, vcc, 0, v47, vcc
	global_load_dword v80, v[48:49], off nt
	global_load_dword v81, v[50:51], off nt
	global_load_dword v82, v[52:53], off nt
	global_load_dword v83, v[54:55], off nt
	global_load_dword v84, v[56:57], off nt
	global_load_dword v85, v[58:59], off nt
	global_load_dword v86, v[60:61], off nt
	s_nop 0
	global_load_dword v62, v[62:63], off nt
	v_add_co_u32_e32 v48, vcc, 0x30000, v46
	s_nop 1
	v_addc_co_u32_e32 v49, vcc, 0, v47, vcc
	v_add_co_u32_e32 v50, vcc, 0x32000, v46
	s_nop 1
	v_addc_co_u32_e32 v51, vcc, 0, v47, vcc
	v_add_co_u32_e32 v52, vcc, 0x34000, v46
	s_nop 1
	v_addc_co_u32_e32 v53, vcc, 0, v47, vcc
	v_add_co_u32_e32 v54, vcc, 0x36000, v46
	s_nop 1
	v_addc_co_u32_e32 v55, vcc, 0, v47, vcc
	v_add_co_u32_e32 v56, vcc, 0x38000, v46
	s_nop 1
	v_addc_co_u32_e32 v57, vcc, 0, v47, vcc
	v_add_co_u32_e32 v58, vcc, 0x3a000, v46
	s_nop 1
	v_addc_co_u32_e32 v59, vcc, 0, v47, vcc
	v_add_co_u32_e32 v60, vcc, 0x3c000, v46
	s_nop 1
	v_addc_co_u32_e32 v61, vcc, 0, v47, vcc
	v_add_co_u32_e32 v46, vcc, 0x3e000, v46
	s_nop 1
	v_addc_co_u32_e32 v47, vcc, 0, v47, vcc
	global_load_dword v48, v[48:49], off nt
	s_nop 0
	global_load_dword v49, v[50:51], off nt
	s_nop 0
	global_load_dword v50, v[52:53], off nt
	global_load_dword v51, v[54:55], off nt
	s_nop 0
	global_load_dword v52, v[56:57], off nt
	global_load_dword v53, v[58:59], off nt
	global_load_dword v54, v[60:61], off nt
	s_nop 0
	global_load_dword v46, v[46:47], off nt
	s_waitcnt vmcnt(30)
	ds_write2_b32 v29, v64, v65 offset1:66
	s_waitcnt vmcnt(28)
	ds_write2_b32 v29, v66, v67 offset0:132 offset1:198
	s_waitcnt vmcnt(26)
	ds_write2_b32 v38, v68, v69 offset0:8 offset1:74
	s_waitcnt vmcnt(24)
	ds_write2_b32 v38, v70, v71 offset0:140 offset1:206
	s_waitcnt vmcnt(22)
	ds_write2_b32 v39, v72, v73 offset0:16 offset1:82
	s_waitcnt vmcnt(20)
	ds_write2_b32 v39, v74, v75 offset0:148 offset1:214
	s_waitcnt vmcnt(18)
	ds_write2_b32 v40, v76, v77 offset0:24 offset1:90
	s_waitcnt vmcnt(16)
	ds_write2_b32 v40, v78, v79 offset0:156 offset1:222
	s_waitcnt vmcnt(14)
	ds_write2_b32 v41, v80, v81 offset0:32 offset1:98
	s_waitcnt vmcnt(12)
	ds_write2_b32 v41, v82, v83 offset0:164 offset1:230
	s_waitcnt vmcnt(10)
; #define GAS __attribute__((address_space(1)))
; #define LAS __attribute__((address_space(3)))
; #define LDS_WAIT() asm volatile("s_waitcnt lgkmcnt(0)" ::: "memory")
; __device__ __forceinline__ unsigned pk2(float lo, float hi) { return f2bf(lo) | (f2bf(hi) << 16); }
; __device__ __forceinline__ void tr_item(const float* W, int ld, int K, int nblk, int item, bf16* WT, bool gu, LAS float* scr, int lane) {
;     ...
;       for (int i = 0; i < 32; ++i) scr[(2 * i + (lane >> 5)) * 33 + (lane & 31)] = t_[i]; }
;     LDS_WAIT(); asm volatile("" ::: "memory");
;     const int c = lane & 7;
; #pragma unroll
;     for (int j = 0; j < 4; ++j) { const int n = (lane >> 3) + 8 * j; const LAS float* s = scr + (8 * c) * 33 + n;
;         v4u o; o.x = pk2(s[0 * 33], s[1 * 33]); o.y = pk2(s[2 * 33], s[3 * 33]); o.z = pk2(s[4 * 33], s[5 * 33]); o.w = pk2(s[6 * 33], s[7 * 33]);
;         *(GAS v4u*)(WT + (size_t)(drow0 + n) * K + k0 + 8 * c) = o; }
;     LDS_WAIT(); asm volatile("" ::: "memory");
	ds_write2_b32 v42, v84, v85 offset0:40 offset1:106
	s_waitcnt vmcnt(8)
	ds_write2_b32 v42, v86, v62 offset0:172 offset1:238
	s_waitcnt vmcnt(6)
	ds_write2_b32 v43, v48, v49 offset0:48 offset1:114
	s_waitcnt vmcnt(4)
	ds_write2_b32 v43, v50, v51 offset0:180 offset1:246
	s_waitcnt vmcnt(2)
	ds_write2_b32 v44, v52, v53 offset0:56 offset1:122
	s_waitcnt vmcnt(0)
	ds_write2_b32 v44, v54, v46 offset0:188 offset1:254
	s_waitcnt lgkmcnt(0)
	ds_read2_b32 v[50:51], v34 offset1:8
	ds_read2_b32 v[54:55], v34 offset0:33 offset1:41
	ds_read2_b32 v[56:57], v34 offset0:66 offset1:74
	ds_read2_b32 v[58:59], v34 offset0:99 offset1:107
	ds_read2_b32 v[60:61], v34 offset0:132 offset1:140
	s_waitcnt lgkmcnt(4)
	v_bfe_u32 v46, v50, 16, 1
	v_add3_u32 v46, v50, v46, s57
	s_waitcnt lgkmcnt(3)
	v_bfe_u32 v47, v54, 16, 1
	v_lshrrev_b32_e32 v46, 16, v46
	v_add3_u32 v47, v54, v47, s57
	ds_read2_b32 v[62:63], v34 offset0:165 offset1:173
	v_and_or_b32 v46, v47, s58, v46
	s_waitcnt lgkmcnt(3)
	v_bfe_u32 v47, v56, 16, 1
	v_add3_u32 v47, v56, v47, s57
	s_waitcnt lgkmcnt(2)
	v_bfe_u32 v48, v58, 16, 1
	ds_read2_b32 v[64:65], v34 offset0:198 offset1:206
	v_lshrrev_b32_e32 v47, 16, v47
	v_add3_u32 v48, v58, v48, s57
	ds_read2_b32 v[66:67], v34 offset0:231 offset1:239
	v_and_or_b32 v47, v48, s58, v47
	s_waitcnt lgkmcnt(3)
	v_bfe_u32 v48, v60, 16, 1
	v_add3_u32 v48, v60, v48, s57
	s_waitcnt lgkmcnt(2)
	v_bfe_u32 v49, v62, 16, 1
	v_lshrrev_b32_e32 v48, 16, v48
	v_add3_u32 v49, v62, v49, s57
	v_and_or_b32 v48, v49, s58, v48
	s_waitcnt lgkmcnt(1)
	v_bfe_u32 v49, v64, 16, 1
	v_add_u32_e32 v68, s4, v33
	v_add3_u32 v49, v64, v49, s57
	s_waitcnt lgkmcnt(0)
	v_bfe_u32 v50, v66, 16, 1
	v_ashrrev_i32_e32 v69, 31, v68
	v_lshl_add_u64 v[52:53], v[20:21], 0, s[0:1]
	v_lshrrev_b32_e32 v49, 16, v49
	v_add3_u32 v50, v66, v50, s57
	v_lshlrev_b64 v[68:69], 11, v[68:69]
	v_and_or_b32 v49, v50, s58, v49
	v_lshl_add_u64 v[68:69], v[52:53], 0, v[68:69]
	global_store_dwordx4 v[68:69], v[46:49], off sc1 nt
	v_bfe_u32 v50, v67, 16, 1
	v_add3_u32 v50, v67, v50, s57
	v_bfe_u32 v46, v51, 16, 1
	v_add3_u32 v46, v51, v46, s57
	v_bfe_u32 v47, v55, 16, 1
	v_lshrrev_b32_e32 v46, 16, v46
	v_add3_u32 v47, v55, v47, s57
	v_and_or_b32 v46, v47, s58, v46
	v_bfe_u32 v47, v57, 16, 1
	v_add3_u32 v47, v57, v47, s57
	v_bfe_u32 v48, v59, 16, 1
	v_lshrrev_b32_e32 v47, 16, v47
	v_add3_u32 v48, v59, v48, s57
	v_and_or_b32 v47, v48, s58, v47
	v_bfe_u32 v48, v61, 16, 1
	v_add3_u32 v48, v61, v48, s57
	v_bfe_u32 v49, v63, 16, 1
	v_lshrrev_b32_e32 v48, 16, v48
	v_add3_u32 v49, v63, v49, s57
	v_and_or_b32 v48, v49, s58, v48
	v_bfe_u32 v49, v65, 16, 1
	v_add3_u32 v49, v65, v49, s57
	v_lshrrev_b32_e32 v49, 16, v49
	v_and_or_b32 v49, v50, s58, v49
	v_add_u32_e32 v50, s4, v35
	v_ashrrev_i32_e32 v51, 31, v50
	v_lshlrev_b64 v[50:51], 11, v[50:51]
	ds_read2_b32 v[54:55], v34 offset0:16 offset1:24
	v_lshl_add_u64 v[50:51], v[52:53], 0, v[50:51]
	global_store_dwordx4 v[50:51], v[46:49], off sc1 nt
	ds_read2_b32 v[50:51], v34 offset0:49 offset1:57
	ds_read2_b32 v[56:57], v34 offset0:82 offset1:90
	ds_read2_b32 v[58:59], v34 offset0:115 offset1:123
	s_waitcnt lgkmcnt(3)
	v_bfe_u32 v46, v54, 16, 1
	v_add3_u32 v46, v54, v46, s57
	s_waitcnt lgkmcnt(2)
	v_bfe_u32 v47, v50, 16, 1
	ds_read2_b32 v[60:61], v34 offset0:148 offset1:156
	v_lshrrev_b32_e32 v46, 16, v46
	v_add3_u32 v47, v50, v47, s57
	ds_read2_b32 v[62:63], v34 offset0:181 offset1:189
	v_and_or_b32 v46, v47, s58, v46
	s_waitcnt lgkmcnt(3)
	v_bfe_u32 v47, v56, 16, 1
	v_add3_u32 v47, v56, v47, s57
	s_waitcnt lgkmcnt(2)
	v_bfe_u32 v48, v58, 16, 1
	ds_read2_b32 v[64:65], v34 offset0:214 offset1:222
	v_lshrrev_b32_e32 v47, 16, v47
	v_add3_u32 v48, v58, v48, s57
	ds_read2_b32 v[66:67], v34 offset0:247 offset1:255
	v_and_or_b32 v47, v48, s58, v47
	s_waitcnt lgkmcnt(3)
	v_bfe_u32 v48, v60, 16, 1
	v_add3_u32 v48, v60, v48, s57
	s_waitcnt lgkmcnt(2)
	v_bfe_u32 v49, v62, 16, 1
	v_lshrrev_b32_e32 v48, 16, v48
	v_add3_u32 v49, v62, v49, s57
	v_and_or_b32 v48, v49, s58, v48
	s_waitcnt lgkmcnt(1)
	v_bfe_u32 v49, v64, 16, 1
	v_add_u32_e32 v68, s4, v36
	v_add3_u32 v49, v64, v49, s57
	s_waitcnt lgkmcnt(0)
	v_bfe_u32 v50, v66, 16, 1
	v_ashrrev_i32_e32 v69, 31, v68
	v_lshrrev_b32_e32 v49, 16, v49
	v_add3_u32 v50, v66, v50, s57
	v_lshlrev_b64 v[68:69], 11, v[68:69]
	v_and_or_b32 v49, v50, s58, v49
	v_lshl_add_u64 v[68:69], v[52:53], 0, v[68:69]
	global_store_dwordx4 v[68:69], v[46:49], off sc1 nt
	v_bfe_u32 v50, v67, 16, 1
	v_add3_u32 v50, v67, v50, s57
	v_bfe_u32 v46, v55, 16, 1
	v_add3_u32 v46, v55, v46, s57
	v_bfe_u32 v47, v51, 16, 1
	v_lshrrev_b32_e32 v46, 16, v46
	v_add3_u32 v47, v51, v47, s57
	v_and_or_b32 v46, v47, s58, v46
	v_bfe_u32 v47, v57, 16, 1
	v_add3_u32 v47, v57, v47, s57
	v_bfe_u32 v48, v59, 16, 1
	v_lshrrev_b32_e32 v47, 16, v47
	v_add3_u32 v48, v59, v48, s57
	v_and_or_b32 v47, v48, s58, v47
	v_bfe_u32 v48, v61, 16, 1
	v_add3_u32 v48, v61, v48, s57
	v_bfe_u32 v49, v63, 16, 1
	v_lshrrev_b32_e32 v48, 16, v48
	v_add3_u32 v49, v63, v49, s57
	v_and_or_b32 v48, v49, s58, v48
	v_bfe_u32 v49, v65, 16, 1
	v_add3_u32 v49, v65, v49, s57
	v_lshrrev_b32_e32 v49, 16, v49
	v_and_or_b32 v49, v50, s58, v49
	v_add_u32_e32 v50, s4, v37
	v_ashrrev_i32_e32 v51, 31, v50
	v_lshlrev_b64 v[50:51], 11, v[50:51]
	v_lshl_add_u64 v[50:51], v[52:53], 0, v[50:51]
	global_store_dwordx4 v[50:51], v[46:49], off sc1 nt
	s_waitcnt lgkmcnt(0)

; __device__ __forceinline__ void tr_item(const float* W, int ld, int K, int nblk, int item, bf16* WT, bool gu, LAS float* scr, int lane) {
;     const int kb = item / nblk, nb = item % nblk, k0 = 64 * kb, n0 = 32 * nb;
;     int drow0 = n0;
;     if (gu) { const int bj = n0 / FF, j = n0 - bj * FF; drow0 = 256 * (j / 128) + 128 * bj + (j % 128); }
;     { float t_[32];
; #pragma unroll
;       for (int i = 0; i < 32; ++i) t_[i] = W[(size_t)(k0 + 2 * i + (lane >> 5)) * ld + n0 + (lane & 31)];
; #pragma unroll
;       for (int i = 0; i < 32; ++i) scr[(2 * i + (lane >> 5)) * 33 + (lane & 31)] = t_[i]; }
; __device__ __forceinline__ void convert_items(Frame& F, const Args& a, int lo, int hi, int w, int nw) {
;     ...
;         if (r < I_SI) { tr_item(a.in[10], D + 512, D, 48, r, (bf16*)(F.ws + WS_WSWAIN), false, scr, lane); continue; } r -= I_SI;
.LBB0_1426:
	s_andn2_b64 vcc, exec, s[4:5]
	s_cbranch_vccnz .LBB0_1428
	s_add_i32 s0, s3, 0xf800
	s_and_b32 s4, s0, 0xffff
	s_mul_i32 s4, s4, 0xaaab
	s_lshr_b32 s5, s4, 21
	s_mul_i32 s4, s5, 48
	s_sub_i32 s0, s0, s4
	s_lshl_b32 s0, s0, 5
	s_and_b32 s4, s0, 0xffe0
	v_lshl_add_u32 v64, s5, 6, v28
	s_lshl_b32 s0, s4, 2
	v_lshl_add_u64 v[46:47], v[10:11], 0, s[0:1]
	v_add_u32_e32 v50, 2, v64
	v_add_u32_e32 v52, 4, v64
	v_add_u32_e32 v54, 6, v64
	v_add_u32_e32 v56, 8, v64
	v_add_u32_e32 v58, 10, v64
	v_add_u32_e32 v60, 12, v64
	v_add_u32_e32 v62, 14, v64
	v_mad_i64_i32 v[48:49], s[6:7], v64, s59, v[46:47]
	v_mad_i64_i32 v[50:51], s[6:7], v50, s59, v[46:47]
	v_mad_i64_i32 v[52:53], s[6:7], v52, s59, v[46:47]
	v_mad_i64_i32 v[54:55], s[6:7], v54, s59, v[46:47]
	v_mad_i64_i32 v[56:57], s[6:7], v56, s59, v[46:47]
	v_mad_i64_i32 v[58:59], s[6:7], v58, s59, v[46:47]
	v_mad_i64_i32 v[60:61], s[6:7], v60, s59, v[46:47]
	v_mad_i64_i32 v[62:63], s[6:7], v62, s59, v[46:47]
	global_load_dword v65, v[48:49], off nt
	global_load_dword v66, v[50:51], off nt
	global_load_dword v67, v[52:53], off nt
	global_load_dword v68, v[54:55], off nt
	global_load_dword v69, v[56:57], off nt
	global_load_dword v70, v[58:59], off nt
	global_load_dword v71, v[60:61], off nt
	global_load_dword v72, v[62:63], off nt
	v_add_u32_e32 v48, 16, v64
	v_add_u32_e32 v50, 18, v64
	v_add_u32_e32 v52, 20, v64
	v_add_u32_e32 v54, 22, v64
	v_add_u32_e32 v56, 24, v64
	v_add_u32_e32 v58, 26, v64
	v_add_u32_e32 v60, 28, v64
	v_add_u32_e32 v62, 30, v64
	v_mad_i64_i32 v[48:49], s[6:7], v48, s59, v[46:47]
	v_mad_i64_i32 v[50:51], s[6:7], v50, s59, v[46:47]
	v_mad_i64_i32 v[52:53], s[6:7], v52, s59, v[46:47]
	v_mad_i64_i32 v[54:55], s[6:7], v54, s59, v[46:47]
	v_mad_i64_i32 v[56:57], s[6:7], v56, s59, v[46:47]
	v_mad_i64_i32 v[58:59], s[6:7], v58, s59, v[46:47]
	v_mad_i64_i32 v[60:61], s[6:7], v60, s59, v[46:47]
	v_mad_i64_i32 v[62:63], s[6:7], v62, s59, v[46:47]
	global_load_dword v73, v[48:49], off nt
	global_load_dword v74, v[50:51], off nt
	global_load_dword v75, v[52:53], off nt
	global_load_dword v76, v[54:55], off nt
	global_load_dword v77, v[56:57], off nt
	global_load_dword v78, v[58:59], off nt
	global_load_dword v79, v[60:61], off nt
	global_load_dword v80, v[62:63], off nt
	v_add_u32_e32 v48, 32, v64
	v_add_u32_e32 v50, 34, v64
	v_add_u32_e32 v52, 36, v64
	v_add_u32_e32 v54, 38, v64
	v_add_u32_e32 v56, 40, v64
	v_add_u32_e32 v58, 42, v64
	v_add_u32_e32 v60, 44, v64
	v_add_u32_e32 v62, 46, v64
	v_mad_i64_i32 v[48:49], s[6:7], v48, s59, v[46:47]
	v_mad_i64_i32 v[50:51], s[6:7], v50, s59, v[46:47]
	v_mad_i64_i32 v[52:53], s[6:7], v52, s59, v[46:47]
	v_mad_i64_i32 v[54:55], s[6:7], v54, s59, v[46:47]
	v_mad_i64_i32 v[56:57], s[6:7], v56, s59, v[46:47]
	v_mad_i64_i32 v[58:59], s[6:7], v58, s59, v[46:47]
	v_mad_i64_i32 v[60:61], s[6:7], v60, s59, v[46:47]
	v_mad_i64_i32 v[62:63], s[6:7], v62, s59, v[46:47]
	global_load_dword v81, v[48:49], off nt
	global_load_dword v82, v[50:51], off nt
	global_load_dword v83, v[52:53], off nt
	global_load_dword v84, v[54:55], off nt
	global_load_dword v85, v[56:57], off nt
	global_load_dword v86, v[58:59], off nt
	global_load_dword v87, v[60:61], off nt
	s_nop 0
	global_load_dword v62, v[62:63], off nt
	v_add_u32_e32 v48, 48, v64
	v_add_u32_e32 v50, 50, v64
	v_add_u32_e32 v52, 52, v64
	v_add_u32_e32 v54, 54, v64
	v_add_u32_e32 v56, 56, v64
	v_add_u32_e32 v58, 58, v64
	v_add_u32_e32 v60, 60, v64
	v_add_u32_e32 v63, 62, v64
	v_mad_i64_i32 v[48:49], s[6:7], v48, s59, v[46:47]
	v_mad_i64_i32 v[50:51], s[6:7], v50, s59, v[46:47]
	v_mad_i64_i32 v[52:53], s[6:7], v52, s59, v[46:47]
	v_mad_i64_i32 v[54:55], s[6:7], v54, s59, v[46:47]
	v_mad_i64_i32 v[56:57], s[6:7], v56, s59, v[46:47]
	v_mad_i64_i32 v[58:59], s[6:7], v58, s59, v[46:47]
	v_mad_i64_i32 v[60:61], s[6:7], v60, s59, v[46:47]
	v_mad_i64_i32 v[46:47], s[6:7], v63, s59, v[46:47]
	global_load_dword v48, v[48:49], off nt
	s_nop 0
	global_load_dword v49, v[50:51], off nt
	s_nop 0
	global_load_dword v50, v[52:53], off nt
	global_load_dword v51, v[54:55], off nt
	s_nop 0
	global_load_dword v52, v[56:57], off nt
	global_load_dword v53, v[58:59], off nt
	global_load_dword v54, v[60:61], off nt
	s_nop 0
	global_load_dword v46, v[46:47], off nt
	s_waitcnt vmcnt(30)
	ds_write2_b32 v29, v65, v66 offset1:66
	s_waitcnt vmcnt(28)
	ds_write2_b32 v29, v67, v68 offset0:132 offset1:198
	s_waitcnt vmcnt(26)
	ds_write2_b32 v38, v69, v70 offset0:8 offset1:74
	s_waitcnt vmcnt(24)
	ds_write2_b32 v38, v71, v72 offset0:140 offset1:206
	s_waitcnt vmcnt(22)
	ds_write2_b32 v39, v73, v74 offset0:16 offset1:82
	s_waitcnt vmcnt(20)
	ds_write2_b32 v39, v75, v76 offset0:148 offset1:214
	s_waitcnt vmcnt(18)
	ds_write2_b32 v40, v77, v78 offset0:24 offset1:90
	s_waitcnt vmcnt(16)
	ds_write2_b32 v40, v79, v80 offset0:156 offset1:222
	s_waitcnt vmcnt(14)
	ds_write2_b32 v41, v81, v82 offset0:32 offset1:98
	s_waitcnt vmcnt(12)
	ds_write2_b32 v41, v83, v84 offset0:164 offset1:230
	s_waitcnt vmcnt(10)
	ds_write2_b32 v42, v85, v86 offset0:40 offset1:106
	s_waitcnt vmcnt(8)
	ds_write2_b32 v42, v87, v62 offset0:172 offset1:238
	s_waitcnt vmcnt(6)
	ds_write2_b32 v43, v48, v49 offset0:48 offset1:114
	s_waitcnt vmcnt(4)
; #define GAS __attribute__((address_space(1)))
; #define LAS __attribute__((address_space(3)))
; #define LDS_WAIT() asm volatile("s_waitcnt lgkmcnt(0)" ::: "memory")
; __device__ __forceinline__ unsigned pk2(float lo, float hi) { return f2bf(lo) | (f2bf(hi) << 16); }
; __device__ __forceinline__ void tr_item(const float* W, int ld, int K, int nblk, int item, bf16* WT, bool gu, LAS float* scr, int lane) {
;     ...
;     LDS_WAIT(); asm volatile("" ::: "memory");
;     const int c = lane & 7;
; #pragma unroll
;     for (int j = 0; j < 4; ++j) { const int n = (lane >> 3) + 8 * j; const LAS float* s = scr + (8 * c) * 33 + n;
;         v4u o; o.x = pk2(s[0 * 33], s[1 * 33]); o.y = pk2(s[2 * 33], s[3 * 33]); o.z = pk2(s[4 * 33], s[5 * 33]); o.w = pk2(s[6 * 33], s[7 * 33]);
;         *(GAS v4u*)(WT + (size_t)(drow0 + n) * K + k0 + 8 * c) = o; }
;     LDS_WAIT(); asm volatile("" ::: "memory");
	ds_write2_b32 v43, v50, v51 offset0:180 offset1:246
	s_waitcnt vmcnt(2)
	ds_write2_b32 v44, v52, v53 offset0:56 offset1:122
	s_waitcnt vmcnt(0)
	ds_write2_b32 v44, v54, v46 offset0:188 offset1:254
	s_waitcnt lgkmcnt(0)
	ds_read2_b32 v[50:51], v34 offset1:8
	ds_read2_b32 v[54:55], v34 offset0:33 offset1:41
	ds_read2_b32 v[56:57], v34 offset0:66 offset1:74
	ds_read2_b32 v[58:59], v34 offset0:99 offset1:107
	ds_read2_b32 v[60:61], v34 offset0:132 offset1:140
	s_waitcnt lgkmcnt(4)
	v_bfe_u32 v46, v50, 16, 1
	v_add3_u32 v46, v50, v46, s57
	s_waitcnt lgkmcnt(3)
	v_bfe_u32 v47, v54, 16, 1
	v_lshrrev_b32_e32 v46, 16, v46
	v_add3_u32 v47, v54, v47, s57
	ds_read2_b32 v[62:63], v34 offset0:165 offset1:173
	v_and_or_b32 v46, v47, s58, v46
	s_waitcnt lgkmcnt(3)
	v_bfe_u32 v47, v56, 16, 1
	v_add3_u32 v47, v56, v47, s57
	s_waitcnt lgkmcnt(2)
	v_bfe_u32 v48, v58, 16, 1
	ds_read2_b32 v[64:65], v34 offset0:198 offset1:206
	v_lshrrev_b32_e32 v47, 16, v47
	v_add3_u32 v48, v58, v48, s57
	ds_read2_b32 v[66:67], v34 offset0:231 offset1:239
	v_and_or_b32 v47, v48, s58, v47
	s_waitcnt lgkmcnt(3)
	v_bfe_u32 v48, v60, 16, 1
	v_add3_u32 v48, v60, v48, s57
	s_waitcnt lgkmcnt(2)
	v_bfe_u32 v49, v62, 16, 1
	v_lshrrev_b32_e32 v48, 16, v48
	v_add3_u32 v49, v62, v49, s57
	v_and_or_b32 v48, v49, s58, v48
	s_waitcnt lgkmcnt(1)
	v_bfe_u32 v49, v64, 16, 1
	v_add_u32_e32 v68, s4, v33
	s_lshl_b32 s0, s5, 7
	v_add3_u32 v49, v64, v49, s57
	s_waitcnt lgkmcnt(0)
	v_bfe_u32 v50, v66, 16, 1
	v_ashrrev_i32_e32 v69, 31, v68
	v_lshl_add_u64 v[52:53], v[22:23], 0, s[0:1]
	v_lshrrev_b32_e32 v49, 16, v49
	v_add3_u32 v50, v66, v50, s57
	v_lshlrev_b64 v[68:69], 11, v[68:69]
	v_and_or_b32 v49, v50, s58, v49
	v_lshl_add_u64 v[68:69], v[52:53], 0, v[68:69]
	global_store_dwordx4 v[68:69], v[46:49], off sc1 nt
	v_bfe_u32 v50, v67, 16, 1
	v_add3_u32 v50, v67, v50, s57
	v_bfe_u32 v46, v51, 16, 1
	v_add3_u32 v46, v51, v46, s57
	v_bfe_u32 v47, v55, 16, 1
	v_lshrrev_b32_e32 v46, 16, v46
	v_add3_u32 v47, v55, v47, s57
	v_and_or_b32 v46, v47, s58, v46
	v_bfe_u32 v47, v57, 16, 1
	v_add3_u32 v47, v57, v47, s57
	v_bfe_u32 v48, v59, 16, 1
	v_lshrrev_b32_e32 v47, 16, v47
	v_add3_u32 v48, v59, v48, s57
	v_and_or_b32 v47, v48, s58, v47
	v_bfe_u32 v48, v61, 16, 1
	v_add3_u32 v48, v61, v48, s57
	v_bfe_u32 v49, v63, 16, 1
	v_lshrrev_b32_e32 v48, 16, v48
	v_add3_u32 v49, v63, v49, s57
	v_and_or_b32 v48, v49, s58, v48
	v_bfe_u32 v49, v65, 16, 1
	v_add3_u32 v49, v65, v49, s57
	v_lshrrev_b32_e32 v49, 16, v49
	v_and_or_b32 v49, v50, s58, v49
	v_add_u32_e32 v50, s4, v35
	v_ashrrev_i32_e32 v51, 31, v50
	v_lshlrev_b64 v[50:51], 11, v[50:51]
	ds_read2_b32 v[54:55], v34 offset0:16 offset1:24
	v_lshl_add_u64 v[50:51], v[52:53], 0, v[50:51]
	global_store_dwordx4 v[50:51], v[46:49], off sc1 nt
	ds_read2_b32 v[50:51], v34 offset0:49 offset1:57
	ds_read2_b32 v[56:57], v34 offset0:82 offset1:90
	ds_read2_b32 v[58:59], v34 offset0:115 offset1:123
	s_waitcnt lgkmcnt(3)
	v_bfe_u32 v46, v54, 16, 1
	v_add3_u32 v46, v54, v46, s57
	s_waitcnt lgkmcnt(2)
	v_bfe_u32 v47, v50, 16, 1
	ds_read2_b32 v[60:61], v34 offset0:148 offset1:156
	v_lshrrev_b32_e32 v46, 16, v46
	v_add3_u32 v47, v50, v47, s57
	ds_read2_b32 v[62:63], v34 offset0:181 offset1:189
	v_and_or_b32 v46, v47, s58, v46
	s_waitcnt lgkmcnt(3)
	v_bfe_u32 v47, v56, 16, 1
	v_add3_u32 v47, v56, v47, s57
	s_waitcnt lgkmcnt(2)
	v_bfe_u32 v48, v58, 16, 1
	ds_read2_b32 v[64:65], v34 offset0:214 offset1:222
	v_lshrrev_b32_e32 v47, 16, v47
	v_add3_u32 v48, v58, v48, s57
	ds_read2_b32 v[66:67], v34 offset0:247 offset1:255
	v_and_or_b32 v47, v48, s58, v47
	s_waitcnt lgkmcnt(3)
	v_bfe_u32 v48, v60, 16, 1
	v_add3_u32 v48, v60, v48, s57
	s_waitcnt lgkmcnt(2)
	v_bfe_u32 v49, v62, 16, 1
	v_lshrrev_b32_e32 v48, 16, v48
	v_add3_u32 v49, v62, v49, s57
	v_and_or_b32 v48, v49, s58, v48
	s_waitcnt lgkmcnt(1)
	v_bfe_u32 v49, v64, 16, 1
	v_add_u32_e32 v68, s4, v36
	v_add3_u32 v49, v64, v49, s57
	s_waitcnt lgkmcnt(0)
	v_bfe_u32 v50, v66, 16, 1
	v_ashrrev_i32_e32 v69, 31, v68
	v_lshrrev_b32_e32 v49, 16, v49
	v_add3_u32 v50, v66, v50, s57
	v_lshlrev_b64 v[68:69], 11, v[68:69]
	v_and_or_b32 v49, v50, s58, v49
	v_lshl_add_u64 v[68:69], v[52:53], 0, v[68:69]
	global_store_dwordx4 v[68:69], v[46:49], off sc1 nt
	v_bfe_u32 v50, v67, 16, 1
	v_add3_u32 v50, v67, v50, s57
	v_bfe_u32 v46, v55, 16, 1
	v_add3_u32 v46, v55, v46, s57
	v_bfe_u32 v47, v51, 16, 1
	v_lshrrev_b32_e32 v46, 16, v46
	v_add3_u32 v47, v51, v47, s57
	v_and_or_b32 v46, v47, s58, v46
	v_bfe_u32 v47, v57, 16, 1
	v_add3_u32 v47, v57, v47, s57
	v_bfe_u32 v48, v59, 16, 1
	v_lshrrev_b32_e32 v47, 16, v47
	v_add3_u32 v48, v59, v48, s57
	v_and_or_b32 v47, v48, s58, v47
	v_bfe_u32 v48, v61, 16, 1
	v_add3_u32 v48, v61, v48, s57
	v_bfe_u32 v49, v63, 16, 1
	v_lshrrev_b32_e32 v48, 16, v48
	v_add3_u32 v49, v63, v49, s57
	v_and_or_b32 v48, v49, s58, v48
	v_bfe_u32 v49, v65, 16, 1
	v_add3_u32 v49, v65, v49, s57
	v_lshrrev_b32_e32 v49, 16, v49
	v_and_or_b32 v49, v50, s58, v49
	v_add_u32_e32 v50, s4, v37
	v_ashrrev_i32_e32 v51, 31, v50
	v_lshlrev_b64 v[50:51], 11, v[50:51]
	v_lshl_add_u64 v[50:51], v[52:53], 0, v[50:51]
	global_store_dwordx4 v[50:51], v[46:49], off sc1 nt
	s_waitcnt lgkmcnt(0)

; __device__ __forceinline__ void tr_item(const float* W, int ld, int K, int nblk, int item, bf16* WT, bool gu, LAS float* scr, int lane) {
;     const int kb = item / nblk, nb = item % nblk, k0 = 64 * kb, n0 = 32 * nb;
;     int drow0 = n0;
;     if (gu) { const int bj = n0 / FF, j = n0 - bj * FF; drow0 = 256 * (j / 128) + 128 * bj + (j % 128); }
;     { float t_[32];
; #pragma unroll
;       for (int i = 0; i < 32; ++i) t_[i] = W[(size_t)(k0 + 2 * i + (lane >> 5)) * ld + n0 + (lane & 31)];
; #pragma unroll
;       for (int i = 0; i < 32; ++i) scr[(2 * i + (lane >> 5)) * 33 + (lane & 31)] = t_[i]; }
.LBB0_1429:
	s_andn2_b64 vcc, exec, s[4:5]
	s_cbranch_vccnz .LBB0_1431
	s_add_i32 s0, s9, 0x2a00
	s_and_b32 s5, s0, 0x1ffc0
	s_and_b32 s4, s8, 0x3e0
	v_add_u32_e32 v46, s5, v28
	s_lshl_b32 s0, s4, 2
	v_ashrrev_i32_e32 v47, 31, v46
	v_lshl_add_u64 v[48:49], v[12:13], 0, s[0:1]
	v_lshlrev_b64 v[46:47], 12, v[46:47]
	v_lshl_add_u64 v[46:47], v[48:49], 0, v[46:47]
	v_add_co_u32_e32 v48, vcc, 0x2000, v46
	s_lshl_b32 s0, s5, 1
	s_nop 0
	v_addc_co_u32_e32 v49, vcc, 0, v47, vcc
	v_add_co_u32_e32 v50, vcc, 0x4000, v46
	s_nop 1
	v_addc_co_u32_e32 v51, vcc, 0, v47, vcc
	v_add_co_u32_e32 v52, vcc, 0x6000, v46
	s_nop 1
	v_addc_co_u32_e32 v53, vcc, 0, v47, vcc
	v_add_co_u32_e32 v54, vcc, 0x8000, v46
	s_nop 1
	v_addc_co_u32_e32 v55, vcc, 0, v47, vcc
	v_add_co_u32_e32 v56, vcc, 0xa000, v46
	s_nop 1
	v_addc_co_u32_e32 v57, vcc, 0, v47, vcc
	v_add_co_u32_e32 v58, vcc, 0xc000, v46
	s_nop 1
	v_addc_co_u32_e32 v59, vcc, 0, v47, vcc
	v_add_co_u32_e32 v60, vcc, 0xe000, v46
	s_nop 1
	v_addc_co_u32_e32 v61, vcc, 0, v47, vcc
	global_load_dword v64, v[46:47], off nt
	global_load_dword v65, v[48:49], off nt
	global_load_dword v66, v[50:51], off nt
	global_load_dword v67, v[52:53], off nt
	global_load_dword v68, v[54:55], off nt
	global_load_dword v69, v[56:57], off nt
	global_load_dword v70, v[58:59], off nt
	global_load_dword v71, v[60:61], off nt
	v_add_co_u32_e32 v48, vcc, 0x10000, v46
	s_nop 1
	v_addc_co_u32_e32 v49, vcc, 0, v47, vcc
	v_add_co_u32_e32 v50, vcc, 0x12000, v46
	s_nop 1
	v_addc_co_u32_e32 v51, vcc, 0, v47, vcc
	v_add_co_u32_e32 v52, vcc, 0x14000, v46
	s_nop 1
	v_addc_co_u32_e32 v53, vcc, 0, v47, vcc
	v_add_co_u32_e32 v54, vcc, 0x16000, v46
	s_nop 1
	v_addc_co_u32_e32 v55, vcc, 0, v47, vcc
	v_add_co_u32_e32 v56, vcc, 0x18000, v46
	s_nop 1
	v_addc_co_u32_e32 v57, vcc, 0, v47, vcc
	v_add_co_u32_e32 v58, vcc, 0x1a000, v46
	s_nop 1
	v_addc_co_u32_e32 v59, vcc, 0, v47, vcc
	v_add_co_u32_e32 v60, vcc, 0x1c000, v46
	s_nop 1
	v_addc_co_u32_e32 v61, vcc, 0, v47, vcc
	v_add_co_u32_e32 v62, vcc, 0x1e000, v46
	s_nop 1
	v_addc_co_u32_e32 v63, vcc, 0, v47, vcc
	global_load_dword v72, v[48:49], off nt
	global_load_dword v73, v[50:51], off nt
	global_load_dword v74, v[52:53], off nt
	global_load_dword v75, v[54:55], off nt
	global_load_dword v76, v[56:57], off nt
	global_load_dword v77, v[58:59], off nt
	global_load_dword v78, v[60:61], off nt
	global_load_dword v79, v[62:63], off nt
	v_add_co_u32_e32 v48, vcc, 0x20000, v46
	s_nop 1
	v_addc_co_u32_e32 v49, vcc, 0, v47, vcc
	v_add_co_u32_e32 v50, vcc, 0x22000, v46
	s_nop 1
	v_addc_co_u32_e32 v51, vcc, 0, v47, vcc
	v_add_co_u32_e32 v52, vcc, 0x24000, v46
	s_nop 1
	v_addc_co_u32_e32 v53, vcc, 0, v47, vcc
	v_add_co_u32_e32 v54, vcc, 0x26000, v46
	s_nop 1
	v_addc_co_u32_e32 v55, vcc, 0, v47, vcc
	v_add_co_u32_e32 v56, vcc, 0x28000, v46
	s_nop 1
	v_addc_co_u32_e32 v57, vcc, 0, v47, vcc
	v_add_co_u32_e32 v58, vcc, 0x2a000, v46
	s_nop 1
	v_addc_co_u32_e32 v59, vcc, 0, v47, vcc
	v_add_co_u32_e32 v60, vcc, 0x2c000, v46
	s_nop 1
	v_addc_co_u32_e32 v61, vcc, 0, v47, vcc
	v_add_co_u32_e32 v62, vcc, 0x2e000, v46
	s_nop 1
	v_addc_co_u32_e32 v63, vcc, 0, v47, vcc
	global_load_dword v80, v[48:49], off nt
	global_load_dword v81, v[50:51], off nt
	global_load_dword v82, v[52:53], off nt
	global_load_dword v83, v[54:55], off nt
	global_load_dword v84, v[56:57], off nt
	global_load_dword v85, v[58:59], off nt
	global_load_dword v86, v[60:61], off nt
	s_nop 0
	global_load_dword v62, v[62:63], off nt
	v_add_co_u32_e32 v48, vcc, 0x30000, v46
	s_nop 1
	v_addc_co_u32_e32 v49, vcc, 0, v47, vcc
	v_add_co_u32_e32 v50, vcc, 0x32000, v46
	s_nop 1
	v_addc_co_u32_e32 v51, vcc, 0, v47, vcc
	v_add_co_u32_e32 v52, vcc, 0x34000, v46
	s_nop 1
	v_addc_co_u32_e32 v53, vcc, 0, v47, vcc
	v_add_co_u32_e32 v54, vcc, 0x36000, v46
	s_nop 1
	v_addc_co_u32_e32 v55, vcc, 0, v47, vcc
	v_add_co_u32_e32 v56, vcc, 0x38000, v46
	s_nop 1
	v_addc_co_u32_e32 v57, vcc, 0, v47, vcc
	v_add_co_u32_e32 v58, vcc, 0x3a000, v46
	s_nop 1
	v_addc_co_u32_e32 v59, vcc, 0, v47, vcc
	v_add_co_u32_e32 v60, vcc, 0x3c000, v46
	s_nop 1
	v_addc_co_u32_e32 v61, vcc, 0, v47, vcc
	v_add_co_u32_e32 v46, vcc, 0x3e000, v46
	s_nop 1
	v_addc_co_u32_e32 v47, vcc, 0, v47, vcc
	global_load_dword v48, v[48:49], off nt
	s_nop 0
	global_load_dword v49, v[50:51], off nt
	s_nop 0
	global_load_dword v50, v[52:53], off nt
	global_load_dword v51, v[54:55], off nt
	s_nop 0
	global_load_dword v52, v[56:57], off nt
	global_load_dword v53, v[58:59], off nt
	global_load_dword v54, v[60:61], off nt
	s_nop 0
	global_load_dword v46, v[46:47], off nt
	s_waitcnt vmcnt(30)
	ds_write2_b32 v29, v64, v65 offset1:66
	s_waitcnt vmcnt(28)
	ds_write2_b32 v29, v66, v67 offset0:132 offset1:198
	s_waitcnt vmcnt(26)
	ds_write2_b32 v38, v68, v69 offset0:8 offset1:74
	s_waitcnt vmcnt(24)
	ds_write2_b32 v38, v70, v71 offset0:140 offset1:206
	s_waitcnt vmcnt(22)
	ds_write2_b32 v39, v72, v73 offset0:16 offset1:82
	s_waitcnt vmcnt(20)
	ds_write2_b32 v39, v74, v75 offset0:148 offset1:214
	s_waitcnt vmcnt(18)
	ds_write2_b32 v40, v76, v77 offset0:24 offset1:90
	s_waitcnt vmcnt(16)
	ds_write2_b32 v40, v78, v79 offset0:156 offset1:222
	s_waitcnt vmcnt(14)
	ds_write2_b32 v41, v80, v81 offset0:32 offset1:98
	s_waitcnt vmcnt(12)
	ds_write2_b32 v41, v82, v83 offset0:164 offset1:230
	s_waitcnt vmcnt(10)
; #define GAS __attribute__((address_space(1)))
; #define LAS __attribute__((address_space(3)))
; #define LDS_WAIT() asm volatile("s_waitcnt lgkmcnt(0)" ::: "memory")
; __device__ __forceinline__ unsigned pk2(float lo, float hi) { return f2bf(lo) | (f2bf(hi) << 16); }
; __device__ __forceinline__ void tr_item(const float* W, int ld, int K, int nblk, int item, bf16* WT, bool gu, LAS float* scr, int lane) {
;     ...
;     LDS_WAIT(); asm volatile("" ::: "memory");
;     const int c = lane & 7;
; #pragma unroll
;     for (int j = 0; j < 4; ++j) { const int n = (lane >> 3) + 8 * j; const LAS float* s = scr + (8 * c) * 33 + n;
;         v4u o; o.x = pk2(s[0 * 33], s[1 * 33]); o.y = pk2(s[2 * 33], s[3 * 33]); o.z = pk2(s[4 * 33], s[5 * 33]); o.w = pk2(s[6 * 33], s[7 * 33]);
;         *(GAS v4u*)(WT + (size_t)(drow0 + n) * K + k0 + 8 * c) = o; }
;     LDS_WAIT(); asm volatile("" ::: "memory");
	ds_write2_b32 v42, v84, v85 offset0:40 offset1:106
	s_waitcnt vmcnt(8)
	ds_write2_b32 v42, v86, v62 offset0:172 offset1:238
	s_waitcnt vmcnt(6)
	ds_write2_b32 v43, v48, v49 offset0:48 offset1:114
	s_waitcnt vmcnt(4)
	ds_write2_b32 v43, v50, v51 offset0:180 offset1:246
	s_waitcnt vmcnt(2)
	ds_write2_b32 v44, v52, v53 offset0:56 offset1:122
	s_waitcnt vmcnt(0)
	ds_write2_b32 v44, v54, v46 offset0:188 offset1:254
	s_waitcnt lgkmcnt(0)
	ds_read2_b32 v[50:51], v34 offset1:8
	ds_read2_b32 v[54:55], v34 offset0:33 offset1:41
	ds_read2_b32 v[56:57], v34 offset0:66 offset1:74
	ds_read2_b32 v[58:59], v34 offset0:99 offset1:107
	ds_read2_b32 v[60:61], v34 offset0:132 offset1:140
	s_waitcnt lgkmcnt(4)
	v_bfe_u32 v46, v50, 16, 1
	v_add3_u32 v46, v50, v46, s57
	s_waitcnt lgkmcnt(3)
	v_bfe_u32 v47, v54, 16, 1
	v_lshrrev_b32_e32 v46, 16, v46
	v_add3_u32 v47, v54, v47, s57
	ds_read2_b32 v[62:63], v34 offset0:165 offset1:173
	v_and_or_b32 v46, v47, s58, v46
	s_waitcnt lgkmcnt(3)
	v_bfe_u32 v47, v56, 16, 1
	v_add3_u32 v47, v56, v47, s57
	s_waitcnt lgkmcnt(2)
	v_bfe_u32 v48, v58, 16, 1
	ds_read2_b32 v[64:65], v34 offset0:198 offset1:206
	v_lshrrev_b32_e32 v47, 16, v47
	v_add3_u32 v48, v58, v48, s57
	ds_read2_b32 v[66:67], v34 offset0:231 offset1:239
	v_and_or_b32 v47, v48, s58, v47
	s_waitcnt lgkmcnt(3)
	v_bfe_u32 v48, v60, 16, 1
	v_add3_u32 v48, v60, v48, s57
	s_waitcnt lgkmcnt(2)
	v_bfe_u32 v49, v62, 16, 1
	v_lshrrev_b32_e32 v48, 16, v48
	v_add3_u32 v49, v62, v49, s57
	v_and_or_b32 v48, v49, s58, v48
	s_waitcnt lgkmcnt(1)
	v_bfe_u32 v49, v64, 16, 1
	v_add_u32_e32 v68, s4, v33
	v_add3_u32 v49, v64, v49, s57
	s_waitcnt lgkmcnt(0)
	v_bfe_u32 v50, v66, 16, 1
	v_ashrrev_i32_e32 v69, 31, v68
	v_lshl_add_u64 v[52:53], v[24:25], 0, s[0:1]
	v_lshrrev_b32_e32 v49, 16, v49
	v_add3_u32 v50, v66, v50, s57
	v_lshlrev_b64 v[68:69], 11, v[68:69]
	v_and_or_b32 v49, v50, s58, v49
	v_lshl_add_u64 v[68:69], v[52:53], 0, v[68:69]
	global_store_dwordx4 v[68:69], v[46:49], off sc1 nt
	v_bfe_u32 v50, v67, 16, 1
	v_add3_u32 v50, v67, v50, s57
	v_bfe_u32 v46, v51, 16, 1
	v_add3_u32 v46, v51, v46, s57
	v_bfe_u32 v47, v55, 16, 1
	v_lshrrev_b32_e32 v46, 16, v46
	v_add3_u32 v47, v55, v47, s57
	v_and_or_b32 v46, v47, s58, v46
	v_bfe_u32 v47, v57, 16, 1
	v_add3_u32 v47, v57, v47, s57
	v_bfe_u32 v48, v59, 16, 1
	v_lshrrev_b32_e32 v47, 16, v47
	v_add3_u32 v48, v59, v48, s57
	v_and_or_b32 v47, v48, s58, v47
	v_bfe_u32 v48, v61, 16, 1
	v_add3_u32 v48, v61, v48, s57
	v_bfe_u32 v49, v63, 16, 1
	v_lshrrev_b32_e32 v48, 16, v48
	v_add3_u32 v49, v63, v49, s57
	v_and_or_b32 v48, v49, s58, v48
	v_bfe_u32 v49, v65, 16, 1
	v_add3_u32 v49, v65, v49, s57
	v_lshrrev_b32_e32 v49, 16, v49
	v_and_or_b32 v49, v50, s58, v49
	v_add_u32_e32 v50, s4, v35
	v_ashrrev_i32_e32 v51, 31, v50
	v_lshlrev_b64 v[50:51], 11, v[50:51]
	ds_read2_b32 v[54:55], v34 offset0:16 offset1:24
	v_lshl_add_u64 v[50:51], v[52:53], 0, v[50:51]
	global_store_dwordx4 v[50:51], v[46:49], off sc1 nt
	ds_read2_b32 v[50:51], v34 offset0:49 offset1:57
	ds_read2_b32 v[56:57], v34 offset0:82 offset1:90
	ds_read2_b32 v[58:59], v34 offset0:115 offset1:123
	s_waitcnt lgkmcnt(3)
	v_bfe_u32 v46, v54, 16, 1
	v_add3_u32 v46, v54, v46, s57
	s_waitcnt lgkmcnt(2)
	v_bfe_u32 v47, v50, 16, 1
	ds_read2_b32 v[60:61], v34 offset0:148 offset1:156
	v_lshrrev_b32_e32 v46, 16, v46
	v_add3_u32 v47, v50, v47, s57
	ds_read2_b32 v[62:63], v34 offset0:181 offset1:189
	v_and_or_b32 v46, v47, s58, v46
	s_waitcnt lgkmcnt(3)
	v_bfe_u32 v47, v56, 16, 1
	v_add3_u32 v47, v56, v47, s57
	s_waitcnt lgkmcnt(2)
	v_bfe_u32 v48, v58, 16, 1
	ds_read2_b32 v[64:65], v34 offset0:214 offset1:222
	v_lshrrev_b32_e32 v47, 16, v47
	v_add3_u32 v48, v58, v48, s57
	ds_read2_b32 v[66:67], v34 offset0:247 offset1:255
	v_and_or_b32 v47, v48, s58, v47
	s_waitcnt lgkmcnt(3)
	v_bfe_u32 v48, v60, 16, 1
	v_add3_u32 v48, v60, v48, s57
	s_waitcnt lgkmcnt(2)
	v_bfe_u32 v49, v62, 16, 1
	v_lshrrev_b32_e32 v48, 16, v48
	v_add3_u32 v49, v62, v49, s57
	v_and_or_b32 v48, v49, s58, v48
	s_waitcnt lgkmcnt(1)
	v_bfe_u32 v49, v64, 16, 1
	v_add_u32_e32 v68, s4, v36
	v_add3_u32 v49, v64, v49, s57
	s_waitcnt lgkmcnt(0)
	v_bfe_u32 v50, v66, 16, 1
	v_ashrrev_i32_e32 v69, 31, v68
	v_lshrrev_b32_e32 v49, 16, v49
	v_add3_u32 v50, v66, v50, s57
	v_lshlrev_b64 v[68:69], 11, v[68:69]
	v_and_or_b32 v49, v50, s58, v49
	v_lshl_add_u64 v[68:69], v[52:53], 0, v[68:69]
	global_store_dwordx4 v[68:69], v[46:49], off sc1 nt
	v_bfe_u32 v50, v67, 16, 1
	v_add3_u32 v50, v67, v50, s57
	v_bfe_u32 v46, v55, 16, 1
	v_add3_u32 v46, v55, v46, s57
	v_bfe_u32 v47, v51, 16, 1
	v_lshrrev_b32_e32 v46, 16, v46
	v_add3_u32 v47, v51, v47, s57
	v_and_or_b32 v46, v47, s58, v46
	v_bfe_u32 v47, v57, 16, 1
	v_add3_u32 v47, v57, v47, s57
	v_bfe_u32 v48, v59, 16, 1
	v_lshrrev_b32_e32 v47, 16, v47
	v_add3_u32 v48, v59, v48, s57
	v_and_or_b32 v47, v48, s58, v47
	v_bfe_u32 v48, v61, 16, 1
	v_add3_u32 v48, v61, v48, s57
	v_bfe_u32 v49, v63, 16, 1
	v_lshrrev_b32_e32 v48, 16, v48
	v_add3_u32 v49, v63, v49, s57
	v_and_or_b32 v48, v49, s58, v48
	v_bfe_u32 v49, v65, 16, 1
	v_add3_u32 v49, v65, v49, s57
	v_lshrrev_b32_e32 v49, 16, v49
	v_and_or_b32 v49, v50, s58, v49
	v_add_u32_e32 v50, s4, v37
	v_ashrrev_i32_e32 v51, 31, v50
	v_lshlrev_b64 v[50:51], 11, v[50:51]
	v_lshl_add_u64 v[50:51], v[52:53], 0, v[50:51]
	global_store_dwordx4 v[50:51], v[46:49], off sc1 nt
	s_waitcnt lgkmcnt(0)

; __device__ __forceinline__ void tr_item(const float* W, int ld, int K, int nblk, int item, bf16* WT, bool gu, LAS float* scr, int lane) {
;     const int kb = item / nblk, nb = item % nblk, k0 = 64 * kb, n0 = 32 * nb;
;     int drow0 = n0;
;     if (gu) { const int bj = n0 / FF, j = n0 - bj * FF; drow0 = 256 * (j / 128) + 128 * bj + (j % 128); }
;     { float t_[32];
; #pragma unroll
;       for (int i = 0; i < 32; ++i) t_[i] = W[(size_t)(k0 + 2 * i + (lane >> 5)) * ld + n0 + (lane & 31)];
; #pragma unroll
;       for (int i = 0; i < 32; ++i) scr[(2 * i + (lane >> 5)) * 33 + (lane & 31)] = t_[i]; }
; __device__ __forceinline__ void convert_items(Frame& F, const Args& a, int lo, int hi, int w, int nw) {
;     ...
;         if (r < I_FI) { tr_item(a.in[7], 3 * D + 16, D, 96, r, (bf16*)(F.ws + WS_WFOXIN), false, scr, lane); continue; } r -= I_FI;
.LBB0_1432:
	s_andn2_b64 vcc, exec, s[4:5]
	s_cbranch_vccnz .LBB0_1405
	s_mul_hi_i32 s0, s3, 0x2aaaaaab
	s_lshr_b32 s4, s0, 31
	s_ashr_i32 s0, s0, 4
	s_add_i32 s0, s0, s4
	s_lshl_b32 s6, s0, 6
	s_mulk_i32 s0, 0xf400
	s_add_i32 s4, s8, s0
	v_add_u32_e32 v64, s6, v28
	s_ashr_i32 s5, s4, 31
	v_lshl_add_u64 v[46:47], s[4:5], 2, v[14:15]
	v_add_u32_e32 v50, 2, v64
	v_add_u32_e32 v52, 4, v64
	v_add_u32_e32 v54, 6, v64
	v_add_u32_e32 v56, 8, v64
	v_add_u32_e32 v58, 10, v64
	v_add_u32_e32 v60, 12, v64
	v_add_u32_e32 v62, 14, v64
	v_mad_i64_i32 v[48:49], s[62:63], v64, s60, v[46:47]
	v_mad_i64_i32 v[50:51], s[62:63], v50, s60, v[46:47]
	v_mad_i64_i32 v[52:53], s[62:63], v52, s60, v[46:47]
	v_mad_i64_i32 v[54:55], s[62:63], v54, s60, v[46:47]
	v_mad_i64_i32 v[56:57], s[62:63], v56, s60, v[46:47]
	v_mad_i64_i32 v[58:59], s[62:63], v58, s60, v[46:47]
	v_mad_i64_i32 v[60:61], s[62:63], v60, s60, v[46:47]
	v_mad_i64_i32 v[62:63], s[62:63], v62, s60, v[46:47]
	global_load_dword v65, v[48:49], off nt
	global_load_dword v66, v[50:51], off nt
	global_load_dword v67, v[52:53], off nt
	global_load_dword v68, v[54:55], off nt
	global_load_dword v69, v[56:57], off nt
	global_load_dword v70, v[58:59], off nt
	global_load_dword v71, v[60:61], off nt
	global_load_dword v72, v[62:63], off nt
	v_add_u32_e32 v48, 16, v64
	v_add_u32_e32 v50, 18, v64
	v_add_u32_e32 v52, 20, v64
	v_add_u32_e32 v54, 22, v64
	v_add_u32_e32 v56, 24, v64
	v_add_u32_e32 v58, 26, v64
	v_add_u32_e32 v60, 28, v64
	v_add_u32_e32 v62, 30, v64
	v_mad_i64_i32 v[48:49], s[62:63], v48, s60, v[46:47]
	v_mad_i64_i32 v[50:51], s[62:63], v50, s60, v[46:47]
	v_mad_i64_i32 v[52:53], s[62:63], v52, s60, v[46:47]
	v_mad_i64_i32 v[54:55], s[62:63], v54, s60, v[46:47]
	v_mad_i64_i32 v[56:57], s[62:63], v56, s60, v[46:47]
	v_mad_i64_i32 v[58:59], s[62:63], v58, s60, v[46:47]
	v_mad_i64_i32 v[60:61], s[62:63], v60, s60, v[46:47]
	v_mad_i64_i32 v[62:63], s[62:63], v62, s60, v[46:47]
	global_load_dword v73, v[48:49], off nt
	global_load_dword v74, v[50:51], off nt
	global_load_dword v75, v[52:53], off nt
	global_load_dword v76, v[54:55], off nt
	global_load_dword v77, v[56:57], off nt
	global_load_dword v78, v[58:59], off nt
	global_load_dword v79, v[60:61], off nt
	global_load_dword v80, v[62:63], off nt
	v_add_u32_e32 v48, 32, v64
	v_add_u32_e32 v50, 34, v64
	v_add_u32_e32 v52, 36, v64
	v_add_u32_e32 v54, 38, v64
	v_add_u32_e32 v56, 40, v64
	v_add_u32_e32 v58, 42, v64
	v_add_u32_e32 v60, 44, v64
	v_add_u32_e32 v62, 46, v64
	v_mad_i64_i32 v[48:49], s[62:63], v48, s60, v[46:47]
	v_mad_i64_i32 v[50:51], s[62:63], v50, s60, v[46:47]
	v_mad_i64_i32 v[52:53], s[62:63], v52, s60, v[46:47]
	v_mad_i64_i32 v[54:55], s[62:63], v54, s60, v[46:47]
	v_mad_i64_i32 v[56:57], s[62:63], v56, s60, v[46:47]
	v_mad_i64_i32 v[58:59], s[62:63], v58, s60, v[46:47]
	v_mad_i64_i32 v[60:61], s[62:63], v60, s60, v[46:47]
	v_mad_i64_i32 v[62:63], s[62:63], v62, s60, v[46:47]
	global_load_dword v81, v[48:49], off nt
	global_load_dword v82, v[50:51], off nt
	global_load_dword v83, v[52:53], off nt
	global_load_dword v84, v[54:55], off nt
	global_load_dword v85, v[56:57], off nt
	global_load_dword v86, v[58:59], off nt
	global_load_dword v87, v[60:61], off nt
	s_nop 0
	global_load_dword v62, v[62:63], off nt
	v_add_u32_e32 v48, 48, v64
	v_add_u32_e32 v50, 50, v64
	v_add_u32_e32 v52, 52, v64
	v_add_u32_e32 v54, 54, v64
	v_add_u32_e32 v56, 56, v64
	v_add_u32_e32 v58, 58, v64
	v_add_u32_e32 v60, 60, v64
	v_add_u32_e32 v63, 62, v64
	v_mad_i64_i32 v[48:49], s[62:63], v48, s60, v[46:47]
	v_mad_i64_i32 v[50:51], s[62:63], v50, s60, v[46:47]
	v_mad_i64_i32 v[52:53], s[62:63], v52, s60, v[46:47]
	v_mad_i64_i32 v[54:55], s[62:63], v54, s60, v[46:47]
	v_mad_i64_i32 v[56:57], s[62:63], v56, s60, v[46:47]
	v_mad_i64_i32 v[58:59], s[62:63], v58, s60, v[46:47]
	v_mad_i64_i32 v[60:61], s[62:63], v60, s60, v[46:47]
	v_mad_i64_i32 v[46:47], s[62:63], v63, s60, v[46:47]
	global_load_dword v48, v[48:49], off nt
	s_nop 0
	global_load_dword v49, v[50:51], off nt
	s_nop 0
	global_load_dword v50, v[52:53], off nt
	global_load_dword v51, v[54:55], off nt
	s_nop 0
	global_load_dword v52, v[56:57], off nt
	global_load_dword v53, v[58:59], off nt
	global_load_dword v54, v[60:61], off nt
	s_nop 0
	global_load_dword v46, v[46:47], off nt
	s_waitcnt vmcnt(30)
	ds_write2_b32 v29, v65, v66 offset1:66
	s_waitcnt vmcnt(28)
	ds_write2_b32 v29, v67, v68 offset0:132 offset1:198
	s_waitcnt vmcnt(26)
	ds_write2_b32 v38, v69, v70 offset0:8 offset1:74
	s_waitcnt vmcnt(24)
	ds_write2_b32 v38, v71, v72 offset0:140 offset1:206
	s_waitcnt vmcnt(22)
	ds_write2_b32 v39, v73, v74 offset0:16 offset1:82
	s_waitcnt vmcnt(20)
	ds_write2_b32 v39, v75, v76 offset0:148 offset1:214
	s_waitcnt vmcnt(18)
	ds_write2_b32 v40, v77, v78 offset0:24 offset1:90
	s_waitcnt vmcnt(16)
	ds_write2_b32 v40, v79, v80 offset0:156 offset1:222
	s_waitcnt vmcnt(14)
	ds_write2_b32 v41, v81, v82 offset0:32 offset1:98
	s_waitcnt vmcnt(12)
	ds_write2_b32 v41, v83, v84 offset0:164 offset1:230
	s_waitcnt vmcnt(10)
	ds_write2_b32 v42, v85, v86 offset0:40 offset1:106
	s_waitcnt vmcnt(8)
	ds_write2_b32 v42, v87, v62 offset0:172 offset1:238
	s_waitcnt vmcnt(6)
	ds_write2_b32 v43, v48, v49 offset0:48 offset1:114
	s_waitcnt vmcnt(4)
; #define GAS __attribute__((address_space(1)))
; #define LAS __attribute__((address_space(3)))
; #define LDS_WAIT() asm volatile("s_waitcnt lgkmcnt(0)" ::: "memory")
; __device__ __forceinline__ unsigned pk2(float lo, float hi) { return f2bf(lo) | (f2bf(hi) << 16); }
; __device__ __forceinline__ void tr_item(const float* W, int ld, int K, int nblk, int item, bf16* WT, bool gu, LAS float* scr, int lane) {
;     ...
;     LDS_WAIT(); asm volatile("" ::: "memory");
;     const int c = lane & 7;
; #pragma unroll
;     for (int j = 0; j < 4; ++j) { const int n = (lane >> 3) + 8 * j; const LAS float* s = scr + (8 * c) * 33 + n;
;         v4u o; o.x = pk2(s[0 * 33], s[1 * 33]); o.y = pk2(s[2 * 33], s[3 * 33]); o.z = pk2(s[4 * 33], s[5 * 33]); o.w = pk2(s[6 * 33], s[7 * 33]);
;         *(GAS v4u*)(WT + (size_t)(drow0 + n) * K + k0 + 8 * c) = o; }
;     LDS_WAIT(); asm volatile("" ::: "memory");
	ds_write2_b32 v43, v50, v51 offset0:180 offset1:246
	s_waitcnt vmcnt(2)
	ds_write2_b32 v44, v52, v53 offset0:56 offset1:122
	s_waitcnt vmcnt(0)
	ds_write2_b32 v44, v54, v46 offset0:188 offset1:254
	s_waitcnt lgkmcnt(0)
	ds_read2_b32 v[50:51], v34 offset1:8
	ds_read2_b32 v[54:55], v34 offset0:33 offset1:41
	ds_read2_b32 v[56:57], v34 offset0:66 offset1:74
	ds_read2_b32 v[58:59], v34 offset0:99 offset1:107
	ds_read2_b32 v[60:61], v34 offset0:132 offset1:140
	s_waitcnt lgkmcnt(4)
	v_bfe_u32 v46, v50, 16, 1
	v_add3_u32 v46, v50, v46, s57
	s_waitcnt lgkmcnt(3)
	v_bfe_u32 v47, v54, 16, 1
	v_lshrrev_b32_e32 v46, 16, v46
	v_add3_u32 v47, v54, v47, s57
	ds_read2_b32 v[62:63], v34 offset0:165 offset1:173
	v_and_or_b32 v46, v47, s58, v46
	s_waitcnt lgkmcnt(3)
	v_bfe_u32 v47, v56, 16, 1
	v_add3_u32 v47, v56, v47, s57
	s_waitcnt lgkmcnt(2)
	v_bfe_u32 v48, v58, 16, 1
	ds_read2_b32 v[64:65], v34 offset0:198 offset1:206
	v_lshrrev_b32_e32 v47, 16, v47
	v_add3_u32 v48, v58, v48, s57
	ds_read2_b32 v[66:67], v34 offset0:231 offset1:239
	v_and_or_b32 v47, v48, s58, v47
	s_waitcnt lgkmcnt(3)
	v_bfe_u32 v48, v60, 16, 1
	v_add3_u32 v48, v60, v48, s57
	s_waitcnt lgkmcnt(2)
	v_bfe_u32 v49, v62, 16, 1
	v_lshrrev_b32_e32 v48, 16, v48
	v_add3_u32 v49, v62, v49, s57
	v_and_or_b32 v48, v49, s58, v48
	s_waitcnt lgkmcnt(1)
	v_bfe_u32 v49, v64, 16, 1
	v_add_u32_e32 v68, s4, v33
	s_ashr_i32 s7, s6, 31
	v_add3_u32 v49, v64, v49, s57
	s_waitcnt lgkmcnt(0)
	v_bfe_u32 v50, v66, 16, 1
	v_ashrrev_i32_e32 v69, 31, v68
	v_lshl_add_u64 v[52:53], s[6:7], 1, v[26:27]
	v_lshrrev_b32_e32 v49, 16, v49
	v_add3_u32 v50, v66, v50, s57
	v_lshlrev_b64 v[70:71], 11, v[68:69]
	v_and_or_b32 v49, v50, s58, v49
	v_lshl_add_u64 v[70:71], v[52:53], 0, v[70:71]
	global_store_dwordx4 v[70:71], v[46:49], off sc1 nt
	v_bfe_u32 v50, v67, 16, 1
	v_add3_u32 v50, v67, v50, s57
	v_bfe_u32 v46, v51, 16, 1
	v_add3_u32 v46, v51, v46, s57
	v_bfe_u32 v47, v55, 16, 1
	v_lshrrev_b32_e32 v46, 16, v46
	v_add3_u32 v47, v55, v47, s57
	v_and_or_b32 v46, v47, s58, v46
	v_bfe_u32 v47, v57, 16, 1
	v_add3_u32 v47, v57, v47, s57
	v_bfe_u32 v48, v59, 16, 1
	v_lshrrev_b32_e32 v47, 16, v47
	v_add3_u32 v48, v59, v48, s57
	v_and_or_b32 v47, v48, s58, v47
	v_bfe_u32 v48, v61, 16, 1
	v_add3_u32 v48, v61, v48, s57
	v_bfe_u32 v49, v63, 16, 1
	v_lshrrev_b32_e32 v48, 16, v48
	v_add3_u32 v49, v63, v49, s57
	v_and_or_b32 v48, v49, s58, v48
	v_bfe_u32 v49, v65, 16, 1
	v_add3_u32 v49, v65, v49, s57
	v_lshrrev_b32_e32 v49, 16, v49
	v_and_or_b32 v49, v50, s58, v49
	v_add_u32_e32 v50, 8, v68
	v_ashrrev_i32_e32 v51, 31, v50
	v_lshlrev_b64 v[50:51], 11, v[50:51]
	ds_read2_b32 v[54:55], v34 offset0:16 offset1:24
	v_lshl_add_u64 v[50:51], v[52:53], 0, v[50:51]
	global_store_dwordx4 v[50:51], v[46:49], off sc1 nt
	ds_read2_b32 v[50:51], v34 offset0:49 offset1:57
	ds_read2_b32 v[56:57], v34 offset0:82 offset1:90
	ds_read2_b32 v[58:59], v34 offset0:115 offset1:123
	s_waitcnt lgkmcnt(3)
	v_bfe_u32 v46, v54, 16, 1
	v_add3_u32 v46, v54, v46, s57
	s_waitcnt lgkmcnt(2)
	v_bfe_u32 v47, v50, 16, 1
	ds_read2_b32 v[60:61], v34 offset0:148 offset1:156
	v_lshrrev_b32_e32 v46, 16, v46
	v_add3_u32 v47, v50, v47, s57
	ds_read2_b32 v[62:63], v34 offset0:181 offset1:189
	v_and_or_b32 v46, v47, s58, v46
	s_waitcnt lgkmcnt(3)
	v_bfe_u32 v47, v56, 16, 1
	v_add3_u32 v47, v56, v47, s57
	s_waitcnt lgkmcnt(2)
	v_bfe_u32 v48, v58, 16, 1
	ds_read2_b32 v[64:65], v34 offset0:214 offset1:222
	v_lshrrev_b32_e32 v47, 16, v47
	v_add3_u32 v48, v58, v48, s57
	ds_read2_b32 v[66:67], v34 offset0:247 offset1:255
	v_and_or_b32 v47, v48, s58, v47
	s_waitcnt lgkmcnt(3)
	v_bfe_u32 v48, v60, 16, 1
	v_add3_u32 v48, v60, v48, s57
	s_waitcnt lgkmcnt(2)
	v_bfe_u32 v49, v62, 16, 1
	v_lshrrev_b32_e32 v48, 16, v48
	v_add3_u32 v49, v62, v49, s57
	v_and_or_b32 v48, v49, s58, v48
	s_waitcnt lgkmcnt(1)
	v_bfe_u32 v49, v64, 16, 1
	v_add_u32_e32 v70, 16, v68
	v_add3_u32 v49, v64, v49, s57
	s_waitcnt lgkmcnt(0)
	v_bfe_u32 v50, v66, 16, 1
	v_ashrrev_i32_e32 v71, 31, v70
	v_lshrrev_b32_e32 v49, 16, v49
	v_add3_u32 v50, v66, v50, s57
	v_lshlrev_b64 v[70:71], 11, v[70:71]
	v_and_or_b32 v49, v50, s58, v49
	v_lshl_add_u64 v[70:71], v[52:53], 0, v[70:71]
	global_store_dwordx4 v[70:71], v[46:49], off sc1 nt
	v_bfe_u32 v50, v67, 16, 1
	v_add3_u32 v50, v67, v50, s57
	v_bfe_u32 v46, v55, 16, 1
	v_add3_u32 v46, v55, v46, s57
	v_bfe_u32 v47, v51, 16, 1
	v_lshrrev_b32_e32 v46, 16, v46
	v_add3_u32 v47, v51, v47, s57
	v_and_or_b32 v46, v47, s58, v46
	v_bfe_u32 v47, v57, 16, 1
	v_add3_u32 v47, v57, v47, s57
	v_bfe_u32 v48, v59, 16, 1
	v_lshrrev_b32_e32 v47, 16, v47
	v_add3_u32 v48, v59, v48, s57
	v_and_or_b32 v47, v48, s58, v47
	v_bfe_u32 v48, v61, 16, 1
	v_add3_u32 v48, v61, v48, s57
	v_bfe_u32 v49, v63, 16, 1
	v_lshrrev_b32_e32 v48, 16, v48
	v_add3_u32 v49, v63, v49, s57
	v_and_or_b32 v48, v49, s58, v48
	v_bfe_u32 v49, v65, 16, 1
	v_add3_u32 v49, v65, v49, s57
	v_lshrrev_b32_e32 v49, 16, v49
	v_and_or_b32 v49, v50, s58, v49
	v_add_u32_e32 v50, 24, v68
	v_ashrrev_i32_e32 v51, 31, v50
	v_lshlrev_b64 v[50:51], 11, v[50:51]
	v_lshl_add_u64 v[50:51], v[52:53], 0, v[50:51]
	global_store_dwordx4 v[50:51], v[46:49], off sc1 nt
	s_waitcnt lgkmcnt(0)
	s_branch .LBB0_1405
